# adds: FFT complex products use one packed FMA with per-lane modifiers instead of two FMAs plus a lane move (437 sites, same values)
# speedup vs baseline: 1.0218x; 1.0119x over previous
; __device__ __forceinline__ void lds_barrier() { asm volatile("s_waitcnt lgkmcnt(0)" ::: "memory"); __builtin_amdgcn_s_barrier(); asm volatile("" ::: "memory"); }
; template <int R, class XT, class TWT>
; __device__ __forceinline__ void dif_task(XT X, TWT tw, int s, int task) {
;     const int lgM = 13 - s, lgq = lgM - R, q = 1 << lgq;
;     const int j0 = task & (q - 1), blk = task >> lgq, base = (blk << lgM) + j0;
;     const int pb = PADI(base), qp = (q >= 32) ? q + (q >> 4) : q;
;     f32x2v v[1 << R];
; #pragma unroll
;     for (int k = 0; k < (1 << R); ++k) v[k] = X[pb + k * qp];
; #pragma unroll
;     for (int r = 0; r < R; ++r) {
;         const int pb = R - 1 - r;
; #pragma unroll
;         for (int k = 0; k < (1 << R); ++k) if (!((k >> pb) & 1)) {
;             const int klo = k & ((1 << pb) - 1);
;             const f32x2v w = tw[(j0 + (klo << lgq)) << (s + r)];
;             const f32x2v a = v[k], b = v[k + (1 << pb)], d = a - b;
;             v[k] = a + b; v[k + (1 << pb)] = (f32x2v){d.x * w.x - d.y * w.y, d.x * w.y + d.y * w.x};
;         }
;     }
; #pragma unroll
;     for (int k = 0; k < (1 << R); ++k) X[pb + k * qp] = v[k];
; }
; __device__ __forceinline__ void phase_spectra(Frame& F0, int l) {
;     ...
;         { float vv[16];
; #pragma unroll
;             for (int r = 0; r < 16; ++r) { const int e = F.tid + 512 * r, seg = e >> lgN, n = e & (N - 1); const int oc = col0 + seg;
;                 float v = 0.f;
;                 if (n < L) v = FT[(size_t)oc * L + n]; else if (n > L) v = FT[(size_t)(512 + oc) * L + (N - n)];
;                 vv[r] = v; }
; #pragma unroll
;             for (int r = 0; r < 16; ++r) X[PADI(F.tid + 512 * r)] = (f32x2v){vv[r], 0.f}; }
;         lds_barrier();
;         fft_fwd_upper(X, tw, 13 - lgN, F.tid);
.LBB0_421:
	s_or_b64 exec, exec, s[2:3]
	v_mov_b32_e32 v3, v181
	v_mov_b32_e32 v5, v181
	v_mov_b32_e32 v7, v181
	v_mov_b32_e32 v9, v181
	v_mov_b32_e32 v11, v181
	v_mov_b32_e32 v13, v181
	v_mov_b32_e32 v15, v181
	v_mov_b32_e32 v17, v181
	v_mov_b32_e32 v19, v181
	v_mov_b32_e32 v21, v181
	v_mov_b32_e32 v23, v181
	v_mov_b32_e32 v25, v181
	v_mov_b32_e32 v27, v181
	v_mov_b32_e32 v29, v181
	v_mov_b32_e32 v31, v181
	s_waitcnt vmcnt(0)
	ds_write_b64 v60, v[2:3]
	ds_write_b64 v61, v[4:5] offset:4096
	ds_write_b64 v62, v[6:7] offset:8192
	ds_write_b64 v63, v[8:9] offset:12288
	ds_write_b64 v64, v[10:11] offset:16384
	ds_write_b64 v65, v[12:13] offset:20480
	ds_write_b64 v66, v[14:15] offset:24576
	ds_write_b64 v67, v[16:17] offset:28672
	ds_write_b64 v68, v[18:19] offset:32768
	ds_write_b64 v69, v[20:21] offset:36864
	ds_write_b64 v70, v[22:23] offset:40960
	ds_write_b64 v71, v[24:25] offset:45056
	ds_write_b64 v72, v[26:27] offset:49152
	ds_write_b64 v73, v[28:29] offset:53248
	ds_write_b64 v74, v[30:31] offset:57344
	ds_write_b64 v75, v[180:181] offset:61440
	s_waitcnt lgkmcnt(0)
	s_barrier
	s_andn2_b64 vcc, exec, s[22:23]
	s_cbranch_vccnz .LBB0_487
	ds_read_b64 v[6:7], v1
	ds_read_b64 v[8:9], v1 offset:4352
	ds_read_b64 v[10:11], v1 offset:8704
	ds_read_b64 v[12:13], v1 offset:13056
	ds_read_b64 v[14:15], v1 offset:17408
	ds_read_b64 v[16:17], v1 offset:21760
	ds_read_b64 v[18:19], v1 offset:26112
	ds_read_b64 v[20:21], v1 offset:30464
	ds_read_b64 v[22:23], v1 offset:34816
	ds_read_b64 v[24:25], v1 offset:39168
	ds_read_b64 v[26:27], v1 offset:43520
	ds_read_b64 v[28:29], v1 offset:47872
	ds_read_b64 v[30:31], v1 offset:52224
	ds_read_b64 v[32:33], v1 offset:56576
	ds_read_b64 v[34:35], v1 offset:60928
	ds_read_b64 v[94:95], v1 offset:65280
	ds_read2st64_b64 v[2:5], v36 offset1:16
	ds_read_b64 v[96:97], v79
	ds_read_b64 v[98:99], v80
	ds_read_b64 v[100:101], v81
	ds_read_b64 v[102:103], v37
	ds_read_b64 v[104:105], v38
	ds_read_b64 v[106:107], v39
	ds_read_b64 v[108:109], v40
	s_waitcnt lgkmcnt(14)
	v_pk_add_f32 v[110:111], v[6:7], v[22:23] neg_lo:[0,1] neg_hi:[0,1]
	v_pk_add_f32 v[6:7], v[6:7], v[22:23]
	s_waitcnt lgkmcnt(7)
	v_pk_mul_f32 v[112:113], v[110:111], v[2:3] op_sel:[1,1] op_sel_hi:[1,0]
	s_mov_b64 s[2:3], 0x20c00000
	v_pk_fma_f32 v[114:115], v[110:111], v[2:3], v[112:113] op_sel_hi:[0,1,1] neg_lo:[0,0,1]
	v_pk_add_f32 v[110:111], v[14:15], v[30:31] neg_lo:[0,1] neg_hi:[0,1]
	v_pk_add_f32 v[14:15], v[14:15], v[30:31]
	v_pk_mul_f32 v[112:113], v[110:111], v[2:3] op_sel:[1,0] op_sel_hi:[0,0]
	v_pk_fma_f32 v[116:117], v[110:111], v[2:3], v[112:113] op_sel:[0,1,0] neg_hi:[0,0,1]
	v_pk_add_f32 v[22:23], v[6:7], v[14:15]
	v_pk_add_f32 v[2:3], v[114:115], v[116:117] neg_lo:[0,1] neg_hi:[0,1]
	v_pk_add_f32 v[6:7], v[6:7], v[14:15] neg_lo:[0,1] neg_hi:[0,1]
	s_waitcnt lgkmcnt(6)
	v_pk_mul_f32 v[110:111], v[96:97], v[2:3] op_sel:[1,1] op_sel_hi:[0,1]
	v_pk_fma_f32 v[112:113], v[96:97], v[2:3], v[110:111] op_sel_hi:[1,0,1] neg_lo:[0,0,1]
	v_pk_mul_f32 v[14:15], v[6:7], v[96:97] op_sel:[1,1] op_sel_hi:[1,0]
	v_pk_add_f32 v[2:3], v[10:11], v[26:27] neg_lo:[0,1] neg_hi:[0,1]
	v_pk_add_f32 v[10:11], v[10:11], v[26:27]
	v_pk_mul_f32 v[110:111], v[2:3], v[4:5] op_sel:[1,1] op_sel_hi:[1,0]
	s_mov_b64 s[0:1], 13
	v_pk_fma_f32 v[118:119], v[2:3], v[4:5], v[110:111] op_sel_hi:[0,1,1] neg_lo:[0,0,1]
	v_pk_add_f32 v[2:3], v[18:19], v[34:35] neg_lo:[0,1] neg_hi:[0,1]
	v_pk_add_f32 v[18:19], v[18:19], v[34:35]
	v_pk_mul_f32 v[110:111], v[2:3], v[4:5] op_sel:[1,0] op_sel_hi:[0,0]
	v_pk_fma_f32 v[120:121], v[2:3], v[4:5], v[110:111] op_sel:[0,1,0] neg_hi:[0,0,1]
	v_pk_add_f32 v[26:27], v[10:11], v[18:19]
	v_pk_add_f32 v[2:3], v[118:119], v[120:121] neg_lo:[0,1] neg_hi:[0,1]
	v_pk_add_f32 v[30:31], v[22:23], v[26:27]
	v_pk_mul_f32 v[4:5], v[96:97], v[2:3] op_sel_hi:[0,1]
	v_pk_fma_f32 v[110:111], v[96:97], v[2:3], v[4:5] op_sel:[1,0,1] op_sel_hi:[1,1,0] neg_hi:[0,0,1]
	v_pk_add_f32 v[22:23], v[22:23], v[26:27] neg_lo:[0,1] neg_hi:[0,1]
	v_pk_add_f32 v[2:3], v[112:113], v[110:111] neg_lo:[0,1] neg_hi:[0,1]
	s_waitcnt lgkmcnt(4)
	v_pk_mul_f32 v[26:27], v[22:23], v[100:101] op_sel:[1,1] op_sel_hi:[1,0]
	v_pk_mul_f32 v[4:5], v[100:101], v[2:3] op_sel:[1,1] op_sel_hi:[0,1]
	v_pk_fma_f32 v[122:123], v[100:101], v[2:3], v[4:5] op_sel_hi:[1,0,1] neg_lo:[0,0,1]
	s_nop 0
	v_pk_add_f32 v[2:3], v[8:9], v[24:25] neg_lo:[0,1] neg_hi:[0,1]
	v_pk_add_f32 v[8:9], v[8:9], v[24:25]
	s_waitcnt lgkmcnt(3)
	v_pk_mul_f32 v[4:5], v[2:3], v[102:103] op_sel:[1,1] op_sel_hi:[1,0]
	s_nop 0
	v_pk_fma_f32 v[124:125], v[2:3], v[102:103], v[4:5] op_sel_hi:[0,1,1] neg_lo:[0,0,1]
	v_pk_add_f32 v[2:3], v[16:17], v[32:33] neg_lo:[0,1] neg_hi:[0,1]
	v_pk_add_f32 v[16:17], v[16:17], v[32:33]
	v_pk_mul_f32 v[4:5], v[2:3], v[102:103] op_sel:[1,0] op_sel_hi:[0,0]
	v_pk_fma_f32 v[126:127], v[2:3], v[102:103], v[4:5] op_sel:[0,1,0] neg_hi:[0,0,1]
	v_pk_add_f32 v[24:25], v[8:9], v[16:17]
	v_pk_add_f32 v[2:3], v[124:125], v[126:127] neg_lo:[0,1] neg_hi:[0,1]
	v_pk_add_f32 v[8:9], v[8:9], v[16:17] neg_lo:[0,1] neg_hi:[0,1]
	v_pk_mul_f32 v[4:5], v[98:99], v[2:3] op_sel:[1,1] op_sel_hi:[0,1]
	v_pk_fma_f32 v[102:103], v[98:99], v[2:3], v[4:5] op_sel_hi:[1,0,1] neg_lo:[0,0,1]
	s_nop 0
	v_pk_add_f32 v[2:3], v[12:13], v[28:29] neg_lo:[0,1] neg_hi:[0,1]
	v_pk_add_f32 v[12:13], v[12:13], v[28:29]
	s_waitcnt lgkmcnt(2)
; template <int R, class XT, class TWT>
; __device__ __forceinline__ void dif_task(XT X, TWT tw, int s, int task) {
;     const int lgM = 13 - s, lgq = lgM - R, q = 1 << lgq;
;     const int j0 = task & (q - 1), blk = task >> lgq, base = (blk << lgM) + j0;
;     const int pb = PADI(base), qp = (q >= 32) ? q + (q >> 4) : q;
;     f32x2v v[1 << R];
; #pragma unroll
;     for (int k = 0; k < (1 << R); ++k) v[k] = X[pb + k * qp];
; #pragma unroll
;     for (int r = 0; r < R; ++r) {
;         const int pb = R - 1 - r;
; #pragma unroll
;         for (int k = 0; k < (1 << R); ++k) if (!((k >> pb) & 1)) {
;             const int klo = k & ((1 << pb) - 1);
;             const f32x2v w = tw[(j0 + (klo << lgq)) << (s + r)];
;             const f32x2v a = v[k], b = v[k + (1 << pb)], d = a - b;
;             v[k] = a + b; v[k + (1 << pb)] = (f32x2v){d.x * w.x - d.y * w.y, d.x * w.y + d.y * w.x};
;         }
;     }
; #pragma unroll
;     for (int k = 0; k < (1 << R); ++k) X[pb + k * qp] = v[k];
; }
	v_pk_mul_f32 v[4:5], v[2:3], v[104:105] op_sel:[1,1] op_sel_hi:[1,0]
	s_nop 0
	v_pk_fma_f32 v[128:129], v[2:3], v[104:105], v[4:5] op_sel_hi:[0,1,1] neg_lo:[0,0,1]
	v_pk_add_f32 v[2:3], v[20:21], v[94:95] neg_lo:[0,1] neg_hi:[0,1]
	v_pk_add_f32 v[20:21], v[20:21], v[94:95]
	v_pk_mul_f32 v[4:5], v[2:3], v[104:105] op_sel:[1,0] op_sel_hi:[0,0]
	v_pk_fma_f32 v[130:131], v[2:3], v[104:105], v[4:5] op_sel:[0,1,0] neg_hi:[0,0,1]
	v_pk_add_f32 v[28:29], v[12:13], v[20:21]
	v_pk_add_f32 v[2:3], v[128:129], v[130:131] neg_lo:[0,1] neg_hi:[0,1]
	v_pk_add_f32 v[32:33], v[24:25], v[28:29]
	s_waitcnt lgkmcnt(1)
	v_pk_mul_f32 v[4:5], v[106:107], v[2:3] op_sel_hi:[0,1]
	v_pk_fma_f32 v[104:105], v[106:107], v[2:3], v[4:5] op_sel:[1,0,1] op_sel_hi:[1,1,0] neg_hi:[0,0,1]
	v_pk_add_f32 v[34:35], v[30:31], v[32:33]
	v_pk_add_f32 v[2:3], v[102:103], v[104:105] neg_lo:[0,1] neg_hi:[0,1]
	v_pk_add_f32 v[30:31], v[30:31], v[32:33] neg_lo:[0,1] neg_hi:[0,1]
	v_pk_mul_f32 v[4:5], v[100:101], v[2:3] op_sel_hi:[0,1]
	v_pk_fma_f32 v[132:133], v[100:101], v[2:3], v[4:5] op_sel:[1,0,1] op_sel_hi:[1,1,0]
	v_pk_fma_f32 v[2:3], v[100:101], v[2:3], v[4:5] op_sel:[1,0,1] op_sel_hi:[1,1,0] neg_lo:[0,0,1] neg_hi:[0,0,1]
	s_waitcnt lgkmcnt(0)
	v_xor_b32_e32 v4, 0x80000000, v108
	v_cndmask_b32_e64 v5, v4, v109, s[36:37]
	v_cndmask_b32_e64 v4, v109, v108, s[36:37]
	v_pk_mul_f32 v[32:33], v[30:31], v[4:5] op_sel:[1,1] op_sel_hi:[1,0]
	v_mov_b32_e32 v133, v3
	v_pk_fma_f32 v[94:95], v[30:31], v[4:5], v[32:33] op_sel_hi:[0,1,1] neg_lo:[0,0,1]
	v_pk_fma_f32 v[30:31], v[22:23], v[100:101], v[26:27] op_sel_hi:[0,1,1] neg_lo:[0,0,1]
	v_pk_add_f32 v[22:23], v[24:25], v[28:29] neg_lo:[0,1] neg_hi:[0,1]
	v_pk_add_f32 v[2:3], v[122:123], v[132:133] neg_lo:[0,1] neg_hi:[0,1]
	v_pk_mul_f32 v[24:25], v[22:23], v[100:101] op_sel_hi:[1,0]
	s_nop 0
	v_pk_fma_f32 v[26:27], v[22:23], v[100:101], v[24:25] op_sel:[0,1,1] op_sel_hi:[1,1,0] neg_hi:[0,0,1]
	s_nop 0
	v_pk_add_f32 v[24:25], v[30:31], v[26:27] neg_lo:[0,1] neg_hi:[0,1]
	v_pk_add_f32 v[22:23], v[30:31], v[26:27]
	v_pk_mul_f32 v[26:27], v[4:5], v[24:25] op_sel:[1,1] op_sel_hi:[0,1]
	v_pk_fma_f32 v[28:29], v[4:5], v[24:25], v[26:27] op_sel_hi:[1,0,1] neg_lo:[0,0,1]
	s_nop 0
	v_pk_fma_f32 v[24:25], v[6:7], v[96:97], v[14:15] op_sel_hi:[0,1,1] neg_lo:[0,0,1]
	v_pk_add_f32 v[6:7], v[10:11], v[18:19] neg_lo:[0,1] neg_hi:[0,1]
	s_nop 0
	v_pk_mul_f32 v[10:11], v[6:7], v[96:97] op_sel_hi:[1,0]
	s_nop 0
	v_pk_fma_f32 v[14:15], v[6:7], v[96:97], v[10:11] op_sel:[0,1,1] op_sel_hi:[1,1,0]
	v_pk_fma_f32 v[6:7], v[6:7], v[96:97], v[10:11] op_sel:[0,1,1] op_sel_hi:[1,1,0] neg_lo:[0,0,1] neg_hi:[0,0,1]
	v_pk_mul_f32 v[10:11], v[8:9], v[98:99] op_sel:[1,1] op_sel_hi:[1,0]
	v_mov_b32_e32 v15, v7
	v_pk_fma_f32 v[16:17], v[8:9], v[98:99], v[10:11] op_sel_hi:[0,1,1] neg_lo:[0,0,1]
	v_pk_add_f32 v[8:9], v[12:13], v[20:21] neg_lo:[0,1] neg_hi:[0,1]
	v_pk_add_f32 v[6:7], v[24:25], v[14:15]
	v_pk_mul_f32 v[10:11], v[8:9], v[106:107] op_sel_hi:[1,0]
	v_pk_add_f32 v[20:21], v[124:125], v[126:127]
	v_pk_fma_f32 v[12:13], v[8:9], v[106:107], v[10:11] op_sel:[0,1,1] op_sel_hi:[1,1,0] neg_hi:[0,0,1]
	s_nop 0
	v_pk_add_f32 v[8:9], v[16:17], v[12:13]
	s_nop 0
	v_pk_add_f32 v[10:11], v[6:7], v[8:9]
	v_pk_add_f32 v[6:7], v[6:7], v[8:9] neg_lo:[0,1] neg_hi:[0,1]
	s_nop 0
	v_pk_mul_f32 v[8:9], v[4:5], v[6:7] op_sel:[1,1] op_sel_hi:[0,1]
	v_pk_fma_f32 v[18:19], v[4:5], v[6:7], v[8:9] op_sel_hi:[1,0,1] neg_lo:[0,0,1]
	s_nop 0
	v_pk_add_f32 v[6:7], v[24:25], v[14:15] neg_lo:[0,1] neg_hi:[0,1]
	v_pk_add_f32 v[24:25], v[128:129], v[130:131]
	v_pk_mul_f32 v[8:9], v[100:101], v[6:7] op_sel:[1,1] op_sel_hi:[0,1]
	v_pk_fma_f32 v[14:15], v[100:101], v[6:7], v[8:9] op_sel_hi:[1,0,1] neg_lo:[0,0,1]
	v_pk_add_f32 v[26:27], v[20:21], v[24:25]
	v_pk_add_f32 v[6:7], v[16:17], v[12:13] neg_lo:[0,1] neg_hi:[0,1]
	s_nop 0
	v_pk_mul_f32 v[8:9], v[100:101], v[6:7] op_sel_hi:[0,1]
	v_pk_fma_f32 v[12:13], v[100:101], v[6:7], v[8:9] op_sel:[1,0,1] op_sel_hi:[1,1,0] neg_hi:[0,0,1]
	s_nop 0
	v_pk_add_f32 v[8:9], v[14:15], v[12:13] neg_lo:[0,1] neg_hi:[0,1]
	v_pk_add_f32 v[6:7], v[14:15], v[12:13]
	v_pk_mul_f32 v[12:13], v[4:5], v[8:9] op_sel:[1,1] op_sel_hi:[0,1]
	v_pk_fma_f32 v[14:15], v[4:5], v[8:9], v[12:13] neg_lo:[0,0,1] neg_hi:[0,0,1]
	v_pk_fma_f32 v[8:9], v[4:5], v[8:9], v[12:13] op_sel_hi:[1,0,1]
	v_pk_add_f32 v[12:13], v[118:119], v[120:121]
	v_mov_b32_e32 v15, v9
	v_pk_add_f32 v[8:9], v[114:115], v[116:117]
	s_nop 0
	v_pk_add_f32 v[16:17], v[8:9], v[12:13]
	v_pk_add_f32 v[8:9], v[8:9], v[12:13] neg_lo:[0,1] neg_hi:[0,1]
	v_pk_add_f32 v[30:31], v[16:17], v[26:27]
	v_pk_add_f32 v[16:17], v[16:17], v[26:27] neg_lo:[0,1] neg_hi:[0,1]
	v_pk_mul_f32 v[12:13], v[100:101], v[8:9] op_sel:[1,1] op_sel_hi:[0,1]
	v_pk_mul_f32 v[26:27], v[16:17], v[4:5] op_sel:[1,1] op_sel_hi:[1,0]
	s_nop 0
	v_pk_fma_f32 v[32:33], v[16:17], v[4:5], v[26:27] op_sel_hi:[0,1,1] neg_lo:[0,0,1]
	v_pk_fma_f32 v[16:17], v[100:101], v[8:9], v[12:13] op_sel_hi:[1,0,1] neg_lo:[0,0,1]
	s_nop 0
	v_pk_add_f32 v[8:9], v[20:21], v[24:25] neg_lo:[0,1] neg_hi:[0,1]
	s_nop 0
	v_pk_mul_f32 v[12:13], v[100:101], v[8:9] op_sel_hi:[0,1]
	v_pk_fma_f32 v[20:21], v[100:101], v[8:9], v[12:13] op_sel:[1,0,1] op_sel_hi:[1,1,0] neg_hi:[0,0,1]
	s_nop 0
	v_pk_add_f32 v[12:13], v[16:17], v[20:21] neg_lo:[0,1] neg_hi:[0,1]
	v_pk_add_f32 v[8:9], v[16:17], v[20:21]
	v_pk_mul_f32 v[16:17], v[4:5], v[12:13] op_sel:[1,1] op_sel_hi:[0,1]
	v_pk_fma_f32 v[20:21], v[4:5], v[12:13], v[16:17] neg_lo:[0,0,1] neg_hi:[0,0,1]
	v_pk_fma_f32 v[12:13], v[4:5], v[12:13], v[16:17] op_sel_hi:[1,0,1]
	v_pk_add_f32 v[16:17], v[102:103], v[104:105]
	v_mov_b32_e32 v21, v13
	v_pk_add_f32 v[12:13], v[112:113], v[110:111]
	s_nop 0
	v_pk_add_f32 v[24:25], v[12:13], v[16:17]
	v_pk_add_f32 v[12:13], v[12:13], v[16:17] neg_lo:[0,1] neg_hi:[0,1]
	s_nop 0
	v_pk_mul_f32 v[16:17], v[4:5], v[12:13] op_sel:[1,1] op_sel_hi:[0,1]
	v_pk_fma_f32 v[26:27], v[4:5], v[12:13], v[16:17] neg_lo:[0,0,1] neg_hi:[0,0,1]
	v_pk_fma_f32 v[12:13], v[4:5], v[12:13], v[16:17] op_sel_hi:[1,0,1]
	v_pk_mul_f32 v[16:17], v[4:5], v[2:3] op_sel:[1,1] op_sel_hi:[0,1]
	v_pk_fma_f32 v[96:97], v[4:5], v[2:3], v[16:17] neg_lo:[0,0,1] neg_hi:[0,0,1]
	v_pk_fma_f32 v[2:3], v[4:5], v[2:3], v[16:17] op_sel_hi:[1,0,1]
	v_mov_b32_e32 v27, v13
	v_pk_add_f32 v[12:13], v[122:123], v[132:133]
	v_mov_b32_e32 v97, v3
	ds_write_b64 v1, v[34:35]
	ds_write_b64 v1, v[94:95] offset:4352
	ds_write_b64 v1, v[22:23] offset:8704
	ds_write_b64 v1, v[28:29] offset:13056
	ds_write_b64 v1, v[10:11] offset:17408
	ds_write_b64 v1, v[18:19] offset:21760
	ds_write_b64 v1, v[6:7] offset:26112
	ds_write_b64 v1, v[14:15] offset:30464
	ds_write_b64 v1, v[30:31] offset:34816
	ds_write_b64 v1, v[32:33] offset:39168
	ds_write_b64 v1, v[8:9] offset:43520
	ds_write_b64 v1, v[20:21] offset:47872
	ds_write_b64 v1, v[24:25] offset:52224
	ds_write_b64 v1, v[26:27] offset:56576
	ds_write_b64 v1, v[12:13] offset:60928
	ds_write_b64 v1, v[96:97] offset:65280
	s_waitcnt lgkmcnt(0)
	s_barrier
	s_branch .LBB0_488

; __device__ __forceinline__ void lds_barrier() { asm volatile("s_waitcnt lgkmcnt(0)" ::: "memory"); __builtin_amdgcn_s_barrier(); asm volatile("" ::: "memory"); }
; template <int R, class XT, class TWT>
; __device__ __forceinline__ void dif_task(XT X, TWT tw, int s, int task) {
;     const int lgM = 13 - s, lgq = lgM - R, q = 1 << lgq;
;     const int j0 = task & (q - 1), blk = task >> lgq, base = (blk << lgM) + j0;
;     const int pb = PADI(base), qp = (q >= 32) ? q + (q >> 4) : q;
;     f32x2v v[1 << R];
; #pragma unroll
;     for (int k = 0; k < (1 << R); ++k) v[k] = X[pb + k * qp];
; #pragma unroll
;     for (int r = 0; r < R; ++r) {
;         const int pb = R - 1 - r;
; #pragma unroll
;         for (int k = 0; k < (1 << R); ++k) if (!((k >> pb) & 1)) {
;             const int klo = k & ((1 << pb) - 1);
;             const f32x2v w = tw[(j0 + (klo << lgq)) << (s + r)];
;             const f32x2v a = v[k], b = v[k + (1 << pb)], d = a - b;
;             v[k] = a + b; v[k + (1 << pb)] = (f32x2v){d.x * w.x - d.y * w.y, d.x * w.y + d.y * w.x};
;         }
;     }
; #pragma unroll
;     for (int k = 0; k < (1 << R); ++k) X[pb + k * qp] = v[k];
; }
; __device__ __forceinline__ void fft_fwd_upper(LAS f32x2v* X, TwHalf tw, int s0, int tid) {
;     ...
;     dif_task<4>(X, tw, 4, tid); lds_barrier();
.LBB0_488:
	ds_read2_b64 v[2:5], v76 offset1:34
	ds_read2_b64 v[6:9], v76 offset0:68 offset1:102
	ds_read2_b64 v[10:13], v76 offset0:136 offset1:170
	ds_read2_b64 v[14:17], v76 offset0:204 offset1:238
	v_add_u32_e32 v134, 0x800, v76
	ds_read2_b64 v[18:21], v134 offset0:16 offset1:50
	ds_read2_b64 v[22:25], v134 offset0:84 offset1:118
	ds_read2_b64 v[26:29], v134 offset0:152 offset1:186
	ds_read2_b64 v[30:33], v134 offset0:220 offset1:254
	ds_read2st64_b64 v[94:97], v82 offset1:16
	ds_read_b64 v[34:35], v85
	ds_read_b64 v[98:99], v86
	ds_read_b64 v[100:101], v87
	ds_read_b64 v[102:103], v83
	ds_read_b64 v[104:105], v84
	ds_read_b64 v[106:107], v41
	ds_read_b64 v[108:109], v42
	s_waitcnt lgkmcnt(11)
	v_pk_add_f32 v[110:111], v[2:3], v[18:19] neg_lo:[0,1] neg_hi:[0,1]
	v_pk_add_f32 v[2:3], v[2:3], v[18:19]
	s_waitcnt lgkmcnt(7)
	v_pk_mul_f32 v[112:113], v[110:111], v[94:95] op_sel:[1,1] op_sel_hi:[1,0]
	s_add_u32 s4, s6, s2
	v_pk_fma_f32 v[114:115], v[110:111], v[94:95], v[112:113] op_sel_hi:[0,1,1] neg_lo:[0,0,1]
	v_pk_add_f32 v[110:111], v[10:11], v[26:27] neg_lo:[0,1] neg_hi:[0,1]
	v_pk_add_f32 v[10:11], v[10:11], v[26:27]
	v_pk_mul_f32 v[112:113], v[110:111], v[94:95] op_sel:[1,0] op_sel_hi:[0,0]
	v_pk_fma_f32 v[116:117], v[110:111], v[94:95], v[112:113] op_sel:[0,1,0] neg_hi:[0,0,1]
	v_pk_add_f32 v[18:19], v[2:3], v[10:11]
	v_pk_add_f32 v[94:95], v[114:115], v[116:117] neg_lo:[0,1] neg_hi:[0,1]
	v_pk_add_f32 v[2:3], v[2:3], v[10:11] neg_lo:[0,1] neg_hi:[0,1]
	s_waitcnt lgkmcnt(6)
	v_pk_mul_f32 v[110:111], v[34:35], v[94:95] op_sel:[1,1] op_sel_hi:[0,1]
	v_pk_fma_f32 v[112:113], v[34:35], v[94:95], v[110:111] op_sel_hi:[1,0,1] neg_lo:[0,0,1]
	v_pk_mul_f32 v[10:11], v[2:3], v[34:35] op_sel:[1,1] op_sel_hi:[1,0]
	v_pk_add_f32 v[94:95], v[6:7], v[22:23] neg_lo:[0,1] neg_hi:[0,1]
	v_pk_add_f32 v[6:7], v[6:7], v[22:23]
	v_pk_mul_f32 v[110:111], v[94:95], v[96:97] op_sel:[1,1] op_sel_hi:[1,0]
	s_addc_u32 s5, s7, s3
	v_pk_fma_f32 v[118:119], v[94:95], v[96:97], v[110:111] op_sel_hi:[0,1,1] neg_lo:[0,0,1]
	v_pk_add_f32 v[94:95], v[14:15], v[30:31] neg_lo:[0,1] neg_hi:[0,1]
	v_pk_add_f32 v[14:15], v[14:15], v[30:31]
	v_pk_mul_f32 v[110:111], v[94:95], v[96:97] op_sel:[1,0] op_sel_hi:[0,0]
	v_pk_fma_f32 v[120:121], v[94:95], v[96:97], v[110:111] op_sel:[0,1,0] neg_hi:[0,0,1]
	v_pk_add_f32 v[22:23], v[6:7], v[14:15]
	v_pk_add_f32 v[94:95], v[118:119], v[120:121] neg_lo:[0,1] neg_hi:[0,1]
	v_pk_add_f32 v[26:27], v[18:19], v[22:23]
	v_pk_mul_f32 v[96:97], v[34:35], v[94:95] op_sel_hi:[0,1]
	v_pk_fma_f32 v[110:111], v[34:35], v[94:95], v[96:97] op_sel:[1,0,1] op_sel_hi:[1,1,0] neg_hi:[0,0,1]
	v_pk_add_f32 v[18:19], v[18:19], v[22:23] neg_lo:[0,1] neg_hi:[0,1]
	v_pk_add_f32 v[94:95], v[112:113], v[110:111] neg_lo:[0,1] neg_hi:[0,1]
	s_waitcnt lgkmcnt(4)
	v_pk_mul_f32 v[22:23], v[18:19], v[100:101] op_sel:[1,1] op_sel_hi:[1,0]
	v_pk_mul_f32 v[96:97], v[100:101], v[94:95] op_sel:[1,1] op_sel_hi:[0,1]
	v_pk_fma_f32 v[122:123], v[100:101], v[94:95], v[96:97] op_sel_hi:[1,0,1] neg_lo:[0,0,1]
	s_ashr_i32 s21, s20, 31
	v_pk_add_f32 v[94:95], v[4:5], v[20:21] neg_lo:[0,1] neg_hi:[0,1]
	v_pk_add_f32 v[4:5], v[4:5], v[20:21]
	s_waitcnt lgkmcnt(3)
	v_pk_mul_f32 v[96:97], v[94:95], v[102:103] op_sel:[1,1] op_sel_hi:[1,0]
	s_lshl_b64 s[0:1], s[20:21], s0
	v_pk_fma_f32 v[124:125], v[94:95], v[102:103], v[96:97] op_sel_hi:[0,1,1] neg_lo:[0,0,1]
	v_pk_add_f32 v[94:95], v[12:13], v[28:29] neg_lo:[0,1] neg_hi:[0,1]
	v_pk_add_f32 v[12:13], v[12:13], v[28:29]
	v_pk_mul_f32 v[96:97], v[94:95], v[102:103] op_sel:[1,0] op_sel_hi:[0,0]
	v_pk_fma_f32 v[126:127], v[94:95], v[102:103], v[96:97] op_sel:[0,1,0] neg_hi:[0,0,1]
	v_pk_add_f32 v[20:21], v[4:5], v[12:13]
	v_pk_add_f32 v[94:95], v[124:125], v[126:127] neg_lo:[0,1] neg_hi:[0,1]
	v_pk_add_f32 v[4:5], v[4:5], v[12:13] neg_lo:[0,1] neg_hi:[0,1]
	v_pk_mul_f32 v[96:97], v[98:99], v[94:95] op_sel:[1,1] op_sel_hi:[0,1]
	v_pk_fma_f32 v[102:103], v[98:99], v[94:95], v[96:97] op_sel_hi:[1,0,1] neg_lo:[0,0,1]
	s_lshl_b64 s[0:1], s[0:1], 3
	v_pk_add_f32 v[94:95], v[8:9], v[24:25] neg_lo:[0,1] neg_hi:[0,1]
	v_pk_add_f32 v[8:9], v[8:9], v[24:25]
	s_waitcnt lgkmcnt(2)
	v_pk_mul_f32 v[96:97], v[94:95], v[104:105] op_sel:[1,1] op_sel_hi:[1,0]
	s_add_u32 s0, s4, s0
	v_pk_fma_f32 v[128:129], v[94:95], v[104:105], v[96:97] op_sel_hi:[0,1,1] neg_lo:[0,0,1]
	v_pk_add_f32 v[94:95], v[16:17], v[32:33] neg_lo:[0,1] neg_hi:[0,1]
	v_pk_add_f32 v[16:17], v[16:17], v[32:33]
	v_pk_mul_f32 v[96:97], v[94:95], v[104:105] op_sel:[1,0] op_sel_hi:[0,0]
	v_pk_fma_f32 v[130:131], v[94:95], v[104:105], v[96:97] op_sel:[0,1,0] neg_hi:[0,0,1]
	v_pk_add_f32 v[24:25], v[8:9], v[16:17]
	v_pk_add_f32 v[94:95], v[128:129], v[130:131] neg_lo:[0,1] neg_hi:[0,1]
	v_pk_add_f32 v[28:29], v[20:21], v[24:25]
	s_waitcnt lgkmcnt(1)
	v_pk_mul_f32 v[96:97], v[106:107], v[94:95] op_sel_hi:[0,1]
	v_pk_fma_f32 v[104:105], v[106:107], v[94:95], v[96:97] op_sel:[1,0,1] op_sel_hi:[1,1,0] neg_hi:[0,0,1]
	v_pk_add_f32 v[30:31], v[26:27], v[28:29]
	v_pk_add_f32 v[94:95], v[102:103], v[104:105] neg_lo:[0,1] neg_hi:[0,1]
	v_pk_add_f32 v[26:27], v[26:27], v[28:29] neg_lo:[0,1] neg_hi:[0,1]
	v_pk_mul_f32 v[96:97], v[100:101], v[94:95] op_sel_hi:[0,1]
	v_pk_fma_f32 v[132:133], v[100:101], v[94:95], v[96:97] op_sel:[1,0,1] op_sel_hi:[1,1,0]
	v_pk_fma_f32 v[94:95], v[100:101], v[94:95], v[96:97] op_sel:[1,0,1] op_sel_hi:[1,1,0] neg_lo:[0,0,1] neg_hi:[0,0,1]
	s_waitcnt lgkmcnt(0)
; template <int R, class XT, class TWT>
; __device__ __forceinline__ void dif_task(XT X, TWT tw, int s, int task) {
;     const int lgM = 13 - s, lgq = lgM - R, q = 1 << lgq;
;     const int j0 = task & (q - 1), blk = task >> lgq, base = (blk << lgM) + j0;
;     const int pb = PADI(base), qp = (q >= 32) ? q + (q >> 4) : q;
;     f32x2v v[1 << R];
; #pragma unroll
;     for (int k = 0; k < (1 << R); ++k) v[k] = X[pb + k * qp];
; #pragma unroll
;     for (int r = 0; r < R; ++r) {
;         const int pb = R - 1 - r;
; #pragma unroll
;         for (int k = 0; k < (1 << R); ++k) if (!((k >> pb) & 1)) {
;             const int klo = k & ((1 << pb) - 1);
;             const f32x2v w = tw[(j0 + (klo << lgq)) << (s + r)];
;             const f32x2v a = v[k], b = v[k + (1 << pb)], d = a - b;
;             v[k] = a + b; v[k + (1 << pb)] = (f32x2v){d.x * w.x - d.y * w.y, d.x * w.y + d.y * w.x};
;         }
;     }
; #pragma unroll
;     for (int k = 0; k < (1 << R); ++k) X[pb + k * qp] = v[k];
; }
	v_xor_b32_e32 v96, 0x80000000, v108
	v_cndmask_b32_e64 v97, v96, v109, s[38:39]
	v_cndmask_b32_e64 v96, v109, v108, s[38:39]
	v_pk_mul_f32 v[28:29], v[26:27], v[96:97] op_sel:[1,1] op_sel_hi:[1,0]
	v_mov_b32_e32 v133, v95
	v_pk_fma_f32 v[32:33], v[26:27], v[96:97], v[28:29] op_sel_hi:[0,1,1] neg_lo:[0,0,1]
	v_pk_fma_f32 v[26:27], v[18:19], v[100:101], v[22:23] op_sel_hi:[0,1,1] neg_lo:[0,0,1]
	v_pk_add_f32 v[18:19], v[20:21], v[24:25] neg_lo:[0,1] neg_hi:[0,1]
	v_pk_add_f32 v[94:95], v[122:123], v[132:133] neg_lo:[0,1] neg_hi:[0,1]
	v_pk_mul_f32 v[20:21], v[18:19], v[100:101] op_sel_hi:[1,0]
	v_mov_b32_e32 v108, s8
	v_pk_fma_f32 v[22:23], v[18:19], v[100:101], v[20:21] op_sel:[0,1,1] op_sel_hi:[1,1,0] neg_hi:[0,0,1]
	s_addc_u32 s1, s5, s1
	v_pk_add_f32 v[20:21], v[26:27], v[22:23] neg_lo:[0,1] neg_hi:[0,1]
	v_pk_add_f32 v[18:19], v[26:27], v[22:23]
	v_pk_mul_f32 v[22:23], v[96:97], v[20:21] op_sel:[1,1] op_sel_hi:[0,1]
	v_pk_fma_f32 v[24:25], v[96:97], v[20:21], v[22:23] op_sel_hi:[1,0,1] neg_lo:[0,0,1]
	s_nop 0
	v_pk_fma_f32 v[20:21], v[2:3], v[34:35], v[10:11] op_sel_hi:[0,1,1] neg_lo:[0,0,1]
	v_pk_add_f32 v[2:3], v[6:7], v[14:15] neg_lo:[0,1] neg_hi:[0,1]
	s_nop 0
	v_pk_mul_f32 v[6:7], v[2:3], v[34:35] op_sel_hi:[1,0]
	s_nop 0
	v_pk_fma_f32 v[10:11], v[2:3], v[34:35], v[6:7] op_sel:[0,1,1] op_sel_hi:[1,1,0]
	v_pk_fma_f32 v[2:3], v[2:3], v[34:35], v[6:7] op_sel:[0,1,1] op_sel_hi:[1,1,0] neg_lo:[0,0,1] neg_hi:[0,0,1]
	v_pk_mul_f32 v[6:7], v[4:5], v[98:99] op_sel:[1,1] op_sel_hi:[1,0]
	v_mov_b32_e32 v11, v3
	v_pk_fma_f32 v[12:13], v[4:5], v[98:99], v[6:7] op_sel_hi:[0,1,1] neg_lo:[0,0,1]
	v_pk_add_f32 v[4:5], v[8:9], v[16:17] neg_lo:[0,1] neg_hi:[0,1]
	v_pk_add_f32 v[2:3], v[20:21], v[10:11]
	v_pk_mul_f32 v[6:7], v[4:5], v[106:107] op_sel_hi:[1,0]
	v_pk_add_f32 v[16:17], v[124:125], v[126:127]
	v_pk_fma_f32 v[8:9], v[4:5], v[106:107], v[6:7] op_sel:[0,1,1] op_sel_hi:[1,1,0] neg_hi:[0,0,1]
	s_nop 0
	v_pk_add_f32 v[4:5], v[12:13], v[8:9]
	s_nop 0
	v_pk_add_f32 v[6:7], v[2:3], v[4:5]
	v_pk_add_f32 v[2:3], v[2:3], v[4:5] neg_lo:[0,1] neg_hi:[0,1]
	s_nop 0
	v_pk_mul_f32 v[4:5], v[96:97], v[2:3] op_sel:[1,1] op_sel_hi:[0,1]
	v_pk_fma_f32 v[14:15], v[96:97], v[2:3], v[4:5] op_sel_hi:[1,0,1] neg_lo:[0,0,1]
	s_nop 0
	v_pk_add_f32 v[2:3], v[20:21], v[10:11] neg_lo:[0,1] neg_hi:[0,1]
	v_pk_add_f32 v[20:21], v[128:129], v[130:131]
	v_pk_mul_f32 v[4:5], v[100:101], v[2:3] op_sel:[1,1] op_sel_hi:[0,1]
	v_pk_fma_f32 v[10:11], v[100:101], v[2:3], v[4:5] op_sel_hi:[1,0,1] neg_lo:[0,0,1]
	v_pk_add_f32 v[22:23], v[16:17], v[20:21]
	v_pk_add_f32 v[2:3], v[12:13], v[8:9] neg_lo:[0,1] neg_hi:[0,1]
	s_nop 0
	v_pk_mul_f32 v[4:5], v[100:101], v[2:3] op_sel_hi:[0,1]
	v_pk_fma_f32 v[8:9], v[100:101], v[2:3], v[4:5] op_sel:[1,0,1] op_sel_hi:[1,1,0] neg_hi:[0,0,1]
	s_nop 0
	v_pk_add_f32 v[4:5], v[10:11], v[8:9] neg_lo:[0,1] neg_hi:[0,1]
	v_pk_add_f32 v[2:3], v[10:11], v[8:9]
	v_pk_mul_f32 v[8:9], v[96:97], v[4:5] op_sel:[1,1] op_sel_hi:[0,1]
	v_pk_fma_f32 v[10:11], v[96:97], v[4:5], v[8:9] neg_lo:[0,0,1] neg_hi:[0,0,1]
	v_pk_fma_f32 v[4:5], v[96:97], v[4:5], v[8:9] op_sel_hi:[1,0,1]
	v_pk_add_f32 v[8:9], v[118:119], v[120:121]
	v_mov_b32_e32 v11, v5
	v_pk_add_f32 v[4:5], v[114:115], v[116:117]
	s_nop 0
	v_pk_add_f32 v[12:13], v[4:5], v[8:9]
	v_pk_add_f32 v[4:5], v[4:5], v[8:9] neg_lo:[0,1] neg_hi:[0,1]
	v_pk_add_f32 v[26:27], v[12:13], v[22:23]
	v_pk_add_f32 v[12:13], v[12:13], v[22:23] neg_lo:[0,1] neg_hi:[0,1]
	v_pk_mul_f32 v[8:9], v[100:101], v[4:5] op_sel:[1,1] op_sel_hi:[0,1]
	v_pk_mul_f32 v[22:23], v[12:13], v[96:97] op_sel:[1,1] op_sel_hi:[1,0]
	s_nop 0
	v_pk_fma_f32 v[28:29], v[12:13], v[96:97], v[22:23] op_sel_hi:[0,1,1] neg_lo:[0,0,1]
	v_pk_fma_f32 v[12:13], v[100:101], v[4:5], v[8:9] op_sel_hi:[1,0,1] neg_lo:[0,0,1]
	s_nop 0
	v_pk_add_f32 v[4:5], v[16:17], v[20:21] neg_lo:[0,1] neg_hi:[0,1]
	s_nop 0
	v_pk_mul_f32 v[8:9], v[100:101], v[4:5] op_sel_hi:[0,1]
	v_pk_fma_f32 v[16:17], v[100:101], v[4:5], v[8:9] op_sel:[1,0,1] op_sel_hi:[1,1,0] neg_hi:[0,0,1]
	s_nop 0
	v_pk_add_f32 v[8:9], v[12:13], v[16:17] neg_lo:[0,1] neg_hi:[0,1]
	v_pk_add_f32 v[4:5], v[12:13], v[16:17]
	v_pk_mul_f32 v[12:13], v[96:97], v[8:9] op_sel:[1,1] op_sel_hi:[0,1]
	v_pk_fma_f32 v[16:17], v[96:97], v[8:9], v[12:13] neg_lo:[0,0,1] neg_hi:[0,0,1]
	v_pk_fma_f32 v[8:9], v[96:97], v[8:9], v[12:13] op_sel_hi:[1,0,1]
	v_pk_add_f32 v[12:13], v[102:103], v[104:105]
	v_mov_b32_e32 v17, v9
	v_pk_add_f32 v[8:9], v[112:113], v[110:111]
	s_nop 0
	v_pk_add_f32 v[20:21], v[8:9], v[12:13]
	v_pk_add_f32 v[8:9], v[8:9], v[12:13] neg_lo:[0,1] neg_hi:[0,1]
	s_nop 0
	v_pk_mul_f32 v[12:13], v[96:97], v[8:9] op_sel:[1,1] op_sel_hi:[0,1]
	v_pk_fma_f32 v[22:23], v[96:97], v[8:9], v[12:13] neg_lo:[0,0,1] neg_hi:[0,0,1]
	v_pk_fma_f32 v[8:9], v[96:97], v[8:9], v[12:13] op_sel_hi:[1,0,1]
	v_pk_mul_f32 v[12:13], v[96:97], v[94:95] op_sel:[1,1] op_sel_hi:[0,1]
	v_pk_fma_f32 v[34:35], v[96:97], v[94:95], v[12:13] op_sel_hi:[1,0,1] neg_lo:[0,0,1]
	v_mov_b32_e32 v23, v9
	v_pk_add_f32 v[8:9], v[122:123], v[132:133]
	ds_write2_b64 v76, v[30:31], v[32:33] offset1:34
	ds_write2_b64 v76, v[18:19], v[24:25] offset0:68 offset1:102
	ds_write2_b64 v76, v[6:7], v[14:15] offset0:136 offset1:170
	ds_write2_b64 v76, v[2:3], v[10:11] offset0:204 offset1:238
	ds_write2_b64 v134, v[26:27], v[28:29] offset0:16 offset1:50
	ds_write2_b64 v134, v[4:5], v[16:17] offset0:84 offset1:118
	ds_write2_b64 v134, v[20:21], v[22:23] offset0:152 offset1:186
	ds_write2_b64 v134, v[8:9], v[34:35] offset0:220 offset1:254
	s_waitcnt lgkmcnt(0)
	s_barrier
; __device__ __forceinline__ void lds_barrier() { asm volatile("s_waitcnt lgkmcnt(0)" ::: "memory"); __builtin_amdgcn_s_barrier(); asm volatile("" ::: "memory"); }
; template <int R, class XT, class TWT>
; __device__ __forceinline__ void dif_task(XT X, TWT tw, int s, int task) {
;     const int lgM = 13 - s, lgq = lgM - R, q = 1 << lgq;
;     const int j0 = task & (q - 1), blk = task >> lgq, base = (blk << lgM) + j0;
;     const int pb = PADI(base), qp = (q >= 32) ? q + (q >> 4) : q;
;     f32x2v v[1 << R];
; #pragma unroll
;     for (int k = 0; k < (1 << R); ++k) v[k] = X[pb + k * qp];
; #pragma unroll
;     for (int r = 0; r < R; ++r) {
;         const int pb = R - 1 - r;
; #pragma unroll
;         for (int k = 0; k < (1 << R); ++k) if (!((k >> pb) & 1)) {
;             const int klo = k & ((1 << pb) - 1);
;             const f32x2v w = tw[(j0 + (klo << lgq)) << (s + r)];
;             const f32x2v a = v[k], b = v[k + (1 << pb)], d = a - b;
;             v[k] = a + b; v[k + (1 << pb)] = (f32x2v){d.x * w.x - d.y * w.y, d.x * w.y + d.y * w.x};
;         }
;     }
; #pragma unroll
;     for (int k = 0; k < (1 << R); ++k) X[pb + k * qp] = v[k];
; }
; __device__ __forceinline__ void fft_fwd_upper(LAS f32x2v* X, TwHalf tw, int s0, int tid) {
;     ...
;     dif_task<4>(X, tw, 8, tid); lds_barrier();
	ds_read2_b64 v[2:5], v77 offset1:2
	ds_read2_b64 v[6:9], v77 offset0:4 offset1:6
	ds_read2_b64 v[10:13], v77 offset0:8 offset1:10
	ds_read2_b64 v[14:17], v77 offset0:12 offset1:14
	ds_read2_b64 v[18:21], v77 offset0:16 offset1:18
	ds_read2_b64 v[22:25], v77 offset0:20 offset1:22
	ds_read2_b64 v[26:29], v77 offset0:24 offset1:26
	ds_read2_b64 v[30:33], v77 offset0:28 offset1:30
	ds_read2st64_b64 v[94:97], v88 offset1:16
	ds_read_b64 v[34:35], v89
	ds_read_b64 v[98:99], v90
	ds_read_b64 v[100:101], v91
	ds_read_b64 v[102:103], v43
	s_waitcnt lgkmcnt(8)
	v_pk_add_f32 v[110:111], v[2:3], v[18:19] neg_lo:[0,1] neg_hi:[0,1]
	ds_read_b64 v[104:105], v92
	ds_read_b64 v[106:107], v93
	ds_read_b64 v[108:109], v108
	s_waitcnt lgkmcnt(7)
	v_pk_mul_f32 v[112:113], v[110:111], v[94:95] op_sel:[1,1] op_sel_hi:[1,0]
	v_pk_add_f32 v[2:3], v[2:3], v[18:19]
	v_pk_fma_f32 v[114:115], v[110:111], v[94:95], v[112:113] op_sel_hi:[0,1,1] neg_lo:[0,0,1]
	v_pk_add_f32 v[110:111], v[10:11], v[26:27] neg_lo:[0,1] neg_hi:[0,1]
	v_pk_add_f32 v[10:11], v[10:11], v[26:27]
	v_pk_mul_f32 v[112:113], v[110:111], v[94:95] op_sel:[1,0] op_sel_hi:[0,0]
	v_pk_fma_f32 v[116:117], v[110:111], v[94:95], v[112:113] op_sel:[0,1,0] neg_hi:[0,0,1]
	v_pk_add_f32 v[18:19], v[2:3], v[10:11]
	v_pk_add_f32 v[94:95], v[114:115], v[116:117] neg_lo:[0,1] neg_hi:[0,1]
	v_pk_add_f32 v[2:3], v[2:3], v[10:11] neg_lo:[0,1] neg_hi:[0,1]
	s_waitcnt lgkmcnt(4)
	v_pk_mul_f32 v[110:111], v[100:101], v[94:95] op_sel:[1,1] op_sel_hi:[0,1]
	v_pk_fma_f32 v[112:113], v[100:101], v[94:95], v[110:111] op_sel_hi:[1,0,1] neg_lo:[0,0,1]
	v_pk_mul_f32 v[10:11], v[2:3], v[100:101] op_sel:[1,1] op_sel_hi:[1,0]
	v_pk_add_f32 v[94:95], v[6:7], v[22:23] neg_lo:[0,1] neg_hi:[0,1]
	v_pk_add_f32 v[6:7], v[6:7], v[22:23]
	v_pk_mul_f32 v[110:111], v[94:95], v[96:97] op_sel:[1,1] op_sel_hi:[1,0]
	s_nop 0
	v_pk_fma_f32 v[118:119], v[94:95], v[96:97], v[110:111] op_sel_hi:[0,1,1] neg_lo:[0,0,1]
	v_pk_add_f32 v[94:95], v[14:15], v[30:31] neg_lo:[0,1] neg_hi:[0,1]
	v_pk_add_f32 v[14:15], v[14:15], v[30:31]
	v_pk_mul_f32 v[110:111], v[94:95], v[96:97] op_sel:[1,0] op_sel_hi:[0,0]
	v_pk_fma_f32 v[120:121], v[94:95], v[96:97], v[110:111] op_sel:[0,1,0] neg_hi:[0,0,1]
	v_pk_add_f32 v[22:23], v[6:7], v[14:15]
	v_pk_add_f32 v[94:95], v[118:119], v[120:121] neg_lo:[0,1] neg_hi:[0,1]
	v_pk_add_f32 v[26:27], v[18:19], v[22:23]
	v_pk_mul_f32 v[96:97], v[100:101], v[94:95] op_sel_hi:[0,1]
	v_pk_fma_f32 v[110:111], v[100:101], v[94:95], v[96:97] op_sel:[1,0,1] op_sel_hi:[1,1,0] neg_hi:[0,0,1]
	v_pk_add_f32 v[18:19], v[18:19], v[22:23] neg_lo:[0,1] neg_hi:[0,1]
	v_pk_add_f32 v[94:95], v[112:113], v[110:111] neg_lo:[0,1] neg_hi:[0,1]
	s_waitcnt lgkmcnt(1)
	v_pk_mul_f32 v[22:23], v[18:19], v[106:107] op_sel:[1,1] op_sel_hi:[1,0]
	v_pk_mul_f32 v[96:97], v[106:107], v[94:95] op_sel:[1,1] op_sel_hi:[0,1]
	v_pk_fma_f32 v[122:123], v[106:107], v[94:95], v[96:97] op_sel_hi:[1,0,1] neg_lo:[0,0,1]
	s_nop 0
	v_pk_add_f32 v[94:95], v[4:5], v[20:21] neg_lo:[0,1] neg_hi:[0,1]
	v_pk_add_f32 v[4:5], v[4:5], v[20:21]
	v_pk_mul_f32 v[96:97], v[94:95], v[34:35] op_sel:[1,1] op_sel_hi:[1,0]
	s_nop 0
	v_pk_fma_f32 v[124:125], v[94:95], v[34:35], v[96:97] op_sel_hi:[0,1,1] neg_lo:[0,0,1]
	v_pk_add_f32 v[94:95], v[12:13], v[28:29] neg_lo:[0,1] neg_hi:[0,1]
	v_pk_add_f32 v[12:13], v[12:13], v[28:29]
	v_pk_mul_f32 v[96:97], v[94:95], v[34:35] op_sel:[1,0] op_sel_hi:[0,0]
	v_pk_fma_f32 v[126:127], v[94:95], v[34:35], v[96:97] op_sel:[0,1,0] neg_hi:[0,0,1]
	v_pk_add_f32 v[20:21], v[4:5], v[12:13]
	v_pk_add_f32 v[34:35], v[124:125], v[126:127] neg_lo:[0,1] neg_hi:[0,1]
	v_pk_add_f32 v[4:5], v[4:5], v[12:13] neg_lo:[0,1] neg_hi:[0,1]
	v_pk_mul_f32 v[94:95], v[104:105], v[34:35] op_sel:[1,1] op_sel_hi:[0,1]
	v_pk_fma_f32 v[96:97], v[104:105], v[34:35], v[94:95] op_sel_hi:[1,0,1] neg_lo:[0,0,1]
	s_nop 0
	v_pk_add_f32 v[34:35], v[8:9], v[24:25] neg_lo:[0,1] neg_hi:[0,1]
	v_pk_add_f32 v[8:9], v[8:9], v[24:25]
	v_pk_mul_f32 v[94:95], v[34:35], v[98:99] op_sel:[1,1] op_sel_hi:[1,0]
	s_nop 0
	v_pk_fma_f32 v[128:129], v[34:35], v[98:99], v[94:95] op_sel_hi:[0,1,1] neg_lo:[0,0,1]
	v_pk_add_f32 v[34:35], v[16:17], v[32:33] neg_lo:[0,1] neg_hi:[0,1]
	v_pk_add_f32 v[16:17], v[16:17], v[32:33]
	v_pk_mul_f32 v[94:95], v[34:35], v[98:99] op_sel:[1,0] op_sel_hi:[0,0]
	v_pk_fma_f32 v[130:131], v[34:35], v[98:99], v[94:95] op_sel:[0,1,0] neg_hi:[0,0,1]
	v_pk_add_f32 v[24:25], v[8:9], v[16:17]
	v_pk_add_f32 v[34:35], v[128:129], v[130:131] neg_lo:[0,1] neg_hi:[0,1]
	v_pk_add_f32 v[28:29], v[20:21], v[24:25]
	v_pk_mul_f32 v[94:95], v[102:103], v[34:35] op_sel_hi:[0,1]
	v_pk_fma_f32 v[98:99], v[102:103], v[34:35], v[94:95] op_sel:[1,0,1] op_sel_hi:[1,1,0] neg_hi:[0,0,1]
	v_pk_add_f32 v[30:31], v[26:27], v[28:29]
	v_pk_add_f32 v[34:35], v[96:97], v[98:99] neg_lo:[0,1] neg_hi:[0,1]
	v_pk_add_f32 v[26:27], v[26:27], v[28:29] neg_lo:[0,1] neg_hi:[0,1]
	v_pk_mul_f32 v[94:95], v[106:107], v[34:35] op_sel_hi:[0,1]
	v_pk_fma_f32 v[132:133], v[106:107], v[34:35], v[94:95] op_sel:[1,0,1] op_sel_hi:[1,1,0]
	v_pk_fma_f32 v[34:35], v[106:107], v[34:35], v[94:95] op_sel:[1,0,1] op_sel_hi:[1,1,0] neg_lo:[0,0,1] neg_hi:[0,0,1]
	s_waitcnt lgkmcnt(0)
; template <int R, class XT, class TWT>
; __device__ __forceinline__ void dif_task(XT X, TWT tw, int s, int task) {
;     const int lgM = 13 - s, lgq = lgM - R, q = 1 << lgq;
;     const int j0 = task & (q - 1), blk = task >> lgq, base = (blk << lgM) + j0;
;     const int pb = PADI(base), qp = (q >= 32) ? q + (q >> 4) : q;
;     f32x2v v[1 << R];
; #pragma unroll
;     for (int k = 0; k < (1 << R); ++k) v[k] = X[pb + k * qp];
; #pragma unroll
;     for (int r = 0; r < R; ++r) {
;         const int pb = R - 1 - r;
; #pragma unroll
;         for (int k = 0; k < (1 << R); ++k) if (!((k >> pb) & 1)) {
;             const int klo = k & ((1 << pb) - 1);
;             const f32x2v w = tw[(j0 + (klo << lgq)) << (s + r)];
;             const f32x2v a = v[k], b = v[k + (1 << pb)], d = a - b;
;             v[k] = a + b; v[k + (1 << pb)] = (f32x2v){d.x * w.x - d.y * w.y, d.x * w.y + d.y * w.x};
;         }
;     }
; #pragma unroll
;     for (int k = 0; k < (1 << R); ++k) X[pb + k * qp] = v[k];
; }
; __device__ __forceinline__ void phase_spectra(Frame& F0, int l) {
;     ...
;         f32x2v* SP = (f32x2v*)(F.ws + (lat ? WS_SPEC : WS_SPECC)) + (size_t)col0 * N; const float sc = 1.0f / (float)N;
; #pragma unroll 2
;         for (int r = 0; r < 8; ++r) { const int e = 2 * (F.tid + 512 * r); const f32x2v a = X[PADI(e)], b = X[PADI(e + 1)];
;             *(f32x4*)(SP + e) = (f32x4){(a.x + b.x) * sc, (a.y + b.y) * sc, (a.x - b.x) * sc, (a.y - b.y) * sc}; }
	v_xor_b32_e32 v94, 0x80000000, v108
	v_cndmask_b32_e64 v95, v94, v109, s[40:41]
	v_cndmask_b32_e64 v94, v109, v108, s[40:41]
	v_pk_mul_f32 v[28:29], v[26:27], v[94:95] op_sel:[1,1] op_sel_hi:[1,0]
	v_mov_b32_e32 v133, v35
	v_pk_fma_f32 v[32:33], v[26:27], v[94:95], v[28:29] op_sel_hi:[0,1,1] neg_lo:[0,0,1]
	v_pk_fma_f32 v[26:27], v[18:19], v[106:107], v[22:23] op_sel_hi:[0,1,1] neg_lo:[0,0,1]
	v_pk_add_f32 v[18:19], v[20:21], v[24:25] neg_lo:[0,1] neg_hi:[0,1]
	v_pk_add_f32 v[34:35], v[122:123], v[132:133] neg_lo:[0,1] neg_hi:[0,1]
	v_pk_mul_f32 v[20:21], v[18:19], v[106:107] op_sel_hi:[1,0]
	s_nop 0
	v_pk_fma_f32 v[22:23], v[18:19], v[106:107], v[20:21] op_sel:[0,1,1] op_sel_hi:[1,1,0] neg_hi:[0,0,1]
	s_nop 0
	v_pk_add_f32 v[20:21], v[26:27], v[22:23] neg_lo:[0,1] neg_hi:[0,1]
	v_pk_add_f32 v[18:19], v[26:27], v[22:23]
	v_pk_mul_f32 v[22:23], v[94:95], v[20:21] op_sel:[1,1] op_sel_hi:[0,1]
	v_pk_fma_f32 v[24:25], v[94:95], v[20:21], v[22:23] op_sel_hi:[1,0,1] neg_lo:[0,0,1]
	s_nop 0
	v_pk_fma_f32 v[20:21], v[2:3], v[100:101], v[10:11] op_sel_hi:[0,1,1] neg_lo:[0,0,1]
	v_pk_add_f32 v[2:3], v[6:7], v[14:15] neg_lo:[0,1] neg_hi:[0,1]
	s_nop 0
	v_pk_mul_f32 v[6:7], v[2:3], v[100:101] op_sel_hi:[1,0]
	s_nop 0
	v_pk_fma_f32 v[10:11], v[2:3], v[100:101], v[6:7] op_sel:[0,1,1] op_sel_hi:[1,1,0]
	v_pk_fma_f32 v[2:3], v[2:3], v[100:101], v[6:7] op_sel:[0,1,1] op_sel_hi:[1,1,0] neg_lo:[0,0,1] neg_hi:[0,0,1]
	v_pk_mul_f32 v[6:7], v[4:5], v[104:105] op_sel:[1,1] op_sel_hi:[1,0]
	v_mov_b32_e32 v11, v3
	v_pk_fma_f32 v[12:13], v[4:5], v[104:105], v[6:7] op_sel_hi:[0,1,1] neg_lo:[0,0,1]
	v_pk_add_f32 v[4:5], v[8:9], v[16:17] neg_lo:[0,1] neg_hi:[0,1]
	v_pk_add_f32 v[2:3], v[20:21], v[10:11]
	v_pk_mul_f32 v[6:7], v[4:5], v[102:103] op_sel_hi:[1,0]
	v_pk_add_f32 v[16:17], v[124:125], v[126:127]
	v_pk_fma_f32 v[8:9], v[4:5], v[102:103], v[6:7] op_sel:[0,1,1] op_sel_hi:[1,1,0] neg_hi:[0,0,1]
	s_nop 0
	v_pk_add_f32 v[4:5], v[12:13], v[8:9]
	s_nop 0
	v_pk_add_f32 v[6:7], v[2:3], v[4:5]
	v_pk_add_f32 v[2:3], v[2:3], v[4:5] neg_lo:[0,1] neg_hi:[0,1]
	s_nop 0
	v_pk_mul_f32 v[4:5], v[94:95], v[2:3] op_sel:[1,1] op_sel_hi:[0,1]
	v_pk_fma_f32 v[14:15], v[94:95], v[2:3], v[4:5] op_sel_hi:[1,0,1] neg_lo:[0,0,1]
	s_nop 0
	v_pk_add_f32 v[2:3], v[20:21], v[10:11] neg_lo:[0,1] neg_hi:[0,1]
	v_pk_add_f32 v[20:21], v[128:129], v[130:131]
	v_pk_mul_f32 v[4:5], v[106:107], v[2:3] op_sel:[1,1] op_sel_hi:[0,1]
	v_pk_fma_f32 v[10:11], v[106:107], v[2:3], v[4:5] op_sel_hi:[1,0,1] neg_lo:[0,0,1]
	v_pk_add_f32 v[22:23], v[16:17], v[20:21]
	v_pk_add_f32 v[2:3], v[12:13], v[8:9] neg_lo:[0,1] neg_hi:[0,1]
	s_nop 0
	v_pk_mul_f32 v[4:5], v[106:107], v[2:3] op_sel_hi:[0,1]
	v_pk_fma_f32 v[8:9], v[106:107], v[2:3], v[4:5] op_sel:[1,0,1] op_sel_hi:[1,1,0] neg_hi:[0,0,1]
	s_nop 0
	v_pk_add_f32 v[4:5], v[10:11], v[8:9] neg_lo:[0,1] neg_hi:[0,1]
	v_pk_add_f32 v[2:3], v[10:11], v[8:9]
	v_pk_mul_f32 v[8:9], v[94:95], v[4:5] op_sel:[1,1] op_sel_hi:[0,1]
	v_pk_fma_f32 v[10:11], v[94:95], v[4:5], v[8:9] neg_lo:[0,0,1] neg_hi:[0,0,1]
	v_pk_fma_f32 v[4:5], v[94:95], v[4:5], v[8:9] op_sel_hi:[1,0,1]
	v_pk_add_f32 v[8:9], v[118:119], v[120:121]
	v_mov_b32_e32 v11, v5
	v_pk_add_f32 v[4:5], v[114:115], v[116:117]
	s_nop 0
	v_pk_add_f32 v[12:13], v[4:5], v[8:9]
	v_pk_add_f32 v[4:5], v[4:5], v[8:9] neg_lo:[0,1] neg_hi:[0,1]
	v_pk_add_f32 v[26:27], v[12:13], v[22:23]
	v_pk_add_f32 v[12:13], v[12:13], v[22:23] neg_lo:[0,1] neg_hi:[0,1]
	v_pk_mul_f32 v[8:9], v[106:107], v[4:5] op_sel:[1,1] op_sel_hi:[0,1]
	v_pk_mul_f32 v[22:23], v[12:13], v[94:95] op_sel:[1,1] op_sel_hi:[1,0]
	s_nop 0
	v_pk_fma_f32 v[28:29], v[12:13], v[94:95], v[22:23] op_sel_hi:[0,1,1] neg_lo:[0,0,1]
	v_pk_fma_f32 v[12:13], v[106:107], v[4:5], v[8:9] op_sel_hi:[1,0,1] neg_lo:[0,0,1]
	s_nop 0
	v_pk_add_f32 v[4:5], v[16:17], v[20:21] neg_lo:[0,1] neg_hi:[0,1]
	s_nop 0
	v_pk_mul_f32 v[8:9], v[106:107], v[4:5] op_sel_hi:[0,1]
	v_pk_fma_f32 v[16:17], v[106:107], v[4:5], v[8:9] op_sel:[1,0,1] op_sel_hi:[1,1,0] neg_hi:[0,0,1]
	s_nop 0
	v_pk_add_f32 v[8:9], v[12:13], v[16:17] neg_lo:[0,1] neg_hi:[0,1]
	v_pk_add_f32 v[4:5], v[12:13], v[16:17]
	v_pk_mul_f32 v[12:13], v[94:95], v[8:9] op_sel:[1,1] op_sel_hi:[0,1]
	v_pk_fma_f32 v[16:17], v[94:95], v[8:9], v[12:13] neg_lo:[0,0,1] neg_hi:[0,0,1]
	v_pk_fma_f32 v[8:9], v[94:95], v[8:9], v[12:13] op_sel_hi:[1,0,1]
	v_pk_add_f32 v[12:13], v[96:97], v[98:99]
	v_mov_b32_e32 v17, v9
	v_pk_add_f32 v[8:9], v[112:113], v[110:111]
	s_nop 0
	v_pk_add_f32 v[20:21], v[8:9], v[12:13]
	v_pk_add_f32 v[8:9], v[8:9], v[12:13] neg_lo:[0,1] neg_hi:[0,1]
	s_nop 0
	v_pk_mul_f32 v[12:13], v[94:95], v[8:9] op_sel:[1,1] op_sel_hi:[0,1]
	v_pk_fma_f32 v[22:23], v[94:95], v[8:9], v[12:13] neg_lo:[0,0,1] neg_hi:[0,0,1]
	v_pk_fma_f32 v[8:9], v[94:95], v[8:9], v[12:13] op_sel_hi:[1,0,1]
	v_pk_mul_f32 v[12:13], v[94:95], v[34:35] op_sel:[1,1] op_sel_hi:[0,1]
	v_pk_fma_f32 v[96:97], v[94:95], v[34:35], v[12:13] neg_lo:[0,0,1] neg_hi:[0,0,1]
	v_pk_fma_f32 v[12:13], v[94:95], v[34:35], v[12:13] op_sel_hi:[1,0,1]
	v_mov_b32_e32 v23, v9
	v_pk_add_f32 v[8:9], v[122:123], v[132:133]
	v_mov_b32_e32 v97, v13
	ds_write2_b64 v77, v[30:31], v[32:33] offset1:2
	ds_write2_b64 v77, v[18:19], v[24:25] offset0:4 offset1:6
	ds_write2_b64 v77, v[6:7], v[14:15] offset0:8 offset1:10
	ds_write2_b64 v77, v[2:3], v[10:11] offset0:12 offset1:14
	ds_write2_b64 v77, v[26:27], v[28:29] offset0:16 offset1:18
	ds_write2_b64 v77, v[4:5], v[16:17] offset0:20 offset1:22
	ds_write2_b64 v77, v[20:21], v[22:23] offset0:24 offset1:26
	ds_write2_b64 v77, v[8:9], v[96:97] offset0:28 offset1:30
	v_cvt_f32_u32_e32 v2, s12
	s_waitcnt lgkmcnt(0)
	s_barrier
	v_div_scale_f32 v3, s[2:3], v2, v2, 1.0
	v_rcp_f32_e32 v4, v3
	s_mov_b32 s2, 0
	v_fma_f32 v5, -v3, v4, 1.0
	v_fmac_f32_e32 v4, v5, v4
	v_div_scale_f32 v5, vcc, 1.0, v2, 1.0
	v_mul_f32_e32 v6, v5, v4
	v_fma_f32 v7, -v3, v6, v5
	v_fmac_f32_e32 v6, v7, v4
	v_fma_f32 v3, -v3, v6, v5
	v_div_fmas_f32 v3, v3, v4, v6
	v_div_fixup_f32 v2, v3, v2, 1.0
	v_mov_b32_e32 v4, v2
	v_mov_b32_e32 v5, v2
	v_mov_b32_e32 v6, v78

; template <int R, class XT, class TWT>
; __device__ __forceinline__ void dif_task(XT X, TWT tw, int s, int task) {
;     const int lgM = 13 - s, lgq = lgM - R, q = 1 << lgq;
;     const int j0 = task & (q - 1), blk = task >> lgq, base = (blk << lgM) + j0;
;     const int pb = PADI(base), qp = (q >= 32) ? q + (q >> 4) : q;
;     f32x2v v[1 << R];
; #pragma unroll
;     for (int k = 0; k < (1 << R); ++k) v[k] = X[pb + k * qp];
; #pragma unroll
;     for (int r = 0; r < R; ++r) {
;         const int pb = R - 1 - r;
; #pragma unroll
;         for (int k = 0; k < (1 << R); ++k) if (!((k >> pb) & 1)) {
;             const int klo = k & ((1 << pb) - 1);
;             const f32x2v w = tw[(j0 + (klo << lgq)) << (s + r)];
;             const f32x2v a = v[k], b = v[k + (1 << pb)], d = a - b;
;             v[k] = a + b; v[k + (1 << pb)] = (f32x2v){d.x * w.x - d.y * w.y, d.x * w.y + d.y * w.x};
;         }
;     }
; #pragma unroll
;     for (int k = 0; k < (1 << R); ++k) X[pb + k * qp] = v[k];
; }
; template <bool LAT>
; __device__ __forceinline__ void hyconv_unit(const Frame& F, LAS f32x2v* X, const TwHalf tw, LAS bf16* OUT, const float* skip, bf16* MIX, int u) {
;     ...
;             const f32x2v* SP = SPb + (size_t)ord * 256 * N;
;             f32x4 kq[8];
; #pragma unroll
;             for (int r = 0; r < 8; ++r) kq[r] = *(const f32x4*)(SP + 2 * (F.tid + 512 * r));
;             fft_fwd_upper(X, tw, 13 - lgN, F.tid);
.LBB0_780:
	s_lshl_b32 s90, s0, 21
	s_xor_b64 s[20:21], s[22:23], -1
	s_lshl_b64 s[2:3], s[90:91], 3
	s_add_u32 s2, s29, s2
	s_addc_u32 s3, s52, s3
	v_lshl_add_u64 v[0:1], v[34:35], 3, s[2:3]
	v_lshl_add_u64 v[2:3], v[36:37], 3, s[2:3]
	global_load_dwordx4 v[28:31], v[0:1], off
	global_load_dwordx4 v[24:27], v[2:3], off
	v_lshl_add_u64 v[0:1], v[38:39], 3, s[2:3]
	v_lshl_add_u64 v[2:3], v[40:41], 3, s[2:3]
	global_load_dwordx4 v[20:23], v[0:1], off
	global_load_dwordx4 v[16:19], v[2:3], off
	v_lshl_add_u64 v[0:1], v[42:43], 3, s[2:3]
	v_lshl_add_u64 v[2:3], v[44:45], 3, s[2:3]
	global_load_dwordx4 v[12:15], v[0:1], off
	global_load_dwordx4 v[8:11], v[2:3], off
	v_lshl_add_u64 v[0:1], v[46:47], 3, s[2:3]
	v_lshl_add_u64 v[2:3], v[48:49], 3, s[2:3]
	global_load_dwordx4 v[4:7], v[0:1], off
	s_nop 0
	global_load_dwordx4 v[0:3], v[2:3], off
	ds_read_b64 v[110:111], v75
	ds_read_b64 v[120:121], v75 offset:4352
	ds_read_b64 v[122:123], v75 offset:8704
	ds_read_b64 v[124:125], v75 offset:13056
	ds_read_b64 v[126:127], v75 offset:17408
	ds_read_b64 v[128:129], v75 offset:21760
	ds_read_b64 v[130:131], v75 offset:26112
	ds_read_b64 v[132:133], v75 offset:30464
	ds_read_b64 v[136:137], v75 offset:34816
	ds_read_b64 v[138:139], v75 offset:39168
	ds_read_b64 v[140:141], v75 offset:43520
	ds_read_b64 v[142:143], v75 offset:47872
	ds_read_b64 v[144:145], v75 offset:52224
	ds_read_b64 v[146:147], v75 offset:56576
	ds_read_b64 v[148:149], v75 offset:60928
	ds_read_b64 v[150:151], v75 offset:65280
	ds_read2st64_b64 v[116:119], v76 offset1:16
	ds_read_b64 v[152:153], v91
	ds_read_b64 v[154:155], v92
	ds_read_b64 v[156:157], v93
	ds_read_b64 v[158:159], v77
	ds_read_b64 v[160:161], v78
	ds_read_b64 v[162:163], v79
	ds_read_b64 v[164:165], v80
	s_waitcnt lgkmcnt(14)
	v_pk_add_f32 v[166:167], v[110:111], v[136:137] neg_lo:[0,1] neg_hi:[0,1]
	v_pk_add_f32 v[110:111], v[110:111], v[136:137]
	s_waitcnt lgkmcnt(7)
	v_pk_mul_f32 v[168:169], v[166:167], v[116:117] op_sel:[1,1] op_sel_hi:[1,0]
	s_lshl_b32 s0, s0, 8
	v_pk_fma_f32 v[170:171], v[166:167], v[116:117], v[168:169] op_sel_hi:[0,1,1] neg_lo:[0,0,1]
	v_pk_add_f32 v[166:167], v[126:127], v[144:145] neg_lo:[0,1] neg_hi:[0,1]
	v_pk_add_f32 v[126:127], v[126:127], v[144:145]
	v_pk_mul_f32 v[168:169], v[166:167], v[116:117] op_sel:[1,0] op_sel_hi:[0,0]
	v_pk_fma_f32 v[172:173], v[166:167], v[116:117], v[168:169] op_sel:[0,1,0] neg_hi:[0,0,1]
	v_pk_add_f32 v[136:137], v[110:111], v[126:127]
	v_pk_add_f32 v[116:117], v[170:171], v[172:173] neg_lo:[0,1] neg_hi:[0,1]
	v_pk_add_f32 v[110:111], v[110:111], v[126:127] neg_lo:[0,1] neg_hi:[0,1]
	s_waitcnt lgkmcnt(6)
	v_pk_mul_f32 v[166:167], v[152:153], v[116:117] op_sel:[1,1] op_sel_hi:[0,1]
	v_pk_fma_f32 v[168:169], v[152:153], v[116:117], v[166:167] op_sel_hi:[1,0,1] neg_lo:[0,0,1]
	v_pk_mul_f32 v[126:127], v[110:111], v[152:153] op_sel:[1,1] op_sel_hi:[1,0]
	v_pk_add_f32 v[116:117], v[122:123], v[140:141] neg_lo:[0,1] neg_hi:[0,1]
	v_pk_add_f32 v[122:123], v[122:123], v[140:141]
	v_pk_mul_f32 v[166:167], v[116:117], v[118:119] op_sel:[1,1] op_sel_hi:[1,0]
	s_add_i32 s90, s0, s28
	v_pk_fma_f32 v[174:175], v[116:117], v[118:119], v[166:167] op_sel_hi:[0,1,1] neg_lo:[0,0,1]
	v_pk_add_f32 v[116:117], v[130:131], v[148:149] neg_lo:[0,1] neg_hi:[0,1]
	v_pk_add_f32 v[130:131], v[130:131], v[148:149]
	v_pk_mul_f32 v[166:167], v[116:117], v[118:119] op_sel:[1,0] op_sel_hi:[0,0]
	v_pk_fma_f32 v[176:177], v[116:117], v[118:119], v[166:167] op_sel:[0,1,0] neg_hi:[0,0,1]
	v_pk_add_f32 v[140:141], v[122:123], v[130:131]
	v_pk_add_f32 v[116:117], v[174:175], v[176:177] neg_lo:[0,1] neg_hi:[0,1]
	v_pk_add_f32 v[144:145], v[136:137], v[140:141]
	v_pk_mul_f32 v[118:119], v[152:153], v[116:117] op_sel_hi:[0,1]
	v_pk_fma_f32 v[166:167], v[152:153], v[116:117], v[118:119] op_sel:[1,0,1] op_sel_hi:[1,1,0] neg_hi:[0,0,1]
	v_pk_add_f32 v[136:137], v[136:137], v[140:141] neg_lo:[0,1] neg_hi:[0,1]
	v_pk_add_f32 v[116:117], v[168:169], v[166:167] neg_lo:[0,1] neg_hi:[0,1]
	s_waitcnt lgkmcnt(4)
	v_pk_mul_f32 v[140:141], v[136:137], v[156:157] op_sel:[1,1] op_sel_hi:[1,0]
	v_pk_mul_f32 v[118:119], v[156:157], v[116:117] op_sel:[1,1] op_sel_hi:[0,1]
	v_pk_fma_f32 v[178:179], v[156:157], v[116:117], v[118:119] op_sel_hi:[1,0,1] neg_lo:[0,0,1]
	s_lshl_b64 s[0:1], s[90:91], 2
	v_pk_add_f32 v[116:117], v[120:121], v[138:139] neg_lo:[0,1] neg_hi:[0,1]
	v_pk_add_f32 v[120:121], v[120:121], v[138:139]
	s_waitcnt lgkmcnt(3)
	v_pk_mul_f32 v[118:119], v[116:117], v[158:159] op_sel:[1,1] op_sel_hi:[1,0]
	s_add_u32 s0, s6, s0
	v_pk_fma_f32 v[182:183], v[116:117], v[158:159], v[118:119] op_sel_hi:[0,1,1] neg_lo:[0,0,1]
	v_pk_add_f32 v[116:117], v[128:129], v[146:147] neg_lo:[0,1] neg_hi:[0,1]
	v_pk_add_f32 v[128:129], v[128:129], v[146:147]
	v_pk_mul_f32 v[118:119], v[116:117], v[158:159] op_sel:[1,0] op_sel_hi:[0,0]
	v_pk_fma_f32 v[184:185], v[116:117], v[158:159], v[118:119] op_sel:[0,1,0] neg_hi:[0,0,1]
	v_pk_add_f32 v[138:139], v[120:121], v[128:129]
	v_pk_add_f32 v[116:117], v[182:183], v[184:185] neg_lo:[0,1] neg_hi:[0,1]
	v_pk_add_f32 v[120:121], v[120:121], v[128:129] neg_lo:[0,1] neg_hi:[0,1]
	v_pk_mul_f32 v[118:119], v[154:155], v[116:117] op_sel:[1,1] op_sel_hi:[0,1]
	v_pk_fma_f32 v[158:159], v[154:155], v[116:117], v[118:119] op_sel_hi:[1,0,1] neg_lo:[0,0,1]
	s_addc_u32 s1, s7, s1
	v_pk_add_f32 v[116:117], v[124:125], v[142:143] neg_lo:[0,1] neg_hi:[0,1]
	v_pk_add_f32 v[124:125], v[124:125], v[142:143]
	s_waitcnt lgkmcnt(2)
; template <int R, class XT, class TWT>
; __device__ __forceinline__ void dif_task(XT X, TWT tw, int s, int task) {
;     const int lgM = 13 - s, lgq = lgM - R, q = 1 << lgq;
;     const int j0 = task & (q - 1), blk = task >> lgq, base = (blk << lgM) + j0;
;     const int pb = PADI(base), qp = (q >= 32) ? q + (q >> 4) : q;
;     f32x2v v[1 << R];
; #pragma unroll
;     for (int k = 0; k < (1 << R); ++k) v[k] = X[pb + k * qp];
; #pragma unroll
;     for (int r = 0; r < R; ++r) {
;         const int pb = R - 1 - r;
; #pragma unroll
;         for (int k = 0; k < (1 << R); ++k) if (!((k >> pb) & 1)) {
;             const int klo = k & ((1 << pb) - 1);
;             const f32x2v w = tw[(j0 + (klo << lgq)) << (s + r)];
;             const f32x2v a = v[k], b = v[k + (1 << pb)], d = a - b;
;             v[k] = a + b; v[k + (1 << pb)] = (f32x2v){d.x * w.x - d.y * w.y, d.x * w.y + d.y * w.x};
;         }
;     }
; #pragma unroll
;     for (int k = 0; k < (1 << R); ++k) X[pb + k * qp] = v[k];
; }
	v_pk_mul_f32 v[118:119], v[116:117], v[160:161] op_sel:[1,1] op_sel_hi:[1,0]
	s_lshl_b64 s[2:3], s[90:91], 13
	v_pk_fma_f32 v[186:187], v[116:117], v[160:161], v[118:119] op_sel_hi:[0,1,1] neg_lo:[0,0,1]
	v_pk_add_f32 v[116:117], v[132:133], v[150:151] neg_lo:[0,1] neg_hi:[0,1]
	v_pk_add_f32 v[132:133], v[132:133], v[150:151]
	v_pk_mul_f32 v[118:119], v[116:117], v[160:161] op_sel:[1,0] op_sel_hi:[0,0]
	v_pk_fma_f32 v[188:189], v[116:117], v[160:161], v[118:119] op_sel:[0,1,0] neg_hi:[0,0,1]
	v_pk_add_f32 v[142:143], v[124:125], v[132:133]
	v_pk_add_f32 v[116:117], v[186:187], v[188:189] neg_lo:[0,1] neg_hi:[0,1]
	v_pk_add_f32 v[146:147], v[138:139], v[142:143]
	s_waitcnt lgkmcnt(1)
	v_pk_mul_f32 v[118:119], v[162:163], v[116:117] op_sel_hi:[0,1]
	v_pk_fma_f32 v[160:161], v[162:163], v[116:117], v[118:119] op_sel:[1,0,1] op_sel_hi:[1,1,0] neg_hi:[0,0,1]
	v_pk_add_f32 v[148:149], v[144:145], v[146:147]
	v_pk_add_f32 v[116:117], v[158:159], v[160:161] neg_lo:[0,1] neg_hi:[0,1]
	v_pk_add_f32 v[144:145], v[144:145], v[146:147] neg_lo:[0,1] neg_hi:[0,1]
	v_pk_mul_f32 v[118:119], v[156:157], v[116:117] op_sel_hi:[0,1]
	v_pk_fma_f32 v[190:191], v[156:157], v[116:117], v[118:119] op_sel:[1,0,1] op_sel_hi:[1,1,0]
	v_pk_fma_f32 v[116:117], v[156:157], v[116:117], v[118:119] op_sel:[1,0,1] op_sel_hi:[1,1,0] neg_lo:[0,0,1] neg_hi:[0,0,1]
	s_waitcnt lgkmcnt(0)
	v_xor_b32_e32 v118, 0x80000000, v164
	v_cndmask_b32_e64 v119, v118, v165, s[38:39]
	v_cndmask_b32_e64 v118, v165, v164, s[38:39]
	v_pk_mul_f32 v[146:147], v[144:145], v[118:119] op_sel:[1,1] op_sel_hi:[1,0]
	v_mov_b32_e32 v191, v117
	v_pk_fma_f32 v[150:151], v[144:145], v[118:119], v[146:147] op_sel_hi:[0,1,1] neg_lo:[0,0,1]
	v_pk_fma_f32 v[144:145], v[136:137], v[156:157], v[140:141] op_sel_hi:[0,1,1] neg_lo:[0,0,1]
	v_pk_add_f32 v[136:137], v[138:139], v[142:143] neg_lo:[0,1] neg_hi:[0,1]
	v_pk_add_f32 v[116:117], v[178:179], v[190:191] neg_lo:[0,1] neg_hi:[0,1]
	v_pk_mul_f32 v[138:139], v[136:137], v[156:157] op_sel_hi:[1,0]
	s_nop 0
	v_pk_fma_f32 v[140:141], v[136:137], v[156:157], v[138:139] op_sel:[0,1,1] op_sel_hi:[1,1,0] neg_hi:[0,0,1]
	s_nop 0
	v_pk_add_f32 v[138:139], v[144:145], v[140:141] neg_lo:[0,1] neg_hi:[0,1]
	v_pk_add_f32 v[136:137], v[144:145], v[140:141]
	v_pk_mul_f32 v[140:141], v[118:119], v[138:139] op_sel:[1,1] op_sel_hi:[0,1]
	v_pk_fma_f32 v[142:143], v[118:119], v[138:139], v[140:141] op_sel_hi:[1,0,1] neg_lo:[0,0,1]
	s_nop 0
	v_pk_fma_f32 v[138:139], v[110:111], v[152:153], v[126:127] op_sel_hi:[0,1,1] neg_lo:[0,0,1]
	v_pk_add_f32 v[110:111], v[122:123], v[130:131] neg_lo:[0,1] neg_hi:[0,1]
	s_nop 0
	v_pk_mul_f32 v[122:123], v[110:111], v[152:153] op_sel_hi:[1,0]
	s_nop 0
	v_pk_fma_f32 v[126:127], v[110:111], v[152:153], v[122:123] op_sel:[0,1,1] op_sel_hi:[1,1,0]
	v_pk_fma_f32 v[110:111], v[110:111], v[152:153], v[122:123] op_sel:[0,1,1] op_sel_hi:[1,1,0] neg_lo:[0,0,1] neg_hi:[0,0,1]
	v_pk_mul_f32 v[122:123], v[120:121], v[154:155] op_sel:[1,1] op_sel_hi:[1,0]
	v_mov_b32_e32 v127, v111
	v_pk_fma_f32 v[128:129], v[120:121], v[154:155], v[122:123] op_sel_hi:[0,1,1] neg_lo:[0,0,1]
	v_pk_add_f32 v[120:121], v[124:125], v[132:133] neg_lo:[0,1] neg_hi:[0,1]
	v_pk_add_f32 v[110:111], v[138:139], v[126:127]
	v_pk_mul_f32 v[122:123], v[120:121], v[162:163] op_sel_hi:[1,0]
	v_pk_add_f32 v[132:133], v[182:183], v[184:185]
	v_pk_fma_f32 v[124:125], v[120:121], v[162:163], v[122:123] op_sel:[0,1,1] op_sel_hi:[1,1,0] neg_hi:[0,0,1]
	s_nop 0
	v_pk_add_f32 v[120:121], v[128:129], v[124:125]
	s_nop 0
	v_pk_add_f32 v[122:123], v[110:111], v[120:121]
	v_pk_add_f32 v[110:111], v[110:111], v[120:121] neg_lo:[0,1] neg_hi:[0,1]
	s_nop 0
	v_pk_mul_f32 v[120:121], v[118:119], v[110:111] op_sel:[1,1] op_sel_hi:[0,1]
	v_pk_fma_f32 v[130:131], v[118:119], v[110:111], v[120:121] op_sel_hi:[1,0,1] neg_lo:[0,0,1]
	s_nop 0
	v_pk_add_f32 v[110:111], v[138:139], v[126:127] neg_lo:[0,1] neg_hi:[0,1]
	v_pk_add_f32 v[138:139], v[186:187], v[188:189]
	v_pk_mul_f32 v[120:121], v[156:157], v[110:111] op_sel:[1,1] op_sel_hi:[0,1]
	v_pk_fma_f32 v[126:127], v[156:157], v[110:111], v[120:121] op_sel_hi:[1,0,1] neg_lo:[0,0,1]
	v_pk_add_f32 v[140:141], v[132:133], v[138:139]
	v_pk_add_f32 v[110:111], v[128:129], v[124:125] neg_lo:[0,1] neg_hi:[0,1]
	s_nop 0
	v_pk_mul_f32 v[120:121], v[156:157], v[110:111] op_sel_hi:[0,1]
	v_pk_fma_f32 v[124:125], v[156:157], v[110:111], v[120:121] op_sel:[1,0,1] op_sel_hi:[1,1,0] neg_hi:[0,0,1]
	s_nop 0
	v_pk_add_f32 v[120:121], v[126:127], v[124:125] neg_lo:[0,1] neg_hi:[0,1]
	v_pk_add_f32 v[110:111], v[126:127], v[124:125]
	v_pk_mul_f32 v[124:125], v[118:119], v[120:121] op_sel:[1,1] op_sel_hi:[0,1]
	v_pk_fma_f32 v[126:127], v[118:119], v[120:121], v[124:125] neg_lo:[0,0,1] neg_hi:[0,0,1]
	v_pk_fma_f32 v[120:121], v[118:119], v[120:121], v[124:125] op_sel_hi:[1,0,1]
	v_pk_add_f32 v[124:125], v[174:175], v[176:177]
	v_mov_b32_e32 v127, v121
	v_pk_add_f32 v[120:121], v[170:171], v[172:173]
	s_nop 0
	v_pk_add_f32 v[128:129], v[120:121], v[124:125]
	v_pk_add_f32 v[120:121], v[120:121], v[124:125] neg_lo:[0,1] neg_hi:[0,1]
	v_pk_add_f32 v[144:145], v[128:129], v[140:141]
	v_pk_add_f32 v[128:129], v[128:129], v[140:141] neg_lo:[0,1] neg_hi:[0,1]
	v_pk_mul_f32 v[124:125], v[156:157], v[120:121] op_sel:[1,1] op_sel_hi:[0,1]
	v_pk_mul_f32 v[140:141], v[128:129], v[118:119] op_sel:[1,1] op_sel_hi:[1,0]
	s_nop 0
	v_pk_fma_f32 v[146:147], v[128:129], v[118:119], v[140:141] op_sel_hi:[0,1,1] neg_lo:[0,0,1]
	v_pk_fma_f32 v[128:129], v[156:157], v[120:121], v[124:125] op_sel_hi:[1,0,1] neg_lo:[0,0,1]
	s_nop 0
	v_pk_add_f32 v[120:121], v[132:133], v[138:139] neg_lo:[0,1] neg_hi:[0,1]
; __device__ __forceinline__ void lds_barrier() { asm volatile("s_waitcnt lgkmcnt(0)" ::: "memory"); __builtin_amdgcn_s_barrier(); asm volatile("" ::: "memory"); }
; template <int R, class XT, class TWT>
; __device__ __forceinline__ void dif_task(XT X, TWT tw, int s, int task) {
;     const int lgM = 13 - s, lgq = lgM - R, q = 1 << lgq;
;     const int j0 = task & (q - 1), blk = task >> lgq, base = (blk << lgM) + j0;
;     const int pb = PADI(base), qp = (q >= 32) ? q + (q >> 4) : q;
;     f32x2v v[1 << R];
; #pragma unroll
;     for (int k = 0; k < (1 << R); ++k) v[k] = X[pb + k * qp];
; #pragma unroll
;     for (int r = 0; r < R; ++r) {
;         const int pb = R - 1 - r;
; #pragma unroll
;         for (int k = 0; k < (1 << R); ++k) if (!((k >> pb) & 1)) {
;             const int klo = k & ((1 << pb) - 1);
;             const f32x2v w = tw[(j0 + (klo << lgq)) << (s + r)];
;             const f32x2v a = v[k], b = v[k + (1 << pb)], d = a - b;
;             v[k] = a + b; v[k + (1 << pb)] = (f32x2v){d.x * w.x - d.y * w.y, d.x * w.y + d.y * w.x};
;         }
;     }
; #pragma unroll
;     for (int k = 0; k < (1 << R); ++k) X[pb + k * qp] = v[k];
; }
; __device__ __forceinline__ void fft_fwd_upper(LAS f32x2v* X, TwHalf tw, int s0, int tid) {
;     if (s0 == 0) { dif_task<4>(X, tw, 0, tid); lds_barrier(); }
;     dif_task<4>(X, tw, 4, tid); lds_barrier();
	s_nop 0
	v_pk_mul_f32 v[124:125], v[156:157], v[120:121] op_sel_hi:[0,1]
	v_pk_fma_f32 v[132:133], v[156:157], v[120:121], v[124:125] op_sel:[1,0,1] op_sel_hi:[1,1,0] neg_hi:[0,0,1]
	s_nop 0
	v_pk_add_f32 v[124:125], v[128:129], v[132:133] neg_lo:[0,1] neg_hi:[0,1]
	v_pk_add_f32 v[120:121], v[128:129], v[132:133]
	v_pk_mul_f32 v[128:129], v[118:119], v[124:125] op_sel:[1,1] op_sel_hi:[0,1]
	v_pk_fma_f32 v[132:133], v[118:119], v[124:125], v[128:129] neg_lo:[0,0,1] neg_hi:[0,0,1]
	v_pk_fma_f32 v[124:125], v[118:119], v[124:125], v[128:129] op_sel_hi:[1,0,1]
	v_pk_add_f32 v[128:129], v[158:159], v[160:161]
	v_mov_b32_e32 v133, v125
	v_pk_add_f32 v[124:125], v[168:169], v[166:167]
	s_nop 0
	v_pk_add_f32 v[138:139], v[124:125], v[128:129]
	v_pk_add_f32 v[124:125], v[124:125], v[128:129] neg_lo:[0,1] neg_hi:[0,1]
	s_nop 0
	v_pk_mul_f32 v[128:129], v[118:119], v[124:125] op_sel:[1,1] op_sel_hi:[0,1]
	v_pk_fma_f32 v[140:141], v[118:119], v[124:125], v[128:129] neg_lo:[0,0,1] neg_hi:[0,0,1]
	v_pk_fma_f32 v[124:125], v[118:119], v[124:125], v[128:129] op_sel_hi:[1,0,1]
	v_pk_mul_f32 v[128:129], v[118:119], v[116:117] op_sel:[1,1] op_sel_hi:[0,1]
	v_pk_fma_f32 v[152:153], v[118:119], v[116:117], v[128:129] op_sel_hi:[1,0,1] neg_lo:[0,0,1]
	v_mov_b32_e32 v141, v125
	v_pk_add_f32 v[124:125], v[178:179], v[190:191]
	ds_write_b64 v75, v[148:149]
	ds_write_b64 v75, v[150:151] offset:4352
	ds_write_b64 v75, v[136:137] offset:8704
	ds_write_b64 v75, v[142:143] offset:13056
	ds_write_b64 v75, v[122:123] offset:17408
	ds_write_b64 v75, v[130:131] offset:21760
	ds_write_b64 v75, v[110:111] offset:26112
	ds_write_b64 v75, v[126:127] offset:30464
	ds_write_b64 v75, v[144:145] offset:34816
	ds_write_b64 v75, v[146:147] offset:39168
	ds_write_b64 v75, v[120:121] offset:43520
	ds_write_b64 v75, v[132:133] offset:47872
	ds_write_b64 v75, v[138:139] offset:52224
	ds_write_b64 v75, v[140:141] offset:56576
	ds_write_b64 v75, v[124:125] offset:60928
	ds_write_b64 v75, v[152:153] offset:65280
	s_waitcnt lgkmcnt(0)
	s_barrier
	ds_read2_b64 v[116:119], v81 offset1:34
	ds_read2_b64 v[120:123], v81 offset0:68 offset1:102
	ds_read2_b64 v[124:127], v81 offset0:136 offset1:170
	ds_read2_b64 v[128:131], v81 offset0:204 offset1:238
	v_add_u32_e32 v110, 0x800, v81
	ds_read2_b64 v[136:139], v110 offset0:16 offset1:50
	ds_read2_b64 v[140:143], v110 offset0:84 offset1:118
	ds_read2_b64 v[144:147], v110 offset0:152 offset1:186
	ds_read2_b64 v[148:151], v110 offset0:220 offset1:254
	ds_read2st64_b64 v[152:155], v94 offset1:16
	ds_read_b64 v[132:133], v97
	ds_read_b64 v[156:157], v98
	ds_read_b64 v[158:159], v99
	ds_read_b64 v[160:161], v95
	ds_read_b64 v[162:163], v96
	ds_read_b64 v[164:165], v82
	ds_read_b64 v[166:167], v83
	s_waitcnt lgkmcnt(11)
	v_pk_add_f32 v[168:169], v[116:117], v[136:137] neg_lo:[0,1] neg_hi:[0,1]
	v_pk_add_f32 v[116:117], v[116:117], v[136:137]
	s_waitcnt lgkmcnt(7)
	v_pk_mul_f32 v[170:171], v[168:169], v[152:153] op_sel:[1,1] op_sel_hi:[1,0]
	s_waitcnt lgkmcnt(0)
	v_xor_b32_e32 v111, 0x80000000, v166
	v_pk_fma_f32 v[172:173], v[168:169], v[152:153], v[170:171] op_sel_hi:[0,1,1] neg_lo:[0,0,1]
	v_pk_add_f32 v[168:169], v[124:125], v[144:145] neg_lo:[0,1] neg_hi:[0,1]
	v_pk_add_f32 v[124:125], v[124:125], v[144:145]
	v_pk_mul_f32 v[170:171], v[168:169], v[152:153] op_sel:[1,0] op_sel_hi:[0,0]
	v_pk_fma_f32 v[174:175], v[168:169], v[152:153], v[170:171] op_sel:[0,1,0] neg_hi:[0,0,1]
	v_pk_add_f32 v[136:137], v[116:117], v[124:125]
	v_pk_add_f32 v[152:153], v[172:173], v[174:175] neg_lo:[0,1] neg_hi:[0,1]
	v_pk_add_f32 v[116:117], v[116:117], v[124:125] neg_lo:[0,1] neg_hi:[0,1]
	v_pk_mul_f32 v[168:169], v[132:133], v[152:153] op_sel:[1,1] op_sel_hi:[0,1]
	v_pk_fma_f32 v[170:171], v[132:133], v[152:153], v[168:169] op_sel_hi:[1,0,1] neg_lo:[0,0,1]
	v_pk_mul_f32 v[124:125], v[116:117], v[132:133] op_sel:[1,1] op_sel_hi:[1,0]
	v_pk_add_f32 v[152:153], v[120:121], v[140:141] neg_lo:[0,1] neg_hi:[0,1]
	v_pk_add_f32 v[120:121], v[120:121], v[140:141]
	v_pk_mul_f32 v[168:169], v[152:153], v[154:155] op_sel:[1,1] op_sel_hi:[1,0]
	s_nop 0
	v_pk_fma_f32 v[176:177], v[152:153], v[154:155], v[168:169] op_sel_hi:[0,1,1] neg_lo:[0,0,1]
	v_pk_add_f32 v[152:153], v[128:129], v[148:149] neg_lo:[0,1] neg_hi:[0,1]
	v_pk_add_f32 v[128:129], v[128:129], v[148:149]
	v_pk_mul_f32 v[168:169], v[152:153], v[154:155] op_sel:[1,0] op_sel_hi:[0,0]
	v_pk_fma_f32 v[178:179], v[152:153], v[154:155], v[168:169] op_sel:[0,1,0] neg_hi:[0,0,1]
	v_pk_add_f32 v[140:141], v[120:121], v[128:129]
	v_pk_add_f32 v[152:153], v[176:177], v[178:179] neg_lo:[0,1] neg_hi:[0,1]
	v_pk_add_f32 v[144:145], v[136:137], v[140:141]
	v_pk_mul_f32 v[154:155], v[132:133], v[152:153] op_sel_hi:[0,1]
	v_pk_fma_f32 v[168:169], v[132:133], v[152:153], v[154:155] op_sel:[1,0,1] op_sel_hi:[1,1,0] neg_hi:[0,0,1]
	v_pk_add_f32 v[136:137], v[136:137], v[140:141] neg_lo:[0,1] neg_hi:[0,1]
	v_pk_add_f32 v[152:153], v[170:171], v[168:169] neg_lo:[0,1] neg_hi:[0,1]
	v_pk_mul_f32 v[140:141], v[136:137], v[158:159] op_sel:[1,1] op_sel_hi:[1,0]
	v_pk_mul_f32 v[154:155], v[158:159], v[152:153] op_sel:[1,1] op_sel_hi:[0,1]
	v_pk_fma_f32 v[182:183], v[158:159], v[152:153], v[154:155] op_sel_hi:[1,0,1] neg_lo:[0,0,1]
	s_nop 0
	v_pk_add_f32 v[152:153], v[118:119], v[138:139] neg_lo:[0,1] neg_hi:[0,1]
	v_pk_add_f32 v[118:119], v[118:119], v[138:139]
	v_pk_mul_f32 v[154:155], v[152:153], v[160:161] op_sel:[1,1] op_sel_hi:[1,0]
	s_nop 0
	v_pk_fma_f32 v[184:185], v[152:153], v[160:161], v[154:155] op_sel_hi:[0,1,1] neg_lo:[0,0,1]
	v_pk_add_f32 v[152:153], v[126:127], v[146:147] neg_lo:[0,1] neg_hi:[0,1]
	v_pk_add_f32 v[126:127], v[126:127], v[146:147]
; template <int R, class XT, class TWT>
; __device__ __forceinline__ void dif_task(XT X, TWT tw, int s, int task) {
;     const int lgM = 13 - s, lgq = lgM - R, q = 1 << lgq;
;     const int j0 = task & (q - 1), blk = task >> lgq, base = (blk << lgM) + j0;
;     const int pb = PADI(base), qp = (q >= 32) ? q + (q >> 4) : q;
;     f32x2v v[1 << R];
; #pragma unroll
;     for (int k = 0; k < (1 << R); ++k) v[k] = X[pb + k * qp];
; #pragma unroll
;     for (int r = 0; r < R; ++r) {
;         const int pb = R - 1 - r;
; #pragma unroll
;         for (int k = 0; k < (1 << R); ++k) if (!((k >> pb) & 1)) {
;             const int klo = k & ((1 << pb) - 1);
;             const f32x2v w = tw[(j0 + (klo << lgq)) << (s + r)];
;             const f32x2v a = v[k], b = v[k + (1 << pb)], d = a - b;
;             v[k] = a + b; v[k + (1 << pb)] = (f32x2v){d.x * w.x - d.y * w.y, d.x * w.y + d.y * w.x};
;         }
;     }
; #pragma unroll
;     for (int k = 0; k < (1 << R); ++k) X[pb + k * qp] = v[k];
; }
	v_pk_mul_f32 v[154:155], v[152:153], v[160:161] op_sel:[1,0] op_sel_hi:[0,0]
	v_pk_fma_f32 v[186:187], v[152:153], v[160:161], v[154:155] op_sel:[0,1,0] neg_hi:[0,0,1]
	v_pk_add_f32 v[138:139], v[118:119], v[126:127]
	v_pk_add_f32 v[152:153], v[184:185], v[186:187] neg_lo:[0,1] neg_hi:[0,1]
	v_pk_add_f32 v[118:119], v[118:119], v[126:127] neg_lo:[0,1] neg_hi:[0,1]
	v_pk_mul_f32 v[154:155], v[156:157], v[152:153] op_sel:[1,1] op_sel_hi:[0,1]
	v_pk_fma_f32 v[160:161], v[156:157], v[152:153], v[154:155] op_sel_hi:[1,0,1] neg_lo:[0,0,1]
	s_nop 0
	v_pk_add_f32 v[152:153], v[122:123], v[142:143] neg_lo:[0,1] neg_hi:[0,1]
	v_pk_add_f32 v[122:123], v[122:123], v[142:143]
	v_pk_mul_f32 v[154:155], v[152:153], v[162:163] op_sel:[1,1] op_sel_hi:[1,0]
	s_nop 0
	v_pk_fma_f32 v[188:189], v[152:153], v[162:163], v[154:155] op_sel_hi:[0,1,1] neg_lo:[0,0,1]
	v_pk_add_f32 v[152:153], v[130:131], v[150:151] neg_lo:[0,1] neg_hi:[0,1]
	v_pk_add_f32 v[130:131], v[130:131], v[150:151]
	v_pk_mul_f32 v[154:155], v[152:153], v[162:163] op_sel:[1,0] op_sel_hi:[0,0]
	v_pk_fma_f32 v[190:191], v[152:153], v[162:163], v[154:155] op_sel:[0,1,0] neg_hi:[0,0,1]
	v_pk_add_f32 v[142:143], v[122:123], v[130:131]
	v_pk_add_f32 v[152:153], v[188:189], v[190:191] neg_lo:[0,1] neg_hi:[0,1]
	v_pk_add_f32 v[146:147], v[138:139], v[142:143]
	v_pk_mul_f32 v[154:155], v[164:165], v[152:153] op_sel_hi:[0,1]
	v_pk_fma_f32 v[162:163], v[164:165], v[152:153], v[154:155] op_sel:[1,0,1] op_sel_hi:[1,1,0] neg_hi:[0,0,1]
	v_pk_add_f32 v[148:149], v[144:145], v[146:147]
	v_pk_add_f32 v[152:153], v[160:161], v[162:163] neg_lo:[0,1] neg_hi:[0,1]
	v_pk_add_f32 v[144:145], v[144:145], v[146:147] neg_lo:[0,1] neg_hi:[0,1]
	v_pk_mul_f32 v[154:155], v[158:159], v[152:153] op_sel_hi:[0,1]
	v_pk_fma_f32 v[192:193], v[158:159], v[152:153], v[154:155] op_sel:[1,0,1] op_sel_hi:[1,1,0]
	v_pk_fma_f32 v[152:153], v[158:159], v[152:153], v[154:155] op_sel:[1,0,1] op_sel_hi:[1,1,0] neg_lo:[0,0,1] neg_hi:[0,0,1]
	v_cndmask_b32_e64 v155, v111, v167, s[40:41]
	v_cndmask_b32_e64 v154, v167, v166, s[40:41]
	v_pk_mul_f32 v[146:147], v[144:145], v[154:155] op_sel:[1,1] op_sel_hi:[1,0]
	v_mov_b32_e32 v193, v153
	v_pk_fma_f32 v[150:151], v[144:145], v[154:155], v[146:147] op_sel_hi:[0,1,1] neg_lo:[0,0,1]
	v_pk_fma_f32 v[144:145], v[136:137], v[158:159], v[140:141] op_sel_hi:[0,1,1] neg_lo:[0,0,1]
	v_pk_add_f32 v[136:137], v[138:139], v[142:143] neg_lo:[0,1] neg_hi:[0,1]
	v_pk_add_f32 v[152:153], v[182:183], v[192:193] neg_lo:[0,1] neg_hi:[0,1]
	v_pk_mul_f32 v[138:139], v[136:137], v[158:159] op_sel_hi:[1,0]
	v_mov_b32_e32 v111, s16
	v_pk_fma_f32 v[140:141], v[136:137], v[158:159], v[138:139] op_sel:[0,1,1] op_sel_hi:[1,1,0] neg_hi:[0,0,1]
	s_nop 0
	v_pk_add_f32 v[138:139], v[144:145], v[140:141] neg_lo:[0,1] neg_hi:[0,1]
	v_pk_add_f32 v[136:137], v[144:145], v[140:141]
	v_pk_mul_f32 v[140:141], v[154:155], v[138:139] op_sel:[1,1] op_sel_hi:[0,1]
	v_pk_fma_f32 v[142:143], v[154:155], v[138:139], v[140:141] op_sel_hi:[1,0,1] neg_lo:[0,0,1]
	s_nop 0
	v_pk_fma_f32 v[138:139], v[116:117], v[132:133], v[124:125] op_sel_hi:[0,1,1] neg_lo:[0,0,1]
	v_pk_add_f32 v[116:117], v[120:121], v[128:129] neg_lo:[0,1] neg_hi:[0,1]
	s_nop 0
	v_pk_mul_f32 v[120:121], v[116:117], v[132:133] op_sel_hi:[1,0]
	s_nop 0
	v_pk_fma_f32 v[124:125], v[116:117], v[132:133], v[120:121] op_sel:[0,1,1] op_sel_hi:[1,1,0]
	v_pk_fma_f32 v[116:117], v[116:117], v[132:133], v[120:121] op_sel:[0,1,1] op_sel_hi:[1,1,0] neg_lo:[0,0,1] neg_hi:[0,0,1]
	v_pk_mul_f32 v[120:121], v[118:119], v[156:157] op_sel:[1,1] op_sel_hi:[1,0]
	v_mov_b32_e32 v125, v117
	v_pk_fma_f32 v[126:127], v[118:119], v[156:157], v[120:121] op_sel_hi:[0,1,1] neg_lo:[0,0,1]
	v_pk_add_f32 v[118:119], v[122:123], v[130:131] neg_lo:[0,1] neg_hi:[0,1]
	v_pk_add_f32 v[116:117], v[138:139], v[124:125]
	v_pk_mul_f32 v[120:121], v[118:119], v[164:165] op_sel_hi:[1,0]
	v_pk_add_f32 v[130:131], v[184:185], v[186:187]
	v_pk_fma_f32 v[122:123], v[118:119], v[164:165], v[120:121] op_sel:[0,1,1] op_sel_hi:[1,1,0] neg_hi:[0,0,1]
	v_pk_add_f32 v[132:133], v[188:189], v[190:191]
	v_pk_add_f32 v[118:119], v[126:127], v[122:123]
	s_nop 0
	v_pk_add_f32 v[120:121], v[116:117], v[118:119]
	v_pk_add_f32 v[116:117], v[116:117], v[118:119] neg_lo:[0,1] neg_hi:[0,1]
	s_nop 0
	v_pk_mul_f32 v[118:119], v[154:155], v[116:117] op_sel:[1,1] op_sel_hi:[0,1]
	v_pk_fma_f32 v[128:129], v[154:155], v[116:117], v[118:119] op_sel_hi:[1,0,1] neg_lo:[0,0,1]
	s_nop 0
	v_pk_add_f32 v[116:117], v[138:139], v[124:125] neg_lo:[0,1] neg_hi:[0,1]
	v_pk_add_f32 v[138:139], v[130:131], v[132:133]
	v_pk_mul_f32 v[118:119], v[158:159], v[116:117] op_sel:[1,1] op_sel_hi:[0,1]
	v_pk_fma_f32 v[124:125], v[158:159], v[116:117], v[118:119] op_sel_hi:[1,0,1] neg_lo:[0,0,1]
	s_nop 0
	v_pk_add_f32 v[116:117], v[126:127], v[122:123] neg_lo:[0,1] neg_hi:[0,1]
	s_nop 0
	v_pk_mul_f32 v[118:119], v[158:159], v[116:117] op_sel_hi:[0,1]
	v_pk_fma_f32 v[122:123], v[158:159], v[116:117], v[118:119] op_sel:[1,0,1] op_sel_hi:[1,1,0] neg_hi:[0,0,1]
	s_nop 0
	v_pk_add_f32 v[118:119], v[124:125], v[122:123] neg_lo:[0,1] neg_hi:[0,1]
	v_pk_add_f32 v[116:117], v[124:125], v[122:123]
	v_pk_mul_f32 v[122:123], v[154:155], v[118:119] op_sel:[1,1] op_sel_hi:[0,1]
	v_pk_fma_f32 v[124:125], v[154:155], v[118:119], v[122:123] neg_lo:[0,0,1] neg_hi:[0,0,1]
	v_pk_fma_f32 v[118:119], v[154:155], v[118:119], v[122:123] op_sel_hi:[1,0,1]
	v_pk_add_f32 v[122:123], v[176:177], v[178:179]
	v_mov_b32_e32 v125, v119
	v_pk_add_f32 v[118:119], v[172:173], v[174:175]
	s_nop 0
	v_pk_add_f32 v[126:127], v[118:119], v[122:123]
	v_pk_add_f32 v[118:119], v[118:119], v[122:123] neg_lo:[0,1] neg_hi:[0,1]
; __device__ __forceinline__ void lds_barrier() { asm volatile("s_waitcnt lgkmcnt(0)" ::: "memory"); __builtin_amdgcn_s_barrier(); asm volatile("" ::: "memory"); }
; template <int R, class XT, class TWT>
; __device__ __forceinline__ void dif_task(XT X, TWT tw, int s, int task) {
;     const int lgM = 13 - s, lgq = lgM - R, q = 1 << lgq;
;     const int j0 = task & (q - 1), blk = task >> lgq, base = (blk << lgM) + j0;
;     const int pb = PADI(base), qp = (q >= 32) ? q + (q >> 4) : q;
;     f32x2v v[1 << R];
; #pragma unroll
;     for (int k = 0; k < (1 << R); ++k) v[k] = X[pb + k * qp];
; #pragma unroll
;     for (int r = 0; r < R; ++r) {
;         const int pb = R - 1 - r;
; #pragma unroll
;         for (int k = 0; k < (1 << R); ++k) if (!((k >> pb) & 1)) {
;             const int klo = k & ((1 << pb) - 1);
;             const f32x2v w = tw[(j0 + (klo << lgq)) << (s + r)];
;             const f32x2v a = v[k], b = v[k + (1 << pb)], d = a - b;
;             v[k] = a + b; v[k + (1 << pb)] = (f32x2v){d.x * w.x - d.y * w.y, d.x * w.y + d.y * w.x};
;         }
;     }
; #pragma unroll
;     for (int k = 0; k < (1 << R); ++k) X[pb + k * qp] = v[k];
; }
; __device__ __forceinline__ void fft_fwd_upper(LAS f32x2v* X, TwHalf tw, int s0, int tid) {
;     ...
;     dif_task<4>(X, tw, 4, tid); lds_barrier();
;     dif_task<4>(X, tw, 8, tid); lds_barrier();
	v_pk_add_f32 v[140:141], v[126:127], v[138:139]
	v_pk_add_f32 v[126:127], v[126:127], v[138:139] neg_lo:[0,1] neg_hi:[0,1]
	v_pk_mul_f32 v[122:123], v[158:159], v[118:119] op_sel:[1,1] op_sel_hi:[0,1]
	v_pk_mul_f32 v[138:139], v[126:127], v[154:155] op_sel:[1,1] op_sel_hi:[1,0]
	s_nop 0
	v_pk_fma_f32 v[144:145], v[126:127], v[154:155], v[138:139] op_sel_hi:[0,1,1] neg_lo:[0,0,1]
	v_pk_fma_f32 v[126:127], v[158:159], v[118:119], v[122:123] op_sel_hi:[1,0,1] neg_lo:[0,0,1]
	s_nop 0
	v_pk_add_f32 v[118:119], v[130:131], v[132:133] neg_lo:[0,1] neg_hi:[0,1]
	s_nop 0
	v_pk_mul_f32 v[122:123], v[158:159], v[118:119] op_sel_hi:[0,1]
	v_pk_fma_f32 v[130:131], v[158:159], v[118:119], v[122:123] op_sel:[1,0,1] op_sel_hi:[1,1,0] neg_hi:[0,0,1]
	s_nop 0
	v_pk_add_f32 v[122:123], v[126:127], v[130:131] neg_lo:[0,1] neg_hi:[0,1]
	v_pk_add_f32 v[118:119], v[126:127], v[130:131]
	v_pk_mul_f32 v[126:127], v[154:155], v[122:123] op_sel:[1,1] op_sel_hi:[0,1]
	v_pk_fma_f32 v[130:131], v[154:155], v[122:123], v[126:127] neg_lo:[0,0,1] neg_hi:[0,0,1]
	v_pk_fma_f32 v[122:123], v[154:155], v[122:123], v[126:127] op_sel_hi:[1,0,1]
	v_pk_add_f32 v[126:127], v[160:161], v[162:163]
	v_mov_b32_e32 v131, v123
	v_pk_add_f32 v[122:123], v[170:171], v[168:169]
	s_nop 0
	v_pk_add_f32 v[132:133], v[122:123], v[126:127]
	v_pk_add_f32 v[122:123], v[122:123], v[126:127] neg_lo:[0,1] neg_hi:[0,1]
	s_nop 0
	v_pk_mul_f32 v[126:127], v[154:155], v[122:123] op_sel:[1,1] op_sel_hi:[0,1]
	v_pk_fma_f32 v[138:139], v[154:155], v[122:123], v[126:127] neg_lo:[0,0,1] neg_hi:[0,0,1]
	v_pk_fma_f32 v[122:123], v[154:155], v[122:123], v[126:127] op_sel_hi:[1,0,1]
	v_pk_mul_f32 v[126:127], v[154:155], v[152:153] op_sel:[1,1] op_sel_hi:[0,1]
	v_pk_fma_f32 v[146:147], v[154:155], v[152:153], v[126:127] op_sel_hi:[1,0,1] neg_lo:[0,0,1]
	v_mov_b32_e32 v139, v123
	v_pk_add_f32 v[122:123], v[182:183], v[192:193]
	ds_write2_b64 v81, v[148:149], v[150:151] offset1:34
	ds_write2_b64 v81, v[136:137], v[142:143] offset0:68 offset1:102
	ds_write2_b64 v81, v[120:121], v[128:129] offset0:136 offset1:170
	ds_write2_b64 v81, v[116:117], v[124:125] offset0:204 offset1:238
	ds_write2_b64 v110, v[140:141], v[144:145] offset0:16 offset1:50
	ds_write2_b64 v110, v[118:119], v[130:131] offset0:84 offset1:118
	ds_write2_b64 v110, v[132:133], v[138:139] offset0:152 offset1:186
	ds_write2_b64 v110, v[122:123], v[146:147] offset0:220 offset1:254
	s_waitcnt lgkmcnt(0)
	s_barrier
	ds_read2_b64 v[116:119], v84 offset1:2
	ds_read2_b64 v[120:123], v84 offset0:4 offset1:6
	ds_read2_b64 v[124:127], v84 offset0:8 offset1:10
	ds_read2_b64 v[128:131], v84 offset0:12 offset1:14
	ds_read2_b64 v[136:139], v84 offset0:16 offset1:18
	ds_read2_b64 v[140:143], v84 offset0:20 offset1:22
	ds_read2_b64 v[144:147], v84 offset0:24 offset1:26
	ds_read2_b64 v[148:151], v84 offset0:28 offset1:30
	ds_read2st64_b64 v[152:155], v100 offset1:16
	ds_read_b64 v[132:133], v101
	ds_read_b64 v[156:157], v102
	ds_read_b64 v[158:159], v103
	ds_read_b64 v[160:161], v85
	s_waitcnt lgkmcnt(8)
	v_pk_add_f32 v[168:169], v[116:117], v[136:137] neg_lo:[0,1] neg_hi:[0,1]
	ds_read_b64 v[162:163], v104
	ds_read_b64 v[164:165], v105
	ds_read_b64 v[166:167], v111
	s_waitcnt lgkmcnt(7)
	v_pk_mul_f32 v[170:171], v[168:169], v[152:153] op_sel:[1,1] op_sel_hi:[1,0]
	v_pk_add_f32 v[116:117], v[116:117], v[136:137]
	v_pk_fma_f32 v[172:173], v[168:169], v[152:153], v[170:171] op_sel_hi:[0,1,1] neg_lo:[0,0,1]
	v_pk_add_f32 v[168:169], v[124:125], v[144:145] neg_lo:[0,1] neg_hi:[0,1]
	v_pk_add_f32 v[124:125], v[124:125], v[144:145]
	v_pk_mul_f32 v[170:171], v[168:169], v[152:153] op_sel:[1,0] op_sel_hi:[0,0]
	v_pk_fma_f32 v[174:175], v[168:169], v[152:153], v[170:171] op_sel:[0,1,0] neg_hi:[0,0,1]
	v_pk_add_f32 v[136:137], v[116:117], v[124:125]
	v_pk_add_f32 v[152:153], v[172:173], v[174:175] neg_lo:[0,1] neg_hi:[0,1]
	s_waitcnt lgkmcnt(0)
	v_xor_b32_e32 v135, 0x80000000, v166
	v_pk_mul_f32 v[168:169], v[158:159], v[152:153] op_sel:[1,1] op_sel_hi:[0,1]
	v_pk_fma_f32 v[170:171], v[158:159], v[152:153], v[168:169] op_sel_hi:[1,0,1] neg_lo:[0,0,1]
	v_pk_add_f32 v[116:117], v[116:117], v[124:125] neg_lo:[0,1] neg_hi:[0,1]
	v_pk_add_f32 v[152:153], v[120:121], v[140:141] neg_lo:[0,1] neg_hi:[0,1]
	v_pk_add_f32 v[120:121], v[120:121], v[140:141]
	v_pk_mul_f32 v[168:169], v[152:153], v[154:155] op_sel:[1,1] op_sel_hi:[1,0]
	v_pk_mul_f32 v[124:125], v[116:117], v[158:159] op_sel:[1,1] op_sel_hi:[1,0]
	v_pk_fma_f32 v[176:177], v[152:153], v[154:155], v[168:169] op_sel_hi:[0,1,1] neg_lo:[0,0,1]
	v_pk_add_f32 v[152:153], v[128:129], v[148:149] neg_lo:[0,1] neg_hi:[0,1]
	v_pk_add_f32 v[128:129], v[128:129], v[148:149]
	v_pk_mul_f32 v[168:169], v[152:153], v[154:155] op_sel:[1,0] op_sel_hi:[0,0]
	v_pk_fma_f32 v[178:179], v[152:153], v[154:155], v[168:169] op_sel:[0,1,0] neg_hi:[0,0,1]
	v_pk_add_f32 v[140:141], v[120:121], v[128:129]
	v_pk_add_f32 v[152:153], v[176:177], v[178:179] neg_lo:[0,1] neg_hi:[0,1]
	v_pk_add_f32 v[144:145], v[136:137], v[140:141]
	v_pk_mul_f32 v[154:155], v[158:159], v[152:153] op_sel_hi:[0,1]
	v_pk_fma_f32 v[168:169], v[158:159], v[152:153], v[154:155] op_sel:[1,0,1] op_sel_hi:[1,1,0] neg_hi:[0,0,1]
	v_pk_add_f32 v[136:137], v[136:137], v[140:141] neg_lo:[0,1] neg_hi:[0,1]
	v_pk_add_f32 v[152:153], v[170:171], v[168:169] neg_lo:[0,1] neg_hi:[0,1]
	v_pk_mul_f32 v[140:141], v[136:137], v[164:165] op_sel:[1,1] op_sel_hi:[1,0]
	v_pk_mul_f32 v[154:155], v[164:165], v[152:153] op_sel:[1,1] op_sel_hi:[0,1]
	v_pk_fma_f32 v[182:183], v[164:165], v[152:153], v[154:155] op_sel_hi:[1,0,1] neg_lo:[0,0,1]
	s_nop 0
	v_pk_add_f32 v[152:153], v[118:119], v[138:139] neg_lo:[0,1] neg_hi:[0,1]
; template <int R, class XT, class TWT>
; __device__ __forceinline__ void dif_task(XT X, TWT tw, int s, int task) {
;     const int lgM = 13 - s, lgq = lgM - R, q = 1 << lgq;
;     const int j0 = task & (q - 1), blk = task >> lgq, base = (blk << lgM) + j0;
;     const int pb = PADI(base), qp = (q >= 32) ? q + (q >> 4) : q;
;     f32x2v v[1 << R];
; #pragma unroll
;     for (int k = 0; k < (1 << R); ++k) v[k] = X[pb + k * qp];
; #pragma unroll
;     for (int r = 0; r < R; ++r) {
;         const int pb = R - 1 - r;
; #pragma unroll
;         for (int k = 0; k < (1 << R); ++k) if (!((k >> pb) & 1)) {
;             const int klo = k & ((1 << pb) - 1);
;             const f32x2v w = tw[(j0 + (klo << lgq)) << (s + r)];
;             const f32x2v a = v[k], b = v[k + (1 << pb)], d = a - b;
;             v[k] = a + b; v[k + (1 << pb)] = (f32x2v){d.x * w.x - d.y * w.y, d.x * w.y + d.y * w.x};
;         }
;     }
; #pragma unroll
;     for (int k = 0; k < (1 << R); ++k) X[pb + k * qp] = v[k];
; }
	v_pk_add_f32 v[118:119], v[118:119], v[138:139]
	v_pk_mul_f32 v[154:155], v[152:153], v[132:133] op_sel:[1,1] op_sel_hi:[1,0]
	s_nop 0
	v_pk_fma_f32 v[184:185], v[152:153], v[132:133], v[154:155] op_sel_hi:[0,1,1] neg_lo:[0,0,1]
	v_pk_add_f32 v[152:153], v[126:127], v[146:147] neg_lo:[0,1] neg_hi:[0,1]
	v_pk_add_f32 v[126:127], v[126:127], v[146:147]
	v_pk_mul_f32 v[154:155], v[152:153], v[132:133] op_sel:[1,0] op_sel_hi:[0,0]
	v_pk_fma_f32 v[186:187], v[152:153], v[132:133], v[154:155] op_sel:[0,1,0] neg_hi:[0,0,1]
	v_pk_add_f32 v[138:139], v[118:119], v[126:127]
	v_pk_add_f32 v[132:133], v[184:185], v[186:187] neg_lo:[0,1] neg_hi:[0,1]
	v_pk_add_f32 v[118:119], v[118:119], v[126:127] neg_lo:[0,1] neg_hi:[0,1]
	v_pk_mul_f32 v[152:153], v[162:163], v[132:133] op_sel:[1,1] op_sel_hi:[0,1]
	v_pk_fma_f32 v[154:155], v[162:163], v[132:133], v[152:153] op_sel_hi:[1,0,1] neg_lo:[0,0,1]
	s_nop 0
	v_pk_add_f32 v[132:133], v[122:123], v[142:143] neg_lo:[0,1] neg_hi:[0,1]
	v_pk_add_f32 v[122:123], v[122:123], v[142:143]
	v_pk_mul_f32 v[152:153], v[132:133], v[156:157] op_sel:[1,1] op_sel_hi:[1,0]
	s_nop 0
	v_pk_fma_f32 v[188:189], v[132:133], v[156:157], v[152:153] op_sel_hi:[0,1,1] neg_lo:[0,0,1]
	v_pk_add_f32 v[132:133], v[130:131], v[150:151] neg_lo:[0,1] neg_hi:[0,1]
	v_pk_add_f32 v[130:131], v[130:131], v[150:151]
	v_pk_mul_f32 v[152:153], v[132:133], v[156:157] op_sel:[1,0] op_sel_hi:[0,0]
	v_pk_fma_f32 v[190:191], v[132:133], v[156:157], v[152:153] op_sel:[0,1,0] neg_hi:[0,0,1]
	v_pk_add_f32 v[142:143], v[122:123], v[130:131]
	v_pk_add_f32 v[132:133], v[188:189], v[190:191] neg_lo:[0,1] neg_hi:[0,1]
	v_pk_add_f32 v[146:147], v[138:139], v[142:143]
	v_pk_mul_f32 v[152:153], v[160:161], v[132:133] op_sel_hi:[0,1]
	v_pk_fma_f32 v[156:157], v[160:161], v[132:133], v[152:153] op_sel:[1,0,1] op_sel_hi:[1,1,0] neg_hi:[0,0,1]
	v_pk_add_f32 v[148:149], v[144:145], v[146:147]
	v_pk_add_f32 v[132:133], v[154:155], v[156:157] neg_lo:[0,1] neg_hi:[0,1]
	v_pk_add_f32 v[144:145], v[144:145], v[146:147] neg_lo:[0,1] neg_hi:[0,1]
	v_pk_mul_f32 v[152:153], v[164:165], v[132:133] op_sel_hi:[0,1]
	v_pk_fma_f32 v[192:193], v[164:165], v[132:133], v[152:153] op_sel:[1,0,1] op_sel_hi:[1,1,0]
	v_pk_fma_f32 v[132:133], v[164:165], v[132:133], v[152:153] op_sel:[1,0,1] op_sel_hi:[1,1,0] neg_lo:[0,0,1] neg_hi:[0,0,1]
	v_cndmask_b32_e64 v153, v135, v167, s[42:43]
	v_cndmask_b32_e64 v152, v167, v166, s[42:43]
	v_pk_mul_f32 v[146:147], v[144:145], v[152:153] op_sel:[1,1] op_sel_hi:[1,0]
	v_mov_b32_e32 v193, v133
	v_pk_fma_f32 v[150:151], v[144:145], v[152:153], v[146:147] op_sel_hi:[0,1,1] neg_lo:[0,0,1]
	v_pk_fma_f32 v[144:145], v[136:137], v[164:165], v[140:141] op_sel_hi:[0,1,1] neg_lo:[0,0,1]
	v_pk_add_f32 v[136:137], v[138:139], v[142:143] neg_lo:[0,1] neg_hi:[0,1]
	v_pk_add_f32 v[132:133], v[182:183], v[192:193] neg_lo:[0,1] neg_hi:[0,1]
	v_pk_mul_f32 v[138:139], v[136:137], v[164:165] op_sel_hi:[1,0]
	s_nop 0
	v_pk_fma_f32 v[140:141], v[136:137], v[164:165], v[138:139] op_sel:[0,1,1] op_sel_hi:[1,1,0] neg_hi:[0,0,1]
	s_nop 0
	v_pk_add_f32 v[138:139], v[144:145], v[140:141] neg_lo:[0,1] neg_hi:[0,1]
	v_pk_add_f32 v[136:137], v[144:145], v[140:141]
	v_pk_mul_f32 v[140:141], v[152:153], v[138:139] op_sel:[1,1] op_sel_hi:[0,1]
	v_pk_fma_f32 v[142:143], v[152:153], v[138:139], v[140:141] op_sel_hi:[1,0,1] neg_lo:[0,0,1]
	s_nop 0
	v_pk_fma_f32 v[138:139], v[116:117], v[158:159], v[124:125] op_sel_hi:[0,1,1] neg_lo:[0,0,1]
	v_pk_add_f32 v[116:117], v[120:121], v[128:129] neg_lo:[0,1] neg_hi:[0,1]
	s_nop 0
	v_pk_mul_f32 v[120:121], v[116:117], v[158:159] op_sel_hi:[1,0]
	s_nop 0
	v_pk_fma_f32 v[124:125], v[116:117], v[158:159], v[120:121] op_sel:[0,1,1] op_sel_hi:[1,1,0]
	v_pk_fma_f32 v[116:117], v[116:117], v[158:159], v[120:121] op_sel:[0,1,1] op_sel_hi:[1,1,0] neg_lo:[0,0,1] neg_hi:[0,0,1]
	v_pk_mul_f32 v[120:121], v[118:119], v[162:163] op_sel:[1,1] op_sel_hi:[1,0]
	v_mov_b32_e32 v125, v117
	v_pk_fma_f32 v[126:127], v[118:119], v[162:163], v[120:121] op_sel_hi:[0,1,1] neg_lo:[0,0,1]
	v_pk_add_f32 v[118:119], v[122:123], v[130:131] neg_lo:[0,1] neg_hi:[0,1]
	v_pk_add_f32 v[116:117], v[138:139], v[124:125]
	v_pk_mul_f32 v[120:121], v[118:119], v[160:161] op_sel_hi:[1,0]
	v_pk_add_f32 v[130:131], v[184:185], v[186:187]
	v_pk_fma_f32 v[122:123], v[118:119], v[160:161], v[120:121] op_sel:[0,1,1] op_sel_hi:[1,1,0] neg_hi:[0,0,1]
	s_nop 0
	v_pk_add_f32 v[118:119], v[126:127], v[122:123]
	s_nop 0
	v_pk_add_f32 v[120:121], v[116:117], v[118:119]
	v_pk_add_f32 v[116:117], v[116:117], v[118:119] neg_lo:[0,1] neg_hi:[0,1]
	s_nop 0
	v_pk_mul_f32 v[118:119], v[152:153], v[116:117] op_sel:[1,1] op_sel_hi:[0,1]
	v_pk_fma_f32 v[128:129], v[152:153], v[116:117], v[118:119] op_sel_hi:[1,0,1] neg_lo:[0,0,1]
	s_nop 0
	v_pk_add_f32 v[116:117], v[138:139], v[124:125] neg_lo:[0,1] neg_hi:[0,1]
	v_pk_add_f32 v[138:139], v[188:189], v[190:191]
	v_pk_mul_f32 v[118:119], v[164:165], v[116:117] op_sel:[1,1] op_sel_hi:[0,1]
	v_pk_fma_f32 v[124:125], v[164:165], v[116:117], v[118:119] op_sel_hi:[1,0,1] neg_lo:[0,0,1]
	v_pk_add_f32 v[140:141], v[130:131], v[138:139]
	v_pk_add_f32 v[116:117], v[126:127], v[122:123] neg_lo:[0,1] neg_hi:[0,1]
	s_nop 0
	v_pk_mul_f32 v[118:119], v[164:165], v[116:117] op_sel_hi:[0,1]
	v_pk_fma_f32 v[122:123], v[164:165], v[116:117], v[118:119] op_sel:[1,0,1] op_sel_hi:[1,1,0] neg_hi:[0,0,1]
	s_nop 0
	v_pk_add_f32 v[118:119], v[124:125], v[122:123] neg_lo:[0,1] neg_hi:[0,1]
	v_pk_add_f32 v[116:117], v[124:125], v[122:123]
	v_pk_mul_f32 v[122:123], v[152:153], v[118:119] op_sel:[1,1] op_sel_hi:[0,1]
	v_pk_fma_f32 v[124:125], v[152:153], v[118:119], v[122:123] neg_lo:[0,0,1] neg_hi:[0,0,1]
; __device__ __forceinline__ void lds_barrier() { asm volatile("s_waitcnt lgkmcnt(0)" ::: "memory"); __builtin_amdgcn_s_barrier(); asm volatile("" ::: "memory"); }
; template <int R, class XT, class TWT>
; __device__ __forceinline__ void dif_task(XT X, TWT tw, int s, int task) {
;     const int lgM = 13 - s, lgq = lgM - R, q = 1 << lgq;
;     const int j0 = task & (q - 1), blk = task >> lgq, base = (blk << lgM) + j0;
;     const int pb = PADI(base), qp = (q >= 32) ? q + (q >> 4) : q;
;     f32x2v v[1 << R];
; #pragma unroll
;     for (int k = 0; k < (1 << R); ++k) v[k] = X[pb + k * qp];
; #pragma unroll
;     for (int r = 0; r < R; ++r) {
;         const int pb = R - 1 - r;
; #pragma unroll
;         for (int k = 0; k < (1 << R); ++k) if (!((k >> pb) & 1)) {
;             const int klo = k & ((1 << pb) - 1);
;             const f32x2v w = tw[(j0 + (klo << lgq)) << (s + r)];
;             const f32x2v a = v[k], b = v[k + (1 << pb)], d = a - b;
;             v[k] = a + b; v[k + (1 << pb)] = (f32x2v){d.x * w.x - d.y * w.y, d.x * w.y + d.y * w.x};
;         }
;     }
; #pragma unroll
;     for (int k = 0; k < (1 << R); ++k) X[pb + k * qp] = v[k];
; }
; template <bool LAT>
; __device__ __forceinline__ void hyconv_unit(const Frame& F, LAS f32x2v* X, const TwHalf tw, LAS bf16* OUT, const float* skip, bf16* MIX, int u) {
;     ...
;             for (int r = 0; r < 8; ++r) { const int e = 2 * (F.tid + 512 * r);
;                 const f32x2v a = X[PADI(e)], b = X[PADI(e + 1)]; const f32x4 k = kq[r];
;                 const f32x2v p = a + b, q = a - b; const f32x2v pk = (f32x2v){p.x * k.x - p.y * k.y, p.x * k.y + p.y * k.x}, qk = (f32x2v){q.x * k.z - q.y * k.w, q.x * k.w + q.y * k.z};
;                 X[PADI(e)] = pk + qk; X[PADI(e + 1)] = pk - qk; }
;             lds_barrier();
	v_pk_fma_f32 v[118:119], v[152:153], v[118:119], v[122:123] op_sel_hi:[1,0,1]
	v_pk_add_f32 v[122:123], v[176:177], v[178:179]
	v_mov_b32_e32 v125, v119
	v_pk_add_f32 v[118:119], v[172:173], v[174:175]
	s_nop 0
	v_pk_add_f32 v[126:127], v[118:119], v[122:123]
	v_pk_add_f32 v[118:119], v[118:119], v[122:123] neg_lo:[0,1] neg_hi:[0,1]
	v_pk_add_f32 v[144:145], v[126:127], v[140:141]
	v_pk_add_f32 v[126:127], v[126:127], v[140:141] neg_lo:[0,1] neg_hi:[0,1]
	v_pk_mul_f32 v[122:123], v[164:165], v[118:119] op_sel:[1,1] op_sel_hi:[0,1]
	v_pk_mul_f32 v[140:141], v[126:127], v[152:153] op_sel:[1,1] op_sel_hi:[1,0]
	s_nop 0
	v_pk_fma_f32 v[146:147], v[126:127], v[152:153], v[140:141] op_sel_hi:[0,1,1] neg_lo:[0,0,1]
	v_pk_fma_f32 v[126:127], v[164:165], v[118:119], v[122:123] op_sel_hi:[1,0,1] neg_lo:[0,0,1]
	s_nop 0
	v_pk_add_f32 v[118:119], v[130:131], v[138:139] neg_lo:[0,1] neg_hi:[0,1]
	s_nop 0
	v_pk_mul_f32 v[122:123], v[164:165], v[118:119] op_sel_hi:[0,1]
	v_pk_fma_f32 v[130:131], v[164:165], v[118:119], v[122:123] op_sel:[1,0,1] op_sel_hi:[1,1,0] neg_hi:[0,0,1]
	s_nop 0
	v_pk_add_f32 v[122:123], v[126:127], v[130:131] neg_lo:[0,1] neg_hi:[0,1]
	v_pk_add_f32 v[118:119], v[126:127], v[130:131]
	v_pk_mul_f32 v[126:127], v[152:153], v[122:123] op_sel:[1,1] op_sel_hi:[0,1]
	v_pk_fma_f32 v[130:131], v[152:153], v[122:123], v[126:127] neg_lo:[0,0,1] neg_hi:[0,0,1]
	v_pk_fma_f32 v[122:123], v[152:153], v[122:123], v[126:127] op_sel_hi:[1,0,1]
	v_pk_add_f32 v[126:127], v[154:155], v[156:157]
	v_mov_b32_e32 v131, v123
	v_pk_add_f32 v[122:123], v[170:171], v[168:169]
	s_nop 0
	v_pk_add_f32 v[138:139], v[122:123], v[126:127]
	v_pk_add_f32 v[122:123], v[122:123], v[126:127] neg_lo:[0,1] neg_hi:[0,1]
	s_nop 0
	v_pk_mul_f32 v[126:127], v[152:153], v[122:123] op_sel:[1,1] op_sel_hi:[0,1]
	v_pk_fma_f32 v[140:141], v[152:153], v[122:123], v[126:127] neg_lo:[0,0,1] neg_hi:[0,0,1]
	v_pk_fma_f32 v[122:123], v[152:153], v[122:123], v[126:127] op_sel_hi:[1,0,1]
	v_pk_mul_f32 v[126:127], v[152:153], v[132:133] op_sel:[1,1] op_sel_hi:[0,1]
	v_pk_fma_f32 v[154:155], v[152:153], v[132:133], v[126:127] op_sel_hi:[1,0,1] neg_lo:[0,0,1]
	v_mov_b32_e32 v141, v123
	v_pk_add_f32 v[122:123], v[182:183], v[192:193]
	ds_write2_b64 v84, v[148:149], v[150:151] offset1:2
	ds_write2_b64 v84, v[136:137], v[142:143] offset0:4 offset1:6
	ds_write2_b64 v84, v[120:121], v[128:129] offset0:8 offset1:10
	ds_write2_b64 v84, v[116:117], v[124:125] offset0:12 offset1:14
	ds_write2_b64 v84, v[144:145], v[146:147] offset0:16 offset1:18
	ds_write2_b64 v84, v[118:119], v[130:131] offset0:20 offset1:22
	ds_write2_b64 v84, v[138:139], v[140:141] offset0:24 offset1:26
	ds_write2_b64 v84, v[122:123], v[154:155] offset0:28 offset1:30
	s_waitcnt lgkmcnt(0)
	s_barrier
	ds_read_b128 v[116:119], v33
	s_waitcnt lgkmcnt(0)
	v_pk_add_f32 v[120:121], v[116:117], v[118:119]
	v_pk_add_f32 v[116:117], v[116:117], v[118:119] neg_lo:[0,1] neg_hi:[0,1]
	s_waitcnt vmcnt(7)
	v_pk_mul_f32 v[118:119], v[28:29], v[120:121] op_sel:[1,1] op_sel_hi:[0,1]
	v_pk_fma_f32 v[122:123], v[28:29], v[120:121], v[118:119] op_sel_hi:[1,0,1] neg_lo:[0,0,1]
	s_nop 0
	v_pk_mul_f32 v[28:29], v[30:31], v[116:117] op_sel:[1,1] op_sel_hi:[0,1]
	v_pk_fma_f32 v[118:119], v[30:31], v[116:117], v[28:29] op_sel_hi:[1,0,1] neg_lo:[0,0,1]
	s_nop 0
	v_pk_add_f32 v[28:29], v[122:123], v[118:119]
	v_pk_add_f32 v[30:31], v[122:123], v[118:119] neg_lo:[0,1] neg_hi:[0,1]
	ds_write_b128 v33, v[28:31]
	ds_read_b128 v[28:31], v68 offset:8192
	s_waitcnt lgkmcnt(0)
	v_pk_add_f32 v[116:117], v[28:29], v[30:31]
	v_pk_add_f32 v[28:29], v[28:29], v[30:31] neg_lo:[0,1] neg_hi:[0,1]
	s_waitcnt vmcnt(6)
	v_pk_mul_f32 v[30:31], v[24:25], v[116:117] op_sel:[1,1] op_sel_hi:[0,1]
	v_pk_fma_f32 v[118:119], v[24:25], v[116:117], v[30:31] op_sel_hi:[1,0,1] neg_lo:[0,0,1]
	s_nop 0
	v_pk_mul_f32 v[24:25], v[26:27], v[28:29] op_sel:[1,1] op_sel_hi:[0,1]
	v_pk_fma_f32 v[30:31], v[26:27], v[28:29], v[24:25] op_sel_hi:[1,0,1] neg_lo:[0,0,1]
	s_nop 0
	v_pk_add_f32 v[24:25], v[118:119], v[30:31]
	v_pk_add_f32 v[26:27], v[118:119], v[30:31] neg_lo:[0,1] neg_hi:[0,1]
	ds_write_b128 v68, v[24:27] offset:8192
	ds_read_b128 v[24:27], v69 offset:16384
	s_waitcnt lgkmcnt(0)
	v_pk_add_f32 v[28:29], v[24:25], v[26:27]
	v_pk_add_f32 v[24:25], v[24:25], v[26:27] neg_lo:[0,1] neg_hi:[0,1]
	s_waitcnt vmcnt(5)
	v_pk_mul_f32 v[26:27], v[20:21], v[28:29] op_sel:[1,1] op_sel_hi:[0,1]
	v_pk_fma_f32 v[30:31], v[20:21], v[28:29], v[26:27] op_sel_hi:[1,0,1] neg_lo:[0,0,1]
	s_nop 0
	v_pk_mul_f32 v[20:21], v[22:23], v[24:25] op_sel:[1,1] op_sel_hi:[0,1]
	v_pk_fma_f32 v[26:27], v[22:23], v[24:25], v[20:21] op_sel_hi:[1,0,1] neg_lo:[0,0,1]
	s_nop 0
	v_pk_add_f32 v[20:21], v[30:31], v[26:27]
	v_pk_add_f32 v[22:23], v[30:31], v[26:27] neg_lo:[0,1] neg_hi:[0,1]
	ds_write_b128 v69, v[20:23] offset:16384
	ds_read_b128 v[20:23], v70 offset:24576
	s_waitcnt lgkmcnt(0)
	v_pk_add_f32 v[24:25], v[20:21], v[22:23]
	v_pk_add_f32 v[20:21], v[20:21], v[22:23] neg_lo:[0,1] neg_hi:[0,1]
	s_waitcnt vmcnt(4)
	v_pk_mul_f32 v[22:23], v[16:17], v[24:25] op_sel:[1,1] op_sel_hi:[0,1]
	v_pk_fma_f32 v[26:27], v[16:17], v[24:25], v[22:23] op_sel_hi:[1,0,1] neg_lo:[0,0,1]
	s_nop 0
	v_pk_mul_f32 v[16:17], v[18:19], v[20:21] op_sel:[1,1] op_sel_hi:[0,1]
	v_pk_fma_f32 v[22:23], v[18:19], v[20:21], v[16:17] op_sel_hi:[1,0,1] neg_lo:[0,0,1]
	s_nop 0
	v_pk_add_f32 v[16:17], v[26:27], v[22:23]
	v_pk_add_f32 v[18:19], v[26:27], v[22:23] neg_lo:[0,1] neg_hi:[0,1]
	ds_write_b128 v70, v[16:19] offset:24576
	ds_read_b128 v[16:19], v71 offset:32768
	s_waitcnt lgkmcnt(0)
; __device__ __forceinline__ void lds_barrier() { asm volatile("s_waitcnt lgkmcnt(0)" ::: "memory"); __builtin_amdgcn_s_barrier(); asm volatile("" ::: "memory"); }
; template <int R, class XT, class TWT>
; __device__ __forceinline__ void dit_task(XT X, TWT tw, int s, int task) {
;     const int lgM = 13 - s, lgq = lgM - R, q = 1 << lgq;
;     const int j0 = task & (q - 1), blk = task >> lgq, base = (blk << lgM) + j0;
;     const int pb = PADI(base), qp = (q >= 32) ? q + (q >> 4) : q;
;     f32x2v v[1 << R];
; #pragma unroll
;     for (int k = 0; k < (1 << R); ++k) v[k] = X[pb + k * qp];
; #pragma unroll
;     for (int r = R - 1; r >= 0; --r) {
;         const int pb = R - 1 - r;
; #pragma unroll
;         for (int k = 0; k < (1 << R); ++k) if (!((k >> pb) & 1)) {
;             const int klo = k & ((1 << pb) - 1);
;             const f32x2v w = tw[(j0 + (klo << lgq)) << (s + r)];
;             const f32x2v a = v[k], qv = v[k + (1 << pb)]; const f32x2v b = (f32x2v){qv.x * w.x + qv.y * w.y, qv.y * w.x - qv.x * w.y};
;             v[k] = a + b; v[k + (1 << pb)] = a - b;
;         }
;     }
; #pragma unroll
;     for (int k = 0; k < (1 << R); ++k) X[pb + k * qp] = v[k];
; }
; template <bool LAT>
; __device__ __forceinline__ void hyconv_unit(const Frame& F, LAS f32x2v* X, const TwHalf tw, LAS bf16* OUT, const float* skip, bf16* MIX, int u) {
;     ...
;             for (int r = 0; r < 8; ++r) { const int e = 2 * (F.tid + 512 * r);
;                 const f32x2v a = X[PADI(e)], b = X[PADI(e + 1)]; const f32x4 k = kq[r];
;                 const f32x2v p = a + b, q = a - b; const f32x2v pk = (f32x2v){p.x * k.x - p.y * k.y, p.x * k.y + p.y * k.x}, qk = (f32x2v){q.x * k.z - q.y * k.w, q.x * k.w + q.y * k.z};
;                 X[PADI(e)] = pk + qk; X[PADI(e + 1)] = pk - qk; }
;             lds_barrier();
;             if constexpr (LAT) {
;                 const float sk = skip[ord * 256 + c0];
;                 const bf16* g0 = H0 + (size_t)(ord * 256 + c0) * L; const bf16* g1 = H1 + (size_t)(ord * 256 + c0) * L; bf16* v0 = H0 + (size_t)(512 + c0) * L; bf16* v1 = H1 + (size_t)(512 + c0) * L;
;                 fft_inv_upper(X, tw, 13 - lgN, F.tid);
	v_pk_add_f32 v[20:21], v[16:17], v[18:19]
	v_pk_add_f32 v[16:17], v[16:17], v[18:19] neg_lo:[0,1] neg_hi:[0,1]
	s_waitcnt vmcnt(3)
	v_pk_mul_f32 v[18:19], v[12:13], v[20:21] op_sel:[1,1] op_sel_hi:[0,1]
	v_pk_fma_f32 v[22:23], v[12:13], v[20:21], v[18:19] op_sel_hi:[1,0,1] neg_lo:[0,0,1]
	s_nop 0
	v_pk_mul_f32 v[12:13], v[14:15], v[16:17] op_sel:[1,1] op_sel_hi:[0,1]
	v_pk_fma_f32 v[18:19], v[14:15], v[16:17], v[12:13] op_sel_hi:[1,0,1] neg_lo:[0,0,1]
	s_nop 0
	v_pk_add_f32 v[12:13], v[22:23], v[18:19]
	v_pk_add_f32 v[14:15], v[22:23], v[18:19] neg_lo:[0,1] neg_hi:[0,1]
	ds_write_b128 v71, v[12:15] offset:32768
	ds_read_b128 v[12:15], v72 offset:40960
	s_waitcnt lgkmcnt(0)
	v_pk_add_f32 v[16:17], v[12:13], v[14:15]
	v_pk_add_f32 v[12:13], v[12:13], v[14:15] neg_lo:[0,1] neg_hi:[0,1]
	s_waitcnt vmcnt(2)
	v_pk_mul_f32 v[14:15], v[8:9], v[16:17] op_sel:[1,1] op_sel_hi:[0,1]
	v_pk_fma_f32 v[18:19], v[8:9], v[16:17], v[14:15] op_sel_hi:[1,0,1] neg_lo:[0,0,1]
	s_nop 0
	v_pk_mul_f32 v[8:9], v[10:11], v[12:13] op_sel:[1,1] op_sel_hi:[0,1]
	v_pk_fma_f32 v[14:15], v[10:11], v[12:13], v[8:9] op_sel_hi:[1,0,1] neg_lo:[0,0,1]
	s_nop 0
	v_pk_add_f32 v[8:9], v[18:19], v[14:15]
	v_pk_add_f32 v[10:11], v[18:19], v[14:15] neg_lo:[0,1] neg_hi:[0,1]
	ds_write_b128 v72, v[8:11] offset:40960
	ds_read_b128 v[8:11], v73 offset:49152
	s_waitcnt lgkmcnt(0)
	v_pk_add_f32 v[12:13], v[8:9], v[10:11]
	v_pk_add_f32 v[8:9], v[8:9], v[10:11] neg_lo:[0,1] neg_hi:[0,1]
	s_waitcnt vmcnt(1)
	v_pk_mul_f32 v[10:11], v[4:5], v[12:13] op_sel:[1,1] op_sel_hi:[0,1]
	v_pk_fma_f32 v[14:15], v[4:5], v[12:13], v[10:11] op_sel_hi:[1,0,1] neg_lo:[0,0,1]
	s_nop 0
	v_pk_mul_f32 v[4:5], v[6:7], v[8:9] op_sel:[1,1] op_sel_hi:[0,1]
	v_pk_fma_f32 v[10:11], v[6:7], v[8:9], v[4:5] op_sel_hi:[1,0,1] neg_lo:[0,0,1]
	s_nop 0
	v_pk_add_f32 v[4:5], v[14:15], v[10:11]
	v_pk_add_f32 v[6:7], v[14:15], v[10:11] neg_lo:[0,1] neg_hi:[0,1]
	ds_write_b128 v73, v[4:7] offset:49152
	ds_read_b128 v[4:7], v74 offset:57344
	s_waitcnt lgkmcnt(0)
	v_pk_add_f32 v[8:9], v[4:5], v[6:7]
	v_pk_add_f32 v[4:5], v[4:5], v[6:7] neg_lo:[0,1] neg_hi:[0,1]
	s_waitcnt vmcnt(0)
	v_pk_mul_f32 v[6:7], v[0:1], v[8:9] op_sel:[1,1] op_sel_hi:[0,1]
	v_pk_fma_f32 v[10:11], v[0:1], v[8:9], v[6:7] op_sel_hi:[1,0,1] neg_lo:[0,0,1]
	s_nop 0
	v_pk_mul_f32 v[0:1], v[2:3], v[4:5] op_sel:[1,1] op_sel_hi:[0,1]
	v_pk_fma_f32 v[6:7], v[2:3], v[4:5], v[0:1] op_sel_hi:[1,0,1] neg_lo:[0,0,1]
	s_nop 0
	v_pk_add_f32 v[0:1], v[10:11], v[6:7]
	v_pk_add_f32 v[2:3], v[10:11], v[6:7] neg_lo:[0,1] neg_hi:[0,1]
	ds_write_b128 v74, v[0:3] offset:57344
	s_waitcnt lgkmcnt(0)
	s_barrier
	global_load_dword v4, v181, s[0:1]
	ds_read2_b64 v[0:3], v84 offset1:2
	ds_read2_b64 v[6:9], v84 offset0:4 offset1:6
	ds_read2_b64 v[10:13], v84 offset0:8 offset1:10
	ds_read2_b64 v[14:17], v84 offset0:12 offset1:14
	ds_read2_b64 v[18:21], v84 offset0:16 offset1:18
	ds_read2_b64 v[22:25], v84 offset0:20 offset1:22
	ds_read2_b64 v[26:29], v84 offset0:24 offset1:26
	ds_read2_b64 v[116:119], v84 offset0:28 offset1:30
	ds_read_b64 v[30:31], v111
	ds_read_b64 v[124:125], v105
	ds_read_b64 v[126:127], v104
	ds_read2st64_b64 v[120:123], v100 offset1:16
	ds_read_b64 v[128:129], v103
	ds_read_b64 v[130:131], v85
	ds_read_b64 v[132:133], v101
	ds_read_b64 v[136:137], v102
	s_waitcnt lgkmcnt(7)
	v_xor_b32_e32 v5, 0x80000000, v30
	v_cndmask_b32_e64 v139, v5, v31, s[42:43]
	v_cndmask_b32_e64 v138, v31, v30, s[42:43]
	v_mov_b32_e32 v30, v139
	v_pk_mul_f32 v[140:141], v[2:3], v[30:31] op_sel_hi:[1,0]
	s_add_u32 s0, s24, s2
	v_pk_fma_f32 v[142:143], v[2:3], v[138:139], v[140:141] op_sel:[0,0,1] op_sel_hi:[1,1,0]
	v_pk_fma_f32 v[2:3], v[2:3], v[138:139], v[140:141] op_sel:[0,0,1] op_sel_hi:[1,0,0] neg_lo:[0,0,1] neg_hi:[0,0,1]
	v_pk_mul_f32 v[140:141], v[8:9], v[30:31] op_sel_hi:[1,0]
	v_mov_b32_e32 v143, v3
	v_pk_fma_f32 v[144:145], v[8:9], v[138:139], v[140:141] op_sel:[0,0,1] op_sel_hi:[1,0,0] neg_hi:[0,0,1]
	v_pk_add_f32 v[2:3], v[0:1], v[142:143]
	v_pk_add_f32 v[8:9], v[6:7], v[144:145]
	v_pk_add_f32 v[6:7], v[6:7], v[144:145] neg_lo:[0,1] neg_hi:[0,1]
	s_waitcnt lgkmcnt(6)
	v_pk_mul_f32 v[140:141], v[124:125], v[8:9] op_sel:[1,0]
	v_pk_add_f32 v[0:1], v[0:1], v[142:143] neg_lo:[0,1] neg_hi:[0,1]
	v_pk_fma_f32 v[146:147], v[124:125], v[8:9], v[140:141] op_sel:[0,0,1] op_sel_hi:[1,1,0]
	v_pk_fma_f32 v[8:9], v[124:125], v[8:9], v[140:141] op_sel:[0,0,1] op_sel_hi:[0,1,0] neg_lo:[0,0,1] neg_hi:[0,0,1]
	v_pk_mul_f32 v[140:141], v[12:13], v[30:31] op_sel_hi:[1,0]
	v_mov_b32_e32 v147, v9
	v_pk_fma_f32 v[148:149], v[12:13], v[138:139], v[140:141] op_sel:[0,0,1] op_sel_hi:[1,1,0]
	v_pk_fma_f32 v[12:13], v[12:13], v[138:139], v[140:141] op_sel:[0,0,1] op_sel_hi:[1,0,0] neg_lo:[0,0,1] neg_hi:[0,0,1]
	v_pk_mul_f32 v[140:141], v[16:17], v[30:31] op_sel_hi:[1,0]
	v_mov_b32_e32 v149, v13
	v_pk_fma_f32 v[150:151], v[16:17], v[138:139], v[140:141] op_sel:[0,0,1] op_sel_hi:[1,0,0] neg_hi:[0,0,1]
	v_pk_add_f32 v[12:13], v[10:11], v[148:149]
	v_pk_add_f32 v[16:17], v[14:15], v[150:151]
	v_pk_add_f32 v[14:15], v[14:15], v[150:151] neg_lo:[0,1] neg_hi:[0,1]
	v_pk_mul_f32 v[140:141], v[124:125], v[16:17] op_sel:[1,0]
	v_pk_add_f32 v[10:11], v[10:11], v[148:149] neg_lo:[0,1] neg_hi:[0,1]
	v_pk_fma_f32 v[152:153], v[124:125], v[16:17], v[140:141] op_sel:[0,0,1] op_sel_hi:[0,1,0] neg_hi:[0,0,1]
	s_nop 0
	v_pk_add_f32 v[16:17], v[12:13], v[152:153]
	v_pk_add_f32 v[12:13], v[12:13], v[152:153] neg_lo:[0,1] neg_hi:[0,1]
	s_waitcnt lgkmcnt(3)
; template <int R, class XT, class TWT>
; __device__ __forceinline__ void dit_task(XT X, TWT tw, int s, int task) {
;     const int lgM = 13 - s, lgq = lgM - R, q = 1 << lgq;
;     const int j0 = task & (q - 1), blk = task >> lgq, base = (blk << lgM) + j0;
;     const int pb = PADI(base), qp = (q >= 32) ? q + (q >> 4) : q;
;     f32x2v v[1 << R];
; #pragma unroll
;     for (int k = 0; k < (1 << R); ++k) v[k] = X[pb + k * qp];
; #pragma unroll
;     for (int r = R - 1; r >= 0; --r) {
;         const int pb = R - 1 - r;
; #pragma unroll
;         for (int k = 0; k < (1 << R); ++k) if (!((k >> pb) & 1)) {
;             const int klo = k & ((1 << pb) - 1);
;             const f32x2v w = tw[(j0 + (klo << lgq)) << (s + r)];
;             const f32x2v a = v[k], qv = v[k + (1 << pb)]; const f32x2v b = (f32x2v){qv.x * w.x + qv.y * w.y, qv.y * w.x - qv.x * w.y};
;             v[k] = a + b; v[k + (1 << pb)] = a - b;
;         }
;     }
; #pragma unroll
;     for (int k = 0; k < (1 << R); ++k) X[pb + k * qp] = v[k];
; }
	v_pk_mul_f32 v[140:141], v[128:129], v[16:17] op_sel:[1,0]
	v_pk_add_f32 v[8:9], v[2:3], v[146:147]
	v_pk_fma_f32 v[154:155], v[128:129], v[16:17], v[140:141] op_sel:[0,0,1] op_sel_hi:[1,1,0]
	v_pk_fma_f32 v[16:17], v[128:129], v[16:17], v[140:141] op_sel:[0,0,1] op_sel_hi:[0,1,0] neg_lo:[0,0,1] neg_hi:[0,0,1]
	v_pk_mul_f32 v[140:141], v[20:21], v[30:31] op_sel_hi:[1,0]
	v_pk_add_f32 v[2:3], v[2:3], v[146:147] neg_lo:[0,1] neg_hi:[0,1]
	v_pk_fma_f32 v[156:157], v[20:21], v[138:139], v[140:141] op_sel:[0,0,1] op_sel_hi:[1,1,0]
	v_pk_fma_f32 v[20:21], v[20:21], v[138:139], v[140:141] op_sel:[0,0,1] op_sel_hi:[1,0,0] neg_lo:[0,0,1] neg_hi:[0,0,1]
	v_pk_mul_f32 v[140:141], v[24:25], v[30:31] op_sel_hi:[1,0]
	v_mov_b32_e32 v157, v21
	v_pk_fma_f32 v[158:159], v[24:25], v[138:139], v[140:141] op_sel:[0,0,1] op_sel_hi:[1,0,0] neg_hi:[0,0,1]
	v_pk_add_f32 v[20:21], v[18:19], v[156:157]
	v_pk_add_f32 v[24:25], v[22:23], v[158:159]
	v_pk_add_f32 v[22:23], v[22:23], v[158:159] neg_lo:[0,1] neg_hi:[0,1]
	v_pk_mul_f32 v[140:141], v[124:125], v[24:25] op_sel:[1,0]
	v_pk_add_f32 v[18:19], v[18:19], v[156:157] neg_lo:[0,1] neg_hi:[0,1]
	v_pk_fma_f32 v[160:161], v[124:125], v[24:25], v[140:141] op_sel:[0,0,1] op_sel_hi:[1,1,0]
	v_pk_fma_f32 v[24:25], v[124:125], v[24:25], v[140:141] op_sel:[0,0,1] op_sel_hi:[0,1,0] neg_lo:[0,0,1] neg_hi:[0,0,1]
	v_pk_mul_f32 v[140:141], v[28:29], v[30:31] op_sel_hi:[1,0]
	v_pk_mul_f32 v[30:31], v[118:119], v[30:31] op_sel_hi:[1,0]
	v_pk_fma_f32 v[162:163], v[28:29], v[138:139], v[140:141] op_sel:[0,0,1] op_sel_hi:[1,1,0]
	v_pk_fma_f32 v[28:29], v[28:29], v[138:139], v[140:141] op_sel:[0,0,1] op_sel_hi:[1,0,0] neg_lo:[0,0,1] neg_hi:[0,0,1]
	v_pk_fma_f32 v[140:141], v[118:119], v[138:139], v[30:31] op_sel:[0,0,1] op_sel_hi:[1,0,0] neg_hi:[0,0,1]
	v_mov_b32_e32 v163, v29
	v_pk_add_f32 v[30:31], v[116:117], v[140:141]
	v_pk_add_f32 v[28:29], v[26:27], v[162:163]
	v_pk_mul_f32 v[118:119], v[124:125], v[30:31] op_sel:[1,0]
	v_mov_b32_e32 v161, v25
	v_pk_fma_f32 v[138:139], v[124:125], v[30:31], v[118:119] op_sel:[0,0,1] op_sel_hi:[0,1,0] neg_hi:[0,0,1]
	s_nop 0
	v_pk_add_f32 v[30:31], v[28:29], v[138:139]
	v_pk_add_f32 v[24:25], v[20:21], v[160:161]
	v_pk_mul_f32 v[118:119], v[128:129], v[30:31] op_sel:[1,0]
	v_pk_add_f32 v[116:117], v[116:117], v[140:141] neg_lo:[0,1] neg_hi:[0,1]
	v_pk_fma_f32 v[164:165], v[128:129], v[30:31], v[118:119] op_sel:[0,0,1] op_sel_hi:[0,1,0] neg_hi:[0,0,1]
	s_nop 0
	v_pk_add_f32 v[30:31], v[24:25], v[164:165]
	v_pk_add_f32 v[26:27], v[26:27], v[162:163] neg_lo:[0,1] neg_hi:[0,1]
	v_pk_mul_f32 v[118:119], v[120:121], v[30:31] op_sel:[1,0]
	v_pk_add_f32 v[28:29], v[28:29], v[138:139] neg_lo:[0,1] neg_hi:[0,1]
	v_pk_fma_f32 v[166:167], v[120:121], v[30:31], v[118:119] op_sel:[0,0,1] op_sel_hi:[1,1,0]
	v_pk_fma_f32 v[30:31], v[120:121], v[30:31], v[118:119] op_sel:[0,0,1] op_sel_hi:[0,1,0] neg_lo:[0,0,1] neg_hi:[0,0,1]
	v_pk_mul_f32 v[118:119], v[124:125], v[6:7] op_sel_hi:[0,1]
	v_pk_fma_f32 v[142:143], v[124:125], v[6:7], v[118:119] op_sel:[1,0,1] op_sel_hi:[1,1,0] neg_lo:[0,0,1] neg_hi:[0,0,1]
	v_pk_fma_f32 v[6:7], v[124:125], v[6:7], v[118:119] op_sel:[1,0,1] op_sel_hi:[1,1,0]
	v_pk_mul_f32 v[118:119], v[124:125], v[14:15] op_sel_hi:[0,1]
	v_pk_fma_f32 v[144:145], v[124:125], v[14:15], v[118:119] op_sel:[1,0,1] op_sel_hi:[1,1,0] neg_lo:[0,0,1]
	v_mov_b32_e32 v143, v7
	v_pk_add_f32 v[14:15], v[10:11], v[144:145]
	v_pk_add_f32 v[6:7], v[0:1], v[142:143]
	v_pk_mul_f32 v[118:119], v[126:127], v[14:15] op_sel:[1,0]
	v_pk_add_f32 v[20:21], v[20:21], v[160:161] neg_lo:[0,1] neg_hi:[0,1]
	v_pk_fma_f32 v[148:149], v[126:127], v[14:15], v[118:119] op_sel:[0,0,1] op_sel_hi:[1,1,0]
	v_pk_fma_f32 v[14:15], v[126:127], v[14:15], v[118:119] op_sel:[0,0,1] op_sel_hi:[0,1,0] neg_lo:[0,0,1] neg_hi:[0,0,1]
	v_pk_mul_f32 v[118:119], v[124:125], v[22:23] op_sel_hi:[0,1]
	v_pk_fma_f32 v[150:151], v[124:125], v[22:23], v[118:119] op_sel:[1,0,1] op_sel_hi:[1,1,0] neg_lo:[0,0,1] neg_hi:[0,0,1]
	v_pk_fma_f32 v[22:23], v[124:125], v[22:23], v[118:119] op_sel:[1,0,1] op_sel_hi:[1,1,0]
	v_pk_mul_f32 v[118:119], v[124:125], v[116:117] op_sel_hi:[0,1]
	v_pk_fma_f32 v[140:141], v[124:125], v[116:117], v[118:119] op_sel:[1,0,1] op_sel_hi:[1,1,0] neg_lo:[0,0,1]
	v_mov_b32_e32 v151, v23
	v_pk_add_f32 v[116:117], v[26:27], v[140:141]
	v_pk_add_f32 v[22:23], v[18:19], v[150:151]
	v_pk_mul_f32 v[118:119], v[126:127], v[116:117] op_sel:[1,0]
	v_mov_b32_e32 v149, v15
	v_pk_fma_f32 v[124:125], v[126:127], v[116:117], v[118:119] op_sel:[0,0,1] op_sel_hi:[0,1,0] neg_hi:[0,0,1]
	s_nop 0
	v_pk_add_f32 v[116:117], v[22:23], v[124:125]
	v_pk_add_f32 v[14:15], v[6:7], v[148:149]
	s_waitcnt lgkmcnt(1)
; template <int R, class XT, class TWT>
; __device__ __forceinline__ void dit_task(XT X, TWT tw, int s, int task) {
;     const int lgM = 13 - s, lgq = lgM - R, q = 1 << lgq;
;     const int j0 = task & (q - 1), blk = task >> lgq, base = (blk << lgM) + j0;
;     const int pb = PADI(base), qp = (q >= 32) ? q + (q >> 4) : q;
;     f32x2v v[1 << R];
; #pragma unroll
;     for (int k = 0; k < (1 << R); ++k) v[k] = X[pb + k * qp];
; #pragma unroll
;     for (int r = R - 1; r >= 0; --r) {
;         const int pb = R - 1 - r;
; #pragma unroll
;         for (int k = 0; k < (1 << R); ++k) if (!((k >> pb) & 1)) {
;             const int klo = k & ((1 << pb) - 1);
;             const f32x2v w = tw[(j0 + (klo << lgq)) << (s + r)];
;             const f32x2v a = v[k], qv = v[k + (1 << pb)]; const f32x2v b = (f32x2v){qv.x * w.x + qv.y * w.y, qv.y * w.x - qv.x * w.y};
;             v[k] = a + b; v[k + (1 << pb)] = a - b;
;         }
;     }
; #pragma unroll
;     for (int k = 0; k < (1 << R); ++k) X[pb + k * qp] = v[k];
; }
	v_pk_mul_f32 v[118:119], v[132:133], v[116:117] op_sel:[1,0]
	v_pk_add_f32 v[10:11], v[10:11], v[144:145] neg_lo:[0,1] neg_hi:[0,1]
	v_pk_fma_f32 v[126:127], v[132:133], v[116:117], v[118:119] op_sel:[0,0,1] op_sel_hi:[0,1,0] neg_hi:[0,0,1]
	v_pk_mul_f32 v[118:119], v[128:129], v[12:13] op_sel_hi:[0,1]
	v_pk_add_f32 v[116:117], v[14:15], v[126:127]
	v_pk_add_f32 v[14:15], v[14:15], v[126:127] neg_lo:[0,1] neg_hi:[0,1]
	v_pk_fma_f32 v[126:127], v[128:129], v[12:13], v[118:119] op_sel:[1,0,1] op_sel_hi:[1,1,0] neg_lo:[0,0,1] neg_hi:[0,0,1]
	v_pk_fma_f32 v[12:13], v[128:129], v[12:13], v[118:119] op_sel:[1,0,1] op_sel_hi:[1,1,0]
	v_pk_mul_f32 v[118:119], v[128:129], v[28:29] op_sel_hi:[0,1]
	v_pk_fma_f32 v[138:139], v[128:129], v[28:29], v[118:119] op_sel:[1,0,1] op_sel_hi:[1,1,0] neg_lo:[0,0,1]
	v_mov_b32_e32 v127, v13
	v_pk_add_f32 v[28:29], v[20:21], v[138:139]
	v_pk_add_f32 v[12:13], v[2:3], v[126:127]
	v_pk_mul_f32 v[118:119], v[122:123], v[28:29] op_sel:[1,0]
	v_pk_add_f32 v[26:27], v[26:27], v[140:141] neg_lo:[0,1] neg_hi:[0,1]
	v_pk_fma_f32 v[128:129], v[122:123], v[28:29], v[118:119] op_sel:[0,0,1] op_sel_hi:[0,1,0] neg_hi:[0,0,1]
	v_pk_mul_f32 v[118:119], v[130:131], v[10:11] op_sel_hi:[0,1]
	v_pk_add_f32 v[28:29], v[12:13], v[128:129]
	v_pk_add_f32 v[12:13], v[12:13], v[128:129] neg_lo:[0,1] neg_hi:[0,1]
	v_pk_fma_f32 v[128:129], v[130:131], v[10:11], v[118:119] op_sel:[1,0,1] op_sel_hi:[1,1,0] neg_lo:[0,0,1] neg_hi:[0,0,1]
	v_pk_fma_f32 v[10:11], v[130:131], v[10:11], v[118:119] op_sel:[1,0,1] op_sel_hi:[1,1,0]
	v_pk_mul_f32 v[118:119], v[130:131], v[26:27] op_sel_hi:[0,1]
	v_pk_fma_f32 v[140:141], v[130:131], v[26:27], v[118:119] op_sel:[1,0,1] op_sel_hi:[1,1,0] neg_lo:[0,0,1]
	v_pk_add_f32 v[18:19], v[18:19], v[150:151] neg_lo:[0,1] neg_hi:[0,1]
	s_nop 0
	v_pk_add_f32 v[26:27], v[18:19], v[140:141]
	v_pk_add_f32 v[0:1], v[0:1], v[142:143] neg_lo:[0,1] neg_hi:[0,1]
	s_waitcnt lgkmcnt(0)
	v_pk_mul_f32 v[118:119], v[136:137], v[26:27] op_sel:[1,0]
	v_mov_b32_e32 v129, v11
	v_pk_fma_f32 v[130:131], v[136:137], v[26:27], v[118:119] op_sel:[0,0,1] op_sel_hi:[0,1,0] neg_hi:[0,0,1]
	v_pk_add_f32 v[24:25], v[24:25], v[164:165] neg_lo:[0,1] neg_hi:[0,1]
	v_pk_add_f32 v[10:11], v[0:1], v[128:129]
	v_pk_mul_f32 v[118:119], v[120:121], v[24:25] op_sel_hi:[0,1]
	v_pk_add_f32 v[22:23], v[22:23], v[124:125] neg_lo:[0,1] neg_hi:[0,1]
	v_pk_add_f32 v[26:27], v[10:11], v[130:131]
	v_pk_add_f32 v[10:11], v[10:11], v[130:131] neg_lo:[0,1] neg_hi:[0,1]
	v_pk_fma_f32 v[130:131], v[120:121], v[24:25], v[118:119] op_sel:[1,0,1] op_sel_hi:[1,1,0] neg_lo:[0,0,1] neg_hi:[0,0,1]
	v_pk_fma_f32 v[24:25], v[120:121], v[24:25], v[118:119] op_sel:[1,0,1] op_sel_hi:[1,1,0]
	v_pk_mul_f32 v[118:119], v[132:133], v[22:23] op_sel_hi:[0,1]
	v_pk_fma_f32 v[120:121], v[132:133], v[22:23], v[118:119] op_sel:[1,0,1] op_sel_hi:[1,1,0] neg_lo:[0,0,1]
	v_pk_add_f32 v[20:21], v[20:21], v[138:139] neg_lo:[0,1] neg_hi:[0,1]
	v_pk_add_f32 v[6:7], v[6:7], v[148:149] neg_lo:[0,1] neg_hi:[0,1]
	v_pk_mul_f32 v[118:119], v[122:123], v[20:21] op_sel_hi:[0,1]
	v_pk_add_f32 v[22:23], v[6:7], v[120:121]
	v_pk_add_f32 v[6:7], v[6:7], v[120:121] neg_lo:[0,1] neg_hi:[0,1]
	v_pk_fma_f32 v[120:121], v[122:123], v[20:21], v[118:119] op_sel:[1,0,1] op_sel_hi:[1,1,0] neg_lo:[0,0,1]
	v_pk_add_f32 v[18:19], v[18:19], v[140:141] neg_lo:[0,1] neg_hi:[0,1]
	v_mov_b32_e32 v155, v17
	v_pk_add_f32 v[2:3], v[2:3], v[126:127] neg_lo:[0,1] neg_hi:[0,1]
	v_pk_mul_f32 v[118:119], v[136:137], v[18:19] op_sel_hi:[0,1]
	v_pk_add_f32 v[16:17], v[8:9], v[154:155]
	v_mov_b32_e32 v167, v31
	v_pk_add_f32 v[20:21], v[2:3], v[120:121]
	v_pk_add_f32 v[2:3], v[2:3], v[120:121] neg_lo:[0,1] neg_hi:[0,1]
	v_pk_fma_f32 v[120:121], v[136:137], v[18:19], v[118:119] op_sel:[1,0,1] op_sel_hi:[1,1,0] neg_lo:[0,0,1]
	v_pk_add_f32 v[30:31], v[16:17], v[166:167]
	v_pk_add_f32 v[8:9], v[8:9], v[154:155] neg_lo:[0,1] neg_hi:[0,1]
	v_mov_b32_e32 v131, v25
	v_pk_add_f32 v[0:1], v[0:1], v[128:129] neg_lo:[0,1] neg_hi:[0,1]
	v_pk_add_f32 v[16:17], v[16:17], v[166:167] neg_lo:[0,1] neg_hi:[0,1]
	v_pk_add_f32 v[24:25], v[8:9], v[130:131]
	v_pk_add_f32 v[8:9], v[8:9], v[130:131] neg_lo:[0,1] neg_hi:[0,1]
	v_pk_add_f32 v[18:19], v[0:1], v[120:121]
	v_pk_add_f32 v[0:1], v[0:1], v[120:121] neg_lo:[0,1] neg_hi:[0,1]
	ds_write2_b64 v84, v[30:31], v[116:117] offset1:2
	ds_write2_b64 v84, v[28:29], v[26:27] offset0:4 offset1:6
	ds_write2_b64 v84, v[24:25], v[22:23] offset0:8 offset1:10
	ds_write2_b64 v84, v[20:21], v[18:19] offset0:12 offset1:14
	ds_write2_b64 v84, v[16:17], v[14:15] offset0:16 offset1:18
	ds_write2_b64 v84, v[12:13], v[10:11] offset0:20 offset1:22
	ds_write2_b64 v84, v[8:9], v[6:7] offset0:24 offset1:26
	ds_write2_b64 v84, v[2:3], v[0:1] offset0:28 offset1:30
	s_waitcnt lgkmcnt(0)
	s_barrier
; template <int R, class XT, class TWT>
; __device__ __forceinline__ void dit_task(XT X, TWT tw, int s, int task) {
;     const int lgM = 13 - s, lgq = lgM - R, q = 1 << lgq;
;     const int j0 = task & (q - 1), blk = task >> lgq, base = (blk << lgM) + j0;
;     const int pb = PADI(base), qp = (q >= 32) ? q + (q >> 4) : q;
;     f32x2v v[1 << R];
; #pragma unroll
;     for (int k = 0; k < (1 << R); ++k) v[k] = X[pb + k * qp];
; #pragma unroll
;     for (int r = R - 1; r >= 0; --r) {
;         const int pb = R - 1 - r;
; #pragma unroll
;         for (int k = 0; k < (1 << R); ++k) if (!((k >> pb) & 1)) {
;             const int klo = k & ((1 << pb) - 1);
;             const f32x2v w = tw[(j0 + (klo << lgq)) << (s + r)];
;             const f32x2v a = v[k], qv = v[k + (1 << pb)]; const f32x2v b = (f32x2v){qv.x * w.x + qv.y * w.y, qv.y * w.x - qv.x * w.y};
;             v[k] = a + b; v[k + (1 << pb)] = a - b;
;         }
;     }
; #pragma unroll
;     for (int k = 0; k < (1 << R); ++k) X[pb + k * qp] = v[k];
; }
; template <bool LAT>
; __device__ __forceinline__ void hyconv_unit(const Frame& F, LAS f32x2v* X, const TwHalf tw, LAS bf16* OUT, const float* skip, bf16* MIX, int u) {
;     ...
;                 fft_inv_upper(X, tw, 13 - lgN, F.tid);
;                 unsigned ga[4], gb[4], za[4], zb[4];
; #pragma unroll
;                 for (int r = 0; r < 4; ++r) { const int pr = F.tid + 512 * r; ga[r] = *(const unsigned*)(g0 + 2 * pr); gb[r] = *(const unsigned*)(g1 + 2 * pr); za[r] = *(const unsigned*)(v0 + 2 * pr); zb[r] = *(const unsigned*)(v1 + 2 * pr); }
	v_lshl_add_u64 v[168:169], s[24:25], 0, v[50:51]
	v_lshl_add_u64 v[168:169], s[2:3], 0, v[168:169]
	global_load_dword v182, v[168:169], off
	global_load_dword v183, v[52:53], off
	v_lshl_add_u64 v[170:171], s[26:27], 0, v[50:51]
	v_lshl_add_u64 v[170:171], s[2:3], 0, v[170:171]
	global_load_dword v184, v[170:171], off
	global_load_dword v185, v[54:55], off
	v_lshl_add_u64 v[172:173], s[24:25], 0, v[56:57]
	v_lshl_add_u64 v[172:173], s[2:3], 0, v[172:173]
	global_load_dword v186, v[172:173], off
	v_lshl_add_u64 v[174:175], s[26:27], 0, v[56:57]
	v_lshl_add_u64 v[174:175], s[2:3], 0, v[174:175]
	global_load_dword v187, v[174:175], off
	v_lshl_add_u64 v[176:177], s[24:25], 0, v[62:63]
	v_lshl_add_u64 v[176:177], s[2:3], 0, v[176:177]
	global_load_dword v188, v[176:177], off
	v_lshl_add_u64 v[178:179], s[26:27], 0, v[62:63]
	v_lshl_add_u64 v[178:179], s[2:3], 0, v[178:179]
	global_load_dword v189, v[178:179], off
	global_load_dword v190, v[170:171], off offset:2048
	global_load_dword v191, v[168:169], off offset:2048
	global_load_dword v192, v[58:59], off
	global_load_dword v193, v[60:61], off
	global_load_dword v194, v[64:65], off
	global_load_dword v195, v[66:67], off
	global_load_dword v196, v[54:55], off offset:2048
	global_load_dword v197, v[52:53], off offset:2048
	ds_read2_b64 v[0:3], v81 offset1:34
	ds_read2_b64 v[6:9], v81 offset0:68 offset1:102
	ds_read2_b64 v[10:13], v81 offset0:136 offset1:170
	ds_read2_b64 v[14:17], v81 offset0:204 offset1:238
	ds_read2_b64 v[18:21], v110 offset0:16 offset1:50
	ds_read2_b64 v[22:25], v110 offset0:84 offset1:118
	ds_read2_b64 v[26:29], v110 offset0:152 offset1:186
	ds_read2_b64 v[116:119], v110 offset0:220 offset1:254
	ds_read_b64 v[30:31], v99
	ds_read_b64 v[124:125], v97
	ds_read_b64 v[126:127], v98
	ds_read_b64 v[128:129], v83
	ds_read_b64 v[130:131], v95
	ds_read_b64 v[132:133], v96
	ds_read_b64 v[136:137], v82
	ds_read2st64_b64 v[120:123], v94 offset1:16
	s_waitcnt lgkmcnt(4)
	v_xor_b32_e32 v5, 0x80000000, v128
	v_cndmask_b32_e64 v139, v5, v129, s[40:41]
	v_cndmask_b32_e64 v138, v129, v128, s[40:41]
	v_mov_b32_e32 v128, v139
	v_pk_mul_f32 v[140:141], v[2:3], v[128:129] op_sel_hi:[1,0]
	s_addc_u32 s1, s25, s3
	v_pk_fma_f32 v[142:143], v[2:3], v[138:139], v[140:141] op_sel:[0,0,1] op_sel_hi:[1,1,0]
	v_pk_fma_f32 v[2:3], v[2:3], v[138:139], v[140:141] op_sel:[0,0,1] op_sel_hi:[1,0,0] neg_lo:[0,0,1] neg_hi:[0,0,1]
	v_pk_mul_f32 v[140:141], v[8:9], v[128:129] op_sel_hi:[1,0]
	v_mov_b32_e32 v143, v3
	v_pk_fma_f32 v[144:145], v[8:9], v[138:139], v[140:141] op_sel:[0,0,1] op_sel_hi:[1,0,0] neg_hi:[0,0,1]
	v_pk_add_f32 v[2:3], v[0:1], v[142:143]
	v_pk_add_f32 v[8:9], v[6:7], v[144:145]
	v_pk_add_f32 v[6:7], v[6:7], v[144:145] neg_lo:[0,1] neg_hi:[0,1]
	v_pk_mul_f32 v[140:141], v[30:31], v[8:9] op_sel:[1,0]
	v_pk_add_f32 v[0:1], v[0:1], v[142:143] neg_lo:[0,1] neg_hi:[0,1]
	v_pk_fma_f32 v[146:147], v[30:31], v[8:9], v[140:141] op_sel:[0,0,1] op_sel_hi:[1,1,0]
	v_pk_fma_f32 v[8:9], v[30:31], v[8:9], v[140:141] op_sel:[0,0,1] op_sel_hi:[0,1,0] neg_lo:[0,0,1] neg_hi:[0,0,1]
	v_pk_mul_f32 v[140:141], v[12:13], v[128:129] op_sel_hi:[1,0]
	v_mov_b32_e32 v147, v9
	v_pk_fma_f32 v[148:149], v[12:13], v[138:139], v[140:141] op_sel:[0,0,1] op_sel_hi:[1,1,0]
	v_pk_fma_f32 v[12:13], v[12:13], v[138:139], v[140:141] op_sel:[0,0,1] op_sel_hi:[1,0,0] neg_lo:[0,0,1] neg_hi:[0,0,1]
	v_pk_mul_f32 v[140:141], v[16:17], v[128:129] op_sel_hi:[1,0]
	v_mov_b32_e32 v149, v13
	v_pk_fma_f32 v[150:151], v[16:17], v[138:139], v[140:141] op_sel:[0,0,1] op_sel_hi:[1,0,0] neg_hi:[0,0,1]
	v_pk_add_f32 v[12:13], v[10:11], v[148:149]
	v_pk_add_f32 v[16:17], v[14:15], v[150:151]
	v_pk_add_f32 v[14:15], v[14:15], v[150:151] neg_lo:[0,1] neg_hi:[0,1]
	v_pk_mul_f32 v[140:141], v[30:31], v[16:17] op_sel:[1,0]
	v_pk_add_f32 v[10:11], v[10:11], v[148:149] neg_lo:[0,1] neg_hi:[0,1]
	v_pk_fma_f32 v[152:153], v[30:31], v[16:17], v[140:141] op_sel:[0,0,1] op_sel_hi:[0,1,0] neg_hi:[0,0,1]
	s_nop 0
	v_pk_add_f32 v[16:17], v[12:13], v[152:153]
	v_pk_add_f32 v[12:13], v[12:13], v[152:153] neg_lo:[0,1] neg_hi:[0,1]
	v_pk_mul_f32 v[140:141], v[124:125], v[16:17] op_sel:[1,0]
	v_pk_add_f32 v[8:9], v[2:3], v[146:147]
	v_pk_fma_f32 v[154:155], v[124:125], v[16:17], v[140:141] op_sel:[0,0,1] op_sel_hi:[1,1,0]
	v_pk_fma_f32 v[16:17], v[124:125], v[16:17], v[140:141] op_sel:[0,0,1] op_sel_hi:[0,1,0] neg_lo:[0,0,1] neg_hi:[0,0,1]
	v_pk_mul_f32 v[140:141], v[20:21], v[128:129] op_sel_hi:[1,0]
	v_pk_add_f32 v[2:3], v[2:3], v[146:147] neg_lo:[0,1] neg_hi:[0,1]
	v_pk_fma_f32 v[156:157], v[20:21], v[138:139], v[140:141] op_sel:[0,0,1] op_sel_hi:[1,1,0]
	v_pk_fma_f32 v[20:21], v[20:21], v[138:139], v[140:141] op_sel:[0,0,1] op_sel_hi:[1,0,0] neg_lo:[0,0,1] neg_hi:[0,0,1]
	v_pk_mul_f32 v[140:141], v[24:25], v[128:129] op_sel_hi:[1,0]
	v_mov_b32_e32 v157, v21
	v_pk_fma_f32 v[158:159], v[24:25], v[138:139], v[140:141] op_sel:[0,0,1] op_sel_hi:[1,0,0] neg_hi:[0,0,1]
	v_pk_add_f32 v[20:21], v[18:19], v[156:157]
	v_pk_add_f32 v[24:25], v[22:23], v[158:159]
	v_pk_add_f32 v[22:23], v[22:23], v[158:159] neg_lo:[0,1] neg_hi:[0,1]
	v_pk_mul_f32 v[140:141], v[30:31], v[24:25] op_sel:[1,0]
	v_pk_add_f32 v[18:19], v[18:19], v[156:157] neg_lo:[0,1] neg_hi:[0,1]
	v_pk_fma_f32 v[160:161], v[30:31], v[24:25], v[140:141] op_sel:[0,0,1] op_sel_hi:[1,1,0]
	v_pk_fma_f32 v[24:25], v[30:31], v[24:25], v[140:141] op_sel:[0,0,1] op_sel_hi:[0,1,0] neg_lo:[0,0,1] neg_hi:[0,0,1]
	v_pk_mul_f32 v[140:141], v[28:29], v[128:129] op_sel_hi:[1,0]
	v_pk_mul_f32 v[128:129], v[118:119], v[128:129] op_sel_hi:[1,0]
	v_pk_fma_f32 v[162:163], v[28:29], v[138:139], v[140:141] op_sel:[0,0,1] op_sel_hi:[1,1,0]
	v_pk_fma_f32 v[28:29], v[28:29], v[138:139], v[140:141] op_sel:[0,0,1] op_sel_hi:[1,0,0] neg_lo:[0,0,1] neg_hi:[0,0,1]
	v_pk_fma_f32 v[140:141], v[118:119], v[138:139], v[128:129] op_sel:[0,0,1] op_sel_hi:[1,0,0] neg_hi:[0,0,1]
	v_mov_b32_e32 v163, v29
	v_pk_add_f32 v[118:119], v[116:117], v[140:141]
	v_pk_add_f32 v[28:29], v[26:27], v[162:163]
	v_pk_mul_f32 v[128:129], v[30:31], v[118:119] op_sel:[1,0]
	v_mov_b32_e32 v161, v25
	v_pk_fma_f32 v[138:139], v[30:31], v[118:119], v[128:129] op_sel:[0,0,1] op_sel_hi:[0,1,0] neg_hi:[0,0,1]
	s_nop 0
	v_pk_add_f32 v[118:119], v[28:29], v[138:139]
	v_pk_add_f32 v[24:25], v[20:21], v[160:161]
	v_pk_mul_f32 v[128:129], v[124:125], v[118:119] op_sel:[1,0]
	v_pk_add_f32 v[116:117], v[116:117], v[140:141] neg_lo:[0,1] neg_hi:[0,1]
	v_pk_fma_f32 v[164:165], v[124:125], v[118:119], v[128:129] op_sel:[0,0,1] op_sel_hi:[0,1,0] neg_hi:[0,0,1]
	s_nop 0
	v_pk_add_f32 v[118:119], v[24:25], v[164:165]
	v_pk_add_f32 v[26:27], v[26:27], v[162:163] neg_lo:[0,1] neg_hi:[0,1]
	s_waitcnt lgkmcnt(0)
; template <int R, class XT, class TWT>
; __device__ __forceinline__ void dit_task(XT X, TWT tw, int s, int task) {
;     const int lgM = 13 - s, lgq = lgM - R, q = 1 << lgq;
;     const int j0 = task & (q - 1), blk = task >> lgq, base = (blk << lgM) + j0;
;     const int pb = PADI(base), qp = (q >= 32) ? q + (q >> 4) : q;
;     f32x2v v[1 << R];
; #pragma unroll
;     for (int k = 0; k < (1 << R); ++k) v[k] = X[pb + k * qp];
; #pragma unroll
;     for (int r = R - 1; r >= 0; --r) {
;         const int pb = R - 1 - r;
; #pragma unroll
;         for (int k = 0; k < (1 << R); ++k) if (!((k >> pb) & 1)) {
;             const int klo = k & ((1 << pb) - 1);
;             const f32x2v w = tw[(j0 + (klo << lgq)) << (s + r)];
;             const f32x2v a = v[k], qv = v[k + (1 << pb)]; const f32x2v b = (f32x2v){qv.x * w.x + qv.y * w.y, qv.y * w.x - qv.x * w.y};
;             v[k] = a + b; v[k + (1 << pb)] = a - b;
;         }
;     }
; #pragma unroll
;     for (int k = 0; k < (1 << R); ++k) X[pb + k * qp] = v[k];
; }
	v_pk_mul_f32 v[128:129], v[120:121], v[118:119] op_sel:[1,0]
	v_pk_add_f32 v[28:29], v[28:29], v[138:139] neg_lo:[0,1] neg_hi:[0,1]
	v_pk_fma_f32 v[166:167], v[120:121], v[118:119], v[128:129] op_sel:[0,0,1] op_sel_hi:[1,1,0]
	v_pk_fma_f32 v[118:119], v[120:121], v[118:119], v[128:129] op_sel:[0,0,1] op_sel_hi:[0,1,0] neg_lo:[0,0,1] neg_hi:[0,0,1]
	v_pk_mul_f32 v[128:129], v[30:31], v[6:7] op_sel_hi:[0,1]
	v_pk_fma_f32 v[142:143], v[30:31], v[6:7], v[128:129] op_sel:[1,0,1] op_sel_hi:[1,1,0] neg_lo:[0,0,1] neg_hi:[0,0,1]
	v_pk_fma_f32 v[6:7], v[30:31], v[6:7], v[128:129] op_sel:[1,0,1] op_sel_hi:[1,1,0]
	v_pk_mul_f32 v[128:129], v[30:31], v[14:15] op_sel_hi:[0,1]
	v_pk_fma_f32 v[144:145], v[30:31], v[14:15], v[128:129] op_sel:[1,0,1] op_sel_hi:[1,1,0] neg_lo:[0,0,1]
	v_mov_b32_e32 v143, v7
	v_pk_add_f32 v[14:15], v[10:11], v[144:145]
	v_pk_add_f32 v[6:7], v[0:1], v[142:143]
	v_pk_mul_f32 v[128:129], v[126:127], v[14:15] op_sel:[1,0]
	v_pk_add_f32 v[20:21], v[20:21], v[160:161] neg_lo:[0,1] neg_hi:[0,1]
	v_pk_fma_f32 v[148:149], v[126:127], v[14:15], v[128:129] op_sel:[0,0,1] op_sel_hi:[1,1,0]
	v_pk_fma_f32 v[14:15], v[126:127], v[14:15], v[128:129] op_sel:[0,0,1] op_sel_hi:[0,1,0] neg_lo:[0,0,1] neg_hi:[0,0,1]
	v_pk_mul_f32 v[128:129], v[30:31], v[22:23] op_sel_hi:[0,1]
	v_pk_fma_f32 v[150:151], v[30:31], v[22:23], v[128:129] op_sel:[1,0,1] op_sel_hi:[1,1,0] neg_lo:[0,0,1] neg_hi:[0,0,1]
	v_pk_fma_f32 v[22:23], v[30:31], v[22:23], v[128:129] op_sel:[1,0,1] op_sel_hi:[1,1,0]
	v_pk_mul_f32 v[128:129], v[30:31], v[116:117] op_sel_hi:[0,1]
	v_pk_fma_f32 v[140:141], v[30:31], v[116:117], v[128:129] op_sel:[1,0,1] op_sel_hi:[1,1,0] neg_lo:[0,0,1]
	v_mov_b32_e32 v151, v23
	v_pk_add_f32 v[30:31], v[26:27], v[140:141]
	v_pk_add_f32 v[22:23], v[18:19], v[150:151]
	v_pk_mul_f32 v[116:117], v[126:127], v[30:31] op_sel:[1,0]
	v_mov_b32_e32 v149, v15
	v_pk_fma_f32 v[128:129], v[126:127], v[30:31], v[116:117] op_sel:[0,0,1] op_sel_hi:[0,1,0] neg_hi:[0,0,1]
	s_nop 0
	v_pk_add_f32 v[30:31], v[22:23], v[128:129]
	v_pk_add_f32 v[14:15], v[6:7], v[148:149]
	v_pk_mul_f32 v[116:117], v[130:131], v[30:31] op_sel:[1,0]
	v_pk_add_f32 v[10:11], v[10:11], v[144:145] neg_lo:[0,1] neg_hi:[0,1]
	v_pk_fma_f32 v[126:127], v[130:131], v[30:31], v[116:117] op_sel:[0,0,1] op_sel_hi:[0,1,0] neg_hi:[0,0,1]
	v_pk_mul_f32 v[116:117], v[124:125], v[12:13] op_sel_hi:[0,1]
	v_pk_add_f32 v[30:31], v[14:15], v[126:127]
	v_pk_add_f32 v[14:15], v[14:15], v[126:127] neg_lo:[0,1] neg_hi:[0,1]
	v_pk_fma_f32 v[126:127], v[124:125], v[12:13], v[116:117] op_sel:[1,0,1] op_sel_hi:[1,1,0] neg_lo:[0,0,1] neg_hi:[0,0,1]
	v_pk_fma_f32 v[12:13], v[124:125], v[12:13], v[116:117] op_sel:[1,0,1] op_sel_hi:[1,1,0]
	v_pk_mul_f32 v[116:117], v[124:125], v[28:29] op_sel_hi:[0,1]
	v_pk_fma_f32 v[138:139], v[124:125], v[28:29], v[116:117] op_sel:[1,0,1] op_sel_hi:[1,1,0] neg_lo:[0,0,1]
	v_mov_b32_e32 v127, v13
	v_pk_add_f32 v[28:29], v[20:21], v[138:139]
	v_pk_add_f32 v[12:13], v[2:3], v[126:127]
	v_pk_mul_f32 v[116:117], v[122:123], v[28:29] op_sel:[1,0]
	v_pk_add_f32 v[26:27], v[26:27], v[140:141] neg_lo:[0,1] neg_hi:[0,1]
	v_pk_fma_f32 v[124:125], v[122:123], v[28:29], v[116:117] op_sel:[0,0,1] op_sel_hi:[0,1,0] neg_hi:[0,0,1]
	v_pk_mul_f32 v[116:117], v[136:137], v[10:11] op_sel_hi:[0,1]
	v_pk_add_f32 v[28:29], v[12:13], v[124:125]
	v_pk_add_f32 v[12:13], v[12:13], v[124:125] neg_lo:[0,1] neg_hi:[0,1]
	v_pk_fma_f32 v[124:125], v[136:137], v[10:11], v[116:117] op_sel:[1,0,1] op_sel_hi:[1,1,0] neg_lo:[0,0,1] neg_hi:[0,0,1]
	v_pk_fma_f32 v[10:11], v[136:137], v[10:11], v[116:117] op_sel:[1,0,1] op_sel_hi:[1,1,0]
	v_pk_mul_f32 v[116:117], v[136:137], v[26:27] op_sel_hi:[0,1]
	v_pk_fma_f32 v[140:141], v[136:137], v[26:27], v[116:117] op_sel:[1,0,1] op_sel_hi:[1,1,0] neg_lo:[0,0,1]
	v_pk_add_f32 v[18:19], v[18:19], v[150:151] neg_lo:[0,1] neg_hi:[0,1]
	s_nop 0
	v_pk_add_f32 v[26:27], v[18:19], v[140:141]
	v_pk_add_f32 v[0:1], v[0:1], v[142:143] neg_lo:[0,1] neg_hi:[0,1]
	v_pk_mul_f32 v[116:117], v[132:133], v[26:27] op_sel:[1,0]
	v_mov_b32_e32 v125, v11
	v_pk_fma_f32 v[136:137], v[132:133], v[26:27], v[116:117] op_sel:[0,0,1] op_sel_hi:[0,1,0] neg_hi:[0,0,1]
	v_pk_add_f32 v[24:25], v[24:25], v[164:165] neg_lo:[0,1] neg_hi:[0,1]
	v_pk_add_f32 v[10:11], v[0:1], v[124:125]
	v_pk_mul_f32 v[116:117], v[120:121], v[24:25] op_sel_hi:[0,1]
	v_pk_add_f32 v[22:23], v[22:23], v[128:129] neg_lo:[0,1] neg_hi:[0,1]
	v_pk_add_f32 v[26:27], v[10:11], v[136:137]
	v_pk_add_f32 v[10:11], v[10:11], v[136:137] neg_lo:[0,1] neg_hi:[0,1]
	v_pk_fma_f32 v[136:137], v[120:121], v[24:25], v[116:117] op_sel:[1,0,1] op_sel_hi:[1,1,0] neg_lo:[0,0,1] neg_hi:[0,0,1]
	v_pk_fma_f32 v[24:25], v[120:121], v[24:25], v[116:117] op_sel:[1,0,1] op_sel_hi:[1,1,0]
	v_pk_mul_f32 v[116:117], v[130:131], v[22:23] op_sel_hi:[0,1]
	v_pk_fma_f32 v[120:121], v[130:131], v[22:23], v[116:117] op_sel:[1,0,1] op_sel_hi:[1,1,0] neg_lo:[0,0,1]
	v_pk_add_f32 v[20:21], v[20:21], v[138:139] neg_lo:[0,1] neg_hi:[0,1]
	v_pk_add_f32 v[6:7], v[6:7], v[148:149] neg_lo:[0,1] neg_hi:[0,1]
	v_pk_mul_f32 v[116:117], v[122:123], v[20:21] op_sel_hi:[0,1]
	v_pk_add_f32 v[22:23], v[6:7], v[120:121]
	v_pk_add_f32 v[6:7], v[6:7], v[120:121] neg_lo:[0,1] neg_hi:[0,1]
	v_pk_fma_f32 v[120:121], v[122:123], v[20:21], v[116:117] op_sel:[1,0,1] op_sel_hi:[1,1,0] neg_lo:[0,0,1]
	v_pk_add_f32 v[18:19], v[18:19], v[140:141] neg_lo:[0,1] neg_hi:[0,1]
	v_mov_b32_e32 v155, v17
	v_pk_add_f32 v[2:3], v[2:3], v[126:127] neg_lo:[0,1] neg_hi:[0,1]
	v_pk_mul_f32 v[116:117], v[132:133], v[18:19] op_sel_hi:[0,1]
	v_pk_add_f32 v[16:17], v[8:9], v[154:155]
	v_mov_b32_e32 v167, v119
	v_pk_add_f32 v[20:21], v[2:3], v[120:121]
	v_pk_add_f32 v[2:3], v[2:3], v[120:121] neg_lo:[0,1] neg_hi:[0,1]
	v_pk_fma_f32 v[120:121], v[132:133], v[18:19], v[116:117] op_sel:[1,0,1] op_sel_hi:[1,1,0] neg_lo:[0,0,1]
	v_pk_add_f32 v[118:119], v[16:17], v[166:167]
	v_pk_add_f32 v[8:9], v[8:9], v[154:155] neg_lo:[0,1] neg_hi:[0,1]
	v_mov_b32_e32 v137, v25
	v_pk_add_f32 v[0:1], v[0:1], v[124:125] neg_lo:[0,1] neg_hi:[0,1]
	v_pk_add_f32 v[16:17], v[16:17], v[166:167] neg_lo:[0,1] neg_hi:[0,1]
	v_pk_add_f32 v[24:25], v[8:9], v[136:137]
	v_pk_add_f32 v[8:9], v[8:9], v[136:137] neg_lo:[0,1] neg_hi:[0,1]
	v_pk_add_f32 v[18:19], v[0:1], v[120:121]
	v_pk_add_f32 v[0:1], v[0:1], v[120:121] neg_lo:[0,1] neg_hi:[0,1]
	ds_write2_b64 v81, v[118:119], v[30:31] offset1:34
	ds_write2_b64 v81, v[28:29], v[26:27] offset0:68 offset1:102
	ds_write2_b64 v81, v[24:25], v[22:23] offset0:136 offset1:170
	ds_write2_b64 v81, v[20:21], v[18:19] offset0:204 offset1:238
	ds_write2_b64 v110, v[16:17], v[14:15] offset0:16 offset1:50
	ds_write2_b64 v110, v[12:13], v[10:11] offset0:84 offset1:118
	ds_write2_b64 v110, v[8:9], v[6:7] offset0:152 offset1:186
	ds_write2_b64 v110, v[2:3], v[0:1] offset0:220 offset1:254
	s_waitcnt lgkmcnt(0)
	s_barrier
; template <int R, class XT, class TWT>
; __device__ __forceinline__ void dit_task(XT X, TWT tw, int s, int task) {
;     const int lgM = 13 - s, lgq = lgM - R, q = 1 << lgq;
;     const int j0 = task & (q - 1), blk = task >> lgq, base = (blk << lgM) + j0;
;     const int pb = PADI(base), qp = (q >= 32) ? q + (q >> 4) : q;
;     f32x2v v[1 << R];
; #pragma unroll
;     for (int k = 0; k < (1 << R); ++k) v[k] = X[pb + k * qp];
; #pragma unroll
;     for (int r = R - 1; r >= 0; --r) {
;         const int pb = R - 1 - r;
; #pragma unroll
;         for (int k = 0; k < (1 << R); ++k) if (!((k >> pb) & 1)) {
;             const int klo = k & ((1 << pb) - 1);
;             const f32x2v w = tw[(j0 + (klo << lgq)) << (s + r)];
;             const f32x2v a = v[k], qv = v[k + (1 << pb)]; const f32x2v b = (f32x2v){qv.x * w.x + qv.y * w.y, qv.y * w.x - qv.x * w.y};
;             v[k] = a + b; v[k + (1 << pb)] = a - b;
;         }
;     }
; #pragma unroll
;     for (int k = 0; k < (1 << R); ++k) X[pb + k * qp] = v[k];
; }
	ds_read_b64 v[6:7], v75
	ds_read_b64 v[8:9], v75 offset:4352
	ds_read_b64 v[10:11], v75 offset:8704
	ds_read_b64 v[12:13], v75 offset:13056
	ds_read_b64 v[14:15], v75 offset:17408
	ds_read_b64 v[16:17], v75 offset:21760
	ds_read_b64 v[18:19], v75 offset:26112
	ds_read_b64 v[20:21], v75 offset:30464
	ds_read_b64 v[22:23], v75 offset:34816
	ds_read_b64 v[24:25], v75 offset:39168
	ds_read_b64 v[26:27], v75 offset:43520
	ds_read_b64 v[28:29], v75 offset:47872
	ds_read_b64 v[30:31], v75 offset:52224
	ds_read_b64 v[110:111], v75 offset:56576
	ds_read_b64 v[116:117], v75 offset:60928
	ds_read_b64 v[118:119], v75 offset:65280
	ds_read_b64 v[120:121], v80
	ds_read_b64 v[122:123], v93
	ds_read_b64 v[124:125], v91
	ds_read_b64 v[126:127], v92
	ds_read2st64_b64 v[0:3], v76 offset1:16
	ds_read_b64 v[128:129], v79
	ds_read_b64 v[130:131], v77
	ds_read_b64 v[132:133], v78
	s_waitcnt lgkmcnt(7)
	v_xor_b32_e32 v5, 0x80000000, v120
	v_cndmask_b32_e64 v137, v5, v121, s[38:39]
	v_cndmask_b32_e64 v136, v121, v120, s[38:39]
	v_mov_b32_e32 v120, v137
	v_pk_mul_f32 v[138:139], v[8:9], v[120:121] op_sel_hi:[1,0]
	s_add_u32 s2, s26, s2
	v_pk_fma_f32 v[140:141], v[8:9], v[136:137], v[138:139] op_sel:[0,0,1] op_sel_hi:[1,1,0]
	v_pk_fma_f32 v[8:9], v[8:9], v[136:137], v[138:139] op_sel:[0,0,1] op_sel_hi:[1,0,0] neg_lo:[0,0,1] neg_hi:[0,0,1]
	v_pk_mul_f32 v[138:139], v[12:13], v[120:121] op_sel_hi:[1,0]
	v_mov_b32_e32 v141, v9
	v_pk_fma_f32 v[142:143], v[12:13], v[136:137], v[138:139] op_sel:[0,0,1] op_sel_hi:[1,0,0] neg_hi:[0,0,1]
	v_pk_add_f32 v[8:9], v[6:7], v[140:141]
	v_pk_add_f32 v[12:13], v[10:11], v[142:143]
	v_pk_add_f32 v[10:11], v[10:11], v[142:143] neg_lo:[0,1] neg_hi:[0,1]
	s_waitcnt lgkmcnt(6)
	v_pk_mul_f32 v[138:139], v[122:123], v[12:13] op_sel:[1,0]
	v_pk_add_f32 v[6:7], v[6:7], v[140:141] neg_lo:[0,1] neg_hi:[0,1]
	v_pk_fma_f32 v[144:145], v[122:123], v[12:13], v[138:139] op_sel:[0,0,1] op_sel_hi:[1,1,0]
	v_pk_fma_f32 v[12:13], v[122:123], v[12:13], v[138:139] op_sel:[0,0,1] op_sel_hi:[0,1,0] neg_lo:[0,0,1] neg_hi:[0,0,1]
	v_pk_mul_f32 v[138:139], v[16:17], v[120:121] op_sel_hi:[1,0]
	v_mov_b32_e32 v145, v13
	v_pk_fma_f32 v[146:147], v[16:17], v[136:137], v[138:139] op_sel:[0,0,1] op_sel_hi:[1,1,0]
	v_pk_fma_f32 v[16:17], v[16:17], v[136:137], v[138:139] op_sel:[0,0,1] op_sel_hi:[1,0,0] neg_lo:[0,0,1] neg_hi:[0,0,1]
	v_pk_mul_f32 v[138:139], v[20:21], v[120:121] op_sel_hi:[1,0]
	v_mov_b32_e32 v147, v17
	v_pk_fma_f32 v[148:149], v[20:21], v[136:137], v[138:139] op_sel:[0,0,1] op_sel_hi:[1,0,0] neg_hi:[0,0,1]
	v_pk_add_f32 v[16:17], v[14:15], v[146:147]
	v_pk_add_f32 v[20:21], v[18:19], v[148:149]
	v_pk_add_f32 v[18:19], v[18:19], v[148:149] neg_lo:[0,1] neg_hi:[0,1]
	v_pk_mul_f32 v[138:139], v[122:123], v[20:21] op_sel:[1,0]
	v_pk_add_f32 v[14:15], v[14:15], v[146:147] neg_lo:[0,1] neg_hi:[0,1]
	v_pk_fma_f32 v[150:151], v[122:123], v[20:21], v[138:139] op_sel:[0,0,1] op_sel_hi:[0,1,0] neg_hi:[0,0,1]
	s_nop 0
	v_pk_add_f32 v[20:21], v[16:17], v[150:151]
	v_pk_add_f32 v[16:17], v[16:17], v[150:151] neg_lo:[0,1] neg_hi:[0,1]
	s_waitcnt lgkmcnt(5)
	v_pk_mul_f32 v[138:139], v[124:125], v[20:21] op_sel:[1,0]
	v_pk_add_f32 v[12:13], v[8:9], v[144:145]
	v_pk_fma_f32 v[152:153], v[124:125], v[20:21], v[138:139] op_sel:[0,0,1] op_sel_hi:[1,1,0]
	v_pk_fma_f32 v[20:21], v[124:125], v[20:21], v[138:139] op_sel:[0,0,1] op_sel_hi:[0,1,0] neg_lo:[0,0,1] neg_hi:[0,0,1]
	v_pk_mul_f32 v[138:139], v[24:25], v[120:121] op_sel_hi:[1,0]
	v_pk_add_f32 v[8:9], v[8:9], v[144:145] neg_lo:[0,1] neg_hi:[0,1]
	v_pk_fma_f32 v[154:155], v[24:25], v[136:137], v[138:139] op_sel:[0,0,1] op_sel_hi:[1,1,0]
	v_pk_fma_f32 v[24:25], v[24:25], v[136:137], v[138:139] op_sel:[0,0,1] op_sel_hi:[1,0,0] neg_lo:[0,0,1] neg_hi:[0,0,1]
	v_pk_mul_f32 v[138:139], v[28:29], v[120:121] op_sel_hi:[1,0]
	v_mov_b32_e32 v155, v25
	v_pk_fma_f32 v[156:157], v[28:29], v[136:137], v[138:139] op_sel:[0,0,1] op_sel_hi:[1,0,0] neg_hi:[0,0,1]
	v_pk_add_f32 v[24:25], v[22:23], v[154:155]
	v_pk_add_f32 v[28:29], v[26:27], v[156:157]
	v_pk_add_f32 v[26:27], v[26:27], v[156:157] neg_lo:[0,1] neg_hi:[0,1]
	v_pk_mul_f32 v[138:139], v[122:123], v[28:29] op_sel:[1,0]
	v_pk_add_f32 v[22:23], v[22:23], v[154:155] neg_lo:[0,1] neg_hi:[0,1]
	v_pk_fma_f32 v[158:159], v[122:123], v[28:29], v[138:139] op_sel:[0,0,1] op_sel_hi:[1,1,0]
	v_pk_fma_f32 v[28:29], v[122:123], v[28:29], v[138:139] op_sel:[0,0,1] op_sel_hi:[0,1,0] neg_lo:[0,0,1] neg_hi:[0,0,1]
	v_pk_mul_f32 v[138:139], v[110:111], v[120:121] op_sel_hi:[1,0]
	v_pk_mul_f32 v[120:121], v[118:119], v[120:121] op_sel_hi:[1,0]
	v_pk_fma_f32 v[160:161], v[110:111], v[136:137], v[138:139] op_sel:[0,0,1] op_sel_hi:[1,1,0]
	v_pk_fma_f32 v[110:111], v[110:111], v[136:137], v[138:139] op_sel:[0,0,1] op_sel_hi:[1,0,0] neg_lo:[0,0,1] neg_hi:[0,0,1]
	v_pk_fma_f32 v[138:139], v[118:119], v[136:137], v[120:121] op_sel:[0,0,1] op_sel_hi:[1,0,0] neg_hi:[0,0,1]
	v_mov_b32_e32 v161, v111
	v_pk_add_f32 v[118:119], v[116:117], v[138:139]
	v_pk_add_f32 v[110:111], v[30:31], v[160:161]
	v_pk_mul_f32 v[120:121], v[122:123], v[118:119] op_sel:[1,0]
	v_mov_b32_e32 v159, v29
	v_pk_fma_f32 v[136:137], v[122:123], v[118:119], v[120:121] op_sel:[0,0,1] op_sel_hi:[0,1,0] neg_hi:[0,0,1]
	s_nop 0
	v_pk_add_f32 v[118:119], v[110:111], v[136:137]
	v_pk_add_f32 v[28:29], v[24:25], v[158:159]
	v_pk_mul_f32 v[120:121], v[124:125], v[118:119] op_sel:[1,0]
	v_pk_add_f32 v[116:117], v[116:117], v[138:139] neg_lo:[0,1] neg_hi:[0,1]
	v_pk_fma_f32 v[162:163], v[124:125], v[118:119], v[120:121] op_sel:[0,0,1] op_sel_hi:[0,1,0] neg_hi:[0,0,1]
	s_nop 0
	v_pk_add_f32 v[118:119], v[28:29], v[162:163]
	v_pk_add_f32 v[30:31], v[30:31], v[160:161] neg_lo:[0,1] neg_hi:[0,1]
	s_waitcnt lgkmcnt(3)
; template <int R, class XT, class TWT>
; __device__ __forceinline__ void dit_task(XT X, TWT tw, int s, int task) {
;     const int lgM = 13 - s, lgq = lgM - R, q = 1 << lgq;
;     const int j0 = task & (q - 1), blk = task >> lgq, base = (blk << lgM) + j0;
;     const int pb = PADI(base), qp = (q >= 32) ? q + (q >> 4) : q;
;     f32x2v v[1 << R];
; #pragma unroll
;     for (int k = 0; k < (1 << R); ++k) v[k] = X[pb + k * qp];
; #pragma unroll
;     for (int r = R - 1; r >= 0; --r) {
;         const int pb = R - 1 - r;
; #pragma unroll
;         for (int k = 0; k < (1 << R); ++k) if (!((k >> pb) & 1)) {
;             const int klo = k & ((1 << pb) - 1);
;             const f32x2v w = tw[(j0 + (klo << lgq)) << (s + r)];
;             const f32x2v a = v[k], qv = v[k + (1 << pb)]; const f32x2v b = (f32x2v){qv.x * w.x + qv.y * w.y, qv.y * w.x - qv.x * w.y};
;             v[k] = a + b; v[k + (1 << pb)] = a - b;
;         }
;     }
; #pragma unroll
;     for (int k = 0; k < (1 << R); ++k) X[pb + k * qp] = v[k];
; }
	v_pk_mul_f32 v[120:121], v[0:1], v[118:119] op_sel:[1,0]
	v_pk_add_f32 v[110:111], v[110:111], v[136:137] neg_lo:[0,1] neg_hi:[0,1]
	v_pk_fma_f32 v[164:165], v[0:1], v[118:119], v[120:121] op_sel:[0,0,1] op_sel_hi:[1,1,0]
	v_pk_fma_f32 v[118:119], v[0:1], v[118:119], v[120:121] op_sel:[0,0,1] op_sel_hi:[0,1,0] neg_lo:[0,0,1] neg_hi:[0,0,1]
	v_pk_mul_f32 v[120:121], v[122:123], v[10:11] op_sel_hi:[0,1]
	v_pk_fma_f32 v[140:141], v[122:123], v[10:11], v[120:121] op_sel:[1,0,1] op_sel_hi:[1,1,0] neg_lo:[0,0,1] neg_hi:[0,0,1]
	v_pk_fma_f32 v[10:11], v[122:123], v[10:11], v[120:121] op_sel:[1,0,1] op_sel_hi:[1,1,0]
	v_pk_mul_f32 v[120:121], v[122:123], v[18:19] op_sel_hi:[0,1]
	v_pk_fma_f32 v[142:143], v[122:123], v[18:19], v[120:121] op_sel:[1,0,1] op_sel_hi:[1,1,0] neg_lo:[0,0,1]
	v_mov_b32_e32 v141, v11
	v_pk_add_f32 v[18:19], v[14:15], v[142:143]
	v_pk_add_f32 v[10:11], v[6:7], v[140:141]
	v_pk_mul_f32 v[120:121], v[126:127], v[18:19] op_sel:[1,0]
	v_pk_add_f32 v[24:25], v[24:25], v[158:159] neg_lo:[0,1] neg_hi:[0,1]
	v_pk_fma_f32 v[146:147], v[126:127], v[18:19], v[120:121] op_sel:[0,0,1] op_sel_hi:[1,1,0]
	v_pk_fma_f32 v[18:19], v[126:127], v[18:19], v[120:121] op_sel:[0,0,1] op_sel_hi:[0,1,0] neg_lo:[0,0,1] neg_hi:[0,0,1]
	v_pk_mul_f32 v[120:121], v[122:123], v[26:27] op_sel_hi:[0,1]
	v_pk_fma_f32 v[148:149], v[122:123], v[26:27], v[120:121] op_sel:[1,0,1] op_sel_hi:[1,1,0] neg_lo:[0,0,1] neg_hi:[0,0,1]
	v_pk_fma_f32 v[26:27], v[122:123], v[26:27], v[120:121] op_sel:[1,0,1] op_sel_hi:[1,1,0]
	v_pk_mul_f32 v[120:121], v[122:123], v[116:117] op_sel_hi:[0,1]
	v_pk_fma_f32 v[138:139], v[122:123], v[116:117], v[120:121] op_sel:[1,0,1] op_sel_hi:[1,1,0] neg_lo:[0,0,1]
	v_mov_b32_e32 v149, v27
	v_pk_add_f32 v[116:117], v[30:31], v[138:139]
	v_pk_add_f32 v[26:27], v[22:23], v[148:149]
	v_pk_mul_f32 v[120:121], v[126:127], v[116:117] op_sel:[1,0]
	v_mov_b32_e32 v147, v19
	v_pk_fma_f32 v[122:123], v[126:127], v[116:117], v[120:121] op_sel:[0,0,1] op_sel_hi:[0,1,0] neg_hi:[0,0,1]
	s_nop 0
	v_pk_add_f32 v[116:117], v[26:27], v[122:123]
	v_pk_add_f32 v[18:19], v[10:11], v[146:147]
	s_waitcnt lgkmcnt(1)
	v_pk_mul_f32 v[120:121], v[130:131], v[116:117] op_sel:[1,0]
	v_pk_add_f32 v[14:15], v[14:15], v[142:143] neg_lo:[0,1] neg_hi:[0,1]
	v_pk_fma_f32 v[126:127], v[130:131], v[116:117], v[120:121] op_sel:[0,0,1] op_sel_hi:[0,1,0] neg_hi:[0,0,1]
	v_pk_mul_f32 v[120:121], v[124:125], v[16:17] op_sel_hi:[0,1]
	v_pk_add_f32 v[116:117], v[18:19], v[126:127]
	v_pk_add_f32 v[18:19], v[18:19], v[126:127] neg_lo:[0,1] neg_hi:[0,1]
	v_pk_fma_f32 v[126:127], v[124:125], v[16:17], v[120:121] op_sel:[1,0,1] op_sel_hi:[1,1,0] neg_lo:[0,0,1] neg_hi:[0,0,1]
	v_pk_fma_f32 v[16:17], v[124:125], v[16:17], v[120:121] op_sel:[1,0,1] op_sel_hi:[1,1,0]
	v_pk_mul_f32 v[120:121], v[124:125], v[110:111] op_sel_hi:[0,1]
	v_pk_fma_f32 v[136:137], v[124:125], v[110:111], v[120:121] op_sel:[1,0,1] op_sel_hi:[1,1,0] neg_lo:[0,0,1]
	v_mov_b32_e32 v127, v17
	v_pk_add_f32 v[110:111], v[24:25], v[136:137]
	v_pk_add_f32 v[16:17], v[8:9], v[126:127]
	v_pk_mul_f32 v[120:121], v[2:3], v[110:111] op_sel:[1,0]
	v_pk_add_f32 v[30:31], v[30:31], v[138:139] neg_lo:[0,1] neg_hi:[0,1]
	v_pk_fma_f32 v[124:125], v[2:3], v[110:111], v[120:121] op_sel:[0,0,1] op_sel_hi:[0,1,0] neg_hi:[0,0,1]
	v_pk_mul_f32 v[120:121], v[128:129], v[14:15] op_sel_hi:[0,1]
	v_pk_add_f32 v[110:111], v[16:17], v[124:125]
	v_pk_add_f32 v[16:17], v[16:17], v[124:125] neg_lo:[0,1] neg_hi:[0,1]
	v_pk_fma_f32 v[124:125], v[128:129], v[14:15], v[120:121] op_sel:[1,0,1] op_sel_hi:[1,1,0] neg_lo:[0,0,1] neg_hi:[0,0,1]
	v_pk_fma_f32 v[14:15], v[128:129], v[14:15], v[120:121] op_sel:[1,0,1] op_sel_hi:[1,1,0]
	v_pk_mul_f32 v[120:121], v[128:129], v[30:31] op_sel_hi:[0,1]
	v_pk_fma_f32 v[138:139], v[128:129], v[30:31], v[120:121] op_sel:[1,0,1] op_sel_hi:[1,1,0] neg_lo:[0,0,1]
	v_pk_add_f32 v[22:23], v[22:23], v[148:149] neg_lo:[0,1] neg_hi:[0,1]
	s_nop 0
	v_pk_add_f32 v[30:31], v[22:23], v[138:139]
	v_pk_add_f32 v[6:7], v[6:7], v[140:141] neg_lo:[0,1] neg_hi:[0,1]
	s_waitcnt lgkmcnt(0)
; #define LAS __attribute__((address_space(3)))
; template <int R, class XT, class TWT>
; __device__ __forceinline__ void dit_task(XT X, TWT tw, int s, int task) {
;     const int lgM = 13 - s, lgq = lgM - R, q = 1 << lgq;
;     const int j0 = task & (q - 1), blk = task >> lgq, base = (blk << lgM) + j0;
;     const int pb = PADI(base), qp = (q >= 32) ? q + (q >> 4) : q;
;     f32x2v v[1 << R];
; #pragma unroll
;     for (int k = 0; k < (1 << R); ++k) v[k] = X[pb + k * qp];
; #pragma unroll
;     for (int r = R - 1; r >= 0; --r) {
;         const int pb = R - 1 - r;
; #pragma unroll
;         for (int k = 0; k < (1 << R); ++k) if (!((k >> pb) & 1)) {
;             const int klo = k & ((1 << pb) - 1);
;             const f32x2v w = tw[(j0 + (klo << lgq)) << (s + r)];
;             const f32x2v a = v[k], qv = v[k + (1 << pb)]; const f32x2v b = (f32x2v){qv.x * w.x + qv.y * w.y, qv.y * w.x - qv.x * w.y};
;             v[k] = a + b; v[k + (1 << pb)] = a - b;
;         }
;     }
; #pragma unroll
;     for (int k = 0; k < (1 << R); ++k) X[pb + k * qp] = v[k];
; }
; template <bool LAT>
; __device__ __forceinline__ void hyconv_unit(const Frame& F, LAS f32x2v* X, const TwHalf tw, LAS bf16* OUT, const float* skip, bf16* MIX, int u) {
;     ...
;                 for (int r = 0; r < 4; ++r) { const int pr = F.tid + 512 * r; ga[r] = *(const unsigned*)(g0 + 2 * pr); gb[r] = *(const unsigned*)(g1 + 2 * pr); za[r] = *(const unsigned*)(v0 + 2 * pr); zb[r] = *(const unsigned*)(v1 + 2 * pr); }
; #pragma unroll
;                 for (int r = 0; r < 8; ++r) { const int e = 2 * (F.tid + 512 * r); f32x4 zz = (f32x4){0.f, 0.f, 0.f, 0.f};
;                     if (r < 4) { const f32x4 xx = *(const LAS f32x4*)(X + PADI(e));
;                         zz.x = bflo(ga[r]) * (xx.x + bflo(za[r]) * sk); zz.y = bflo(gb[r]) * (xx.y + bflo(zb[r]) * sk); zz.z = bfhi(ga[r]) * (xx.z + bfhi(za[r]) * sk); zz.w = bfhi(gb[r]) * (xx.w + bfhi(zb[r]) * sk);
;                         if (ord == 0) { *(unsigned*)(v0 + e) = pk2(zz.x, zz.z); *(unsigned*)(v1 + e) = pk2(zz.y, zz.w); }
;                         else { OUT[e * 4 + ci] = (bf16)f2bf(zz.x); OUT[(e + 1) * 4 + ci] = (bf16)f2bf(zz.z); OUT[(T + e) * 4 + ci] = (bf16)f2bf(zz.y); OUT[(T + e + 1) * 4 + ci] = (bf16)f2bf(zz.w); } }
;                     if (ord == 0) *(LAS f32x4*)(X + PADI(e)) = zz; }
	v_pk_mul_f32 v[120:121], v[132:133], v[30:31] op_sel:[1,0]
	v_mov_b32_e32 v125, v15
	v_pk_fma_f32 v[128:129], v[132:133], v[30:31], v[120:121] op_sel:[0,0,1] op_sel_hi:[0,1,0] neg_hi:[0,0,1]
	v_pk_add_f32 v[28:29], v[28:29], v[162:163] neg_lo:[0,1] neg_hi:[0,1]
	v_pk_add_f32 v[14:15], v[6:7], v[124:125]
	v_pk_mul_f32 v[120:121], v[0:1], v[28:29] op_sel_hi:[0,1]
	v_pk_add_f32 v[26:27], v[26:27], v[122:123] neg_lo:[0,1] neg_hi:[0,1]
	v_pk_add_f32 v[30:31], v[14:15], v[128:129]
	v_pk_add_f32 v[14:15], v[14:15], v[128:129] neg_lo:[0,1] neg_hi:[0,1]
	v_pk_fma_f32 v[128:129], v[0:1], v[28:29], v[120:121] op_sel:[1,0,1] op_sel_hi:[1,1,0] neg_lo:[0,0,1] neg_hi:[0,0,1]
	v_pk_fma_f32 v[0:1], v[0:1], v[28:29], v[120:121] op_sel:[1,0,1] op_sel_hi:[1,1,0]
	v_pk_mul_f32 v[28:29], v[130:131], v[26:27] op_sel_hi:[0,1]
	v_pk_fma_f32 v[120:121], v[130:131], v[26:27], v[28:29] op_sel:[1,0,1] op_sel_hi:[1,1,0] neg_lo:[0,0,1]
	v_pk_add_f32 v[24:25], v[24:25], v[136:137] neg_lo:[0,1] neg_hi:[0,1]
	v_pk_add_f32 v[10:11], v[10:11], v[146:147] neg_lo:[0,1] neg_hi:[0,1]
	v_pk_mul_f32 v[28:29], v[2:3], v[24:25] op_sel_hi:[0,1]
	v_pk_add_f32 v[22:23], v[22:23], v[138:139] neg_lo:[0,1] neg_hi:[0,1]
	v_mov_b32_e32 v153, v21
	v_pk_add_f32 v[26:27], v[10:11], v[120:121]
	v_pk_add_f32 v[10:11], v[10:11], v[120:121] neg_lo:[0,1] neg_hi:[0,1]
	v_pk_fma_f32 v[120:121], v[2:3], v[24:25], v[28:29] op_sel:[1,0,1] op_sel_hi:[1,1,0] neg_lo:[0,0,1] neg_hi:[0,0,1]
	v_pk_fma_f32 v[2:3], v[2:3], v[24:25], v[28:29] op_sel:[1,0,1] op_sel_hi:[1,1,0]
	v_pk_mul_f32 v[24:25], v[132:133], v[22:23] op_sel_hi:[0,1]
	v_pk_add_f32 v[20:21], v[12:13], v[152:153]
	v_mov_b32_e32 v165, v119
	v_pk_fma_f32 v[28:29], v[132:133], v[22:23], v[24:25] op_sel:[1,0,1] op_sel_hi:[1,1,0] neg_lo:[0,0,1]
	v_pk_add_f32 v[118:119], v[20:21], v[164:165]
	v_pk_add_f32 v[12:13], v[12:13], v[152:153] neg_lo:[0,1] neg_hi:[0,1]
	v_mov_b32_e32 v129, v1
	v_pk_add_f32 v[8:9], v[8:9], v[126:127] neg_lo:[0,1] neg_hi:[0,1]
	v_mov_b32_e32 v121, v3
	v_pk_add_f32 v[6:7], v[6:7], v[124:125] neg_lo:[0,1] neg_hi:[0,1]
	s_addc_u32 s3, s27, s3
	v_pk_add_f32 v[20:21], v[20:21], v[164:165] neg_lo:[0,1] neg_hi:[0,1]
	v_pk_add_f32 v[0:1], v[12:13], v[128:129]
	v_pk_add_f32 v[12:13], v[12:13], v[128:129] neg_lo:[0,1] neg_hi:[0,1]
	v_pk_add_f32 v[2:3], v[8:9], v[120:121]
	v_pk_add_f32 v[8:9], v[8:9], v[120:121] neg_lo:[0,1] neg_hi:[0,1]
	v_pk_add_f32 v[22:23], v[6:7], v[28:29]
	v_pk_add_f32 v[6:7], v[6:7], v[28:29] neg_lo:[0,1] neg_hi:[0,1]
	ds_write_b64 v75, v[118:119]
	ds_write_b64 v75, v[116:117] offset:4352
	ds_write_b64 v75, v[110:111] offset:8704
	ds_write_b64 v75, v[30:31] offset:13056
	ds_write_b64 v75, v[0:1] offset:17408
	ds_write_b64 v75, v[26:27] offset:21760
	ds_write_b64 v75, v[2:3] offset:26112
	ds_write_b64 v75, v[22:23] offset:30464
	ds_write_b64 v75, v[20:21] offset:34816
	ds_write_b64 v75, v[18:19] offset:39168
	ds_write_b64 v75, v[16:17] offset:43520
	ds_write_b64 v75, v[14:15] offset:47872
	ds_write_b64 v75, v[12:13] offset:52224
	ds_write_b64 v75, v[10:11] offset:56576
	ds_write_b64 v75, v[8:9] offset:60928
	ds_write_b64 v75, v[6:7] offset:65280
	s_waitcnt lgkmcnt(0)
	s_barrier
	s_waitcnt vmcnt(0)
	v_mov_b32_e32 v5, v182
	v_mov_b32_e32 v21, v183
	v_mov_b32_e32 v23, v184
	v_mov_b32_e32 v25, v185
	v_mov_b32_e32 v13, v186
	v_mov_b32_e32 v12, v187
	v_mov_b32_e32 v9, v188
	v_mov_b32_e32 v8, v189
	v_mov_b32_e32 v16, v190
	v_mov_b32_e32 v18, v191
	v_mov_b32_e32 v15, v192
	v_mov_b32_e32 v14, v193
	v_mov_b32_e32 v11, v194
	v_mov_b32_e32 v10, v195
	v_mov_b32_e32 v17, v196
	v_mov_b32_e32 v19, v197
	ds_read_b128 v[0:3], v33
	s_and_b64 vcc, exec, s[20:21]
	s_mov_b64 s[0:1], -1
	s_waitcnt lgkmcnt(0)
	v_mov_b32_e32 v26, v0
	v_mov_b32_e32 v27, v2
	v_mov_b32_e32 v2, v1
	s_waitcnt vmcnt(15)
	v_lshlrev_b32_e32 v6, 16, v5
	s_waitcnt vmcnt(14)
	v_lshlrev_b32_e32 v20, 16, v21
	v_and_b32_e32 v21, 0xffff0000, v21
	s_waitcnt vmcnt(12)
	v_lshlrev_b32_e32 v24, 16, v25
	v_and_b32_e32 v25, 0xffff0000, v25
	v_lshlrev_b32_e32 v22, 16, v23
	v_and_b32_e32 v7, 0xffff0000, v5
	v_pk_fma_f32 v[20:21], v[4:5], v[20:21], v[26:27] op_sel_hi:[0,1,1]
	v_and_b32_e32 v23, 0xffff0000, v23
	v_pk_fma_f32 v[0:1], v[4:5], v[24:25], v[2:3] op_sel_hi:[0,1,1]
	v_pk_mul_f32 v[6:7], v[20:21], v[6:7]
	v_pk_mul_f32 v[2:3], v[0:1], v[22:23]
	s_cbranch_vccnz .LBB0_795
	s_andn2_b64 vcc, exec, s[0:1]
	s_cbranch_vccz .LBB0_796

; template <int R, class XT, class TWT>
; __device__ __forceinline__ void dif_task(XT X, TWT tw, int s, int task) {
;     const int lgM = 13 - s, lgq = lgM - R, q = 1 << lgq;
;     const int j0 = task & (q - 1), blk = task >> lgq, base = (blk << lgM) + j0;
;     const int pb = PADI(base), qp = (q >= 32) ? q + (q >> 4) : q;
;     f32x2v v[1 << R];
; #pragma unroll
;     for (int k = 0; k < (1 << R); ++k) v[k] = X[pb + k * qp];
; #pragma unroll
;     for (int r = 0; r < R; ++r) {
;         const int pb = R - 1 - r;
; #pragma unroll
;         for (int k = 0; k < (1 << R); ++k) if (!((k >> pb) & 1)) {
;             const int klo = k & ((1 << pb) - 1);
;             const f32x2v w = tw[(j0 + (klo << lgq)) << (s + r)];
;             const f32x2v a = v[k], b = v[k + (1 << pb)], d = a - b;
;             v[k] = a + b; v[k + (1 << pb)] = (f32x2v){d.x * w.x - d.y * w.y, d.x * w.y + d.y * w.x};
;         }
;     }
; #pragma unroll
;     for (int k = 0; k < (1 << R); ++k) X[pb + k * qp] = v[k];
; }
; template <bool LAT>
; __device__ __forceinline__ void hyconv_unit(const Frame& F, LAS f32x2v* X, const TwHalf tw, LAS bf16* OUT, const float* skip, bf16* MIX, int u) {
;     ...
;             const f32x2v* SP = SPb + (size_t)ord * 256 * N;
;             f32x4 kq[8];
; #pragma unroll
;             for (int r = 0; r < 8; ++r) kq[r] = *(const f32x4*)(SP + 2 * (F.tid + 512 * r));
;             fft_fwd_upper(X, tw, 13 - lgN, F.tid);
.LBB0_847:
	s_lshl_b32 s90, s2, 17
	s_lshl_b64 s[0:1], s[90:91], 3
	s_add_u32 s0, s4, s0
	s_addc_u32 s1, s5, s1
	v_lshl_add_u64 v[0:1], v[34:35], 3, s[0:1]
	v_lshl_add_u64 v[2:3], v[36:37], 3, s[0:1]
	global_load_dwordx4 v[28:31], v[0:1], off
	global_load_dwordx4 v[24:27], v[2:3], off
	v_lshl_add_u64 v[0:1], v[38:39], 3, s[0:1]
	v_lshl_add_u64 v[2:3], v[40:41], 3, s[0:1]
	global_load_dwordx4 v[20:23], v[0:1], off
	global_load_dwordx4 v[16:19], v[2:3], off
	v_lshl_add_u64 v[0:1], v[42:43], 3, s[0:1]
	v_lshl_add_u64 v[2:3], v[44:45], 3, s[0:1]
	global_load_dwordx4 v[12:15], v[0:1], off
	global_load_dwordx4 v[8:11], v[2:3], off
	v_lshl_add_u64 v[0:1], v[46:47], 3, s[0:1]
	v_lshl_add_u64 v[2:3], v[48:49], 3, s[0:1]
	global_load_dwordx4 v[4:7], v[0:1], off
	s_nop 0
	global_load_dwordx4 v[0:3], v[2:3], off
	ds_read2_b64 v[100:103], v135 offset1:34
	ds_read2_b64 v[104:107], v135 offset0:68 offset1:102
	ds_read2_b64 v[108:111], v135 offset0:136 offset1:170
	ds_read2_b64 v[112:115], v135 offset0:204 offset1:238
	v_add_u32_e32 v98, 0x800, v135
	ds_read2_b64 v[116:119], v98 offset0:16 offset1:50
	ds_read2_b64 v[120:123], v98 offset0:84 offset1:118
	ds_read2_b64 v[124:127], v98 offset0:152 offset1:186
	ds_read2_b64 v[128:131], v98 offset0:220 offset1:254
	ds_read2st64_b64 v[176:179], v33 offset1:16
	ds_read_b64 v[132:133], v165
	ds_read_b64 v[182:183], v166
	ds_read_b64 v[184:185], v167
	ds_read_b64 v[186:187], v168
	ds_read_b64 v[188:189], v169
	ds_read_b64 v[190:191], v139
	ds_read_b64 v[192:193], v136
	s_waitcnt lgkmcnt(11)
	v_pk_add_f32 v[194:195], v[100:101], v[116:117] neg_lo:[0,1] neg_hi:[0,1]
	v_pk_add_f32 v[100:101], v[100:101], v[116:117]
	s_waitcnt lgkmcnt(7)
	v_pk_mul_f32 v[196:197], v[194:195], v[176:177] op_sel:[1,1] op_sel_hi:[1,0]
	s_lshl_b32 s0, s2, 8
	v_pk_fma_f32 v[198:199], v[194:195], v[176:177], v[196:197] op_sel_hi:[0,1,1] neg_lo:[0,0,1]
	v_pk_add_f32 v[194:195], v[108:109], v[124:125] neg_lo:[0,1] neg_hi:[0,1]
	v_pk_add_f32 v[108:109], v[108:109], v[124:125]
	v_pk_mul_f32 v[196:197], v[194:195], v[176:177] op_sel:[1,0] op_sel_hi:[0,0]
	v_pk_fma_f32 v[202:203], v[194:195], v[176:177], v[196:197] op_sel:[0,1,0] neg_hi:[0,0,1]
	v_pk_add_f32 v[116:117], v[100:101], v[108:109]
	v_pk_add_f32 v[176:177], v[198:199], v[202:203] neg_lo:[0,1] neg_hi:[0,1]
	s_waitcnt lgkmcnt(0)
	v_xor_b32_e32 v99, 0x80000000, v192
	v_pk_mul_f32 v[194:195], v[184:185], v[176:177] op_sel:[1,1] op_sel_hi:[0,1]
	v_pk_fma_f32 v[196:197], v[184:185], v[176:177], v[194:195] op_sel_hi:[1,0,1] neg_lo:[0,0,1]
	v_pk_add_f32 v[100:101], v[100:101], v[108:109] neg_lo:[0,1] neg_hi:[0,1]
	v_pk_add_f32 v[176:177], v[104:105], v[120:121] neg_lo:[0,1] neg_hi:[0,1]
	v_pk_add_f32 v[104:105], v[104:105], v[120:121]
	v_pk_mul_f32 v[194:195], v[176:177], v[178:179] op_sel:[1,1] op_sel_hi:[1,0]
	v_pk_mul_f32 v[108:109], v[100:101], v[184:185] op_sel:[1,1] op_sel_hi:[1,0]
	v_pk_fma_f32 v[204:205], v[176:177], v[178:179], v[194:195] op_sel_hi:[0,1,1] neg_lo:[0,0,1]
	v_pk_add_f32 v[176:177], v[112:113], v[128:129] neg_lo:[0,1] neg_hi:[0,1]
	v_pk_add_f32 v[112:113], v[112:113], v[128:129]
	v_pk_mul_f32 v[194:195], v[176:177], v[178:179] op_sel:[1,0] op_sel_hi:[0,0]
	v_pk_fma_f32 v[206:207], v[176:177], v[178:179], v[194:195] op_sel:[0,1,0] neg_hi:[0,0,1]
	v_pk_add_f32 v[120:121], v[104:105], v[112:113]
	v_pk_add_f32 v[176:177], v[204:205], v[206:207] neg_lo:[0,1] neg_hi:[0,1]
	v_pk_add_f32 v[124:125], v[116:117], v[120:121]
	v_pk_mul_f32 v[178:179], v[184:185], v[176:177] op_sel_hi:[0,1]
	v_pk_fma_f32 v[194:195], v[184:185], v[176:177], v[178:179] op_sel:[1,0,1] op_sel_hi:[1,1,0] neg_hi:[0,0,1]
	v_pk_add_f32 v[116:117], v[116:117], v[120:121] neg_lo:[0,1] neg_hi:[0,1]
	v_pk_add_f32 v[176:177], v[196:197], v[194:195] neg_lo:[0,1] neg_hi:[0,1]
	v_pk_mul_f32 v[120:121], v[116:117], v[188:189] op_sel:[1,1] op_sel_hi:[1,0]
	v_pk_mul_f32 v[178:179], v[188:189], v[176:177] op_sel:[1,1] op_sel_hi:[0,1]
	v_pk_fma_f32 v[208:209], v[188:189], v[176:177], v[178:179] op_sel_hi:[1,0,1] neg_lo:[0,0,1]
	s_or_b32 s14, s0, s24
	v_pk_add_f32 v[176:177], v[102:103], v[118:119] neg_lo:[0,1] neg_hi:[0,1]
	v_pk_add_f32 v[102:103], v[102:103], v[118:119]
	v_pk_mul_f32 v[178:179], v[176:177], v[132:133] op_sel:[1,1] op_sel_hi:[1,0]
	s_nop 0
	s_lshl_b32 s90, s14, 9
	v_pk_fma_f32 v[220:221], v[176:177], v[132:133], v[178:179] op_sel_hi:[0,1,1] neg_lo:[0,0,1]
	v_pk_add_f32 v[176:177], v[110:111], v[126:127] neg_lo:[0,1] neg_hi:[0,1]
	v_pk_add_f32 v[110:111], v[110:111], v[126:127]
	v_pk_mul_f32 v[178:179], v[176:177], v[132:133] op_sel:[1,0] op_sel_hi:[0,0]
	v_pk_fma_f32 v[222:223], v[176:177], v[132:133], v[178:179] op_sel:[0,1,0] neg_hi:[0,0,1]
	v_pk_add_f32 v[118:119], v[102:103], v[110:111]
	v_pk_add_f32 v[132:133], v[220:221], v[222:223] neg_lo:[0,1] neg_hi:[0,1]
	v_pk_add_f32 v[102:103], v[102:103], v[110:111] neg_lo:[0,1] neg_hi:[0,1]
	v_pk_mul_f32 v[176:177], v[186:187], v[132:133] op_sel:[1,1] op_sel_hi:[0,1]
	v_pk_fma_f32 v[178:179], v[186:187], v[132:133], v[176:177] op_sel_hi:[1,0,1] neg_lo:[0,0,1]
	s_nop 0
	v_pk_add_f32 v[132:133], v[106:107], v[122:123] neg_lo:[0,1] neg_hi:[0,1]
	v_pk_add_f32 v[106:107], v[106:107], v[122:123]
	v_pk_mul_f32 v[176:177], v[132:133], v[182:183] op_sel:[1,1] op_sel_hi:[1,0]
	s_nop 0
	v_pk_fma_f32 v[224:225], v[132:133], v[182:183], v[176:177] op_sel_hi:[0,1,1] neg_lo:[0,0,1]
	v_pk_add_f32 v[132:133], v[114:115], v[130:131] neg_lo:[0,1] neg_hi:[0,1]
	v_pk_add_f32 v[114:115], v[114:115], v[130:131]
	v_pk_mul_f32 v[176:177], v[132:133], v[182:183] op_sel:[1,0] op_sel_hi:[0,0]
	v_pk_fma_f32 v[226:227], v[132:133], v[182:183], v[176:177] op_sel:[0,1,0] neg_hi:[0,0,1]
; template <int R, class XT, class TWT>
; __device__ __forceinline__ void dif_task(XT X, TWT tw, int s, int task) {
;     const int lgM = 13 - s, lgq = lgM - R, q = 1 << lgq;
;     const int j0 = task & (q - 1), blk = task >> lgq, base = (blk << lgM) + j0;
;     const int pb = PADI(base), qp = (q >= 32) ? q + (q >> 4) : q;
;     f32x2v v[1 << R];
; #pragma unroll
;     for (int k = 0; k < (1 << R); ++k) v[k] = X[pb + k * qp];
; #pragma unroll
;     for (int r = 0; r < R; ++r) {
;         const int pb = R - 1 - r;
; #pragma unroll
;         for (int k = 0; k < (1 << R); ++k) if (!((k >> pb) & 1)) {
;             const int klo = k & ((1 << pb) - 1);
;             const f32x2v w = tw[(j0 + (klo << lgq)) << (s + r)];
;             const f32x2v a = v[k], b = v[k + (1 << pb)], d = a - b;
;             v[k] = a + b; v[k + (1 << pb)] = (f32x2v){d.x * w.x - d.y * w.y, d.x * w.y + d.y * w.x};
;         }
;     }
; #pragma unroll
;     for (int k = 0; k < (1 << R); ++k) X[pb + k * qp] = v[k];
; }
	v_pk_add_f32 v[122:123], v[106:107], v[114:115]
	v_pk_add_f32 v[132:133], v[224:225], v[226:227] neg_lo:[0,1] neg_hi:[0,1]
	v_pk_add_f32 v[126:127], v[118:119], v[122:123]
	v_pk_mul_f32 v[176:177], v[190:191], v[132:133] op_sel_hi:[0,1]
	v_pk_fma_f32 v[182:183], v[190:191], v[132:133], v[176:177] op_sel:[1,0,1] op_sel_hi:[1,1,0] neg_hi:[0,0,1]
	v_pk_add_f32 v[128:129], v[124:125], v[126:127]
	v_pk_add_f32 v[132:133], v[178:179], v[182:183] neg_lo:[0,1] neg_hi:[0,1]
	v_pk_add_f32 v[124:125], v[124:125], v[126:127] neg_lo:[0,1] neg_hi:[0,1]
	v_pk_mul_f32 v[176:177], v[188:189], v[132:133] op_sel_hi:[0,1]
	v_pk_fma_f32 v[228:229], v[188:189], v[132:133], v[176:177] op_sel:[1,0,1] op_sel_hi:[1,1,0]
	v_pk_fma_f32 v[132:133], v[188:189], v[132:133], v[176:177] op_sel:[1,0,1] op_sel_hi:[1,1,0] neg_lo:[0,0,1] neg_hi:[0,0,1]
	v_cndmask_b32_e64 v177, v99, v193, s[44:45]
	v_cndmask_b32_e64 v176, v193, v192, s[44:45]
	v_pk_mul_f32 v[126:127], v[124:125], v[176:177] op_sel:[1,1] op_sel_hi:[1,0]
	v_mov_b32_e32 v229, v133
	v_pk_fma_f32 v[130:131], v[124:125], v[176:177], v[126:127] op_sel_hi:[0,1,1] neg_lo:[0,0,1]
	v_pk_fma_f32 v[124:125], v[116:117], v[188:189], v[120:121] op_sel_hi:[0,1,1] neg_lo:[0,0,1]
	v_pk_add_f32 v[116:117], v[118:119], v[122:123] neg_lo:[0,1] neg_hi:[0,1]
	v_pk_add_f32 v[132:133], v[208:209], v[228:229] neg_lo:[0,1] neg_hi:[0,1]
	v_pk_mul_f32 v[118:119], v[116:117], v[188:189] op_sel_hi:[1,0]
	v_mov_b32_e32 v99, s18
	v_pk_fma_f32 v[120:121], v[116:117], v[188:189], v[118:119] op_sel:[0,1,1] op_sel_hi:[1,1,0] neg_hi:[0,0,1]
	s_nop 0
	v_pk_add_f32 v[118:119], v[124:125], v[120:121] neg_lo:[0,1] neg_hi:[0,1]
	v_pk_add_f32 v[116:117], v[124:125], v[120:121]
	v_pk_mul_f32 v[120:121], v[176:177], v[118:119] op_sel:[1,1] op_sel_hi:[0,1]
	v_pk_fma_f32 v[122:123], v[176:177], v[118:119], v[120:121] op_sel_hi:[1,0,1] neg_lo:[0,0,1]
	s_nop 0
	v_pk_fma_f32 v[118:119], v[100:101], v[184:185], v[108:109] op_sel_hi:[0,1,1] neg_lo:[0,0,1]
	v_pk_add_f32 v[100:101], v[104:105], v[112:113] neg_lo:[0,1] neg_hi:[0,1]
	s_nop 0
	v_pk_mul_f32 v[104:105], v[100:101], v[184:185] op_sel_hi:[1,0]
	s_nop 0
	v_pk_fma_f32 v[108:109], v[100:101], v[184:185], v[104:105] op_sel:[0,1,1] op_sel_hi:[1,1,0]
	v_pk_fma_f32 v[100:101], v[100:101], v[184:185], v[104:105] op_sel:[0,1,1] op_sel_hi:[1,1,0] neg_lo:[0,0,1] neg_hi:[0,0,1]
	v_pk_mul_f32 v[104:105], v[102:103], v[186:187] op_sel:[1,1] op_sel_hi:[1,0]
	v_mov_b32_e32 v109, v101
	v_pk_fma_f32 v[110:111], v[102:103], v[186:187], v[104:105] op_sel_hi:[0,1,1] neg_lo:[0,0,1]
	v_pk_add_f32 v[102:103], v[106:107], v[114:115] neg_lo:[0,1] neg_hi:[0,1]
	v_pk_add_f32 v[100:101], v[118:119], v[108:109]
	v_pk_mul_f32 v[104:105], v[102:103], v[190:191] op_sel_hi:[1,0]
	v_pk_add_f32 v[114:115], v[220:221], v[222:223]
	v_pk_fma_f32 v[106:107], v[102:103], v[190:191], v[104:105] op_sel:[0,1,1] op_sel_hi:[1,1,0] neg_hi:[0,0,1]
	s_nop 0
	v_pk_add_f32 v[102:103], v[110:111], v[106:107]
	s_nop 0
	v_pk_add_f32 v[104:105], v[100:101], v[102:103]
	v_pk_add_f32 v[100:101], v[100:101], v[102:103] neg_lo:[0,1] neg_hi:[0,1]
	s_nop 0
	v_pk_mul_f32 v[102:103], v[176:177], v[100:101] op_sel:[1,1] op_sel_hi:[0,1]
	v_pk_fma_f32 v[112:113], v[176:177], v[100:101], v[102:103] op_sel_hi:[1,0,1] neg_lo:[0,0,1]
	s_nop 0
	v_pk_add_f32 v[100:101], v[118:119], v[108:109] neg_lo:[0,1] neg_hi:[0,1]
	v_pk_add_f32 v[118:119], v[224:225], v[226:227]
	v_pk_mul_f32 v[102:103], v[188:189], v[100:101] op_sel:[1,1] op_sel_hi:[0,1]
	v_pk_fma_f32 v[108:109], v[188:189], v[100:101], v[102:103] op_sel_hi:[1,0,1] neg_lo:[0,0,1]
	v_pk_add_f32 v[120:121], v[114:115], v[118:119]
	v_pk_add_f32 v[100:101], v[110:111], v[106:107] neg_lo:[0,1] neg_hi:[0,1]
	s_nop 0
	v_pk_mul_f32 v[102:103], v[188:189], v[100:101] op_sel_hi:[0,1]
	v_pk_fma_f32 v[106:107], v[188:189], v[100:101], v[102:103] op_sel:[1,0,1] op_sel_hi:[1,1,0] neg_hi:[0,0,1]
	s_nop 0
	v_pk_add_f32 v[102:103], v[108:109], v[106:107] neg_lo:[0,1] neg_hi:[0,1]
	v_pk_add_f32 v[100:101], v[108:109], v[106:107]
	v_pk_mul_f32 v[106:107], v[176:177], v[102:103] op_sel:[1,1] op_sel_hi:[0,1]
	v_pk_fma_f32 v[108:109], v[176:177], v[102:103], v[106:107] neg_lo:[0,0,1] neg_hi:[0,0,1]
	v_pk_fma_f32 v[102:103], v[176:177], v[102:103], v[106:107] op_sel_hi:[1,0,1]
	v_pk_add_f32 v[106:107], v[204:205], v[206:207]
	v_mov_b32_e32 v109, v103
	v_pk_add_f32 v[102:103], v[198:199], v[202:203]
	s_nop 0
	v_pk_add_f32 v[110:111], v[102:103], v[106:107]
	v_pk_add_f32 v[102:103], v[102:103], v[106:107] neg_lo:[0,1] neg_hi:[0,1]
	v_pk_add_f32 v[124:125], v[110:111], v[120:121]
	v_pk_add_f32 v[110:111], v[110:111], v[120:121] neg_lo:[0,1] neg_hi:[0,1]
	v_pk_mul_f32 v[106:107], v[188:189], v[102:103] op_sel:[1,1] op_sel_hi:[0,1]
	v_pk_mul_f32 v[120:121], v[110:111], v[176:177] op_sel:[1,1] op_sel_hi:[1,0]
	s_nop 0
	v_pk_fma_f32 v[126:127], v[110:111], v[176:177], v[120:121] op_sel_hi:[0,1,1] neg_lo:[0,0,1]
	v_pk_fma_f32 v[110:111], v[188:189], v[102:103], v[106:107] op_sel_hi:[1,0,1] neg_lo:[0,0,1]
	s_nop 0
	v_pk_add_f32 v[102:103], v[114:115], v[118:119] neg_lo:[0,1] neg_hi:[0,1]
	s_nop 0
	v_pk_mul_f32 v[106:107], v[188:189], v[102:103] op_sel_hi:[0,1]
	v_pk_fma_f32 v[114:115], v[188:189], v[102:103], v[106:107] op_sel:[1,0,1] op_sel_hi:[1,1,0] neg_hi:[0,0,1]
	s_nop 0
	v_pk_add_f32 v[106:107], v[110:111], v[114:115] neg_lo:[0,1] neg_hi:[0,1]
	v_pk_add_f32 v[102:103], v[110:111], v[114:115]
	v_pk_mul_f32 v[110:111], v[176:177], v[106:107] op_sel:[1,1] op_sel_hi:[0,1]
	v_pk_fma_f32 v[114:115], v[176:177], v[106:107], v[110:111] neg_lo:[0,0,1] neg_hi:[0,0,1]
	v_pk_fma_f32 v[106:107], v[176:177], v[106:107], v[110:111] op_sel_hi:[1,0,1]
	v_pk_add_f32 v[110:111], v[178:179], v[182:183]
	v_mov_b32_e32 v115, v107
	v_pk_add_f32 v[106:107], v[196:197], v[194:195]
	s_nop 0
	v_pk_add_f32 v[118:119], v[106:107], v[110:111]
	v_pk_add_f32 v[106:107], v[106:107], v[110:111] neg_lo:[0,1] neg_hi:[0,1]
	s_nop 0
	v_pk_mul_f32 v[110:111], v[176:177], v[106:107] op_sel:[1,1] op_sel_hi:[0,1]
	v_pk_fma_f32 v[120:121], v[176:177], v[106:107], v[110:111] neg_lo:[0,0,1] neg_hi:[0,0,1]
	v_pk_fma_f32 v[106:107], v[176:177], v[106:107], v[110:111] op_sel_hi:[1,0,1]
	v_pk_mul_f32 v[110:111], v[176:177], v[132:133] op_sel:[1,1] op_sel_hi:[0,1]
	v_pk_fma_f32 v[178:179], v[176:177], v[132:133], v[110:111] op_sel_hi:[1,0,1] neg_lo:[0,0,1]
	v_mov_b32_e32 v121, v107
	v_pk_add_f32 v[106:107], v[208:209], v[228:229]
	ds_write2_b64 v135, v[128:129], v[130:131] offset1:34
	ds_write2_b64 v135, v[116:117], v[122:123] offset0:68 offset1:102
	ds_write2_b64 v135, v[104:105], v[112:113] offset0:136 offset1:170
	ds_write2_b64 v135, v[100:101], v[108:109] offset0:204 offset1:238
	ds_write2_b64 v98, v[124:125], v[126:127] offset0:16 offset1:50
	ds_write2_b64 v98, v[102:103], v[114:115] offset0:84 offset1:118
	ds_write2_b64 v98, v[118:119], v[120:121] offset0:152 offset1:186
	ds_write2_b64 v98, v[106:107], v[178:179] offset0:220 offset1:254
	s_waitcnt lgkmcnt(0)
	s_barrier
; template <int R, class XT, class TWT>
; __device__ __forceinline__ void dif_task(XT X, TWT tw, int s, int task) {
;     const int lgM = 13 - s, lgq = lgM - R, q = 1 << lgq;
;     const int j0 = task & (q - 1), blk = task >> lgq, base = (blk << lgM) + j0;
;     const int pb = PADI(base), qp = (q >= 32) ? q + (q >> 4) : q;
;     f32x2v v[1 << R];
; #pragma unroll
;     for (int k = 0; k < (1 << R); ++k) v[k] = X[pb + k * qp];
; #pragma unroll
;     for (int r = 0; r < R; ++r) {
;         const int pb = R - 1 - r;
; #pragma unroll
;         for (int k = 0; k < (1 << R); ++k) if (!((k >> pb) & 1)) {
;             const int klo = k & ((1 << pb) - 1);
;             const f32x2v w = tw[(j0 + (klo << lgq)) << (s + r)];
;             const f32x2v a = v[k], b = v[k + (1 << pb)], d = a - b;
;             v[k] = a + b; v[k + (1 << pb)] = (f32x2v){d.x * w.x - d.y * w.y, d.x * w.y + d.y * w.x};
;         }
;     }
; #pragma unroll
;     for (int k = 0; k < (1 << R); ++k) X[pb + k * qp] = v[k];
; }
	ds_read2_b64 v[100:103], v137 offset1:2
	ds_read2_b64 v[104:107], v137 offset0:4 offset1:6
	ds_read2_b64 v[108:111], v137 offset0:8 offset1:10
	ds_read2_b64 v[112:115], v137 offset0:12 offset1:14
	ds_read2_b64 v[116:119], v137 offset0:16 offset1:18
	ds_read2_b64 v[120:123], v137 offset0:20 offset1:22
	ds_read2_b64 v[124:127], v137 offset0:24 offset1:26
	ds_read2_b64 v[128:131], v137 offset0:28 offset1:30
	ds_read2st64_b64 v[176:179], v170 offset1:16
	ds_read_b64 v[132:133], v171
	ds_read_b64 v[182:183], v172
	ds_read_b64 v[184:185], v173
	ds_read_b64 v[186:187], v156
	s_waitcnt lgkmcnt(8)
	v_pk_add_f32 v[194:195], v[100:101], v[116:117] neg_lo:[0,1] neg_hi:[0,1]
	ds_read_b64 v[188:189], v174
	ds_read_b64 v[190:191], v175
	ds_read_b64 v[192:193], v99
	s_waitcnt lgkmcnt(7)
	v_pk_mul_f32 v[196:197], v[194:195], v[176:177] op_sel:[1,1] op_sel_hi:[1,0]
	v_pk_add_f32 v[100:101], v[100:101], v[116:117]
	v_pk_fma_f32 v[198:199], v[194:195], v[176:177], v[196:197] op_sel_hi:[0,1,1] neg_lo:[0,0,1]
	v_pk_add_f32 v[194:195], v[108:109], v[124:125] neg_lo:[0,1] neg_hi:[0,1]
	v_pk_add_f32 v[108:109], v[108:109], v[124:125]
	v_pk_mul_f32 v[196:197], v[194:195], v[176:177] op_sel:[1,0] op_sel_hi:[0,0]
	v_pk_fma_f32 v[202:203], v[194:195], v[176:177], v[196:197] op_sel:[0,1,0] neg_hi:[0,0,1]
	v_pk_add_f32 v[116:117], v[100:101], v[108:109]
	v_pk_add_f32 v[176:177], v[198:199], v[202:203] neg_lo:[0,1] neg_hi:[0,1]
	v_pk_add_f32 v[100:101], v[100:101], v[108:109] neg_lo:[0,1] neg_hi:[0,1]
	s_waitcnt lgkmcnt(4)
	v_pk_mul_f32 v[194:195], v[184:185], v[176:177] op_sel:[1,1] op_sel_hi:[0,1]
	v_pk_fma_f32 v[196:197], v[184:185], v[176:177], v[194:195] op_sel_hi:[1,0,1] neg_lo:[0,0,1]
	v_pk_mul_f32 v[108:109], v[100:101], v[184:185] op_sel:[1,1] op_sel_hi:[1,0]
	v_pk_add_f32 v[176:177], v[104:105], v[120:121] neg_lo:[0,1] neg_hi:[0,1]
	v_pk_add_f32 v[104:105], v[104:105], v[120:121]
	v_pk_mul_f32 v[194:195], v[176:177], v[178:179] op_sel:[1,1] op_sel_hi:[1,0]
	s_nop 0
	v_pk_fma_f32 v[204:205], v[176:177], v[178:179], v[194:195] op_sel_hi:[0,1,1] neg_lo:[0,0,1]
	v_pk_add_f32 v[176:177], v[112:113], v[128:129] neg_lo:[0,1] neg_hi:[0,1]
	v_pk_add_f32 v[112:113], v[112:113], v[128:129]
	v_pk_mul_f32 v[194:195], v[176:177], v[178:179] op_sel:[1,0] op_sel_hi:[0,0]
	v_pk_fma_f32 v[206:207], v[176:177], v[178:179], v[194:195] op_sel:[0,1,0] neg_hi:[0,0,1]
	v_pk_add_f32 v[120:121], v[104:105], v[112:113]
	v_pk_add_f32 v[176:177], v[204:205], v[206:207] neg_lo:[0,1] neg_hi:[0,1]
	v_pk_add_f32 v[124:125], v[116:117], v[120:121]
	v_pk_mul_f32 v[178:179], v[184:185], v[176:177] op_sel_hi:[0,1]
	v_pk_fma_f32 v[194:195], v[184:185], v[176:177], v[178:179] op_sel:[1,0,1] op_sel_hi:[1,1,0] neg_hi:[0,0,1]
	v_pk_add_f32 v[116:117], v[116:117], v[120:121] neg_lo:[0,1] neg_hi:[0,1]
	v_pk_add_f32 v[176:177], v[196:197], v[194:195] neg_lo:[0,1] neg_hi:[0,1]
	s_waitcnt lgkmcnt(1)
	v_pk_mul_f32 v[120:121], v[116:117], v[190:191] op_sel:[1,1] op_sel_hi:[1,0]
	v_pk_mul_f32 v[178:179], v[190:191], v[176:177] op_sel:[1,1] op_sel_hi:[0,1]
	v_pk_fma_f32 v[208:209], v[190:191], v[176:177], v[178:179] op_sel_hi:[1,0,1] neg_lo:[0,0,1]
	s_nop 0
	v_pk_add_f32 v[176:177], v[102:103], v[118:119] neg_lo:[0,1] neg_hi:[0,1]
	v_pk_add_f32 v[102:103], v[102:103], v[118:119]
	v_pk_mul_f32 v[178:179], v[176:177], v[132:133] op_sel:[1,1] op_sel_hi:[1,0]
	s_nop 0
	v_pk_fma_f32 v[220:221], v[176:177], v[132:133], v[178:179] op_sel_hi:[0,1,1] neg_lo:[0,0,1]
	v_pk_add_f32 v[176:177], v[110:111], v[126:127] neg_lo:[0,1] neg_hi:[0,1]
	v_pk_add_f32 v[110:111], v[110:111], v[126:127]
	v_pk_mul_f32 v[178:179], v[176:177], v[132:133] op_sel:[1,0] op_sel_hi:[0,0]
	v_pk_fma_f32 v[222:223], v[176:177], v[132:133], v[178:179] op_sel:[0,1,0] neg_hi:[0,0,1]
	v_pk_add_f32 v[118:119], v[102:103], v[110:111]
	v_pk_add_f32 v[132:133], v[220:221], v[222:223] neg_lo:[0,1] neg_hi:[0,1]
	v_pk_add_f32 v[102:103], v[102:103], v[110:111] neg_lo:[0,1] neg_hi:[0,1]
	v_pk_mul_f32 v[176:177], v[188:189], v[132:133] op_sel:[1,1] op_sel_hi:[0,1]
	v_pk_fma_f32 v[178:179], v[188:189], v[132:133], v[176:177] op_sel_hi:[1,0,1] neg_lo:[0,0,1]
	s_nop 0
	v_pk_add_f32 v[132:133], v[106:107], v[122:123] neg_lo:[0,1] neg_hi:[0,1]
	v_pk_add_f32 v[106:107], v[106:107], v[122:123]
	v_pk_mul_f32 v[176:177], v[132:133], v[182:183] op_sel:[1,1] op_sel_hi:[1,0]
	s_nop 0
	v_pk_fma_f32 v[224:225], v[132:133], v[182:183], v[176:177] op_sel_hi:[0,1,1] neg_lo:[0,0,1]
	v_pk_add_f32 v[132:133], v[114:115], v[130:131] neg_lo:[0,1] neg_hi:[0,1]
	v_pk_add_f32 v[114:115], v[114:115], v[130:131]
	v_pk_mul_f32 v[176:177], v[132:133], v[182:183] op_sel:[1,0] op_sel_hi:[0,0]
	v_pk_fma_f32 v[226:227], v[132:133], v[182:183], v[176:177] op_sel:[0,1,0] neg_hi:[0,0,1]
	v_pk_add_f32 v[122:123], v[106:107], v[114:115]
	v_pk_add_f32 v[132:133], v[224:225], v[226:227] neg_lo:[0,1] neg_hi:[0,1]
	v_pk_add_f32 v[126:127], v[118:119], v[122:123]
	v_pk_mul_f32 v[176:177], v[186:187], v[132:133] op_sel_hi:[0,1]
	v_pk_fma_f32 v[182:183], v[186:187], v[132:133], v[176:177] op_sel:[1,0,1] op_sel_hi:[1,1,0] neg_hi:[0,0,1]
	v_pk_add_f32 v[128:129], v[124:125], v[126:127]
	v_pk_add_f32 v[132:133], v[178:179], v[182:183] neg_lo:[0,1] neg_hi:[0,1]
	v_pk_add_f32 v[124:125], v[124:125], v[126:127] neg_lo:[0,1] neg_hi:[0,1]
	v_pk_mul_f32 v[176:177], v[190:191], v[132:133] op_sel_hi:[0,1]
	v_pk_fma_f32 v[228:229], v[190:191], v[132:133], v[176:177] op_sel:[1,0,1] op_sel_hi:[1,1,0]
	v_pk_fma_f32 v[132:133], v[190:191], v[132:133], v[176:177] op_sel:[1,0,1] op_sel_hi:[1,1,0] neg_lo:[0,0,1] neg_hi:[0,0,1]
	s_waitcnt lgkmcnt(0)
; template <int R, class XT, class TWT>
; __device__ __forceinline__ void dif_task(XT X, TWT tw, int s, int task) {
;     const int lgM = 13 - s, lgq = lgM - R, q = 1 << lgq;
;     const int j0 = task & (q - 1), blk = task >> lgq, base = (blk << lgM) + j0;
;     const int pb = PADI(base), qp = (q >= 32) ? q + (q >> 4) : q;
;     f32x2v v[1 << R];
; #pragma unroll
;     for (int k = 0; k < (1 << R); ++k) v[k] = X[pb + k * qp];
; #pragma unroll
;     for (int r = 0; r < R; ++r) {
;         const int pb = R - 1 - r;
; #pragma unroll
;         for (int k = 0; k < (1 << R); ++k) if (!((k >> pb) & 1)) {
;             const int klo = k & ((1 << pb) - 1);
;             const f32x2v w = tw[(j0 + (klo << lgq)) << (s + r)];
;             const f32x2v a = v[k], b = v[k + (1 << pb)], d = a - b;
;             v[k] = a + b; v[k + (1 << pb)] = (f32x2v){d.x * w.x - d.y * w.y, d.x * w.y + d.y * w.x};
;         }
;     }
; #pragma unroll
;     for (int k = 0; k < (1 << R); ++k) X[pb + k * qp] = v[k];
; }
	v_xor_b32_e32 v176, 0x80000000, v192
	v_cndmask_b32_e64 v177, v176, v193, s[42:43]
	v_cndmask_b32_e64 v176, v193, v192, s[42:43]
	v_pk_mul_f32 v[126:127], v[124:125], v[176:177] op_sel:[1,1] op_sel_hi:[1,0]
	v_mov_b32_e32 v229, v133
	v_pk_fma_f32 v[130:131], v[124:125], v[176:177], v[126:127] op_sel_hi:[0,1,1] neg_lo:[0,0,1]
	v_pk_fma_f32 v[124:125], v[116:117], v[190:191], v[120:121] op_sel_hi:[0,1,1] neg_lo:[0,0,1]
	v_pk_add_f32 v[116:117], v[118:119], v[122:123] neg_lo:[0,1] neg_hi:[0,1]
	v_pk_add_f32 v[132:133], v[208:209], v[228:229] neg_lo:[0,1] neg_hi:[0,1]
	v_pk_mul_f32 v[118:119], v[116:117], v[190:191] op_sel_hi:[1,0]
	s_nop 0
	v_pk_fma_f32 v[120:121], v[116:117], v[190:191], v[118:119] op_sel:[0,1,1] op_sel_hi:[1,1,0] neg_hi:[0,0,1]
	s_nop 0
	v_pk_add_f32 v[118:119], v[124:125], v[120:121] neg_lo:[0,1] neg_hi:[0,1]
	v_pk_add_f32 v[116:117], v[124:125], v[120:121]
	v_pk_mul_f32 v[120:121], v[176:177], v[118:119] op_sel:[1,1] op_sel_hi:[0,1]
	v_pk_fma_f32 v[122:123], v[176:177], v[118:119], v[120:121] op_sel_hi:[1,0,1] neg_lo:[0,0,1]
	s_nop 0
	v_pk_fma_f32 v[118:119], v[100:101], v[184:185], v[108:109] op_sel_hi:[0,1,1] neg_lo:[0,0,1]
	v_pk_add_f32 v[100:101], v[104:105], v[112:113] neg_lo:[0,1] neg_hi:[0,1]
	s_nop 0
	v_pk_mul_f32 v[104:105], v[100:101], v[184:185] op_sel_hi:[1,0]
	s_nop 0
	v_pk_fma_f32 v[108:109], v[100:101], v[184:185], v[104:105] op_sel:[0,1,1] op_sel_hi:[1,1,0]
	v_pk_fma_f32 v[100:101], v[100:101], v[184:185], v[104:105] op_sel:[0,1,1] op_sel_hi:[1,1,0] neg_lo:[0,0,1] neg_hi:[0,0,1]
	v_pk_mul_f32 v[104:105], v[102:103], v[188:189] op_sel:[1,1] op_sel_hi:[1,0]
	v_mov_b32_e32 v109, v101
	v_pk_fma_f32 v[110:111], v[102:103], v[188:189], v[104:105] op_sel_hi:[0,1,1] neg_lo:[0,0,1]
	v_pk_add_f32 v[102:103], v[106:107], v[114:115] neg_lo:[0,1] neg_hi:[0,1]
	v_pk_add_f32 v[100:101], v[118:119], v[108:109]
	v_pk_mul_f32 v[104:105], v[102:103], v[186:187] op_sel_hi:[1,0]
	v_pk_add_f32 v[114:115], v[220:221], v[222:223]
	v_pk_fma_f32 v[106:107], v[102:103], v[186:187], v[104:105] op_sel:[0,1,1] op_sel_hi:[1,1,0] neg_hi:[0,0,1]
	s_nop 0
	v_pk_add_f32 v[102:103], v[110:111], v[106:107]
	s_nop 0
	v_pk_add_f32 v[104:105], v[100:101], v[102:103]
	v_pk_add_f32 v[100:101], v[100:101], v[102:103] neg_lo:[0,1] neg_hi:[0,1]
	s_nop 0
	v_pk_mul_f32 v[102:103], v[176:177], v[100:101] op_sel:[1,1] op_sel_hi:[0,1]
	v_pk_fma_f32 v[112:113], v[176:177], v[100:101], v[102:103] op_sel_hi:[1,0,1] neg_lo:[0,0,1]
	s_nop 0
	v_pk_add_f32 v[100:101], v[118:119], v[108:109] neg_lo:[0,1] neg_hi:[0,1]
	v_pk_add_f32 v[118:119], v[224:225], v[226:227]
	v_pk_mul_f32 v[102:103], v[190:191], v[100:101] op_sel:[1,1] op_sel_hi:[0,1]
	v_pk_fma_f32 v[108:109], v[190:191], v[100:101], v[102:103] op_sel_hi:[1,0,1] neg_lo:[0,0,1]
	v_pk_add_f32 v[120:121], v[114:115], v[118:119]
	v_pk_add_f32 v[100:101], v[110:111], v[106:107] neg_lo:[0,1] neg_hi:[0,1]
	s_nop 0
	v_pk_mul_f32 v[102:103], v[190:191], v[100:101] op_sel_hi:[0,1]
	v_pk_fma_f32 v[106:107], v[190:191], v[100:101], v[102:103] op_sel:[1,0,1] op_sel_hi:[1,1,0] neg_hi:[0,0,1]
	s_nop 0
	v_pk_add_f32 v[102:103], v[108:109], v[106:107] neg_lo:[0,1] neg_hi:[0,1]
	v_pk_add_f32 v[100:101], v[108:109], v[106:107]
	v_pk_mul_f32 v[106:107], v[176:177], v[102:103] op_sel:[1,1] op_sel_hi:[0,1]
	v_pk_fma_f32 v[108:109], v[176:177], v[102:103], v[106:107] neg_lo:[0,0,1] neg_hi:[0,0,1]
	v_pk_fma_f32 v[102:103], v[176:177], v[102:103], v[106:107] op_sel_hi:[1,0,1]
	v_pk_add_f32 v[106:107], v[204:205], v[206:207]
	v_mov_b32_e32 v109, v103
	v_pk_add_f32 v[102:103], v[198:199], v[202:203]
	s_nop 0
	v_pk_add_f32 v[110:111], v[102:103], v[106:107]
	v_pk_add_f32 v[102:103], v[102:103], v[106:107] neg_lo:[0,1] neg_hi:[0,1]
	v_pk_add_f32 v[124:125], v[110:111], v[120:121]
	v_pk_add_f32 v[110:111], v[110:111], v[120:121] neg_lo:[0,1] neg_hi:[0,1]
	v_pk_mul_f32 v[106:107], v[190:191], v[102:103] op_sel:[1,1] op_sel_hi:[0,1]
	v_pk_mul_f32 v[120:121], v[110:111], v[176:177] op_sel:[1,1] op_sel_hi:[1,0]
	s_nop 0
	v_pk_fma_f32 v[126:127], v[110:111], v[176:177], v[120:121] op_sel_hi:[0,1,1] neg_lo:[0,0,1]
	v_pk_fma_f32 v[110:111], v[190:191], v[102:103], v[106:107] op_sel_hi:[1,0,1] neg_lo:[0,0,1]
	s_nop 0
	v_pk_add_f32 v[102:103], v[114:115], v[118:119] neg_lo:[0,1] neg_hi:[0,1]
	s_nop 0
	v_pk_mul_f32 v[106:107], v[190:191], v[102:103] op_sel_hi:[0,1]
	v_pk_fma_f32 v[114:115], v[190:191], v[102:103], v[106:107] op_sel:[1,0,1] op_sel_hi:[1,1,0] neg_hi:[0,0,1]
	s_nop 0
	v_pk_add_f32 v[106:107], v[110:111], v[114:115] neg_lo:[0,1] neg_hi:[0,1]
	v_pk_add_f32 v[102:103], v[110:111], v[114:115]
	v_pk_mul_f32 v[110:111], v[176:177], v[106:107] op_sel:[1,1] op_sel_hi:[0,1]
	v_pk_fma_f32 v[114:115], v[176:177], v[106:107], v[110:111] neg_lo:[0,0,1] neg_hi:[0,0,1]
	v_pk_fma_f32 v[106:107], v[176:177], v[106:107], v[110:111] op_sel_hi:[1,0,1]
	v_pk_add_f32 v[110:111], v[178:179], v[182:183]
	v_mov_b32_e32 v115, v107
	v_pk_add_f32 v[106:107], v[196:197], v[194:195]
	s_nop 0
	v_pk_add_f32 v[118:119], v[106:107], v[110:111]
	v_pk_add_f32 v[106:107], v[106:107], v[110:111] neg_lo:[0,1] neg_hi:[0,1]
	s_nop 0
	v_pk_mul_f32 v[110:111], v[176:177], v[106:107] op_sel:[1,1] op_sel_hi:[0,1]
	v_pk_fma_f32 v[120:121], v[176:177], v[106:107], v[110:111] neg_lo:[0,0,1] neg_hi:[0,0,1]
	v_pk_fma_f32 v[106:107], v[176:177], v[106:107], v[110:111] op_sel_hi:[1,0,1]
	v_pk_mul_f32 v[110:111], v[176:177], v[132:133] op_sel:[1,1] op_sel_hi:[0,1]
	v_pk_fma_f32 v[178:179], v[176:177], v[132:133], v[110:111] op_sel_hi:[1,0,1] neg_lo:[0,0,1]
	v_mov_b32_e32 v121, v107
	v_pk_add_f32 v[106:107], v[208:209], v[228:229]
	ds_write2_b64 v137, v[128:129], v[130:131] offset1:2
	ds_write2_b64 v137, v[116:117], v[122:123] offset0:4 offset1:6
	ds_write2_b64 v137, v[104:105], v[112:113] offset0:8 offset1:10
	ds_write2_b64 v137, v[100:101], v[108:109] offset0:12 offset1:14
	ds_write2_b64 v137, v[124:125], v[126:127] offset0:16 offset1:18
	ds_write2_b64 v137, v[102:103], v[114:115] offset0:20 offset1:22
	ds_write2_b64 v137, v[118:119], v[120:121] offset0:24 offset1:26
	ds_write2_b64 v137, v[106:107], v[178:179] offset0:28 offset1:30
	s_waitcnt lgkmcnt(0)
	s_barrier
; template <bool LAT>
; __device__ __forceinline__ void hyconv_unit(const Frame& F, LAS f32x2v* X, const TwHalf tw, LAS bf16* OUT, const float* skip, bf16* MIX, int u) {
;     ...
;             for (int r = 0; r < 8; ++r) { const int e = 2 * (F.tid + 512 * r);
;                 const f32x2v a = X[PADI(e)], b = X[PADI(e + 1)]; const f32x4 k = kq[r];
;                 const f32x2v p = a + b, q = a - b; const f32x2v pk = (f32x2v){p.x * k.x - p.y * k.y, p.x * k.y + p.y * k.x}, qk = (f32x2v){q.x * k.z - q.y * k.w, q.x * k.w + q.y * k.z};
;                 X[PADI(e)] = pk + qk; X[PADI(e + 1)] = pk - qk; }
	ds_read_b128 v[100:103], v157
	s_waitcnt lgkmcnt(0)
	v_pk_add_f32 v[104:105], v[100:101], v[102:103]
	v_pk_add_f32 v[100:101], v[100:101], v[102:103] neg_lo:[0,1] neg_hi:[0,1]
	s_waitcnt vmcnt(7)
	v_pk_mul_f32 v[102:103], v[28:29], v[104:105] op_sel:[1,1] op_sel_hi:[0,1]
	v_pk_fma_f32 v[106:107], v[28:29], v[104:105], v[102:103] op_sel_hi:[1,0,1] neg_lo:[0,0,1]
	s_nop 0
	v_pk_mul_f32 v[28:29], v[30:31], v[100:101] op_sel:[1,1] op_sel_hi:[0,1]
	v_pk_fma_f32 v[102:103], v[30:31], v[100:101], v[28:29] op_sel_hi:[1,0,1] neg_lo:[0,0,1]
	s_nop 0
	v_pk_add_f32 v[28:29], v[106:107], v[102:103]
	v_pk_add_f32 v[30:31], v[106:107], v[102:103] neg_lo:[0,1] neg_hi:[0,1]
	ds_write_b128 v157, v[28:31]
	ds_read_b128 v[28:31], v158 offset:8192
	s_waitcnt lgkmcnt(0)
	v_pk_add_f32 v[100:101], v[28:29], v[30:31]
	v_pk_add_f32 v[28:29], v[28:29], v[30:31] neg_lo:[0,1] neg_hi:[0,1]
	s_waitcnt vmcnt(6)
	v_pk_mul_f32 v[30:31], v[24:25], v[100:101] op_sel:[1,1] op_sel_hi:[0,1]
	v_pk_fma_f32 v[102:103], v[24:25], v[100:101], v[30:31] op_sel_hi:[1,0,1] neg_lo:[0,0,1]
	s_nop 0
	v_pk_mul_f32 v[24:25], v[26:27], v[28:29] op_sel:[1,1] op_sel_hi:[0,1]
	v_pk_fma_f32 v[30:31], v[26:27], v[28:29], v[24:25] op_sel_hi:[1,0,1] neg_lo:[0,0,1]
	s_nop 0
	v_pk_add_f32 v[24:25], v[102:103], v[30:31]
	v_pk_add_f32 v[26:27], v[102:103], v[30:31] neg_lo:[0,1] neg_hi:[0,1]
	ds_write_b128 v158, v[24:27] offset:8192
	ds_read_b128 v[24:27], v159 offset:16384
	s_waitcnt lgkmcnt(0)
	v_pk_add_f32 v[28:29], v[24:25], v[26:27]
	v_pk_add_f32 v[24:25], v[24:25], v[26:27] neg_lo:[0,1] neg_hi:[0,1]
	s_waitcnt vmcnt(5)
	v_pk_mul_f32 v[26:27], v[20:21], v[28:29] op_sel:[1,1] op_sel_hi:[0,1]
	v_pk_fma_f32 v[30:31], v[20:21], v[28:29], v[26:27] op_sel_hi:[1,0,1] neg_lo:[0,0,1]
	s_nop 0
	v_pk_mul_f32 v[20:21], v[22:23], v[24:25] op_sel:[1,1] op_sel_hi:[0,1]
	v_pk_fma_f32 v[26:27], v[22:23], v[24:25], v[20:21] op_sel_hi:[1,0,1] neg_lo:[0,0,1]
	s_nop 0
	v_pk_add_f32 v[20:21], v[30:31], v[26:27]
	v_pk_add_f32 v[22:23], v[30:31], v[26:27] neg_lo:[0,1] neg_hi:[0,1]
	ds_write_b128 v159, v[20:23] offset:16384
	ds_read_b128 v[20:23], v160 offset:24576
	s_waitcnt lgkmcnt(0)
	v_pk_add_f32 v[24:25], v[20:21], v[22:23]
	v_pk_add_f32 v[20:21], v[20:21], v[22:23] neg_lo:[0,1] neg_hi:[0,1]
	s_waitcnt vmcnt(4)
	v_pk_mul_f32 v[22:23], v[16:17], v[24:25] op_sel:[1,1] op_sel_hi:[0,1]
	v_pk_fma_f32 v[26:27], v[16:17], v[24:25], v[22:23] op_sel_hi:[1,0,1] neg_lo:[0,0,1]
	s_nop 0
	v_pk_mul_f32 v[16:17], v[18:19], v[20:21] op_sel:[1,1] op_sel_hi:[0,1]
	v_pk_fma_f32 v[22:23], v[18:19], v[20:21], v[16:17] op_sel_hi:[1,0,1] neg_lo:[0,0,1]
	s_nop 0
	v_pk_add_f32 v[16:17], v[26:27], v[22:23]
	v_pk_add_f32 v[18:19], v[26:27], v[22:23] neg_lo:[0,1] neg_hi:[0,1]
	ds_write_b128 v160, v[16:19] offset:24576
	ds_read_b128 v[16:19], v161 offset:32768
	s_waitcnt lgkmcnt(0)
	v_pk_add_f32 v[20:21], v[16:17], v[18:19]
	v_pk_add_f32 v[16:17], v[16:17], v[18:19] neg_lo:[0,1] neg_hi:[0,1]
	s_waitcnt vmcnt(3)
	v_pk_mul_f32 v[18:19], v[12:13], v[20:21] op_sel:[1,1] op_sel_hi:[0,1]
	v_pk_fma_f32 v[22:23], v[12:13], v[20:21], v[18:19] op_sel_hi:[1,0,1] neg_lo:[0,0,1]
	s_nop 0
	v_pk_mul_f32 v[12:13], v[14:15], v[16:17] op_sel:[1,1] op_sel_hi:[0,1]
	v_pk_fma_f32 v[18:19], v[14:15], v[16:17], v[12:13] op_sel_hi:[1,0,1] neg_lo:[0,0,1]
	s_nop 0
	v_pk_add_f32 v[12:13], v[22:23], v[18:19]
	v_pk_add_f32 v[14:15], v[22:23], v[18:19] neg_lo:[0,1] neg_hi:[0,1]
	ds_write_b128 v161, v[12:15] offset:32768
	ds_read_b128 v[12:15], v162 offset:40960
	s_waitcnt lgkmcnt(0)
	v_pk_add_f32 v[16:17], v[12:13], v[14:15]
	v_pk_add_f32 v[12:13], v[12:13], v[14:15] neg_lo:[0,1] neg_hi:[0,1]
	s_waitcnt vmcnt(2)
	v_pk_mul_f32 v[14:15], v[8:9], v[16:17] op_sel:[1,1] op_sel_hi:[0,1]
	v_pk_fma_f32 v[18:19], v[8:9], v[16:17], v[14:15] op_sel_hi:[1,0,1] neg_lo:[0,0,1]
	s_nop 0
	v_pk_mul_f32 v[8:9], v[10:11], v[12:13] op_sel:[1,1] op_sel_hi:[0,1]
	v_pk_fma_f32 v[14:15], v[10:11], v[12:13], v[8:9] op_sel_hi:[1,0,1] neg_lo:[0,0,1]
	s_nop 0
	v_pk_add_f32 v[8:9], v[18:19], v[14:15]
	v_pk_add_f32 v[10:11], v[18:19], v[14:15] neg_lo:[0,1] neg_hi:[0,1]
	ds_write_b128 v162, v[8:11] offset:40960
	ds_read_b128 v[8:11], v163 offset:49152
	s_waitcnt lgkmcnt(0)
	v_pk_add_f32 v[12:13], v[8:9], v[10:11]
	v_pk_add_f32 v[8:9], v[8:9], v[10:11] neg_lo:[0,1] neg_hi:[0,1]
	s_waitcnt vmcnt(1)
	v_pk_mul_f32 v[10:11], v[4:5], v[12:13] op_sel:[1,1] op_sel_hi:[0,1]
	v_pk_fma_f32 v[14:15], v[4:5], v[12:13], v[10:11] op_sel_hi:[1,0,1] neg_lo:[0,0,1]
	s_nop 0
	v_pk_mul_f32 v[4:5], v[6:7], v[8:9] op_sel:[1,1] op_sel_hi:[0,1]
	v_pk_fma_f32 v[10:11], v[6:7], v[8:9], v[4:5] op_sel_hi:[1,0,1] neg_lo:[0,0,1]
	s_nop 0
	v_pk_add_f32 v[4:5], v[14:15], v[10:11]
	v_pk_add_f32 v[6:7], v[14:15], v[10:11] neg_lo:[0,1] neg_hi:[0,1]
	ds_write_b128 v163, v[4:7] offset:49152
	ds_read_b128 v[4:7], v164 offset:57344
	s_waitcnt lgkmcnt(0)
	v_pk_add_f32 v[8:9], v[4:5], v[6:7]
	v_pk_add_f32 v[4:5], v[4:5], v[6:7] neg_lo:[0,1] neg_hi:[0,1]
	s_waitcnt vmcnt(0)
	v_pk_mul_f32 v[6:7], v[0:1], v[8:9] op_sel:[1,1] op_sel_hi:[0,1]
	v_pk_fma_f32 v[10:11], v[0:1], v[8:9], v[6:7] op_sel_hi:[1,0,1] neg_lo:[0,0,1]
	s_nop 0
	v_pk_mul_f32 v[0:1], v[2:3], v[4:5] op_sel:[1,1] op_sel_hi:[0,1]
	v_pk_fma_f32 v[6:7], v[2:3], v[4:5], v[0:1] op_sel_hi:[1,0,1] neg_lo:[0,0,1]
	s_nop 0
	v_pk_add_f32 v[0:1], v[10:11], v[6:7]
	v_pk_add_f32 v[2:3], v[10:11], v[6:7] neg_lo:[0,1] neg_hi:[0,1]
	ds_write_b128 v164, v[0:3] offset:57344
	s_waitcnt lgkmcnt(0)
	s_barrier
; template <int R, class XT, class TWT>
; __device__ __forceinline__ void dit_task(XT X, TWT tw, int s, int task) {
;     const int lgM = 13 - s, lgq = lgM - R, q = 1 << lgq;
;     const int j0 = task & (q - 1), blk = task >> lgq, base = (blk << lgM) + j0;
;     const int pb = PADI(base), qp = (q >= 32) ? q + (q >> 4) : q;
;     f32x2v v[1 << R];
; #pragma unroll
;     for (int k = 0; k < (1 << R); ++k) v[k] = X[pb + k * qp];
; #pragma unroll
;     for (int r = R - 1; r >= 0; --r) {
;         const int pb = R - 1 - r;
; #pragma unroll
;         for (int k = 0; k < (1 << R); ++k) if (!((k >> pb) & 1)) {
;             const int klo = k & ((1 << pb) - 1);
;             const f32x2v w = tw[(j0 + (klo << lgq)) << (s + r)];
;             const f32x2v a = v[k], qv = v[k + (1 << pb)]; const f32x2v b = (f32x2v){qv.x * w.x + qv.y * w.y, qv.y * w.x - qv.x * w.y};
;             v[k] = a + b; v[k + (1 << pb)] = a - b;
;         }
;     }
; #pragma unroll
;     for (int k = 0; k < (1 << R); ++k) X[pb + k * qp] = v[k];
; }
	ds_read2_b64 v[0:3], v137 offset1:2
	ds_read2_b64 v[4:7], v137 offset0:4 offset1:6
	ds_read2_b64 v[8:11], v137 offset0:8 offset1:10
	ds_read2_b64 v[12:15], v137 offset0:12 offset1:14
	ds_read2_b64 v[16:19], v137 offset0:16 offset1:18
	ds_read2_b64 v[20:23], v137 offset0:20 offset1:22
	ds_read2_b64 v[24:27], v137 offset0:24 offset1:26
	ds_read2_b64 v[28:31], v137 offset0:28 offset1:30
	ds_read_b64 v[104:105], v99
	ds_read_b64 v[106:107], v175
	ds_read_b64 v[108:109], v174
	ds_read2st64_b64 v[100:103], v170 offset1:16
	ds_read_b64 v[110:111], v173
	ds_read_b64 v[112:113], v156
	ds_read_b64 v[114:115], v171
	ds_read_b64 v[116:117], v172
	s_waitcnt lgkmcnt(7)
	v_xor_b32_e32 v99, 0x80000000, v104
	v_cndmask_b32_e64 v119, v99, v105, s[42:43]
	v_cndmask_b32_e64 v118, v105, v104, s[42:43]
	v_mov_b32_e32 v104, v119
	v_pk_mul_f32 v[120:121], v[2:3], v[104:105] op_sel_hi:[1,0]
	s_nop 0
	v_pk_fma_f32 v[122:123], v[2:3], v[118:119], v[120:121] op_sel:[0,0,1] op_sel_hi:[1,1,0]
	v_pk_fma_f32 v[2:3], v[2:3], v[118:119], v[120:121] op_sel:[0,0,1] op_sel_hi:[1,0,0] neg_lo:[0,0,1] neg_hi:[0,0,1]
	v_pk_mul_f32 v[120:121], v[6:7], v[104:105] op_sel_hi:[1,0]
	v_mov_b32_e32 v123, v3
	v_pk_fma_f32 v[124:125], v[6:7], v[118:119], v[120:121] op_sel:[0,0,1] op_sel_hi:[1,0,0] neg_hi:[0,0,1]
	v_pk_add_f32 v[2:3], v[0:1], v[122:123]
	v_pk_add_f32 v[6:7], v[4:5], v[124:125]
	v_pk_add_f32 v[4:5], v[4:5], v[124:125] neg_lo:[0,1] neg_hi:[0,1]
	s_waitcnt lgkmcnt(6)
	v_pk_mul_f32 v[120:121], v[106:107], v[6:7] op_sel:[1,0]
	v_pk_add_f32 v[0:1], v[0:1], v[122:123] neg_lo:[0,1] neg_hi:[0,1]
	v_pk_fma_f32 v[126:127], v[106:107], v[6:7], v[120:121] op_sel:[0,0,1] op_sel_hi:[1,1,0]
	v_pk_fma_f32 v[6:7], v[106:107], v[6:7], v[120:121] op_sel:[0,0,1] op_sel_hi:[0,1,0] neg_lo:[0,0,1] neg_hi:[0,0,1]
	v_pk_mul_f32 v[120:121], v[10:11], v[104:105] op_sel_hi:[1,0]
	v_mov_b32_e32 v127, v7
	v_pk_fma_f32 v[128:129], v[10:11], v[118:119], v[120:121] op_sel:[0,0,1] op_sel_hi:[1,1,0]
	v_pk_fma_f32 v[10:11], v[10:11], v[118:119], v[120:121] op_sel:[0,0,1] op_sel_hi:[1,0,0] neg_lo:[0,0,1] neg_hi:[0,0,1]
	v_pk_mul_f32 v[120:121], v[14:15], v[104:105] op_sel_hi:[1,0]
	v_mov_b32_e32 v129, v11
	v_pk_fma_f32 v[130:131], v[14:15], v[118:119], v[120:121] op_sel:[0,0,1] op_sel_hi:[1,0,0] neg_hi:[0,0,1]
	v_pk_add_f32 v[10:11], v[8:9], v[128:129]
	v_pk_add_f32 v[14:15], v[12:13], v[130:131]
	v_pk_add_f32 v[12:13], v[12:13], v[130:131] neg_lo:[0,1] neg_hi:[0,1]
	v_pk_mul_f32 v[120:121], v[106:107], v[14:15] op_sel:[1,0]
	v_pk_add_f32 v[8:9], v[8:9], v[128:129] neg_lo:[0,1] neg_hi:[0,1]
	v_pk_fma_f32 v[132:133], v[106:107], v[14:15], v[120:121] op_sel:[0,0,1] op_sel_hi:[0,1,0] neg_hi:[0,0,1]
	s_nop 0
	v_pk_add_f32 v[14:15], v[10:11], v[132:133]
	v_pk_add_f32 v[10:11], v[10:11], v[132:133] neg_lo:[0,1] neg_hi:[0,1]
	s_waitcnt lgkmcnt(3)
	v_pk_mul_f32 v[120:121], v[110:111], v[14:15] op_sel:[1,0]
	v_pk_add_f32 v[6:7], v[2:3], v[126:127]
	v_pk_fma_f32 v[176:177], v[110:111], v[14:15], v[120:121] op_sel:[0,0,1] op_sel_hi:[1,1,0]
	v_pk_fma_f32 v[14:15], v[110:111], v[14:15], v[120:121] op_sel:[0,0,1] op_sel_hi:[0,1,0] neg_lo:[0,0,1] neg_hi:[0,0,1]
	v_pk_mul_f32 v[120:121], v[18:19], v[104:105] op_sel_hi:[1,0]
	v_pk_add_f32 v[2:3], v[2:3], v[126:127] neg_lo:[0,1] neg_hi:[0,1]
	v_pk_fma_f32 v[178:179], v[18:19], v[118:119], v[120:121] op_sel:[0,0,1] op_sel_hi:[1,1,0]
	v_pk_fma_f32 v[18:19], v[18:19], v[118:119], v[120:121] op_sel:[0,0,1] op_sel_hi:[1,0,0] neg_lo:[0,0,1] neg_hi:[0,0,1]
	v_pk_mul_f32 v[120:121], v[22:23], v[104:105] op_sel_hi:[1,0]
	v_mov_b32_e32 v179, v19
	v_pk_fma_f32 v[182:183], v[22:23], v[118:119], v[120:121] op_sel:[0,0,1] op_sel_hi:[1,0,0] neg_hi:[0,0,1]
	v_pk_add_f32 v[18:19], v[16:17], v[178:179]
	v_pk_add_f32 v[22:23], v[20:21], v[182:183]
	v_pk_add_f32 v[20:21], v[20:21], v[182:183] neg_lo:[0,1] neg_hi:[0,1]
	v_pk_mul_f32 v[120:121], v[106:107], v[22:23] op_sel:[1,0]
	v_pk_add_f32 v[16:17], v[16:17], v[178:179] neg_lo:[0,1] neg_hi:[0,1]
	v_pk_fma_f32 v[184:185], v[106:107], v[22:23], v[120:121] op_sel:[0,0,1] op_sel_hi:[1,1,0]
	v_pk_fma_f32 v[22:23], v[106:107], v[22:23], v[120:121] op_sel:[0,0,1] op_sel_hi:[0,1,0] neg_lo:[0,0,1] neg_hi:[0,0,1]
	v_pk_mul_f32 v[120:121], v[26:27], v[104:105] op_sel_hi:[1,0]
	v_pk_mul_f32 v[104:105], v[30:31], v[104:105] op_sel_hi:[1,0]
	v_pk_fma_f32 v[186:187], v[26:27], v[118:119], v[120:121] op_sel:[0,0,1] op_sel_hi:[1,1,0]
	v_pk_fma_f32 v[26:27], v[26:27], v[118:119], v[120:121] op_sel:[0,0,1] op_sel_hi:[1,0,0] neg_lo:[0,0,1] neg_hi:[0,0,1]
	v_pk_fma_f32 v[120:121], v[30:31], v[118:119], v[104:105] op_sel:[0,0,1] op_sel_hi:[1,0,0] neg_hi:[0,0,1]
	v_mov_b32_e32 v187, v27
	v_pk_add_f32 v[30:31], v[28:29], v[120:121]
	v_pk_add_f32 v[26:27], v[24:25], v[186:187]
	v_pk_mul_f32 v[104:105], v[106:107], v[30:31] op_sel:[1,0]
	v_mov_b32_e32 v185, v23
	v_pk_fma_f32 v[118:119], v[106:107], v[30:31], v[104:105] op_sel:[0,0,1] op_sel_hi:[0,1,0] neg_hi:[0,0,1]
	s_nop 0
	v_pk_add_f32 v[30:31], v[26:27], v[118:119]
	v_pk_add_f32 v[22:23], v[18:19], v[184:185]
	v_pk_mul_f32 v[104:105], v[110:111], v[30:31] op_sel:[1,0]
	v_pk_add_f32 v[28:29], v[28:29], v[120:121] neg_lo:[0,1] neg_hi:[0,1]
	v_pk_fma_f32 v[188:189], v[110:111], v[30:31], v[104:105] op_sel:[0,0,1] op_sel_hi:[0,1,0] neg_hi:[0,0,1]
	s_nop 0
	v_pk_add_f32 v[30:31], v[22:23], v[188:189]
	v_pk_add_f32 v[24:25], v[24:25], v[186:187] neg_lo:[0,1] neg_hi:[0,1]
	v_pk_mul_f32 v[104:105], v[100:101], v[30:31] op_sel:[1,0]
	v_pk_add_f32 v[26:27], v[26:27], v[118:119] neg_lo:[0,1] neg_hi:[0,1]
	v_pk_fma_f32 v[190:191], v[100:101], v[30:31], v[104:105] op_sel:[0,0,1] op_sel_hi:[1,1,0]
; template <int R, class XT, class TWT>
; __device__ __forceinline__ void dit_task(XT X, TWT tw, int s, int task) {
;     const int lgM = 13 - s, lgq = lgM - R, q = 1 << lgq;
;     const int j0 = task & (q - 1), blk = task >> lgq, base = (blk << lgM) + j0;
;     const int pb = PADI(base), qp = (q >= 32) ? q + (q >> 4) : q;
;     f32x2v v[1 << R];
; #pragma unroll
;     for (int k = 0; k < (1 << R); ++k) v[k] = X[pb + k * qp];
; #pragma unroll
;     for (int r = R - 1; r >= 0; --r) {
;         const int pb = R - 1 - r;
; #pragma unroll
;         for (int k = 0; k < (1 << R); ++k) if (!((k >> pb) & 1)) {
;             const int klo = k & ((1 << pb) - 1);
;             const f32x2v w = tw[(j0 + (klo << lgq)) << (s + r)];
;             const f32x2v a = v[k], qv = v[k + (1 << pb)]; const f32x2v b = (f32x2v){qv.x * w.x + qv.y * w.y, qv.y * w.x - qv.x * w.y};
;             v[k] = a + b; v[k + (1 << pb)] = a - b;
;         }
;     }
; #pragma unroll
;     for (int k = 0; k < (1 << R); ++k) X[pb + k * qp] = v[k];
; }
	v_pk_fma_f32 v[30:31], v[100:101], v[30:31], v[104:105] op_sel:[0,0,1] op_sel_hi:[0,1,0] neg_lo:[0,0,1] neg_hi:[0,0,1]
	v_pk_mul_f32 v[104:105], v[106:107], v[4:5] op_sel_hi:[0,1]
	v_pk_fma_f32 v[122:123], v[106:107], v[4:5], v[104:105] op_sel:[1,0,1] op_sel_hi:[1,1,0] neg_lo:[0,0,1] neg_hi:[0,0,1]
	v_pk_fma_f32 v[4:5], v[106:107], v[4:5], v[104:105] op_sel:[1,0,1] op_sel_hi:[1,1,0]
	v_pk_mul_f32 v[104:105], v[106:107], v[12:13] op_sel_hi:[0,1]
	v_pk_fma_f32 v[124:125], v[106:107], v[12:13], v[104:105] op_sel:[1,0,1] op_sel_hi:[1,1,0] neg_lo:[0,0,1]
	v_mov_b32_e32 v123, v5
	v_pk_add_f32 v[12:13], v[8:9], v[124:125]
	v_pk_add_f32 v[4:5], v[0:1], v[122:123]
	v_pk_mul_f32 v[104:105], v[108:109], v[12:13] op_sel:[1,0]
	v_pk_add_f32 v[18:19], v[18:19], v[184:185] neg_lo:[0,1] neg_hi:[0,1]
	v_pk_fma_f32 v[128:129], v[108:109], v[12:13], v[104:105] op_sel:[0,0,1] op_sel_hi:[1,1,0]
	v_pk_fma_f32 v[12:13], v[108:109], v[12:13], v[104:105] op_sel:[0,0,1] op_sel_hi:[0,1,0] neg_lo:[0,0,1] neg_hi:[0,0,1]
	v_pk_mul_f32 v[104:105], v[106:107], v[20:21] op_sel_hi:[0,1]
	v_pk_fma_f32 v[130:131], v[106:107], v[20:21], v[104:105] op_sel:[1,0,1] op_sel_hi:[1,1,0] neg_lo:[0,0,1] neg_hi:[0,0,1]
	v_pk_fma_f32 v[20:21], v[106:107], v[20:21], v[104:105] op_sel:[1,0,1] op_sel_hi:[1,1,0]
	v_pk_mul_f32 v[104:105], v[106:107], v[28:29] op_sel_hi:[0,1]
	v_pk_fma_f32 v[120:121], v[106:107], v[28:29], v[104:105] op_sel:[1,0,1] op_sel_hi:[1,1,0] neg_lo:[0,0,1]
	v_mov_b32_e32 v131, v21
	v_pk_add_f32 v[28:29], v[24:25], v[120:121]
	v_pk_add_f32 v[20:21], v[16:17], v[130:131]
	v_pk_mul_f32 v[104:105], v[108:109], v[28:29] op_sel:[1,0]
	v_mov_b32_e32 v129, v13
	v_pk_fma_f32 v[106:107], v[108:109], v[28:29], v[104:105] op_sel:[0,0,1] op_sel_hi:[0,1,0] neg_hi:[0,0,1]
	s_nop 0
	v_pk_add_f32 v[28:29], v[20:21], v[106:107]
	v_pk_add_f32 v[12:13], v[4:5], v[128:129]
	s_waitcnt lgkmcnt(1)
	v_pk_mul_f32 v[104:105], v[114:115], v[28:29] op_sel:[1,0]
	v_pk_add_f32 v[8:9], v[8:9], v[124:125] neg_lo:[0,1] neg_hi:[0,1]
	v_pk_fma_f32 v[108:109], v[114:115], v[28:29], v[104:105] op_sel:[0,0,1] op_sel_hi:[0,1,0] neg_hi:[0,0,1]
	v_pk_mul_f32 v[104:105], v[110:111], v[10:11] op_sel_hi:[0,1]
	v_pk_add_f32 v[28:29], v[12:13], v[108:109]
	v_pk_add_f32 v[12:13], v[12:13], v[108:109] neg_lo:[0,1] neg_hi:[0,1]
	v_pk_fma_f32 v[108:109], v[110:111], v[10:11], v[104:105] op_sel:[1,0,1] op_sel_hi:[1,1,0] neg_lo:[0,0,1] neg_hi:[0,0,1]
	v_pk_fma_f32 v[10:11], v[110:111], v[10:11], v[104:105] op_sel:[1,0,1] op_sel_hi:[1,1,0]
	v_pk_mul_f32 v[104:105], v[110:111], v[26:27] op_sel_hi:[0,1]
	v_pk_fma_f32 v[118:119], v[110:111], v[26:27], v[104:105] op_sel:[1,0,1] op_sel_hi:[1,1,0] neg_lo:[0,0,1]
	v_mov_b32_e32 v109, v11
	v_pk_add_f32 v[26:27], v[18:19], v[118:119]
	v_pk_add_f32 v[10:11], v[2:3], v[108:109]
	v_pk_mul_f32 v[104:105], v[102:103], v[26:27] op_sel:[1,0]
	v_pk_add_f32 v[24:25], v[24:25], v[120:121] neg_lo:[0,1] neg_hi:[0,1]
	v_pk_fma_f32 v[110:111], v[102:103], v[26:27], v[104:105] op_sel:[0,0,1] op_sel_hi:[0,1,0] neg_hi:[0,0,1]
	v_pk_mul_f32 v[104:105], v[112:113], v[8:9] op_sel_hi:[0,1]
	v_pk_add_f32 v[26:27], v[10:11], v[110:111]
	v_pk_add_f32 v[10:11], v[10:11], v[110:111] neg_lo:[0,1] neg_hi:[0,1]
	v_pk_fma_f32 v[110:111], v[112:113], v[8:9], v[104:105] op_sel:[1,0,1] op_sel_hi:[1,1,0] neg_lo:[0,0,1] neg_hi:[0,0,1]
	v_pk_fma_f32 v[8:9], v[112:113], v[8:9], v[104:105] op_sel:[1,0,1] op_sel_hi:[1,1,0]
	v_pk_mul_f32 v[104:105], v[112:113], v[24:25] op_sel_hi:[0,1]
	v_pk_fma_f32 v[120:121], v[112:113], v[24:25], v[104:105] op_sel:[1,0,1] op_sel_hi:[1,1,0] neg_lo:[0,0,1]
	v_pk_add_f32 v[16:17], v[16:17], v[130:131] neg_lo:[0,1] neg_hi:[0,1]
	s_nop 0
	v_pk_add_f32 v[24:25], v[16:17], v[120:121]
	v_pk_add_f32 v[0:1], v[0:1], v[122:123] neg_lo:[0,1] neg_hi:[0,1]
	s_waitcnt lgkmcnt(0)
	v_pk_mul_f32 v[104:105], v[116:117], v[24:25] op_sel:[1,0]
	v_mov_b32_e32 v111, v9
	v_pk_fma_f32 v[112:113], v[116:117], v[24:25], v[104:105] op_sel:[0,0,1] op_sel_hi:[0,1,0] neg_hi:[0,0,1]
	v_pk_add_f32 v[22:23], v[22:23], v[188:189] neg_lo:[0,1] neg_hi:[0,1]
	v_pk_add_f32 v[8:9], v[0:1], v[110:111]
	v_pk_mul_f32 v[104:105], v[100:101], v[22:23] op_sel_hi:[0,1]
	v_pk_add_f32 v[20:21], v[20:21], v[106:107] neg_lo:[0,1] neg_hi:[0,1]
	v_pk_add_f32 v[24:25], v[8:9], v[112:113]
	v_pk_add_f32 v[8:9], v[8:9], v[112:113] neg_lo:[0,1] neg_hi:[0,1]
	v_pk_fma_f32 v[112:113], v[100:101], v[22:23], v[104:105] op_sel:[1,0,1] op_sel_hi:[1,1,0] neg_lo:[0,0,1] neg_hi:[0,0,1]
	v_pk_fma_f32 v[22:23], v[100:101], v[22:23], v[104:105] op_sel:[1,0,1] op_sel_hi:[1,1,0]
	v_pk_mul_f32 v[100:101], v[114:115], v[20:21] op_sel_hi:[0,1]
	v_pk_fma_f32 v[104:105], v[114:115], v[20:21], v[100:101] op_sel:[1,0,1] op_sel_hi:[1,1,0] neg_lo:[0,0,1]
	v_pk_add_f32 v[18:19], v[18:19], v[118:119] neg_lo:[0,1] neg_hi:[0,1]
	v_pk_add_f32 v[4:5], v[4:5], v[128:129] neg_lo:[0,1] neg_hi:[0,1]
	v_pk_mul_f32 v[100:101], v[102:103], v[18:19] op_sel_hi:[0,1]
	v_pk_add_f32 v[16:17], v[16:17], v[120:121] neg_lo:[0,1] neg_hi:[0,1]
	v_mov_b32_e32 v177, v15
	v_pk_add_f32 v[20:21], v[4:5], v[104:105]
	v_pk_add_f32 v[4:5], v[4:5], v[104:105] neg_lo:[0,1] neg_hi:[0,1]
	v_pk_fma_f32 v[104:105], v[102:103], v[18:19], v[100:101] op_sel:[1,0,1] op_sel_hi:[1,1,0] neg_lo:[0,0,1] neg_hi:[0,0,1]
	v_pk_fma_f32 v[18:19], v[102:103], v[18:19], v[100:101] op_sel:[1,0,1] op_sel_hi:[1,1,0]
	v_pk_mul_f32 v[100:101], v[116:117], v[16:17] op_sel_hi:[0,1]
	v_pk_add_f32 v[14:15], v[6:7], v[176:177]
	v_mov_b32_e32 v191, v31
	v_pk_fma_f32 v[102:103], v[116:117], v[16:17], v[100:101] op_sel:[1,0,1] op_sel_hi:[1,1,0] neg_lo:[0,0,1]
	v_pk_add_f32 v[30:31], v[14:15], v[190:191]
	v_pk_add_f32 v[6:7], v[6:7], v[176:177] neg_lo:[0,1] neg_hi:[0,1]
	v_mov_b32_e32 v113, v23
	v_pk_add_f32 v[2:3], v[2:3], v[108:109] neg_lo:[0,1] neg_hi:[0,1]
	v_mov_b32_e32 v105, v19
	v_pk_add_f32 v[0:1], v[0:1], v[110:111] neg_lo:[0,1] neg_hi:[0,1]
	v_pk_add_f32 v[14:15], v[14:15], v[190:191] neg_lo:[0,1] neg_hi:[0,1]
	v_pk_add_f32 v[22:23], v[6:7], v[112:113]
	v_pk_add_f32 v[6:7], v[6:7], v[112:113] neg_lo:[0,1] neg_hi:[0,1]
	v_pk_add_f32 v[18:19], v[2:3], v[104:105]
	v_pk_add_f32 v[2:3], v[2:3], v[104:105] neg_lo:[0,1] neg_hi:[0,1]
	v_pk_add_f32 v[16:17], v[0:1], v[102:103]
	v_pk_add_f32 v[0:1], v[0:1], v[102:103] neg_lo:[0,1] neg_hi:[0,1]
	ds_write2_b64 v137, v[30:31], v[28:29] offset1:2
	ds_write2_b64 v137, v[26:27], v[24:25] offset0:4 offset1:6
	ds_write2_b64 v137, v[22:23], v[20:21] offset0:8 offset1:10
	ds_write2_b64 v137, v[18:19], v[16:17] offset0:12 offset1:14
	ds_write2_b64 v137, v[14:15], v[12:13] offset0:16 offset1:18
	ds_write2_b64 v137, v[10:11], v[8:9] offset0:20 offset1:22
	ds_write2_b64 v137, v[6:7], v[4:5] offset0:24 offset1:26
	ds_write2_b64 v137, v[2:3], v[0:1] offset0:28 offset1:30
	s_waitcnt lgkmcnt(0)
	s_barrier
; template <int R, class XT, class TWT>
; __device__ __forceinline__ void dit_task(XT X, TWT tw, int s, int task) {
;     const int lgM = 13 - s, lgq = lgM - R, q = 1 << lgq;
;     const int j0 = task & (q - 1), blk = task >> lgq, base = (blk << lgM) + j0;
;     const int pb = PADI(base), qp = (q >= 32) ? q + (q >> 4) : q;
;     f32x2v v[1 << R];
; #pragma unroll
;     for (int k = 0; k < (1 << R); ++k) v[k] = X[pb + k * qp];
; #pragma unroll
;     for (int r = R - 1; r >= 0; --r) {
;         const int pb = R - 1 - r;
; #pragma unroll
;         for (int k = 0; k < (1 << R); ++k) if (!((k >> pb) & 1)) {
;             const int klo = k & ((1 << pb) - 1);
;             const f32x2v w = tw[(j0 + (klo << lgq)) << (s + r)];
;             const f32x2v a = v[k], qv = v[k + (1 << pb)]; const f32x2v b = (f32x2v){qv.x * w.x + qv.y * w.y, qv.y * w.x - qv.x * w.y};
;             v[k] = a + b; v[k + (1 << pb)] = a - b;
;         }
;     }
; #pragma unroll
;     for (int k = 0; k < (1 << R); ++k) X[pb + k * qp] = v[k];
; }
	ds_read2_b64 v[0:3], v135 offset1:34
	ds_read2_b64 v[4:7], v135 offset0:68 offset1:102
	ds_read2_b64 v[8:11], v135 offset0:136 offset1:170
	ds_read2_b64 v[12:15], v135 offset0:204 offset1:238
	ds_read2_b64 v[16:19], v98 offset0:16 offset1:50
	ds_read2_b64 v[20:23], v98 offset0:84 offset1:118
	ds_read2_b64 v[24:27], v98 offset0:152 offset1:186
	ds_read2_b64 v[28:31], v98 offset0:220 offset1:254
	ds_read_b64 v[104:105], v136
	ds_read_b64 v[106:107], v169
	ds_read_b64 v[108:109], v167
	ds_read_b64 v[110:111], v168
	ds_read2st64_b64 v[100:103], v33 offset1:16
	ds_read_b64 v[112:113], v139
	ds_read_b64 v[114:115], v165
	ds_read_b64 v[116:117], v166
	s_waitcnt lgkmcnt(7)
	v_xor_b32_e32 v99, 0x80000000, v104
	v_cndmask_b32_e64 v119, v99, v105, s[44:45]
	v_cndmask_b32_e64 v118, v105, v104, s[44:45]
	v_mov_b32_e32 v104, v119
	v_pk_mul_f32 v[120:121], v[2:3], v[104:105] op_sel_hi:[1,0]
	s_nop 0
	v_pk_fma_f32 v[122:123], v[2:3], v[118:119], v[120:121] op_sel:[0,0,1] op_sel_hi:[1,1,0]
	v_pk_fma_f32 v[2:3], v[2:3], v[118:119], v[120:121] op_sel:[0,0,1] op_sel_hi:[1,0,0] neg_lo:[0,0,1] neg_hi:[0,0,1]
	v_pk_mul_f32 v[120:121], v[6:7], v[104:105] op_sel_hi:[1,0]
	v_mov_b32_e32 v123, v3
	v_pk_fma_f32 v[124:125], v[6:7], v[118:119], v[120:121] op_sel:[0,0,1] op_sel_hi:[1,0,0] neg_hi:[0,0,1]
	v_pk_add_f32 v[2:3], v[0:1], v[122:123]
	v_pk_add_f32 v[6:7], v[4:5], v[124:125]
	v_pk_add_f32 v[4:5], v[4:5], v[124:125] neg_lo:[0,1] neg_hi:[0,1]
	s_waitcnt lgkmcnt(6)
	v_pk_mul_f32 v[120:121], v[106:107], v[6:7] op_sel:[1,0]
	v_pk_add_f32 v[0:1], v[0:1], v[122:123] neg_lo:[0,1] neg_hi:[0,1]
	v_pk_fma_f32 v[126:127], v[106:107], v[6:7], v[120:121] op_sel:[0,0,1] op_sel_hi:[1,1,0]
	v_pk_fma_f32 v[6:7], v[106:107], v[6:7], v[120:121] op_sel:[0,0,1] op_sel_hi:[0,1,0] neg_lo:[0,0,1] neg_hi:[0,0,1]
	v_pk_mul_f32 v[120:121], v[10:11], v[104:105] op_sel_hi:[1,0]
	v_mov_b32_e32 v127, v7
	v_pk_fma_f32 v[128:129], v[10:11], v[118:119], v[120:121] op_sel:[0,0,1] op_sel_hi:[1,1,0]
	v_pk_fma_f32 v[10:11], v[10:11], v[118:119], v[120:121] op_sel:[0,0,1] op_sel_hi:[1,0,0] neg_lo:[0,0,1] neg_hi:[0,0,1]
	v_pk_mul_f32 v[120:121], v[14:15], v[104:105] op_sel_hi:[1,0]
	v_mov_b32_e32 v129, v11
	v_pk_fma_f32 v[130:131], v[14:15], v[118:119], v[120:121] op_sel:[0,0,1] op_sel_hi:[1,0,0] neg_hi:[0,0,1]
	v_pk_add_f32 v[10:11], v[8:9], v[128:129]
	v_pk_add_f32 v[14:15], v[12:13], v[130:131]
	v_pk_add_f32 v[12:13], v[12:13], v[130:131] neg_lo:[0,1] neg_hi:[0,1]
	v_pk_mul_f32 v[120:121], v[106:107], v[14:15] op_sel:[1,0]
	v_pk_add_f32 v[8:9], v[8:9], v[128:129] neg_lo:[0,1] neg_hi:[0,1]
	v_pk_fma_f32 v[132:133], v[106:107], v[14:15], v[120:121] op_sel:[0,0,1] op_sel_hi:[0,1,0] neg_hi:[0,0,1]
	s_nop 0
	v_pk_add_f32 v[14:15], v[10:11], v[132:133]
	v_pk_add_f32 v[10:11], v[10:11], v[132:133] neg_lo:[0,1] neg_hi:[0,1]
	s_waitcnt lgkmcnt(5)
	v_pk_mul_f32 v[120:121], v[108:109], v[14:15] op_sel:[1,0]
	v_pk_add_f32 v[6:7], v[2:3], v[126:127]
	v_pk_fma_f32 v[176:177], v[108:109], v[14:15], v[120:121] op_sel:[0,0,1] op_sel_hi:[1,1,0]
	v_pk_fma_f32 v[14:15], v[108:109], v[14:15], v[120:121] op_sel:[0,0,1] op_sel_hi:[0,1,0] neg_lo:[0,0,1] neg_hi:[0,0,1]
	v_pk_mul_f32 v[120:121], v[18:19], v[104:105] op_sel_hi:[1,0]
	v_pk_add_f32 v[2:3], v[2:3], v[126:127] neg_lo:[0,1] neg_hi:[0,1]
	v_pk_fma_f32 v[178:179], v[18:19], v[118:119], v[120:121] op_sel:[0,0,1] op_sel_hi:[1,1,0]
	v_pk_fma_f32 v[18:19], v[18:19], v[118:119], v[120:121] op_sel:[0,0,1] op_sel_hi:[1,0,0] neg_lo:[0,0,1] neg_hi:[0,0,1]
	v_pk_mul_f32 v[120:121], v[22:23], v[104:105] op_sel_hi:[1,0]
	v_mov_b32_e32 v179, v19
	v_pk_fma_f32 v[182:183], v[22:23], v[118:119], v[120:121] op_sel:[0,0,1] op_sel_hi:[1,0,0] neg_hi:[0,0,1]
	v_pk_add_f32 v[18:19], v[16:17], v[178:179]
	v_pk_add_f32 v[22:23], v[20:21], v[182:183]
	v_pk_add_f32 v[20:21], v[20:21], v[182:183] neg_lo:[0,1] neg_hi:[0,1]
	v_pk_mul_f32 v[120:121], v[106:107], v[22:23] op_sel:[1,0]
	v_pk_add_f32 v[16:17], v[16:17], v[178:179] neg_lo:[0,1] neg_hi:[0,1]
	v_pk_fma_f32 v[184:185], v[106:107], v[22:23], v[120:121] op_sel:[0,0,1] op_sel_hi:[1,1,0]
	v_pk_fma_f32 v[22:23], v[106:107], v[22:23], v[120:121] op_sel:[0,0,1] op_sel_hi:[0,1,0] neg_lo:[0,0,1] neg_hi:[0,0,1]
	v_pk_mul_f32 v[120:121], v[26:27], v[104:105] op_sel_hi:[1,0]
	v_pk_mul_f32 v[104:105], v[30:31], v[104:105] op_sel_hi:[1,0]
	v_pk_fma_f32 v[186:187], v[26:27], v[118:119], v[120:121] op_sel:[0,0,1] op_sel_hi:[1,1,0]
	v_pk_fma_f32 v[26:27], v[26:27], v[118:119], v[120:121] op_sel:[0,0,1] op_sel_hi:[1,0,0] neg_lo:[0,0,1] neg_hi:[0,0,1]
	v_pk_fma_f32 v[120:121], v[30:31], v[118:119], v[104:105] op_sel:[0,0,1] op_sel_hi:[1,0,0] neg_hi:[0,0,1]
	v_mov_b32_e32 v187, v27
	v_pk_add_f32 v[30:31], v[28:29], v[120:121]
	v_pk_add_f32 v[26:27], v[24:25], v[186:187]
	v_pk_mul_f32 v[104:105], v[106:107], v[30:31] op_sel:[1,0]
	v_mov_b32_e32 v185, v23
	v_pk_fma_f32 v[118:119], v[106:107], v[30:31], v[104:105] op_sel:[0,0,1] op_sel_hi:[0,1,0] neg_hi:[0,0,1]
	s_nop 0
	v_pk_add_f32 v[30:31], v[26:27], v[118:119]
	v_pk_add_f32 v[22:23], v[18:19], v[184:185]
	v_pk_mul_f32 v[104:105], v[108:109], v[30:31] op_sel:[1,0]
	v_pk_add_f32 v[28:29], v[28:29], v[120:121] neg_lo:[0,1] neg_hi:[0,1]
	v_pk_fma_f32 v[188:189], v[108:109], v[30:31], v[104:105] op_sel:[0,0,1] op_sel_hi:[0,1,0] neg_hi:[0,0,1]
	s_nop 0
	v_pk_add_f32 v[30:31], v[22:23], v[188:189]
	v_pk_add_f32 v[24:25], v[24:25], v[186:187] neg_lo:[0,1] neg_hi:[0,1]
	s_waitcnt lgkmcnt(3)
; template <int R, class XT, class TWT>
; __device__ __forceinline__ void dit_task(XT X, TWT tw, int s, int task) {
;     const int lgM = 13 - s, lgq = lgM - R, q = 1 << lgq;
;     const int j0 = task & (q - 1), blk = task >> lgq, base = (blk << lgM) + j0;
;     const int pb = PADI(base), qp = (q >= 32) ? q + (q >> 4) : q;
;     f32x2v v[1 << R];
; #pragma unroll
;     for (int k = 0; k < (1 << R); ++k) v[k] = X[pb + k * qp];
; #pragma unroll
;     for (int r = R - 1; r >= 0; --r) {
;         const int pb = R - 1 - r;
; #pragma unroll
;         for (int k = 0; k < (1 << R); ++k) if (!((k >> pb) & 1)) {
;             const int klo = k & ((1 << pb) - 1);
;             const f32x2v w = tw[(j0 + (klo << lgq)) << (s + r)];
;             const f32x2v a = v[k], qv = v[k + (1 << pb)]; const f32x2v b = (f32x2v){qv.x * w.x + qv.y * w.y, qv.y * w.x - qv.x * w.y};
;             v[k] = a + b; v[k + (1 << pb)] = a - b;
;         }
;     }
; #pragma unroll
;     for (int k = 0; k < (1 << R); ++k) X[pb + k * qp] = v[k];
; }
	v_pk_mul_f32 v[104:105], v[100:101], v[30:31] op_sel:[1,0]
	v_pk_add_f32 v[26:27], v[26:27], v[118:119] neg_lo:[0,1] neg_hi:[0,1]
	v_pk_fma_f32 v[190:191], v[100:101], v[30:31], v[104:105] op_sel:[0,0,1] op_sel_hi:[1,1,0]
	v_pk_fma_f32 v[30:31], v[100:101], v[30:31], v[104:105] op_sel:[0,0,1] op_sel_hi:[0,1,0] neg_lo:[0,0,1] neg_hi:[0,0,1]
	v_pk_mul_f32 v[104:105], v[106:107], v[4:5] op_sel_hi:[0,1]
	v_pk_fma_f32 v[122:123], v[106:107], v[4:5], v[104:105] op_sel:[1,0,1] op_sel_hi:[1,1,0] neg_lo:[0,0,1] neg_hi:[0,0,1]
	v_pk_fma_f32 v[4:5], v[106:107], v[4:5], v[104:105] op_sel:[1,0,1] op_sel_hi:[1,1,0]
	v_pk_mul_f32 v[104:105], v[106:107], v[12:13] op_sel_hi:[0,1]
	v_pk_fma_f32 v[124:125], v[106:107], v[12:13], v[104:105] op_sel:[1,0,1] op_sel_hi:[1,1,0] neg_lo:[0,0,1]
	v_mov_b32_e32 v123, v5
	v_pk_add_f32 v[12:13], v[8:9], v[124:125]
	v_pk_add_f32 v[4:5], v[0:1], v[122:123]
	v_pk_mul_f32 v[104:105], v[110:111], v[12:13] op_sel:[1,0]
	v_pk_add_f32 v[18:19], v[18:19], v[184:185] neg_lo:[0,1] neg_hi:[0,1]
	v_pk_fma_f32 v[128:129], v[110:111], v[12:13], v[104:105] op_sel:[0,0,1] op_sel_hi:[1,1,0]
	v_pk_fma_f32 v[12:13], v[110:111], v[12:13], v[104:105] op_sel:[0,0,1] op_sel_hi:[0,1,0] neg_lo:[0,0,1] neg_hi:[0,0,1]
	v_pk_mul_f32 v[104:105], v[106:107], v[20:21] op_sel_hi:[0,1]
	v_pk_fma_f32 v[130:131], v[106:107], v[20:21], v[104:105] op_sel:[1,0,1] op_sel_hi:[1,1,0] neg_lo:[0,0,1] neg_hi:[0,0,1]
	v_pk_fma_f32 v[20:21], v[106:107], v[20:21], v[104:105] op_sel:[1,0,1] op_sel_hi:[1,1,0]
	v_pk_mul_f32 v[104:105], v[106:107], v[28:29] op_sel_hi:[0,1]
	v_pk_fma_f32 v[120:121], v[106:107], v[28:29], v[104:105] op_sel:[1,0,1] op_sel_hi:[1,1,0] neg_lo:[0,0,1]
	v_mov_b32_e32 v131, v21
	v_pk_add_f32 v[28:29], v[24:25], v[120:121]
	v_pk_add_f32 v[20:21], v[16:17], v[130:131]
	v_pk_mul_f32 v[104:105], v[110:111], v[28:29] op_sel:[1,0]
	v_mov_b32_e32 v129, v13
	v_pk_fma_f32 v[106:107], v[110:111], v[28:29], v[104:105] op_sel:[0,0,1] op_sel_hi:[0,1,0] neg_hi:[0,0,1]
	s_nop 0
	v_pk_add_f32 v[28:29], v[20:21], v[106:107]
	v_pk_add_f32 v[12:13], v[4:5], v[128:129]
	s_waitcnt lgkmcnt(1)
	v_pk_mul_f32 v[104:105], v[114:115], v[28:29] op_sel:[1,0]
	v_pk_add_f32 v[8:9], v[8:9], v[124:125] neg_lo:[0,1] neg_hi:[0,1]
	v_pk_fma_f32 v[110:111], v[114:115], v[28:29], v[104:105] op_sel:[0,0,1] op_sel_hi:[0,1,0] neg_hi:[0,0,1]
	v_pk_mul_f32 v[104:105], v[108:109], v[10:11] op_sel_hi:[0,1]
	v_pk_add_f32 v[28:29], v[12:13], v[110:111]
	v_pk_add_f32 v[12:13], v[12:13], v[110:111] neg_lo:[0,1] neg_hi:[0,1]
	v_pk_fma_f32 v[110:111], v[108:109], v[10:11], v[104:105] op_sel:[1,0,1] op_sel_hi:[1,1,0] neg_lo:[0,0,1] neg_hi:[0,0,1]
	v_pk_fma_f32 v[10:11], v[108:109], v[10:11], v[104:105] op_sel:[1,0,1] op_sel_hi:[1,1,0]
	v_pk_mul_f32 v[104:105], v[108:109], v[26:27] op_sel_hi:[0,1]
	v_pk_fma_f32 v[118:119], v[108:109], v[26:27], v[104:105] op_sel:[1,0,1] op_sel_hi:[1,1,0] neg_lo:[0,0,1]
	v_mov_b32_e32 v111, v11
	v_pk_add_f32 v[26:27], v[18:19], v[118:119]
	v_pk_add_f32 v[10:11], v[2:3], v[110:111]
	v_pk_mul_f32 v[104:105], v[102:103], v[26:27] op_sel:[1,0]
	v_pk_add_f32 v[24:25], v[24:25], v[120:121] neg_lo:[0,1] neg_hi:[0,1]
	v_pk_fma_f32 v[108:109], v[102:103], v[26:27], v[104:105] op_sel:[0,0,1] op_sel_hi:[0,1,0] neg_hi:[0,0,1]
	v_pk_mul_f32 v[104:105], v[112:113], v[8:9] op_sel_hi:[0,1]
	v_pk_add_f32 v[26:27], v[10:11], v[108:109]
	v_pk_add_f32 v[10:11], v[10:11], v[108:109] neg_lo:[0,1] neg_hi:[0,1]
	v_pk_fma_f32 v[108:109], v[112:113], v[8:9], v[104:105] op_sel:[1,0,1] op_sel_hi:[1,1,0] neg_lo:[0,0,1] neg_hi:[0,0,1]
	v_pk_fma_f32 v[8:9], v[112:113], v[8:9], v[104:105] op_sel:[1,0,1] op_sel_hi:[1,1,0]
	v_pk_mul_f32 v[104:105], v[112:113], v[24:25] op_sel_hi:[0,1]
	v_pk_fma_f32 v[120:121], v[112:113], v[24:25], v[104:105] op_sel:[1,0,1] op_sel_hi:[1,1,0] neg_lo:[0,0,1]
	v_pk_add_f32 v[16:17], v[16:17], v[130:131] neg_lo:[0,1] neg_hi:[0,1]
	s_nop 0
	v_pk_add_f32 v[24:25], v[16:17], v[120:121]
	v_pk_add_f32 v[0:1], v[0:1], v[122:123] neg_lo:[0,1] neg_hi:[0,1]
	s_waitcnt lgkmcnt(0)
	v_pk_mul_f32 v[104:105], v[116:117], v[24:25] op_sel:[1,0]
	v_mov_b32_e32 v109, v9
	v_pk_fma_f32 v[112:113], v[116:117], v[24:25], v[104:105] op_sel:[0,0,1] op_sel_hi:[0,1,0] neg_hi:[0,0,1]
	v_pk_add_f32 v[22:23], v[22:23], v[188:189] neg_lo:[0,1] neg_hi:[0,1]
	v_pk_add_f32 v[8:9], v[0:1], v[108:109]
	v_pk_mul_f32 v[104:105], v[100:101], v[22:23] op_sel_hi:[0,1]
	v_pk_add_f32 v[20:21], v[20:21], v[106:107] neg_lo:[0,1] neg_hi:[0,1]
	v_pk_add_f32 v[24:25], v[8:9], v[112:113]
	v_pk_add_f32 v[8:9], v[8:9], v[112:113] neg_lo:[0,1] neg_hi:[0,1]
	v_pk_fma_f32 v[112:113], v[100:101], v[22:23], v[104:105] op_sel:[1,0,1] op_sel_hi:[1,1,0] neg_lo:[0,0,1] neg_hi:[0,0,1]
	v_pk_fma_f32 v[22:23], v[100:101], v[22:23], v[104:105] op_sel:[1,0,1] op_sel_hi:[1,1,0]
	v_pk_mul_f32 v[100:101], v[114:115], v[20:21] op_sel_hi:[0,1]
	v_pk_fma_f32 v[104:105], v[114:115], v[20:21], v[100:101] op_sel:[1,0,1] op_sel_hi:[1,1,0] neg_lo:[0,0,1]
	v_pk_add_f32 v[18:19], v[18:19], v[118:119] neg_lo:[0,1] neg_hi:[0,1]
	v_pk_add_f32 v[4:5], v[4:5], v[128:129] neg_lo:[0,1] neg_hi:[0,1]
	v_pk_mul_f32 v[100:101], v[102:103], v[18:19] op_sel_hi:[0,1]
	v_pk_add_f32 v[16:17], v[16:17], v[120:121] neg_lo:[0,1] neg_hi:[0,1]
	v_mov_b32_e32 v177, v15
	v_pk_add_f32 v[20:21], v[4:5], v[104:105]
	v_pk_add_f32 v[4:5], v[4:5], v[104:105] neg_lo:[0,1] neg_hi:[0,1]
	v_pk_fma_f32 v[104:105], v[102:103], v[18:19], v[100:101] op_sel:[1,0,1] op_sel_hi:[1,1,0] neg_lo:[0,0,1] neg_hi:[0,0,1]
	v_pk_fma_f32 v[18:19], v[102:103], v[18:19], v[100:101] op_sel:[1,0,1] op_sel_hi:[1,1,0]
	v_pk_mul_f32 v[100:101], v[116:117], v[16:17] op_sel_hi:[0,1]
	v_pk_add_f32 v[14:15], v[6:7], v[176:177]
	v_mov_b32_e32 v191, v31
	v_pk_fma_f32 v[102:103], v[116:117], v[16:17], v[100:101] op_sel:[1,0,1] op_sel_hi:[1,1,0] neg_lo:[0,0,1]
	v_pk_add_f32 v[30:31], v[14:15], v[190:191]
	v_pk_add_f32 v[6:7], v[6:7], v[176:177] neg_lo:[0,1] neg_hi:[0,1]
	v_mov_b32_e32 v113, v23
	v_pk_add_f32 v[2:3], v[2:3], v[110:111] neg_lo:[0,1] neg_hi:[0,1]
	v_mov_b32_e32 v105, v19
	v_pk_add_f32 v[0:1], v[0:1], v[108:109] neg_lo:[0,1] neg_hi:[0,1]
	v_pk_add_f32 v[14:15], v[14:15], v[190:191] neg_lo:[0,1] neg_hi:[0,1]
	v_pk_add_f32 v[22:23], v[6:7], v[112:113]
	v_pk_add_f32 v[6:7], v[6:7], v[112:113] neg_lo:[0,1] neg_hi:[0,1]
	v_pk_add_f32 v[18:19], v[2:3], v[104:105]
	v_pk_add_f32 v[2:3], v[2:3], v[104:105] neg_lo:[0,1] neg_hi:[0,1]
	v_pk_add_f32 v[16:17], v[0:1], v[102:103]
	v_pk_add_f32 v[0:1], v[0:1], v[102:103] neg_lo:[0,1] neg_hi:[0,1]
	ds_write2_b64 v135, v[30:31], v[28:29] offset1:34
	ds_write2_b64 v135, v[26:27], v[24:25] offset0:68 offset1:102
	ds_write2_b64 v135, v[22:23], v[20:21] offset0:136 offset1:170
	ds_write2_b64 v135, v[18:19], v[16:17] offset0:204 offset1:238
	ds_write2_b64 v98, v[14:15], v[12:13] offset0:16 offset1:50
	ds_write2_b64 v98, v[10:11], v[8:9] offset0:84 offset1:118
	ds_write2_b64 v98, v[6:7], v[4:5] offset0:152 offset1:186
	ds_write2_b64 v98, v[2:3], v[0:1] offset0:220 offset1:254
	s_waitcnt lgkmcnt(0)
	s_barrier
; template <bool LAT>
; __device__ __forceinline__ void hyconv_unit(const Frame& F, LAS f32x2v* X, const TwHalf tw, LAS bf16* OUT, const float* skip, bf16* MIX, int u) {
;     ...
;                 f32x2v g[16], zp[16];
;                 { const bf16* g0 = H0 + (size_t)(ord * 256 + c0) * L + n; const bf16* g1 = H1 + (size_t)(ord * 256 + c0) * L + n; const bf16* v0 = H0 + (size_t)(512 + c0) * L + n; const bf16* v1 = H1 + (size_t)(512 + c0) * L + n;
; #pragma unroll
;                   for (int r = 0; r < 16; ++r) { g[r] = (f32x2v){0.f, 0.f}; zp[r] = g[r]; if (act) { g[r] = (f32x2v){bf2f(g0[r * L]), bf2f(g1[r * L])}; zp[r] = (f32x2v){bf2f(v0[r * L]), bf2f(v1[r * L])}; } } }
	v_lshl_add_u64 v[104:105], v[56:57], 0, s[90:91]
	v_lshl_add_u64 v[102:103], v[62:63], 0, s[90:91]
	v_mov_b32_e32 v2, 0
	v_mov_b32_e32 v3, 0
	v_mov_b32_e32 v4, 0
	v_mov_b32_e32 v5, 0
	v_mov_b32_e32 v0, 0
	v_mov_b32_e32 v1, 0
	v_mov_b32_e32 v6, 0
	v_mov_b32_e32 v7, 0
	v_mov_b32_e32 v10, 0
	v_mov_b32_e32 v11, 0
	v_mov_b32_e32 v12, 0
	v_mov_b32_e32 v13, 0
	v_mov_b32_e32 v8, 0
	v_mov_b32_e32 v9, 0
	v_mov_b32_e32 v14, 0
	v_mov_b32_e32 v15, 0
	v_mov_b32_e32 v18, 0
	v_mov_b32_e32 v19, 0
	v_mov_b32_e32 v20, 0
	v_mov_b32_e32 v21, 0
	v_mov_b32_e32 v16, 0
	v_mov_b32_e32 v17, 0
	v_mov_b32_e32 v22, 0
	v_mov_b32_e32 v23, 0
	v_mov_b32_e32 v26, 0
	v_mov_b32_e32 v27, 0
	v_mov_b32_e32 v28, 0
	v_mov_b32_e32 v29, 0
	v_mov_b32_e32 v24, 0
	v_mov_b32_e32 v25, 0
	v_mov_b32_e32 v98, 0
	v_mov_b32_e32 v99, 0
	v_mov_b32_e32 v100, 0
	v_mov_b32_e32 v101, 0
	v_mov_b32_e32 v106, 0
	v_mov_b32_e32 v107, 0
	v_mov_b32_e32 v30, 0
	v_mov_b32_e32 v31, 0
	v_mov_b32_e32 v108, 0
	v_mov_b32_e32 v109, 0
	v_mov_b32_e32 v112, 0
	v_mov_b32_e32 v113, 0
	v_mov_b32_e32 v114, 0
	v_mov_b32_e32 v115, 0
	v_mov_b32_e32 v110, 0
	v_mov_b32_e32 v111, 0
	v_mov_b32_e32 v116, 0
	v_mov_b32_e32 v117, 0
	v_mov_b32_e32 v120, 0
	v_mov_b32_e32 v121, 0
	v_mov_b32_e32 v122, 0
	v_mov_b32_e32 v123, 0
	v_mov_b32_e32 v118, 0
	v_mov_b32_e32 v119, 0
	v_mov_b32_e32 v124, 0
	v_mov_b32_e32 v125, 0
	v_mov_b32_e32 v128, 0
	v_mov_b32_e32 v129, 0
	v_mov_b32_e32 v130, 0
	v_mov_b32_e32 v131, 0
	v_mov_b32_e32 v126, 0
	v_mov_b32_e32 v127, 0
	v_mov_b32_e32 v132, 0
	v_mov_b32_e32 v133, 0
	s_and_saveexec_b64 s[0:1], s[38:39]
	s_mov_b64 s[2:3], 0x1000
	v_lshl_add_u64 v[192:193], v[104:105], 0, s[2:3]
	v_lshl_add_u64 v[194:195], v[102:103], 0, s[2:3]
	global_load_ushort v2, v[104:105], off
	global_load_ushort v3, v[102:103], off
	global_load_ushort v4, v[52:53], off
	global_load_ushort v5, v[54:55], off
	global_load_ushort v0, v[104:105], off offset:512
	global_load_ushort v1, v[102:103], off offset:512
	global_load_ushort v6, v[52:53], off offset:512
	global_load_ushort v7, v[54:55], off offset:512
	global_load_ushort v10, v[104:105], off offset:1024
	global_load_ushort v11, v[102:103], off offset:1024
	global_load_ushort v12, v[52:53], off offset:1024
	global_load_ushort v13, v[54:55], off offset:1024
	global_load_ushort v8, v[104:105], off offset:1536
	global_load_ushort v9, v[102:103], off offset:1536
	global_load_ushort v14, v[52:53], off offset:1536
	global_load_ushort v15, v[54:55], off offset:1536
	global_load_ushort v18, v[104:105], off offset:2048
	global_load_ushort v19, v[102:103], off offset:2048
	global_load_ushort v20, v[52:53], off offset:2048
	global_load_ushort v21, v[54:55], off offset:2048
	global_load_ushort v16, v[104:105], off offset:2560
	global_load_ushort v17, v[102:103], off offset:2560
	global_load_ushort v22, v[52:53], off offset:2560
	global_load_ushort v23, v[54:55], off offset:2560
	global_load_ushort v26, v[104:105], off offset:3072
	global_load_ushort v27, v[102:103], off offset:3072
	global_load_ushort v28, v[52:53], off offset:3072
	global_load_ushort v29, v[54:55], off offset:3072
	global_load_ushort v24, v[104:105], off offset:3584
	global_load_ushort v25, v[102:103], off offset:3584
	global_load_ushort v98, v[52:53], off offset:3584
	global_load_ushort v99, v[54:55], off offset:3584
	global_load_ushort v100, v[192:193], off
	global_load_ushort v101, v[194:195], off
	global_load_ushort v106, v[66:67], off
	global_load_ushort v107, v[68:69], off
	global_load_ushort v30, v[192:193], off offset:512
	global_load_ushort v31, v[194:195], off offset:512
	global_load_ushort v108, v[70:71], off
	global_load_ushort v109, v[72:73], off
	global_load_ushort v112, v[192:193], off offset:1024
	global_load_ushort v113, v[194:195], off offset:1024
	global_load_ushort v114, v[74:75], off
	global_load_ushort v115, v[76:77], off
	global_load_ushort v110, v[192:193], off offset:1536
	global_load_ushort v111, v[194:195], off offset:1536
	global_load_ushort v116, v[78:79], off
	global_load_ushort v117, v[80:81], off
	s_waitcnt vmcnt(24)
	global_load_ushort v120, v[192:193], off offset:2048
	global_load_ushort v121, v[194:195], off offset:2048
	global_load_ushort v122, v[82:83], off
	global_load_ushort v123, v[84:85], off
	global_load_ushort v118, v[192:193], off offset:2560
	global_load_ushort v119, v[194:195], off offset:2560
	global_load_ushort v124, v[86:87], off
	global_load_ushort v125, v[88:89], off
	global_load_ushort v128, v[192:193], off offset:3072
	global_load_ushort v129, v[194:195], off offset:3072
	global_load_ushort v130, v[90:91], off
	global_load_ushort v131, v[92:93], off
	global_load_ushort v126, v[192:193], off offset:3584
	global_load_ushort v127, v[194:195], off offset:3584
	global_load_ushort v132, v[94:95], off
	global_load_ushort v133, v[96:97], off
	s_waitcnt vmcnt(0)
; __device__ __forceinline__ unsigned pk2(float lo, float hi) { const f32x2cv v = {lo, hi}; return __builtin_bit_cast(unsigned, __builtin_convertvector(v, bf16x2cv)); }
; __device__ __forceinline__ unsigned f2bf(float f) { return pk2(f, 0.f); }
; template <bool LAT>
; __device__ __forceinline__ void hyconv_unit(const Frame& F, LAS f32x2v* X, const TwHalf tw, LAS bf16* OUT, const float* skip, bf16* MIX, int u) {
;     ...
;                 f32x2v z[16];
; #pragma unroll
;                 for (int r = 0; r < 16; ++r) { z[r] = g[r] * (X[PADI(F.tid + 512 * r)] + zp[r] * skip[ord * 256 + c0 + r]); }
;                 if (ord == 0) { bf16* v0 = H0 + (size_t)(512 + c0) * L + n; bf16* v1 = H1 + (size_t)(512 + c0) * L + n;
; #pragma unroll
;                     for (int r = 0; r < 16; ++r) { if (act) { v0[r * L] = (bf16)f2bf(z[r].x); v1[r * L] = (bf16)f2bf(z[r].y); } X[PADI(F.tid + 512 * r)] = z[r]; } }
;                 else if (act) {
;                     v4u oa, ob, oc, od;
;                     oa.x = pk2(z[0].x, z[1].x); oa.y = pk2(z[2].x, z[3].x); oa.z = pk2(z[4].x, z[5].x); oa.w = pk2(z[6].x, z[7].x); ob.x = pk2(z[8].x, z[9].x); ob.y = pk2(z[10].x, z[11].x); ob.z = pk2(z[12].x, z[13].x); ob.w = pk2(z[14].x, z[15].x);
;                     oc.x = pk2(z[0].y, z[1].y); oc.y = pk2(z[2].y, z[3].y); oc.z = pk2(z[4].y, z[5].y); oc.w = pk2(z[6].y, z[7].y); od.x = pk2(z[8].y, z[9].y); od.y = pk2(z[10].y, z[11].y); od.z = pk2(z[12].y, z[13].y); od.w = pk2(z[14].y, z[15].y);
;                     bf16* m0 = MIX + (size_t)(rowb + n) * 1024 + c0; bf16* m1 = m0 + (size_t)L * 1024;
;                     *(v4u*)m0 = oa; *(v4u*)(m0 + 8) = ob; *(v4u*)m1 = oc; *(v4u*)(m1 + 8) = od; }
	v_lshlrev_b32_e32 v2, 16, v2
	v_lshlrev_b32_e32 v3, 16, v3
	v_lshlrev_b32_e32 v4, 16, v4
	v_lshlrev_b32_e32 v5, 16, v5
	v_lshlrev_b32_e32 v0, 16, v0
	v_lshlrev_b32_e32 v1, 16, v1
	v_lshlrev_b32_e32 v6, 16, v6
	v_lshlrev_b32_e32 v7, 16, v7
	v_lshlrev_b32_e32 v10, 16, v10
	v_lshlrev_b32_e32 v11, 16, v11
	v_lshlrev_b32_e32 v12, 16, v12
	v_lshlrev_b32_e32 v13, 16, v13
	v_lshlrev_b32_e32 v8, 16, v8
	v_lshlrev_b32_e32 v9, 16, v9
	v_lshlrev_b32_e32 v14, 16, v14
	v_lshlrev_b32_e32 v15, 16, v15
	v_lshlrev_b32_e32 v18, 16, v18
	v_lshlrev_b32_e32 v19, 16, v19
	v_lshlrev_b32_e32 v20, 16, v20
	v_lshlrev_b32_e32 v21, 16, v21
	v_lshlrev_b32_e32 v16, 16, v16
	v_lshlrev_b32_e32 v17, 16, v17
	v_lshlrev_b32_e32 v22, 16, v22
	v_lshlrev_b32_e32 v23, 16, v23
	v_lshlrev_b32_e32 v26, 16, v26
	v_lshlrev_b32_e32 v27, 16, v27
	v_lshlrev_b32_e32 v28, 16, v28
	v_lshlrev_b32_e32 v29, 16, v29
	v_lshlrev_b32_e32 v24, 16, v24
	v_lshlrev_b32_e32 v25, 16, v25
	v_lshlrev_b32_e32 v98, 16, v98
	v_lshlrev_b32_e32 v99, 16, v99
	v_lshlrev_b32_e32 v100, 16, v100
	v_lshlrev_b32_e32 v101, 16, v101
	v_lshlrev_b32_e32 v106, 16, v106
	v_lshlrev_b32_e32 v107, 16, v107
	v_lshlrev_b32_e32 v30, 16, v30
	v_lshlrev_b32_e32 v31, 16, v31
	v_lshlrev_b32_e32 v108, 16, v108
	v_lshlrev_b32_e32 v109, 16, v109
	v_lshlrev_b32_e32 v112, 16, v112
	v_lshlrev_b32_e32 v113, 16, v113
	v_lshlrev_b32_e32 v114, 16, v114
	v_lshlrev_b32_e32 v115, 16, v115
	v_lshlrev_b32_e32 v110, 16, v110
	v_lshlrev_b32_e32 v111, 16, v111
	v_lshlrev_b32_e32 v116, 16, v116
	v_lshlrev_b32_e32 v117, 16, v117
	v_lshlrev_b32_e32 v120, 16, v120
	v_lshlrev_b32_e32 v121, 16, v121
	v_lshlrev_b32_e32 v122, 16, v122
	v_lshlrev_b32_e32 v123, 16, v123
	v_lshlrev_b32_e32 v118, 16, v118
	v_lshlrev_b32_e32 v119, 16, v119
	v_lshlrev_b32_e32 v124, 16, v124
	v_lshlrev_b32_e32 v125, 16, v125
	v_lshlrev_b32_e32 v128, 16, v128
	v_lshlrev_b32_e32 v129, 16, v129
	v_lshlrev_b32_e32 v130, 16, v130
	v_lshlrev_b32_e32 v131, 16, v131
	v_lshlrev_b32_e32 v126, 16, v126
	v_lshlrev_b32_e32 v127, 16, v127
	v_lshlrev_b32_e32 v132, 16, v132
	v_lshlrev_b32_e32 v133, 16, v133
	s_or_b64 exec, exec, s[0:1]
	s_mov_b32 s15, s91
	s_xor_b64 s[0:1], s[20:21], -1
	s_lshl_b64 s[2:3], s[14:15], 2
	s_add_u32 s2, s6, s2
	s_addc_u32 s3, s7, s3
	ds_read_b64 v[190:191], v140
	global_load_dwordx4 v[176:179], v181, s[2:3] offset:48
	global_load_dwordx4 v[182:185], v181, s[2:3] offset:32
	global_load_dwordx4 v[186:189], v181, s[2:3] offset:16
	global_load_dwordx4 v[102:105], v181, s[2:3]
	s_mov_b64 s[2:3], -1
	s_and_b64 vcc, exec, s[0:1]
	s_waitcnt vmcnt(0) lgkmcnt(0)
	v_pk_fma_f32 v[4:5], v[4:5], v[102:103], v[190:191] op_sel_hi:[1,0,1]
	s_nop 0
	v_pk_mul_f32 v[2:3], v[2:3], v[4:5]
	ds_read_b64 v[4:5], v141 offset:4096
	s_waitcnt lgkmcnt(0)
	v_pk_fma_f32 v[4:5], v[6:7], v[102:103], v[4:5] op_sel:[0,1,0]
	s_nop 0
	v_pk_mul_f32 v[102:103], v[0:1], v[4:5]
	ds_read_b64 v[0:1], v142 offset:8192
	v_mov_b32_e32 v6, v105
	s_waitcnt lgkmcnt(0)
	v_pk_fma_f32 v[0:1], v[12:13], v[104:105], v[0:1] op_sel_hi:[1,0,1]
	s_nop 0
	v_pk_mul_f32 v[4:5], v[10:11], v[0:1]
	ds_read_b64 v[0:1], v143 offset:12288
	v_mov_b32_e32 v10, v189
	s_waitcnt lgkmcnt(0)
	v_pk_fma_f32 v[0:1], v[14:15], v[6:7], v[0:1] op_sel_hi:[1,0,1]
	s_nop 0
	v_pk_mul_f32 v[104:105], v[8:9], v[0:1]
	ds_read_b64 v[0:1], v144 offset:16384
	ds_read_b64 v[6:7], v145 offset:20480
	s_waitcnt lgkmcnt(1)
	v_pk_fma_f32 v[0:1], v[20:21], v[186:187], v[0:1] op_sel_hi:[1,0,1]
	s_waitcnt lgkmcnt(0)
	v_pk_fma_f32 v[6:7], v[22:23], v[186:187], v[6:7] op_sel:[0,1,0]
	v_pk_mul_f32 v[0:1], v[18:19], v[0:1]
	v_pk_mul_f32 v[12:13], v[16:17], v[6:7]
	ds_read_b64 v[6:7], v146 offset:24576
	v_mov_b32_e32 v18, v185
	s_waitcnt lgkmcnt(0)
	v_pk_fma_f32 v[6:7], v[28:29], v[188:189], v[6:7] op_sel_hi:[1,0,1]
	s_nop 0
	v_pk_mul_f32 v[8:9], v[26:27], v[6:7]
	ds_read_b64 v[6:7], v147 offset:28672
	ds_read_b64 v[26:27], v155 offset:61440
	v_mov_b32_e32 v28, v179
	s_waitcnt lgkmcnt(1)
	v_pk_fma_f32 v[6:7], v[98:99], v[10:11], v[6:7] op_sel_hi:[1,0,1]
	s_nop 0
	v_pk_mul_f32 v[22:23], v[24:25], v[6:7]
	ds_read_b64 v[6:7], v148 offset:32768
	ds_read_b64 v[10:11], v149 offset:36864
	s_waitcnt lgkmcnt(2)
	v_pk_fma_f32 v[26:27], v[132:133], v[28:29], v[26:27] op_sel_hi:[1,0,1]
	s_waitcnt lgkmcnt(1)
	v_pk_fma_f32 v[6:7], v[106:107], v[182:183], v[6:7] op_sel_hi:[1,0,1]
	s_waitcnt lgkmcnt(0)
	v_pk_fma_f32 v[10:11], v[108:109], v[182:183], v[10:11] op_sel:[0,1,0]
	v_pk_mul_f32 v[6:7], v[100:101], v[6:7]
	v_pk_mul_f32 v[16:17], v[30:31], v[10:11]
	ds_read_b64 v[10:11], v150 offset:40960
	v_pk_mul_f32 v[26:27], v[126:127], v[26:27]
	s_waitcnt lgkmcnt(0)
	v_pk_fma_f32 v[10:11], v[114:115], v[184:185], v[10:11] op_sel_hi:[1,0,1]
	s_nop 0
	v_pk_mul_f32 v[14:15], v[112:113], v[10:11]
	ds_read_b64 v[10:11], v151 offset:45056
	s_waitcnt lgkmcnt(0)
	v_pk_fma_f32 v[10:11], v[116:117], v[18:19], v[10:11] op_sel_hi:[1,0,1]
	s_nop 0
	v_pk_mul_f32 v[24:25], v[110:111], v[10:11]
	ds_read_b64 v[10:11], v152 offset:49152
	ds_read_b64 v[18:19], v153 offset:53248
	s_waitcnt lgkmcnt(1)
	v_pk_fma_f32 v[10:11], v[122:123], v[176:177], v[10:11] op_sel_hi:[1,0,1]
	s_waitcnt lgkmcnt(0)
	v_pk_fma_f32 v[18:19], v[124:125], v[176:177], v[18:19] op_sel:[0,1,0]
	v_pk_mul_f32 v[10:11], v[120:121], v[10:11]
	v_pk_mul_f32 v[20:21], v[118:119], v[18:19]
	ds_read_b64 v[18:19], v154 offset:57344
	s_waitcnt lgkmcnt(0)
	v_pk_fma_f32 v[18:19], v[130:131], v[178:179], v[18:19] op_sel_hi:[1,0,1]
	s_nop 0
	v_pk_mul_f32 v[18:19], v[128:129], v[18:19]
	s_cbranch_vccz .LBB0_883
	s_and_saveexec_b64 s[2:3], s[38:39]
	s_cbranch_execz .LBB0_882
	v_cvt_pk_bf16_f32 v28, v2, v102
	v_cvt_pk_bf16_f32 v29, v4, v104
	v_cvt_pk_bf16_f32 v30, v0, v12
	v_cvt_pk_bf16_f32 v31, v8, v22
	v_cvt_pk_bf16_f32 v98, v6, v16
	v_cvt_pk_bf16_f32 v99, v14, v24
	v_cvt_pk_bf16_f32 v100, v10, v20
	v_cvt_pk_bf16_f32 v101, v18, v26
	v_cvt_pk_bf16_f32 v106, v3, v103
	v_cvt_pk_bf16_f32 v107, v5, v105
	v_cvt_pk_bf16_f32 v108, v1, v13
	v_cvt_pk_bf16_f32 v109, v9, v23
	v_cvt_pk_bf16_f32 v110, v7, v17
	v_cvt_pk_bf16_f32 v111, v15, v25
	v_cvt_pk_bf16_f32 v112, v11, v21
	v_cvt_pk_bf16_f32 v113, v19, v27
	global_store_dwordx4 v[58:59], v[28:31], off
	global_store_dwordx4 v[58:59], v[98:101], off offset:16
	global_store_dwordx4 v[60:61], v[106:109], off
	global_store_dwordx4 v[64:65], v[110:113], off

; template <int R, class XT, class TWT>
; __device__ __forceinline__ void dif_task(XT X, TWT tw, int s, int task) {
;     const int lgM = 13 - s, lgq = lgM - R, q = 1 << lgq;
;     const int j0 = task & (q - 1), blk = task >> lgq, base = (blk << lgM) + j0;
;     const int pb = PADI(base), qp = (q >= 32) ? q + (q >> 4) : q;
;     f32x2v v[1 << R];
; #pragma unroll
;     for (int k = 0; k < (1 << R); ++k) v[k] = X[pb + k * qp];
; #pragma unroll
;     for (int r = 0; r < R; ++r) {
;         const int pb = R - 1 - r;
; #pragma unroll
;         for (int k = 0; k < (1 << R); ++k) if (!((k >> pb) & 1)) {
;             const int klo = k & ((1 << pb) - 1);
;             const f32x2v w = tw[(j0 + (klo << lgq)) << (s + r)];
;             const f32x2v a = v[k], b = v[k + (1 << pb)], d = a - b;
;             v[k] = a + b; v[k + (1 << pb)] = (f32x2v){d.x * w.x - d.y * w.y, d.x * w.y + d.y * w.x};
;         }
;     }
; #pragma unroll
;     for (int k = 0; k < (1 << R); ++k) X[pb + k * qp] = v[k];
; }
; template <bool LAT>
; __device__ __forceinline__ void hyconv_unit(const Frame& F, LAS f32x2v* X, const TwHalf tw, LAS bf16* OUT, const float* skip, bf16* MIX, int u) {
;     ...
;             const f32x2v* SP = SPb + (size_t)ord * 256 * N;
;             f32x4 kq[8];
; #pragma unroll
;             for (int r = 0; r < 8; ++r) kq[r] = *(const f32x4*)(SP + 2 * (F.tid + 512 * r));
;             fft_fwd_upper(X, tw, 13 - lgN, F.tid);
.LBB0_937:
	s_lshl_b32 s90, s2, 17
	s_lshl_b64 s[0:1], s[90:91], 3
	s_add_u32 s0, s5, s0
	s_addc_u32 s1, s8, s1
	v_lshl_add_u64 v[0:1], v[44:45], 3, s[0:1]
	v_lshl_add_u64 v[2:3], v[50:51], 3, s[0:1]
	global_load_dwordx4 v[28:31], v[0:1], off
	global_load_dwordx4 v[24:27], v[2:3], off
	v_lshl_add_u64 v[0:1], v[52:53], 3, s[0:1]
	v_lshl_add_u64 v[2:3], v[54:55], 3, s[0:1]
	global_load_dwordx4 v[20:23], v[0:1], off
	global_load_dwordx4 v[16:19], v[2:3], off
	v_lshl_add_u64 v[0:1], v[56:57], 3, s[0:1]
	v_lshl_add_u64 v[2:3], v[58:59], 3, s[0:1]
	global_load_dwordx4 v[12:15], v[0:1], off
	global_load_dwordx4 v[8:11], v[2:3], off
	v_lshl_add_u64 v[0:1], v[60:61], 3, s[0:1]
	v_lshl_add_u64 v[2:3], v[62:63], 3, s[0:1]
	global_load_dwordx4 v[4:7], v[0:1], off
	s_nop 0
	global_load_dwordx4 v[0:3], v[2:3], off
	ds_read2_b64 v[96:99], v130 offset1:34
	ds_read2_b64 v[100:103], v130 offset0:68 offset1:102
	ds_read2_b64 v[104:107], v130 offset0:136 offset1:170
	ds_read2_b64 v[108:111], v130 offset0:204 offset1:238
	v_add_u32_e32 v94, 0x800, v130
	ds_read2_b64 v[112:115], v94 offset0:16 offset1:50
	ds_read2_b64 v[116:119], v94 offset0:84 offset1:118
	ds_read2_b64 v[120:123], v94 offset0:152 offset1:186
	ds_read2_b64 v[124:127], v94 offset0:220 offset1:254
	ds_read2st64_b64 v[172:175], v159 offset1:16
	ds_read_b64 v[128:129], v160
	ds_read_b64 v[176:177], v161
	ds_read_b64 v[178:179], v162
	ds_read_b64 v[182:183], v163
	ds_read_b64 v[184:185], v164
	ds_read_b64 v[186:187], v133
	ds_read_b64 v[188:189], v131
	s_waitcnt lgkmcnt(11)
	v_pk_add_f32 v[190:191], v[96:97], v[112:113] neg_lo:[0,1] neg_hi:[0,1]
	v_pk_add_f32 v[96:97], v[96:97], v[112:113]
	s_waitcnt lgkmcnt(7)
	v_pk_mul_f32 v[192:193], v[190:191], v[172:173] op_sel:[1,1] op_sel_hi:[1,0]
	s_lshl_b32 s0, s2, 8
	v_pk_fma_f32 v[194:195], v[190:191], v[172:173], v[192:193] op_sel_hi:[0,1,1] neg_lo:[0,0,1]
	v_pk_add_f32 v[190:191], v[104:105], v[120:121] neg_lo:[0,1] neg_hi:[0,1]
	v_pk_add_f32 v[104:105], v[104:105], v[120:121]
	v_pk_mul_f32 v[192:193], v[190:191], v[172:173] op_sel:[1,0] op_sel_hi:[0,0]
	v_pk_fma_f32 v[196:197], v[190:191], v[172:173], v[192:193] op_sel:[0,1,0] neg_hi:[0,0,1]
	v_pk_add_f32 v[112:113], v[96:97], v[104:105]
	v_pk_add_f32 v[172:173], v[194:195], v[196:197] neg_lo:[0,1] neg_hi:[0,1]
	s_waitcnt lgkmcnt(0)
	v_xor_b32_e32 v95, 0x80000000, v188
	v_pk_mul_f32 v[190:191], v[178:179], v[172:173] op_sel:[1,1] op_sel_hi:[0,1]
	v_pk_fma_f32 v[192:193], v[178:179], v[172:173], v[190:191] op_sel_hi:[1,0,1] neg_lo:[0,0,1]
	v_pk_add_f32 v[96:97], v[96:97], v[104:105] neg_lo:[0,1] neg_hi:[0,1]
	v_pk_add_f32 v[172:173], v[100:101], v[116:117] neg_lo:[0,1] neg_hi:[0,1]
	v_pk_add_f32 v[100:101], v[100:101], v[116:117]
	v_pk_mul_f32 v[190:191], v[172:173], v[174:175] op_sel:[1,1] op_sel_hi:[1,0]
	v_pk_mul_f32 v[104:105], v[96:97], v[178:179] op_sel:[1,1] op_sel_hi:[1,0]
	v_pk_fma_f32 v[198:199], v[172:173], v[174:175], v[190:191] op_sel_hi:[0,1,1] neg_lo:[0,0,1]
	v_pk_add_f32 v[172:173], v[108:109], v[124:125] neg_lo:[0,1] neg_hi:[0,1]
	v_pk_add_f32 v[108:109], v[108:109], v[124:125]
	v_pk_mul_f32 v[190:191], v[172:173], v[174:175] op_sel:[1,0] op_sel_hi:[0,0]
	v_pk_fma_f32 v[202:203], v[172:173], v[174:175], v[190:191] op_sel:[0,1,0] neg_hi:[0,0,1]
	v_pk_add_f32 v[116:117], v[100:101], v[108:109]
	v_pk_add_f32 v[172:173], v[198:199], v[202:203] neg_lo:[0,1] neg_hi:[0,1]
	v_pk_add_f32 v[120:121], v[112:113], v[116:117]
	v_pk_mul_f32 v[174:175], v[178:179], v[172:173] op_sel_hi:[0,1]
	v_pk_fma_f32 v[190:191], v[178:179], v[172:173], v[174:175] op_sel:[1,0,1] op_sel_hi:[1,1,0] neg_hi:[0,0,1]
	v_pk_add_f32 v[112:113], v[112:113], v[116:117] neg_lo:[0,1] neg_hi:[0,1]
	v_pk_add_f32 v[172:173], v[192:193], v[190:191] neg_lo:[0,1] neg_hi:[0,1]
	v_pk_mul_f32 v[116:117], v[112:113], v[184:185] op_sel:[1,1] op_sel_hi:[1,0]
	v_pk_mul_f32 v[174:175], v[184:185], v[172:173] op_sel:[1,1] op_sel_hi:[0,1]
	v_pk_fma_f32 v[204:205], v[184:185], v[172:173], v[174:175] op_sel_hi:[1,0,1] neg_lo:[0,0,1]
	s_or_b32 s14, s0, s16
	v_pk_add_f32 v[172:173], v[98:99], v[114:115] neg_lo:[0,1] neg_hi:[0,1]
	v_pk_add_f32 v[98:99], v[98:99], v[114:115]
	v_pk_mul_f32 v[174:175], v[172:173], v[128:129] op_sel:[1,1] op_sel_hi:[1,0]
	s_nop 0
	s_lshl_b32 s90, s14, 9
	v_pk_fma_f32 v[206:207], v[172:173], v[128:129], v[174:175] op_sel_hi:[0,1,1] neg_lo:[0,0,1]
	v_pk_add_f32 v[172:173], v[106:107], v[122:123] neg_lo:[0,1] neg_hi:[0,1]
	v_pk_add_f32 v[106:107], v[106:107], v[122:123]
	v_pk_mul_f32 v[174:175], v[172:173], v[128:129] op_sel:[1,0] op_sel_hi:[0,0]
	v_pk_fma_f32 v[208:209], v[172:173], v[128:129], v[174:175] op_sel:[0,1,0] neg_hi:[0,0,1]
	v_pk_add_f32 v[114:115], v[98:99], v[106:107]
	v_pk_add_f32 v[128:129], v[206:207], v[208:209] neg_lo:[0,1] neg_hi:[0,1]
	v_pk_add_f32 v[98:99], v[98:99], v[106:107] neg_lo:[0,1] neg_hi:[0,1]
	v_pk_mul_f32 v[172:173], v[182:183], v[128:129] op_sel:[1,1] op_sel_hi:[0,1]
	v_pk_fma_f32 v[174:175], v[182:183], v[128:129], v[172:173] op_sel_hi:[1,0,1] neg_lo:[0,0,1]
	s_nop 0
	v_pk_add_f32 v[128:129], v[102:103], v[118:119] neg_lo:[0,1] neg_hi:[0,1]
	v_pk_add_f32 v[102:103], v[102:103], v[118:119]
	v_pk_mul_f32 v[172:173], v[128:129], v[176:177] op_sel:[1,1] op_sel_hi:[1,0]
	s_nop 0
	v_pk_fma_f32 v[220:221], v[128:129], v[176:177], v[172:173] op_sel_hi:[0,1,1] neg_lo:[0,0,1]
	v_pk_add_f32 v[128:129], v[110:111], v[126:127] neg_lo:[0,1] neg_hi:[0,1]
	v_pk_add_f32 v[110:111], v[110:111], v[126:127]
	v_pk_mul_f32 v[172:173], v[128:129], v[176:177] op_sel:[1,0] op_sel_hi:[0,0]
	v_pk_fma_f32 v[222:223], v[128:129], v[176:177], v[172:173] op_sel:[0,1,0] neg_hi:[0,0,1]
	v_pk_add_f32 v[118:119], v[102:103], v[110:111]
; template <int R, class XT, class TWT>
; __device__ __forceinline__ void dif_task(XT X, TWT tw, int s, int task) {
;     const int lgM = 13 - s, lgq = lgM - R, q = 1 << lgq;
;     const int j0 = task & (q - 1), blk = task >> lgq, base = (blk << lgM) + j0;
;     const int pb = PADI(base), qp = (q >= 32) ? q + (q >> 4) : q;
;     f32x2v v[1 << R];
; #pragma unroll
;     for (int k = 0; k < (1 << R); ++k) v[k] = X[pb + k * qp];
; #pragma unroll
;     for (int r = 0; r < R; ++r) {
;         const int pb = R - 1 - r;
; #pragma unroll
;         for (int k = 0; k < (1 << R); ++k) if (!((k >> pb) & 1)) {
;             const int klo = k & ((1 << pb) - 1);
;             const f32x2v w = tw[(j0 + (klo << lgq)) << (s + r)];
;             const f32x2v a = v[k], b = v[k + (1 << pb)], d = a - b;
;             v[k] = a + b; v[k + (1 << pb)] = (f32x2v){d.x * w.x - d.y * w.y, d.x * w.y + d.y * w.x};
;         }
;     }
; #pragma unroll
;     for (int k = 0; k < (1 << R); ++k) X[pb + k * qp] = v[k];
; }
	v_pk_add_f32 v[128:129], v[220:221], v[222:223] neg_lo:[0,1] neg_hi:[0,1]
	v_pk_add_f32 v[122:123], v[114:115], v[118:119]
	v_pk_mul_f32 v[172:173], v[186:187], v[128:129] op_sel_hi:[0,1]
	v_pk_fma_f32 v[176:177], v[186:187], v[128:129], v[172:173] op_sel:[1,0,1] op_sel_hi:[1,1,0] neg_hi:[0,0,1]
	v_pk_add_f32 v[124:125], v[120:121], v[122:123]
	v_pk_add_f32 v[128:129], v[174:175], v[176:177] neg_lo:[0,1] neg_hi:[0,1]
	v_pk_add_f32 v[120:121], v[120:121], v[122:123] neg_lo:[0,1] neg_hi:[0,1]
	v_pk_mul_f32 v[172:173], v[184:185], v[128:129] op_sel_hi:[0,1]
	v_pk_fma_f32 v[224:225], v[184:185], v[128:129], v[172:173] op_sel:[1,0,1] op_sel_hi:[1,1,0]
	v_pk_fma_f32 v[128:129], v[184:185], v[128:129], v[172:173] op_sel:[1,0,1] op_sel_hi:[1,1,0] neg_lo:[0,0,1] neg_hi:[0,0,1]
	v_cndmask_b32_e64 v173, v95, v189, s[44:45]
	v_cndmask_b32_e64 v172, v189, v188, s[44:45]
	v_pk_mul_f32 v[122:123], v[120:121], v[172:173] op_sel:[1,1] op_sel_hi:[1,0]
	v_mov_b32_e32 v225, v129
	v_pk_fma_f32 v[126:127], v[120:121], v[172:173], v[122:123] op_sel_hi:[0,1,1] neg_lo:[0,0,1]
	v_pk_fma_f32 v[120:121], v[112:113], v[184:185], v[116:117] op_sel_hi:[0,1,1] neg_lo:[0,0,1]
	v_pk_add_f32 v[112:113], v[114:115], v[118:119] neg_lo:[0,1] neg_hi:[0,1]
	v_pk_add_f32 v[128:129], v[204:205], v[224:225] neg_lo:[0,1] neg_hi:[0,1]
	v_pk_mul_f32 v[114:115], v[112:113], v[184:185] op_sel_hi:[1,0]
	v_mov_b32_e32 v95, s4
	v_pk_fma_f32 v[116:117], v[112:113], v[184:185], v[114:115] op_sel:[0,1,1] op_sel_hi:[1,1,0] neg_hi:[0,0,1]
	s_nop 0
	v_pk_add_f32 v[114:115], v[120:121], v[116:117] neg_lo:[0,1] neg_hi:[0,1]
	v_pk_add_f32 v[112:113], v[120:121], v[116:117]
	v_pk_mul_f32 v[116:117], v[172:173], v[114:115] op_sel:[1,1] op_sel_hi:[0,1]
	v_pk_fma_f32 v[118:119], v[172:173], v[114:115], v[116:117] op_sel_hi:[1,0,1] neg_lo:[0,0,1]
	s_nop 0
	v_pk_fma_f32 v[114:115], v[96:97], v[178:179], v[104:105] op_sel_hi:[0,1,1] neg_lo:[0,0,1]
	v_pk_add_f32 v[96:97], v[100:101], v[108:109] neg_lo:[0,1] neg_hi:[0,1]
	s_nop 0
	v_pk_mul_f32 v[100:101], v[96:97], v[178:179] op_sel_hi:[1,0]
	s_nop 0
	v_pk_fma_f32 v[104:105], v[96:97], v[178:179], v[100:101] op_sel:[0,1,1] op_sel_hi:[1,1,0]
	v_pk_fma_f32 v[96:97], v[96:97], v[178:179], v[100:101] op_sel:[0,1,1] op_sel_hi:[1,1,0] neg_lo:[0,0,1] neg_hi:[0,0,1]
	v_pk_mul_f32 v[100:101], v[98:99], v[182:183] op_sel:[1,1] op_sel_hi:[1,0]
	v_mov_b32_e32 v105, v97
	v_pk_fma_f32 v[106:107], v[98:99], v[182:183], v[100:101] op_sel_hi:[0,1,1] neg_lo:[0,0,1]
	v_pk_add_f32 v[98:99], v[102:103], v[110:111] neg_lo:[0,1] neg_hi:[0,1]
	v_pk_add_f32 v[96:97], v[114:115], v[104:105]
	v_pk_mul_f32 v[100:101], v[98:99], v[186:187] op_sel_hi:[1,0]
	v_pk_add_f32 v[110:111], v[206:207], v[208:209]
	v_pk_fma_f32 v[102:103], v[98:99], v[186:187], v[100:101] op_sel:[0,1,1] op_sel_hi:[1,1,0] neg_hi:[0,0,1]
	s_nop 0
	v_pk_add_f32 v[98:99], v[106:107], v[102:103]
	s_nop 0
	v_pk_add_f32 v[100:101], v[96:97], v[98:99]
	v_pk_add_f32 v[96:97], v[96:97], v[98:99] neg_lo:[0,1] neg_hi:[0,1]
	s_nop 0
	v_pk_mul_f32 v[98:99], v[172:173], v[96:97] op_sel:[1,1] op_sel_hi:[0,1]
	v_pk_fma_f32 v[108:109], v[172:173], v[96:97], v[98:99] op_sel_hi:[1,0,1] neg_lo:[0,0,1]
	s_nop 0
	v_pk_add_f32 v[96:97], v[114:115], v[104:105] neg_lo:[0,1] neg_hi:[0,1]
	v_pk_add_f32 v[114:115], v[220:221], v[222:223]
	v_pk_mul_f32 v[98:99], v[184:185], v[96:97] op_sel:[1,1] op_sel_hi:[0,1]
	v_pk_fma_f32 v[104:105], v[184:185], v[96:97], v[98:99] op_sel_hi:[1,0,1] neg_lo:[0,0,1]
	v_pk_add_f32 v[116:117], v[110:111], v[114:115]
	v_pk_add_f32 v[96:97], v[106:107], v[102:103] neg_lo:[0,1] neg_hi:[0,1]
	s_nop 0
	v_pk_mul_f32 v[98:99], v[184:185], v[96:97] op_sel_hi:[0,1]
	v_pk_fma_f32 v[102:103], v[184:185], v[96:97], v[98:99] op_sel:[1,0,1] op_sel_hi:[1,1,0] neg_hi:[0,0,1]
	s_nop 0
	v_pk_add_f32 v[98:99], v[104:105], v[102:103] neg_lo:[0,1] neg_hi:[0,1]
	v_pk_add_f32 v[96:97], v[104:105], v[102:103]
	v_pk_mul_f32 v[102:103], v[172:173], v[98:99] op_sel:[1,1] op_sel_hi:[0,1]
	v_pk_fma_f32 v[104:105], v[172:173], v[98:99], v[102:103] neg_lo:[0,0,1] neg_hi:[0,0,1]
	v_pk_fma_f32 v[98:99], v[172:173], v[98:99], v[102:103] op_sel_hi:[1,0,1]
	v_pk_add_f32 v[102:103], v[198:199], v[202:203]
	v_mov_b32_e32 v105, v99
	v_pk_add_f32 v[98:99], v[194:195], v[196:197]
	s_nop 0
	v_pk_add_f32 v[106:107], v[98:99], v[102:103]
	v_pk_add_f32 v[98:99], v[98:99], v[102:103] neg_lo:[0,1] neg_hi:[0,1]
	v_pk_add_f32 v[120:121], v[106:107], v[116:117]
	v_pk_add_f32 v[106:107], v[106:107], v[116:117] neg_lo:[0,1] neg_hi:[0,1]
	v_pk_mul_f32 v[102:103], v[184:185], v[98:99] op_sel:[1,1] op_sel_hi:[0,1]
	v_pk_mul_f32 v[116:117], v[106:107], v[172:173] op_sel:[1,1] op_sel_hi:[1,0]
	s_nop 0
	v_pk_fma_f32 v[122:123], v[106:107], v[172:173], v[116:117] op_sel_hi:[0,1,1] neg_lo:[0,0,1]
	v_pk_fma_f32 v[106:107], v[184:185], v[98:99], v[102:103] op_sel_hi:[1,0,1] neg_lo:[0,0,1]
	s_nop 0
	v_pk_add_f32 v[98:99], v[110:111], v[114:115] neg_lo:[0,1] neg_hi:[0,1]
	s_nop 0
	v_pk_mul_f32 v[102:103], v[184:185], v[98:99] op_sel_hi:[0,1]
	v_pk_fma_f32 v[110:111], v[184:185], v[98:99], v[102:103] op_sel:[1,0,1] op_sel_hi:[1,1,0] neg_hi:[0,0,1]
	s_nop 0
	v_pk_add_f32 v[102:103], v[106:107], v[110:111] neg_lo:[0,1] neg_hi:[0,1]
	v_pk_add_f32 v[98:99], v[106:107], v[110:111]
	v_pk_mul_f32 v[106:107], v[172:173], v[102:103] op_sel:[1,1] op_sel_hi:[0,1]
	v_pk_fma_f32 v[110:111], v[172:173], v[102:103], v[106:107] neg_lo:[0,0,1] neg_hi:[0,0,1]
	v_pk_fma_f32 v[102:103], v[172:173], v[102:103], v[106:107] op_sel_hi:[1,0,1]
	v_pk_add_f32 v[106:107], v[174:175], v[176:177]
	v_mov_b32_e32 v111, v103
	v_pk_add_f32 v[102:103], v[192:193], v[190:191]
	s_nop 0
	v_pk_add_f32 v[114:115], v[102:103], v[106:107]
	v_pk_add_f32 v[102:103], v[102:103], v[106:107] neg_lo:[0,1] neg_hi:[0,1]
	s_nop 0
	v_pk_mul_f32 v[106:107], v[172:173], v[102:103] op_sel:[1,1] op_sel_hi:[0,1]
	v_pk_fma_f32 v[116:117], v[172:173], v[102:103], v[106:107] neg_lo:[0,0,1] neg_hi:[0,0,1]
	v_pk_fma_f32 v[102:103], v[172:173], v[102:103], v[106:107] op_sel_hi:[1,0,1]
	v_pk_mul_f32 v[106:107], v[172:173], v[128:129] op_sel:[1,1] op_sel_hi:[0,1]
	v_pk_fma_f32 v[174:175], v[172:173], v[128:129], v[106:107] op_sel_hi:[1,0,1] neg_lo:[0,0,1]
	v_mov_b32_e32 v117, v103
	v_pk_add_f32 v[102:103], v[204:205], v[224:225]
	ds_write2_b64 v130, v[124:125], v[126:127] offset1:34
	ds_write2_b64 v130, v[112:113], v[118:119] offset0:68 offset1:102
	ds_write2_b64 v130, v[100:101], v[108:109] offset0:136 offset1:170
	ds_write2_b64 v130, v[96:97], v[104:105] offset0:204 offset1:238
	ds_write2_b64 v94, v[120:121], v[122:123] offset0:16 offset1:50
	ds_write2_b64 v94, v[98:99], v[110:111] offset0:84 offset1:118
	ds_write2_b64 v94, v[114:115], v[116:117] offset0:152 offset1:186
	ds_write2_b64 v94, v[102:103], v[174:175] offset0:220 offset1:254
	s_waitcnt lgkmcnt(0)
	s_barrier
; template <int R, class XT, class TWT>
; __device__ __forceinline__ void dif_task(XT X, TWT tw, int s, int task) {
;     const int lgM = 13 - s, lgq = lgM - R, q = 1 << lgq;
;     const int j0 = task & (q - 1), blk = task >> lgq, base = (blk << lgM) + j0;
;     const int pb = PADI(base), qp = (q >= 32) ? q + (q >> 4) : q;
;     f32x2v v[1 << R];
; #pragma unroll
;     for (int k = 0; k < (1 << R); ++k) v[k] = X[pb + k * qp];
; #pragma unroll
;     for (int r = 0; r < R; ++r) {
;         const int pb = R - 1 - r;
; #pragma unroll
;         for (int k = 0; k < (1 << R); ++k) if (!((k >> pb) & 1)) {
;             const int klo = k & ((1 << pb) - 1);
;             const f32x2v w = tw[(j0 + (klo << lgq)) << (s + r)];
;             const f32x2v a = v[k], b = v[k + (1 << pb)], d = a - b;
;             v[k] = a + b; v[k + (1 << pb)] = (f32x2v){d.x * w.x - d.y * w.y, d.x * w.y + d.y * w.x};
;         }
;     }
; #pragma unroll
;     for (int k = 0; k < (1 << R); ++k) X[pb + k * qp] = v[k];
; }
	ds_read2_b64 v[96:99], v132 offset1:2
	ds_read2_b64 v[100:103], v132 offset0:4 offset1:6
	ds_read2_b64 v[104:107], v132 offset0:8 offset1:10
	ds_read2_b64 v[108:111], v132 offset0:12 offset1:14
	ds_read2_b64 v[112:115], v132 offset0:16 offset1:18
	ds_read2_b64 v[116:119], v132 offset0:20 offset1:22
	ds_read2_b64 v[120:123], v132 offset0:24 offset1:26
	ds_read2_b64 v[124:127], v132 offset0:28 offset1:30
	ds_read2st64_b64 v[172:175], v165 offset1:16
	ds_read_b64 v[128:129], v166
	ds_read_b64 v[176:177], v167
	ds_read_b64 v[178:179], v168
	ds_read_b64 v[182:183], v150
	s_waitcnt lgkmcnt(8)
	v_pk_add_f32 v[190:191], v[96:97], v[112:113] neg_lo:[0,1] neg_hi:[0,1]
	ds_read_b64 v[184:185], v169
	ds_read_b64 v[186:187], v170
	ds_read_b64 v[188:189], v95
	s_waitcnt lgkmcnt(7)
	v_pk_mul_f32 v[192:193], v[190:191], v[172:173] op_sel:[1,1] op_sel_hi:[1,0]
	v_pk_add_f32 v[96:97], v[96:97], v[112:113]
	v_pk_fma_f32 v[194:195], v[190:191], v[172:173], v[192:193] op_sel_hi:[0,1,1] neg_lo:[0,0,1]
	v_pk_add_f32 v[190:191], v[104:105], v[120:121] neg_lo:[0,1] neg_hi:[0,1]
	v_pk_add_f32 v[104:105], v[104:105], v[120:121]
	v_pk_mul_f32 v[192:193], v[190:191], v[172:173] op_sel:[1,0] op_sel_hi:[0,0]
	v_pk_fma_f32 v[196:197], v[190:191], v[172:173], v[192:193] op_sel:[0,1,0] neg_hi:[0,0,1]
	v_pk_add_f32 v[112:113], v[96:97], v[104:105]
	v_pk_add_f32 v[172:173], v[194:195], v[196:197] neg_lo:[0,1] neg_hi:[0,1]
	s_waitcnt lgkmcnt(0)
	v_xor_b32_e32 v171, 0x80000000, v188
	v_pk_mul_f32 v[190:191], v[178:179], v[172:173] op_sel:[1,1] op_sel_hi:[0,1]
	v_pk_fma_f32 v[192:193], v[178:179], v[172:173], v[190:191] op_sel_hi:[1,0,1] neg_lo:[0,0,1]
	v_pk_add_f32 v[96:97], v[96:97], v[104:105] neg_lo:[0,1] neg_hi:[0,1]
	v_pk_add_f32 v[172:173], v[100:101], v[116:117] neg_lo:[0,1] neg_hi:[0,1]
	v_pk_add_f32 v[100:101], v[100:101], v[116:117]
	v_pk_mul_f32 v[190:191], v[172:173], v[174:175] op_sel:[1,1] op_sel_hi:[1,0]
	v_pk_mul_f32 v[104:105], v[96:97], v[178:179] op_sel:[1,1] op_sel_hi:[1,0]
	v_pk_fma_f32 v[198:199], v[172:173], v[174:175], v[190:191] op_sel_hi:[0,1,1] neg_lo:[0,0,1]
	v_pk_add_f32 v[172:173], v[108:109], v[124:125] neg_lo:[0,1] neg_hi:[0,1]
	v_pk_add_f32 v[108:109], v[108:109], v[124:125]
	v_pk_mul_f32 v[190:191], v[172:173], v[174:175] op_sel:[1,0] op_sel_hi:[0,0]
	v_pk_fma_f32 v[202:203], v[172:173], v[174:175], v[190:191] op_sel:[0,1,0] neg_hi:[0,0,1]
	v_pk_add_f32 v[116:117], v[100:101], v[108:109]
	v_pk_add_f32 v[172:173], v[198:199], v[202:203] neg_lo:[0,1] neg_hi:[0,1]
	v_pk_add_f32 v[120:121], v[112:113], v[116:117]
	v_pk_mul_f32 v[174:175], v[178:179], v[172:173] op_sel_hi:[0,1]
	v_pk_fma_f32 v[190:191], v[178:179], v[172:173], v[174:175] op_sel:[1,0,1] op_sel_hi:[1,1,0] neg_hi:[0,0,1]
	v_pk_add_f32 v[112:113], v[112:113], v[116:117] neg_lo:[0,1] neg_hi:[0,1]
	v_pk_add_f32 v[172:173], v[192:193], v[190:191] neg_lo:[0,1] neg_hi:[0,1]
	v_pk_mul_f32 v[116:117], v[112:113], v[186:187] op_sel:[1,1] op_sel_hi:[1,0]
	v_pk_mul_f32 v[174:175], v[186:187], v[172:173] op_sel:[1,1] op_sel_hi:[0,1]
	v_pk_fma_f32 v[204:205], v[186:187], v[172:173], v[174:175] op_sel_hi:[1,0,1] neg_lo:[0,0,1]
	s_nop 0
	v_pk_add_f32 v[172:173], v[98:99], v[114:115] neg_lo:[0,1] neg_hi:[0,1]
	v_pk_add_f32 v[98:99], v[98:99], v[114:115]
	v_pk_mul_f32 v[174:175], v[172:173], v[128:129] op_sel:[1,1] op_sel_hi:[1,0]
	s_nop 0
	v_pk_fma_f32 v[206:207], v[172:173], v[128:129], v[174:175] op_sel_hi:[0,1,1] neg_lo:[0,0,1]
	v_pk_add_f32 v[172:173], v[106:107], v[122:123] neg_lo:[0,1] neg_hi:[0,1]
	v_pk_add_f32 v[106:107], v[106:107], v[122:123]
	v_pk_mul_f32 v[174:175], v[172:173], v[128:129] op_sel:[1,0] op_sel_hi:[0,0]
	v_pk_fma_f32 v[208:209], v[172:173], v[128:129], v[174:175] op_sel:[0,1,0] neg_hi:[0,0,1]
	v_pk_add_f32 v[114:115], v[98:99], v[106:107]
	v_pk_add_f32 v[128:129], v[206:207], v[208:209] neg_lo:[0,1] neg_hi:[0,1]
	v_pk_add_f32 v[98:99], v[98:99], v[106:107] neg_lo:[0,1] neg_hi:[0,1]
	v_pk_mul_f32 v[172:173], v[184:185], v[128:129] op_sel:[1,1] op_sel_hi:[0,1]
	v_pk_fma_f32 v[174:175], v[184:185], v[128:129], v[172:173] op_sel_hi:[1,0,1] neg_lo:[0,0,1]
	s_nop 0
	v_pk_add_f32 v[128:129], v[102:103], v[118:119] neg_lo:[0,1] neg_hi:[0,1]
	v_pk_add_f32 v[102:103], v[102:103], v[118:119]
	v_pk_mul_f32 v[172:173], v[128:129], v[176:177] op_sel:[1,1] op_sel_hi:[1,0]
	s_nop 0
	v_pk_fma_f32 v[220:221], v[128:129], v[176:177], v[172:173] op_sel_hi:[0,1,1] neg_lo:[0,0,1]
	v_pk_add_f32 v[128:129], v[110:111], v[126:127] neg_lo:[0,1] neg_hi:[0,1]
	v_pk_add_f32 v[110:111], v[110:111], v[126:127]
	v_pk_mul_f32 v[172:173], v[128:129], v[176:177] op_sel:[1,0] op_sel_hi:[0,0]
	v_pk_fma_f32 v[222:223], v[128:129], v[176:177], v[172:173] op_sel:[0,1,0] neg_hi:[0,0,1]
	v_pk_add_f32 v[118:119], v[102:103], v[110:111]
	v_pk_add_f32 v[128:129], v[220:221], v[222:223] neg_lo:[0,1] neg_hi:[0,1]
	v_pk_add_f32 v[122:123], v[114:115], v[118:119]
	v_pk_mul_f32 v[172:173], v[182:183], v[128:129] op_sel_hi:[0,1]
	v_pk_fma_f32 v[176:177], v[182:183], v[128:129], v[172:173] op_sel:[1,0,1] op_sel_hi:[1,1,0] neg_hi:[0,0,1]
	v_pk_add_f32 v[124:125], v[120:121], v[122:123]
	v_pk_add_f32 v[128:129], v[174:175], v[176:177] neg_lo:[0,1] neg_hi:[0,1]
	v_pk_add_f32 v[120:121], v[120:121], v[122:123] neg_lo:[0,1] neg_hi:[0,1]
	v_pk_mul_f32 v[172:173], v[186:187], v[128:129] op_sel_hi:[0,1]
	v_pk_fma_f32 v[224:225], v[186:187], v[128:129], v[172:173] op_sel:[1,0,1] op_sel_hi:[1,1,0]
	v_pk_fma_f32 v[128:129], v[186:187], v[128:129], v[172:173] op_sel:[1,0,1] op_sel_hi:[1,1,0] neg_lo:[0,0,1] neg_hi:[0,0,1]
	v_cndmask_b32_e64 v173, v171, v189, s[42:43]
	v_cndmask_b32_e64 v172, v189, v188, s[42:43]
; template <int R, class XT, class TWT>
; __device__ __forceinline__ void dif_task(XT X, TWT tw, int s, int task) {
;     const int lgM = 13 - s, lgq = lgM - R, q = 1 << lgq;
;     const int j0 = task & (q - 1), blk = task >> lgq, base = (blk << lgM) + j0;
;     const int pb = PADI(base), qp = (q >= 32) ? q + (q >> 4) : q;
;     f32x2v v[1 << R];
; #pragma unroll
;     for (int k = 0; k < (1 << R); ++k) v[k] = X[pb + k * qp];
; #pragma unroll
;     for (int r = 0; r < R; ++r) {
;         const int pb = R - 1 - r;
; #pragma unroll
;         for (int k = 0; k < (1 << R); ++k) if (!((k >> pb) & 1)) {
;             const int klo = k & ((1 << pb) - 1);
;             const f32x2v w = tw[(j0 + (klo << lgq)) << (s + r)];
;             const f32x2v a = v[k], b = v[k + (1 << pb)], d = a - b;
;             v[k] = a + b; v[k + (1 << pb)] = (f32x2v){d.x * w.x - d.y * w.y, d.x * w.y + d.y * w.x};
;         }
;     }
; #pragma unroll
;     for (int k = 0; k < (1 << R); ++k) X[pb + k * qp] = v[k];
; }
	v_pk_mul_f32 v[122:123], v[120:121], v[172:173] op_sel:[1,1] op_sel_hi:[1,0]
	v_mov_b32_e32 v225, v129
	v_pk_fma_f32 v[126:127], v[120:121], v[172:173], v[122:123] op_sel_hi:[0,1,1] neg_lo:[0,0,1]
	v_pk_fma_f32 v[120:121], v[112:113], v[186:187], v[116:117] op_sel_hi:[0,1,1] neg_lo:[0,0,1]
	v_pk_add_f32 v[112:113], v[114:115], v[118:119] neg_lo:[0,1] neg_hi:[0,1]
	v_pk_add_f32 v[128:129], v[204:205], v[224:225] neg_lo:[0,1] neg_hi:[0,1]
	v_pk_mul_f32 v[114:115], v[112:113], v[186:187] op_sel_hi:[1,0]
	s_nop 0
	v_pk_fma_f32 v[116:117], v[112:113], v[186:187], v[114:115] op_sel:[0,1,1] op_sel_hi:[1,1,0] neg_hi:[0,0,1]
	s_nop 0
	v_pk_add_f32 v[114:115], v[120:121], v[116:117] neg_lo:[0,1] neg_hi:[0,1]
	v_pk_add_f32 v[112:113], v[120:121], v[116:117]
	v_pk_mul_f32 v[116:117], v[172:173], v[114:115] op_sel:[1,1] op_sel_hi:[0,1]
	v_pk_fma_f32 v[118:119], v[172:173], v[114:115], v[116:117] op_sel_hi:[1,0,1] neg_lo:[0,0,1]
	s_nop 0
	v_pk_fma_f32 v[114:115], v[96:97], v[178:179], v[104:105] op_sel_hi:[0,1,1] neg_lo:[0,0,1]
	v_pk_add_f32 v[96:97], v[100:101], v[108:109] neg_lo:[0,1] neg_hi:[0,1]
	s_nop 0
	v_pk_mul_f32 v[100:101], v[96:97], v[178:179] op_sel_hi:[1,0]
	s_nop 0
	v_pk_fma_f32 v[104:105], v[96:97], v[178:179], v[100:101] op_sel:[0,1,1] op_sel_hi:[1,1,0]
	v_pk_fma_f32 v[96:97], v[96:97], v[178:179], v[100:101] op_sel:[0,1,1] op_sel_hi:[1,1,0] neg_lo:[0,0,1] neg_hi:[0,0,1]
	v_pk_mul_f32 v[100:101], v[98:99], v[184:185] op_sel:[1,1] op_sel_hi:[1,0]
	v_mov_b32_e32 v105, v97
	v_pk_fma_f32 v[106:107], v[98:99], v[184:185], v[100:101] op_sel_hi:[0,1,1] neg_lo:[0,0,1]
	v_pk_add_f32 v[98:99], v[102:103], v[110:111] neg_lo:[0,1] neg_hi:[0,1]
	v_pk_add_f32 v[96:97], v[114:115], v[104:105]
	v_pk_mul_f32 v[100:101], v[98:99], v[182:183] op_sel_hi:[1,0]
	v_pk_add_f32 v[110:111], v[206:207], v[208:209]
	v_pk_fma_f32 v[102:103], v[98:99], v[182:183], v[100:101] op_sel:[0,1,1] op_sel_hi:[1,1,0] neg_hi:[0,0,1]
	s_nop 0
	v_pk_add_f32 v[98:99], v[106:107], v[102:103]
	s_nop 0
	v_pk_add_f32 v[100:101], v[96:97], v[98:99]
	v_pk_add_f32 v[96:97], v[96:97], v[98:99] neg_lo:[0,1] neg_hi:[0,1]
	s_nop 0
	v_pk_mul_f32 v[98:99], v[172:173], v[96:97] op_sel:[1,1] op_sel_hi:[0,1]
	v_pk_fma_f32 v[108:109], v[172:173], v[96:97], v[98:99] op_sel_hi:[1,0,1] neg_lo:[0,0,1]
	s_nop 0
	v_pk_add_f32 v[96:97], v[114:115], v[104:105] neg_lo:[0,1] neg_hi:[0,1]
	v_pk_add_f32 v[114:115], v[220:221], v[222:223]
	v_pk_mul_f32 v[98:99], v[186:187], v[96:97] op_sel:[1,1] op_sel_hi:[0,1]
	v_pk_fma_f32 v[104:105], v[186:187], v[96:97], v[98:99] op_sel_hi:[1,0,1] neg_lo:[0,0,1]
	v_pk_add_f32 v[116:117], v[110:111], v[114:115]
	v_pk_add_f32 v[96:97], v[106:107], v[102:103] neg_lo:[0,1] neg_hi:[0,1]
	s_nop 0
	v_pk_mul_f32 v[98:99], v[186:187], v[96:97] op_sel_hi:[0,1]
	v_pk_fma_f32 v[102:103], v[186:187], v[96:97], v[98:99] op_sel:[1,0,1] op_sel_hi:[1,1,0] neg_hi:[0,0,1]
	s_nop 0
	v_pk_add_f32 v[98:99], v[104:105], v[102:103] neg_lo:[0,1] neg_hi:[0,1]
	v_pk_add_f32 v[96:97], v[104:105], v[102:103]
	v_pk_mul_f32 v[102:103], v[172:173], v[98:99] op_sel:[1,1] op_sel_hi:[0,1]
	v_pk_fma_f32 v[104:105], v[172:173], v[98:99], v[102:103] neg_lo:[0,0,1] neg_hi:[0,0,1]
	v_pk_fma_f32 v[98:99], v[172:173], v[98:99], v[102:103] op_sel_hi:[1,0,1]
	v_pk_add_f32 v[102:103], v[198:199], v[202:203]
	v_mov_b32_e32 v105, v99
	v_pk_add_f32 v[98:99], v[194:195], v[196:197]
	s_nop 0
	v_pk_add_f32 v[106:107], v[98:99], v[102:103]
	v_pk_add_f32 v[98:99], v[98:99], v[102:103] neg_lo:[0,1] neg_hi:[0,1]
	v_pk_add_f32 v[120:121], v[106:107], v[116:117]
	v_pk_add_f32 v[106:107], v[106:107], v[116:117] neg_lo:[0,1] neg_hi:[0,1]
	v_pk_mul_f32 v[102:103], v[186:187], v[98:99] op_sel:[1,1] op_sel_hi:[0,1]
	v_pk_mul_f32 v[116:117], v[106:107], v[172:173] op_sel:[1,1] op_sel_hi:[1,0]
	s_nop 0
	v_pk_fma_f32 v[122:123], v[106:107], v[172:173], v[116:117] op_sel_hi:[0,1,1] neg_lo:[0,0,1]
	v_pk_fma_f32 v[106:107], v[186:187], v[98:99], v[102:103] op_sel_hi:[1,0,1] neg_lo:[0,0,1]
	s_nop 0
	v_pk_add_f32 v[98:99], v[110:111], v[114:115] neg_lo:[0,1] neg_hi:[0,1]
	s_nop 0
	v_pk_mul_f32 v[102:103], v[186:187], v[98:99] op_sel_hi:[0,1]
	v_pk_fma_f32 v[110:111], v[186:187], v[98:99], v[102:103] op_sel:[1,0,1] op_sel_hi:[1,1,0] neg_hi:[0,0,1]
	s_nop 0
	v_pk_add_f32 v[102:103], v[106:107], v[110:111] neg_lo:[0,1] neg_hi:[0,1]
	v_pk_add_f32 v[98:99], v[106:107], v[110:111]
	v_pk_mul_f32 v[106:107], v[172:173], v[102:103] op_sel:[1,1] op_sel_hi:[0,1]
	v_pk_fma_f32 v[110:111], v[172:173], v[102:103], v[106:107] neg_lo:[0,0,1] neg_hi:[0,0,1]
	v_pk_fma_f32 v[102:103], v[172:173], v[102:103], v[106:107] op_sel_hi:[1,0,1]
	v_pk_add_f32 v[106:107], v[174:175], v[176:177]
	v_mov_b32_e32 v111, v103
	v_pk_add_f32 v[102:103], v[192:193], v[190:191]
	s_nop 0
	v_pk_add_f32 v[114:115], v[102:103], v[106:107]
	v_pk_add_f32 v[102:103], v[102:103], v[106:107] neg_lo:[0,1] neg_hi:[0,1]
	s_nop 0
	v_pk_mul_f32 v[106:107], v[172:173], v[102:103] op_sel:[1,1] op_sel_hi:[0,1]
	v_pk_fma_f32 v[116:117], v[172:173], v[102:103], v[106:107] neg_lo:[0,0,1] neg_hi:[0,0,1]
	v_pk_fma_f32 v[102:103], v[172:173], v[102:103], v[106:107] op_sel_hi:[1,0,1]
	v_pk_mul_f32 v[106:107], v[172:173], v[128:129] op_sel:[1,1] op_sel_hi:[0,1]
	v_pk_fma_f32 v[174:175], v[172:173], v[128:129], v[106:107] op_sel_hi:[1,0,1] neg_lo:[0,0,1]
	v_mov_b32_e32 v117, v103
	v_pk_add_f32 v[102:103], v[204:205], v[224:225]
	ds_write2_b64 v132, v[124:125], v[126:127] offset1:2
	ds_write2_b64 v132, v[112:113], v[118:119] offset0:4 offset1:6
	ds_write2_b64 v132, v[100:101], v[108:109] offset0:8 offset1:10
	ds_write2_b64 v132, v[96:97], v[104:105] offset0:12 offset1:14
	ds_write2_b64 v132, v[120:121], v[122:123] offset0:16 offset1:18
	ds_write2_b64 v132, v[98:99], v[110:111] offset0:20 offset1:22
	ds_write2_b64 v132, v[114:115], v[116:117] offset0:24 offset1:26
	ds_write2_b64 v132, v[102:103], v[174:175] offset0:28 offset1:30
	s_waitcnt lgkmcnt(0)
	s_barrier
; template <bool LAT>
; __device__ __forceinline__ void hyconv_unit(const Frame& F, LAS f32x2v* X, const TwHalf tw, LAS bf16* OUT, const float* skip, bf16* MIX, int u) {
;     ...
; #pragma unroll
;             for (int r = 0; r < 8; ++r) { const int e = 2 * (F.tid + 512 * r);
;                 const f32x2v a = X[PADI(e)], b = X[PADI(e + 1)]; const f32x4 k = kq[r];
;                 const f32x2v p = a + b, q = a - b; const f32x2v pk = (f32x2v){p.x * k.x - p.y * k.y, p.x * k.y + p.y * k.x}, qk = (f32x2v){q.x * k.z - q.y * k.w, q.x * k.w + q.y * k.z};
;                 X[PADI(e)] = pk + qk; X[PADI(e + 1)] = pk - qk; }
	ds_read_b128 v[96:99], v151
	s_waitcnt lgkmcnt(0)
	v_pk_add_f32 v[100:101], v[96:97], v[98:99]
	v_pk_add_f32 v[96:97], v[96:97], v[98:99] neg_lo:[0,1] neg_hi:[0,1]
	s_waitcnt vmcnt(7)
	v_pk_mul_f32 v[98:99], v[28:29], v[100:101] op_sel:[1,1] op_sel_hi:[0,1]
	v_pk_fma_f32 v[102:103], v[28:29], v[100:101], v[98:99] op_sel_hi:[1,0,1] neg_lo:[0,0,1]
	s_nop 0
	v_pk_mul_f32 v[28:29], v[30:31], v[96:97] op_sel:[1,1] op_sel_hi:[0,1]
	v_pk_fma_f32 v[98:99], v[30:31], v[96:97], v[28:29] op_sel_hi:[1,0,1] neg_lo:[0,0,1]
	s_nop 0
	v_pk_add_f32 v[28:29], v[102:103], v[98:99]
	v_pk_add_f32 v[30:31], v[102:103], v[98:99] neg_lo:[0,1] neg_hi:[0,1]
	ds_write_b128 v151, v[28:31]
	ds_read_b128 v[28:31], v152 offset:8192
	s_waitcnt lgkmcnt(0)
	v_pk_add_f32 v[96:97], v[28:29], v[30:31]
	v_pk_add_f32 v[28:29], v[28:29], v[30:31] neg_lo:[0,1] neg_hi:[0,1]
	s_waitcnt vmcnt(6)
	v_pk_mul_f32 v[30:31], v[24:25], v[96:97] op_sel:[1,1] op_sel_hi:[0,1]
	v_pk_fma_f32 v[98:99], v[24:25], v[96:97], v[30:31] op_sel_hi:[1,0,1] neg_lo:[0,0,1]
	s_nop 0
	v_pk_mul_f32 v[24:25], v[26:27], v[28:29] op_sel:[1,1] op_sel_hi:[0,1]
	v_pk_fma_f32 v[30:31], v[26:27], v[28:29], v[24:25] op_sel_hi:[1,0,1] neg_lo:[0,0,1]
	s_nop 0
	v_pk_add_f32 v[24:25], v[98:99], v[30:31]
	v_pk_add_f32 v[26:27], v[98:99], v[30:31] neg_lo:[0,1] neg_hi:[0,1]
	ds_write_b128 v152, v[24:27] offset:8192
	ds_read_b128 v[24:27], v153 offset:16384
	s_waitcnt lgkmcnt(0)
	v_pk_add_f32 v[28:29], v[24:25], v[26:27]
	v_pk_add_f32 v[24:25], v[24:25], v[26:27] neg_lo:[0,1] neg_hi:[0,1]
	s_waitcnt vmcnt(5)
	v_pk_mul_f32 v[26:27], v[20:21], v[28:29] op_sel:[1,1] op_sel_hi:[0,1]
	v_pk_fma_f32 v[30:31], v[20:21], v[28:29], v[26:27] op_sel_hi:[1,0,1] neg_lo:[0,0,1]
	s_nop 0
	v_pk_mul_f32 v[20:21], v[22:23], v[24:25] op_sel:[1,1] op_sel_hi:[0,1]
	v_pk_fma_f32 v[26:27], v[22:23], v[24:25], v[20:21] op_sel_hi:[1,0,1] neg_lo:[0,0,1]
	s_nop 0
	v_pk_add_f32 v[20:21], v[30:31], v[26:27]
	v_pk_add_f32 v[22:23], v[30:31], v[26:27] neg_lo:[0,1] neg_hi:[0,1]
	ds_write_b128 v153, v[20:23] offset:16384
	ds_read_b128 v[20:23], v154 offset:24576
	s_waitcnt lgkmcnt(0)
	v_pk_add_f32 v[24:25], v[20:21], v[22:23]
	v_pk_add_f32 v[20:21], v[20:21], v[22:23] neg_lo:[0,1] neg_hi:[0,1]
	s_waitcnt vmcnt(4)
	v_pk_mul_f32 v[22:23], v[16:17], v[24:25] op_sel:[1,1] op_sel_hi:[0,1]
	v_pk_fma_f32 v[26:27], v[16:17], v[24:25], v[22:23] op_sel_hi:[1,0,1] neg_lo:[0,0,1]
	s_nop 0
	v_pk_mul_f32 v[16:17], v[18:19], v[20:21] op_sel:[1,1] op_sel_hi:[0,1]
	v_pk_fma_f32 v[22:23], v[18:19], v[20:21], v[16:17] op_sel_hi:[1,0,1] neg_lo:[0,0,1]
	s_nop 0
	v_pk_add_f32 v[16:17], v[26:27], v[22:23]
	v_pk_add_f32 v[18:19], v[26:27], v[22:23] neg_lo:[0,1] neg_hi:[0,1]
	ds_write_b128 v154, v[16:19] offset:24576
	ds_read_b128 v[16:19], v155 offset:32768
	s_waitcnt lgkmcnt(0)
	v_pk_add_f32 v[20:21], v[16:17], v[18:19]
	v_pk_add_f32 v[16:17], v[16:17], v[18:19] neg_lo:[0,1] neg_hi:[0,1]
	s_waitcnt vmcnt(3)
	v_pk_mul_f32 v[18:19], v[12:13], v[20:21] op_sel:[1,1] op_sel_hi:[0,1]
	v_pk_fma_f32 v[22:23], v[12:13], v[20:21], v[18:19] op_sel_hi:[1,0,1] neg_lo:[0,0,1]
	s_nop 0
	v_pk_mul_f32 v[12:13], v[14:15], v[16:17] op_sel:[1,1] op_sel_hi:[0,1]
	v_pk_fma_f32 v[18:19], v[14:15], v[16:17], v[12:13] op_sel_hi:[1,0,1] neg_lo:[0,0,1]
	s_nop 0
	v_pk_add_f32 v[12:13], v[22:23], v[18:19]
	v_pk_add_f32 v[14:15], v[22:23], v[18:19] neg_lo:[0,1] neg_hi:[0,1]
	ds_write_b128 v155, v[12:15] offset:32768
	ds_read_b128 v[12:15], v156 offset:40960
	s_waitcnt lgkmcnt(0)
	v_pk_add_f32 v[16:17], v[12:13], v[14:15]
	v_pk_add_f32 v[12:13], v[12:13], v[14:15] neg_lo:[0,1] neg_hi:[0,1]
	s_waitcnt vmcnt(2)
	v_pk_mul_f32 v[14:15], v[8:9], v[16:17] op_sel:[1,1] op_sel_hi:[0,1]
	v_pk_fma_f32 v[18:19], v[8:9], v[16:17], v[14:15] op_sel_hi:[1,0,1] neg_lo:[0,0,1]
	s_nop 0
	v_pk_mul_f32 v[8:9], v[10:11], v[12:13] op_sel:[1,1] op_sel_hi:[0,1]
	v_pk_fma_f32 v[14:15], v[10:11], v[12:13], v[8:9] op_sel_hi:[1,0,1] neg_lo:[0,0,1]
	s_nop 0
	v_pk_add_f32 v[8:9], v[18:19], v[14:15]
	v_pk_add_f32 v[10:11], v[18:19], v[14:15] neg_lo:[0,1] neg_hi:[0,1]
	ds_write_b128 v156, v[8:11] offset:40960
	ds_read_b128 v[8:11], v157 offset:49152
	s_waitcnt lgkmcnt(0)
	v_pk_add_f32 v[12:13], v[8:9], v[10:11]
	v_pk_add_f32 v[8:9], v[8:9], v[10:11] neg_lo:[0,1] neg_hi:[0,1]
	s_waitcnt vmcnt(1)
	v_pk_mul_f32 v[10:11], v[4:5], v[12:13] op_sel:[1,1] op_sel_hi:[0,1]
	v_pk_fma_f32 v[14:15], v[4:5], v[12:13], v[10:11] op_sel_hi:[1,0,1] neg_lo:[0,0,1]
	s_nop 0
	v_pk_mul_f32 v[4:5], v[6:7], v[8:9] op_sel:[1,1] op_sel_hi:[0,1]
	v_pk_fma_f32 v[10:11], v[6:7], v[8:9], v[4:5] op_sel_hi:[1,0,1] neg_lo:[0,0,1]
	s_nop 0
	v_pk_add_f32 v[4:5], v[14:15], v[10:11]
	v_pk_add_f32 v[6:7], v[14:15], v[10:11] neg_lo:[0,1] neg_hi:[0,1]
	ds_write_b128 v157, v[4:7] offset:49152
	ds_read_b128 v[4:7], v158 offset:57344
	s_waitcnt lgkmcnt(0)
	v_pk_add_f32 v[8:9], v[4:5], v[6:7]
	v_pk_add_f32 v[4:5], v[4:5], v[6:7] neg_lo:[0,1] neg_hi:[0,1]
	s_waitcnt vmcnt(0)
	v_pk_mul_f32 v[6:7], v[0:1], v[8:9] op_sel:[1,1] op_sel_hi:[0,1]
	v_pk_fma_f32 v[10:11], v[0:1], v[8:9], v[6:7] op_sel_hi:[1,0,1] neg_lo:[0,0,1]
	s_nop 0
	v_pk_mul_f32 v[0:1], v[2:3], v[4:5] op_sel:[1,1] op_sel_hi:[0,1]
	v_pk_fma_f32 v[6:7], v[2:3], v[4:5], v[0:1] op_sel_hi:[1,0,1] neg_lo:[0,0,1]
	s_nop 0
	v_pk_add_f32 v[0:1], v[10:11], v[6:7]
	v_pk_add_f32 v[2:3], v[10:11], v[6:7] neg_lo:[0,1] neg_hi:[0,1]
	ds_write_b128 v158, v[0:3] offset:57344
	s_waitcnt lgkmcnt(0)
	s_barrier
; template <int R, class XT, class TWT>
; __device__ __forceinline__ void dit_task(XT X, TWT tw, int s, int task) {
;     const int lgM = 13 - s, lgq = lgM - R, q = 1 << lgq;
;     const int j0 = task & (q - 1), blk = task >> lgq, base = (blk << lgM) + j0;
;     const int pb = PADI(base), qp = (q >= 32) ? q + (q >> 4) : q;
;     f32x2v v[1 << R];
; #pragma unroll
;     for (int k = 0; k < (1 << R); ++k) v[k] = X[pb + k * qp];
; #pragma unroll
;     for (int r = R - 1; r >= 0; --r) {
;         const int pb = R - 1 - r;
; #pragma unroll
;         for (int k = 0; k < (1 << R); ++k) if (!((k >> pb) & 1)) {
;             const int klo = k & ((1 << pb) - 1);
;             const f32x2v w = tw[(j0 + (klo << lgq)) << (s + r)];
;             const f32x2v a = v[k], qv = v[k + (1 << pb)]; const f32x2v b = (f32x2v){qv.x * w.x + qv.y * w.y, qv.y * w.x - qv.x * w.y};
;             v[k] = a + b; v[k + (1 << pb)] = a - b;
;         }
;     }
; #pragma unroll
;     for (int k = 0; k < (1 << R); ++k) X[pb + k * qp] = v[k];
; }
	ds_read2_b64 v[0:3], v132 offset1:2
	ds_read2_b64 v[4:7], v132 offset0:4 offset1:6
	ds_read2_b64 v[8:11], v132 offset0:8 offset1:10
	ds_read2_b64 v[12:15], v132 offset0:12 offset1:14
	ds_read2_b64 v[16:19], v132 offset0:16 offset1:18
	ds_read2_b64 v[20:23], v132 offset0:20 offset1:22
	ds_read2_b64 v[24:27], v132 offset0:24 offset1:26
	ds_read2_b64 v[28:31], v132 offset0:28 offset1:30
	ds_read_b64 v[100:101], v95
	ds_read_b64 v[102:103], v170
	ds_read_b64 v[104:105], v169
	ds_read2st64_b64 v[96:99], v165 offset1:16
	ds_read_b64 v[106:107], v168
	ds_read_b64 v[108:109], v150
	ds_read_b64 v[110:111], v166
	ds_read_b64 v[112:113], v167
	s_waitcnt lgkmcnt(7)
	v_xor_b32_e32 v95, 0x80000000, v100
	v_cndmask_b32_e64 v115, v95, v101, s[42:43]
	v_cndmask_b32_e64 v114, v101, v100, s[42:43]
	v_mov_b32_e32 v100, v115
	v_pk_mul_f32 v[116:117], v[2:3], v[100:101] op_sel_hi:[1,0]
	s_nop 0
	v_pk_fma_f32 v[118:119], v[2:3], v[114:115], v[116:117] op_sel:[0,0,1] op_sel_hi:[1,1,0]
	v_pk_fma_f32 v[2:3], v[2:3], v[114:115], v[116:117] op_sel:[0,0,1] op_sel_hi:[1,0,0] neg_lo:[0,0,1] neg_hi:[0,0,1]
	v_pk_mul_f32 v[116:117], v[6:7], v[100:101] op_sel_hi:[1,0]
	v_mov_b32_e32 v119, v3
	v_pk_fma_f32 v[120:121], v[6:7], v[114:115], v[116:117] op_sel:[0,0,1] op_sel_hi:[1,0,0] neg_hi:[0,0,1]
	v_pk_add_f32 v[2:3], v[0:1], v[118:119]
	v_pk_add_f32 v[6:7], v[4:5], v[120:121]
	v_pk_add_f32 v[4:5], v[4:5], v[120:121] neg_lo:[0,1] neg_hi:[0,1]
	s_waitcnt lgkmcnt(6)
	v_pk_mul_f32 v[116:117], v[102:103], v[6:7] op_sel:[1,0]
	v_pk_add_f32 v[0:1], v[0:1], v[118:119] neg_lo:[0,1] neg_hi:[0,1]
	v_pk_fma_f32 v[122:123], v[102:103], v[6:7], v[116:117] op_sel:[0,0,1] op_sel_hi:[1,1,0]
	v_pk_fma_f32 v[6:7], v[102:103], v[6:7], v[116:117] op_sel:[0,0,1] op_sel_hi:[0,1,0] neg_lo:[0,0,1] neg_hi:[0,0,1]
	v_pk_mul_f32 v[116:117], v[10:11], v[100:101] op_sel_hi:[1,0]
	v_mov_b32_e32 v123, v7
	v_pk_fma_f32 v[124:125], v[10:11], v[114:115], v[116:117] op_sel:[0,0,1] op_sel_hi:[1,1,0]
	v_pk_fma_f32 v[10:11], v[10:11], v[114:115], v[116:117] op_sel:[0,0,1] op_sel_hi:[1,0,0] neg_lo:[0,0,1] neg_hi:[0,0,1]
	v_pk_mul_f32 v[116:117], v[14:15], v[100:101] op_sel_hi:[1,0]
	v_mov_b32_e32 v125, v11
	v_pk_fma_f32 v[126:127], v[14:15], v[114:115], v[116:117] op_sel:[0,0,1] op_sel_hi:[1,0,0] neg_hi:[0,0,1]
	v_pk_add_f32 v[10:11], v[8:9], v[124:125]
	v_pk_add_f32 v[14:15], v[12:13], v[126:127]
	v_pk_add_f32 v[12:13], v[12:13], v[126:127] neg_lo:[0,1] neg_hi:[0,1]
	v_pk_mul_f32 v[116:117], v[102:103], v[14:15] op_sel:[1,0]
	v_pk_add_f32 v[8:9], v[8:9], v[124:125] neg_lo:[0,1] neg_hi:[0,1]
	v_pk_fma_f32 v[128:129], v[102:103], v[14:15], v[116:117] op_sel:[0,0,1] op_sel_hi:[0,1,0] neg_hi:[0,0,1]
	s_nop 0
	v_pk_add_f32 v[14:15], v[10:11], v[128:129]
	v_pk_add_f32 v[10:11], v[10:11], v[128:129] neg_lo:[0,1] neg_hi:[0,1]
	s_waitcnt lgkmcnt(3)
	v_pk_mul_f32 v[116:117], v[106:107], v[14:15] op_sel:[1,0]
	v_pk_add_f32 v[6:7], v[2:3], v[122:123]
	v_pk_fma_f32 v[172:173], v[106:107], v[14:15], v[116:117] op_sel:[0,0,1] op_sel_hi:[1,1,0]
	v_pk_fma_f32 v[14:15], v[106:107], v[14:15], v[116:117] op_sel:[0,0,1] op_sel_hi:[0,1,0] neg_lo:[0,0,1] neg_hi:[0,0,1]
	v_pk_mul_f32 v[116:117], v[18:19], v[100:101] op_sel_hi:[1,0]
	v_pk_add_f32 v[2:3], v[2:3], v[122:123] neg_lo:[0,1] neg_hi:[0,1]
	v_pk_fma_f32 v[174:175], v[18:19], v[114:115], v[116:117] op_sel:[0,0,1] op_sel_hi:[1,1,0]
	v_pk_fma_f32 v[18:19], v[18:19], v[114:115], v[116:117] op_sel:[0,0,1] op_sel_hi:[1,0,0] neg_lo:[0,0,1] neg_hi:[0,0,1]
	v_pk_mul_f32 v[116:117], v[22:23], v[100:101] op_sel_hi:[1,0]
	v_mov_b32_e32 v175, v19
	v_pk_fma_f32 v[176:177], v[22:23], v[114:115], v[116:117] op_sel:[0,0,1] op_sel_hi:[1,0,0] neg_hi:[0,0,1]
	v_pk_add_f32 v[18:19], v[16:17], v[174:175]
	v_pk_add_f32 v[22:23], v[20:21], v[176:177]
	v_pk_add_f32 v[20:21], v[20:21], v[176:177] neg_lo:[0,1] neg_hi:[0,1]
	v_pk_mul_f32 v[116:117], v[102:103], v[22:23] op_sel:[1,0]
	v_pk_add_f32 v[16:17], v[16:17], v[174:175] neg_lo:[0,1] neg_hi:[0,1]
	v_pk_fma_f32 v[178:179], v[102:103], v[22:23], v[116:117] op_sel:[0,0,1] op_sel_hi:[1,1,0]
	v_pk_fma_f32 v[22:23], v[102:103], v[22:23], v[116:117] op_sel:[0,0,1] op_sel_hi:[0,1,0] neg_lo:[0,0,1] neg_hi:[0,0,1]
	v_pk_mul_f32 v[116:117], v[26:27], v[100:101] op_sel_hi:[1,0]
	v_pk_mul_f32 v[100:101], v[30:31], v[100:101] op_sel_hi:[1,0]
	v_pk_fma_f32 v[182:183], v[26:27], v[114:115], v[116:117] op_sel:[0,0,1] op_sel_hi:[1,1,0]
	v_pk_fma_f32 v[26:27], v[26:27], v[114:115], v[116:117] op_sel:[0,0,1] op_sel_hi:[1,0,0] neg_lo:[0,0,1] neg_hi:[0,0,1]
	v_pk_fma_f32 v[116:117], v[30:31], v[114:115], v[100:101] op_sel:[0,0,1] op_sel_hi:[1,0,0] neg_hi:[0,0,1]
	v_mov_b32_e32 v183, v27
	v_pk_add_f32 v[30:31], v[28:29], v[116:117]
	v_pk_add_f32 v[26:27], v[24:25], v[182:183]
	v_pk_mul_f32 v[100:101], v[102:103], v[30:31] op_sel:[1,0]
	v_mov_b32_e32 v179, v23
	v_pk_fma_f32 v[114:115], v[102:103], v[30:31], v[100:101] op_sel:[0,0,1] op_sel_hi:[0,1,0] neg_hi:[0,0,1]
	s_nop 0
	v_pk_add_f32 v[30:31], v[26:27], v[114:115]
	v_pk_add_f32 v[22:23], v[18:19], v[178:179]
	v_pk_mul_f32 v[100:101], v[106:107], v[30:31] op_sel:[1,0]
	v_pk_add_f32 v[28:29], v[28:29], v[116:117] neg_lo:[0,1] neg_hi:[0,1]
	v_pk_fma_f32 v[184:185], v[106:107], v[30:31], v[100:101] op_sel:[0,0,1] op_sel_hi:[0,1,0] neg_hi:[0,0,1]
	s_nop 0
	v_pk_add_f32 v[30:31], v[22:23], v[184:185]
	v_pk_add_f32 v[24:25], v[24:25], v[182:183] neg_lo:[0,1] neg_hi:[0,1]
	v_pk_mul_f32 v[100:101], v[96:97], v[30:31] op_sel:[1,0]
	v_pk_add_f32 v[26:27], v[26:27], v[114:115] neg_lo:[0,1] neg_hi:[0,1]
	v_pk_fma_f32 v[186:187], v[96:97], v[30:31], v[100:101] op_sel:[0,0,1] op_sel_hi:[1,1,0]
; template <int R, class XT, class TWT>
; __device__ __forceinline__ void dit_task(XT X, TWT tw, int s, int task) {
;     const int lgM = 13 - s, lgq = lgM - R, q = 1 << lgq;
;     const int j0 = task & (q - 1), blk = task >> lgq, base = (blk << lgM) + j0;
;     const int pb = PADI(base), qp = (q >= 32) ? q + (q >> 4) : q;
;     f32x2v v[1 << R];
; #pragma unroll
;     for (int k = 0; k < (1 << R); ++k) v[k] = X[pb + k * qp];
; #pragma unroll
;     for (int r = R - 1; r >= 0; --r) {
;         const int pb = R - 1 - r;
; #pragma unroll
;         for (int k = 0; k < (1 << R); ++k) if (!((k >> pb) & 1)) {
;             const int klo = k & ((1 << pb) - 1);
;             const f32x2v w = tw[(j0 + (klo << lgq)) << (s + r)];
;             const f32x2v a = v[k], qv = v[k + (1 << pb)]; const f32x2v b = (f32x2v){qv.x * w.x + qv.y * w.y, qv.y * w.x - qv.x * w.y};
;             v[k] = a + b; v[k + (1 << pb)] = a - b;
;         }
;     }
; #pragma unroll
;     for (int k = 0; k < (1 << R); ++k) X[pb + k * qp] = v[k];
; }
	v_pk_fma_f32 v[30:31], v[96:97], v[30:31], v[100:101] op_sel:[0,0,1] op_sel_hi:[0,1,0] neg_lo:[0,0,1] neg_hi:[0,0,1]
	v_pk_mul_f32 v[100:101], v[102:103], v[4:5] op_sel_hi:[0,1]
	v_pk_fma_f32 v[118:119], v[102:103], v[4:5], v[100:101] op_sel:[1,0,1] op_sel_hi:[1,1,0] neg_lo:[0,0,1] neg_hi:[0,0,1]
	v_pk_fma_f32 v[4:5], v[102:103], v[4:5], v[100:101] op_sel:[1,0,1] op_sel_hi:[1,1,0]
	v_pk_mul_f32 v[100:101], v[102:103], v[12:13] op_sel_hi:[0,1]
	v_pk_fma_f32 v[120:121], v[102:103], v[12:13], v[100:101] op_sel:[1,0,1] op_sel_hi:[1,1,0] neg_lo:[0,0,1]
	v_mov_b32_e32 v119, v5
	v_pk_add_f32 v[12:13], v[8:9], v[120:121]
	v_pk_add_f32 v[4:5], v[0:1], v[118:119]
	v_pk_mul_f32 v[100:101], v[104:105], v[12:13] op_sel:[1,0]
	v_pk_add_f32 v[18:19], v[18:19], v[178:179] neg_lo:[0,1] neg_hi:[0,1]
	v_pk_fma_f32 v[124:125], v[104:105], v[12:13], v[100:101] op_sel:[0,0,1] op_sel_hi:[1,1,0]
	v_pk_fma_f32 v[12:13], v[104:105], v[12:13], v[100:101] op_sel:[0,0,1] op_sel_hi:[0,1,0] neg_lo:[0,0,1] neg_hi:[0,0,1]
	v_pk_mul_f32 v[100:101], v[102:103], v[20:21] op_sel_hi:[0,1]
	v_pk_fma_f32 v[126:127], v[102:103], v[20:21], v[100:101] op_sel:[1,0,1] op_sel_hi:[1,1,0] neg_lo:[0,0,1] neg_hi:[0,0,1]
	v_pk_fma_f32 v[20:21], v[102:103], v[20:21], v[100:101] op_sel:[1,0,1] op_sel_hi:[1,1,0]
	v_pk_mul_f32 v[100:101], v[102:103], v[28:29] op_sel_hi:[0,1]
	v_pk_fma_f32 v[116:117], v[102:103], v[28:29], v[100:101] op_sel:[1,0,1] op_sel_hi:[1,1,0] neg_lo:[0,0,1]
	v_mov_b32_e32 v127, v21
	v_pk_add_f32 v[28:29], v[24:25], v[116:117]
	v_pk_add_f32 v[20:21], v[16:17], v[126:127]
	v_pk_mul_f32 v[100:101], v[104:105], v[28:29] op_sel:[1,0]
	v_mov_b32_e32 v125, v13
	v_pk_fma_f32 v[102:103], v[104:105], v[28:29], v[100:101] op_sel:[0,0,1] op_sel_hi:[0,1,0] neg_hi:[0,0,1]
	s_nop 0
	v_pk_add_f32 v[28:29], v[20:21], v[102:103]
	v_pk_add_f32 v[12:13], v[4:5], v[124:125]
	s_waitcnt lgkmcnt(1)
	v_pk_mul_f32 v[100:101], v[110:111], v[28:29] op_sel:[1,0]
	v_pk_add_f32 v[8:9], v[8:9], v[120:121] neg_lo:[0,1] neg_hi:[0,1]
	v_pk_fma_f32 v[104:105], v[110:111], v[28:29], v[100:101] op_sel:[0,0,1] op_sel_hi:[0,1,0] neg_hi:[0,0,1]
	v_pk_mul_f32 v[100:101], v[106:107], v[10:11] op_sel_hi:[0,1]
	v_pk_add_f32 v[28:29], v[12:13], v[104:105]
	v_pk_add_f32 v[12:13], v[12:13], v[104:105] neg_lo:[0,1] neg_hi:[0,1]
	v_pk_fma_f32 v[104:105], v[106:107], v[10:11], v[100:101] op_sel:[1,0,1] op_sel_hi:[1,1,0] neg_lo:[0,0,1] neg_hi:[0,0,1]
	v_pk_fma_f32 v[10:11], v[106:107], v[10:11], v[100:101] op_sel:[1,0,1] op_sel_hi:[1,1,0]
	v_pk_mul_f32 v[100:101], v[106:107], v[26:27] op_sel_hi:[0,1]
	v_pk_fma_f32 v[114:115], v[106:107], v[26:27], v[100:101] op_sel:[1,0,1] op_sel_hi:[1,1,0] neg_lo:[0,0,1]
	v_mov_b32_e32 v105, v11
	v_pk_add_f32 v[26:27], v[18:19], v[114:115]
	v_pk_add_f32 v[10:11], v[2:3], v[104:105]
	v_pk_mul_f32 v[100:101], v[98:99], v[26:27] op_sel:[1,0]
	v_pk_add_f32 v[24:25], v[24:25], v[116:117] neg_lo:[0,1] neg_hi:[0,1]
	v_pk_fma_f32 v[106:107], v[98:99], v[26:27], v[100:101] op_sel:[0,0,1] op_sel_hi:[0,1,0] neg_hi:[0,0,1]
	v_pk_mul_f32 v[100:101], v[108:109], v[8:9] op_sel_hi:[0,1]
	v_pk_add_f32 v[26:27], v[10:11], v[106:107]
	v_pk_add_f32 v[10:11], v[10:11], v[106:107] neg_lo:[0,1] neg_hi:[0,1]
	v_pk_fma_f32 v[106:107], v[108:109], v[8:9], v[100:101] op_sel:[1,0,1] op_sel_hi:[1,1,0] neg_lo:[0,0,1] neg_hi:[0,0,1]
	v_pk_fma_f32 v[8:9], v[108:109], v[8:9], v[100:101] op_sel:[1,0,1] op_sel_hi:[1,1,0]
	v_pk_mul_f32 v[100:101], v[108:109], v[24:25] op_sel_hi:[0,1]
	v_pk_fma_f32 v[116:117], v[108:109], v[24:25], v[100:101] op_sel:[1,0,1] op_sel_hi:[1,1,0] neg_lo:[0,0,1]
	v_pk_add_f32 v[16:17], v[16:17], v[126:127] neg_lo:[0,1] neg_hi:[0,1]
	s_nop 0
	v_pk_add_f32 v[24:25], v[16:17], v[116:117]
	v_pk_add_f32 v[0:1], v[0:1], v[118:119] neg_lo:[0,1] neg_hi:[0,1]
	s_waitcnt lgkmcnt(0)
	v_pk_mul_f32 v[100:101], v[112:113], v[24:25] op_sel:[1,0]
	v_mov_b32_e32 v107, v9
	v_pk_fma_f32 v[108:109], v[112:113], v[24:25], v[100:101] op_sel:[0,0,1] op_sel_hi:[0,1,0] neg_hi:[0,0,1]
	v_pk_add_f32 v[22:23], v[22:23], v[184:185] neg_lo:[0,1] neg_hi:[0,1]
	v_pk_add_f32 v[8:9], v[0:1], v[106:107]
	v_pk_mul_f32 v[100:101], v[96:97], v[22:23] op_sel_hi:[0,1]
	v_pk_add_f32 v[20:21], v[20:21], v[102:103] neg_lo:[0,1] neg_hi:[0,1]
	v_pk_add_f32 v[24:25], v[8:9], v[108:109]
	v_pk_add_f32 v[8:9], v[8:9], v[108:109] neg_lo:[0,1] neg_hi:[0,1]
	v_pk_fma_f32 v[108:109], v[96:97], v[22:23], v[100:101] op_sel:[1,0,1] op_sel_hi:[1,1,0] neg_lo:[0,0,1] neg_hi:[0,0,1]
	v_pk_fma_f32 v[22:23], v[96:97], v[22:23], v[100:101] op_sel:[1,0,1] op_sel_hi:[1,1,0]
	v_pk_mul_f32 v[96:97], v[110:111], v[20:21] op_sel_hi:[0,1]
	v_pk_fma_f32 v[100:101], v[110:111], v[20:21], v[96:97] op_sel:[1,0,1] op_sel_hi:[1,1,0] neg_lo:[0,0,1]
	v_pk_add_f32 v[18:19], v[18:19], v[114:115] neg_lo:[0,1] neg_hi:[0,1]
	v_pk_add_f32 v[4:5], v[4:5], v[124:125] neg_lo:[0,1] neg_hi:[0,1]
	v_pk_mul_f32 v[96:97], v[98:99], v[18:19] op_sel_hi:[0,1]
	v_pk_add_f32 v[16:17], v[16:17], v[116:117] neg_lo:[0,1] neg_hi:[0,1]
	v_mov_b32_e32 v173, v15
	v_pk_add_f32 v[20:21], v[4:5], v[100:101]
	v_pk_add_f32 v[4:5], v[4:5], v[100:101] neg_lo:[0,1] neg_hi:[0,1]
	v_pk_fma_f32 v[100:101], v[98:99], v[18:19], v[96:97] op_sel:[1,0,1] op_sel_hi:[1,1,0] neg_lo:[0,0,1] neg_hi:[0,0,1]
	v_pk_fma_f32 v[18:19], v[98:99], v[18:19], v[96:97] op_sel:[1,0,1] op_sel_hi:[1,1,0]
	v_pk_mul_f32 v[96:97], v[112:113], v[16:17] op_sel_hi:[0,1]
	v_pk_add_f32 v[14:15], v[6:7], v[172:173]
	v_mov_b32_e32 v187, v31
	v_pk_fma_f32 v[98:99], v[112:113], v[16:17], v[96:97] op_sel:[1,0,1] op_sel_hi:[1,1,0] neg_lo:[0,0,1]
	v_pk_add_f32 v[30:31], v[14:15], v[186:187]
	v_pk_add_f32 v[6:7], v[6:7], v[172:173] neg_lo:[0,1] neg_hi:[0,1]
	v_mov_b32_e32 v109, v23
	v_pk_add_f32 v[2:3], v[2:3], v[104:105] neg_lo:[0,1] neg_hi:[0,1]
	v_mov_b32_e32 v101, v19
	v_pk_add_f32 v[0:1], v[0:1], v[106:107] neg_lo:[0,1] neg_hi:[0,1]
	v_pk_add_f32 v[14:15], v[14:15], v[186:187] neg_lo:[0,1] neg_hi:[0,1]
	v_pk_add_f32 v[22:23], v[6:7], v[108:109]
	v_pk_add_f32 v[6:7], v[6:7], v[108:109] neg_lo:[0,1] neg_hi:[0,1]
	v_pk_add_f32 v[18:19], v[2:3], v[100:101]
	v_pk_add_f32 v[2:3], v[2:3], v[100:101] neg_lo:[0,1] neg_hi:[0,1]
	v_pk_add_f32 v[16:17], v[0:1], v[98:99]
	v_pk_add_f32 v[0:1], v[0:1], v[98:99] neg_lo:[0,1] neg_hi:[0,1]
	ds_write2_b64 v132, v[30:31], v[28:29] offset1:2
	ds_write2_b64 v132, v[26:27], v[24:25] offset0:4 offset1:6
	ds_write2_b64 v132, v[22:23], v[20:21] offset0:8 offset1:10
	ds_write2_b64 v132, v[18:19], v[16:17] offset0:12 offset1:14
	ds_write2_b64 v132, v[14:15], v[12:13] offset0:16 offset1:18
	ds_write2_b64 v132, v[10:11], v[8:9] offset0:20 offset1:22
	ds_write2_b64 v132, v[6:7], v[4:5] offset0:24 offset1:26
	ds_write2_b64 v132, v[2:3], v[0:1] offset0:28 offset1:30
	s_waitcnt lgkmcnt(0)
	s_barrier
; template <int R, class XT, class TWT>
; __device__ __forceinline__ void dit_task(XT X, TWT tw, int s, int task) {
;     const int lgM = 13 - s, lgq = lgM - R, q = 1 << lgq;
;     const int j0 = task & (q - 1), blk = task >> lgq, base = (blk << lgM) + j0;
;     const int pb = PADI(base), qp = (q >= 32) ? q + (q >> 4) : q;
;     f32x2v v[1 << R];
; #pragma unroll
;     for (int k = 0; k < (1 << R); ++k) v[k] = X[pb + k * qp];
; #pragma unroll
;     for (int r = R - 1; r >= 0; --r) {
;         const int pb = R - 1 - r;
; #pragma unroll
;         for (int k = 0; k < (1 << R); ++k) if (!((k >> pb) & 1)) {
;             const int klo = k & ((1 << pb) - 1);
;             const f32x2v w = tw[(j0 + (klo << lgq)) << (s + r)];
;             const f32x2v a = v[k], qv = v[k + (1 << pb)]; const f32x2v b = (f32x2v){qv.x * w.x + qv.y * w.y, qv.y * w.x - qv.x * w.y};
;             v[k] = a + b; v[k + (1 << pb)] = a - b;
;         }
;     }
; #pragma unroll
;     for (int k = 0; k < (1 << R); ++k) X[pb + k * qp] = v[k];
; }
	ds_read2_b64 v[0:3], v130 offset1:34
	ds_read2_b64 v[4:7], v130 offset0:68 offset1:102
	ds_read2_b64 v[8:11], v130 offset0:136 offset1:170
	ds_read2_b64 v[12:15], v130 offset0:204 offset1:238
	ds_read2_b64 v[16:19], v94 offset0:16 offset1:50
	ds_read2_b64 v[20:23], v94 offset0:84 offset1:118
	ds_read2_b64 v[24:27], v94 offset0:152 offset1:186
	ds_read2_b64 v[28:31], v94 offset0:220 offset1:254
	ds_read_b64 v[100:101], v131
	ds_read_b64 v[102:103], v164
	ds_read_b64 v[104:105], v162
	ds_read_b64 v[106:107], v163
	ds_read2st64_b64 v[96:99], v159 offset1:16
	ds_read_b64 v[108:109], v133
	ds_read_b64 v[110:111], v160
	ds_read_b64 v[112:113], v161
	s_waitcnt lgkmcnt(7)
	v_xor_b32_e32 v95, 0x80000000, v100
	v_cndmask_b32_e64 v115, v95, v101, s[44:45]
	v_cndmask_b32_e64 v114, v101, v100, s[44:45]
	v_mov_b32_e32 v100, v115
	v_pk_mul_f32 v[116:117], v[2:3], v[100:101] op_sel_hi:[1,0]
	s_nop 0
	v_pk_fma_f32 v[118:119], v[2:3], v[114:115], v[116:117] op_sel:[0,0,1] op_sel_hi:[1,1,0]
	v_pk_fma_f32 v[2:3], v[2:3], v[114:115], v[116:117] op_sel:[0,0,1] op_sel_hi:[1,0,0] neg_lo:[0,0,1] neg_hi:[0,0,1]
	v_pk_mul_f32 v[116:117], v[6:7], v[100:101] op_sel_hi:[1,0]
	v_mov_b32_e32 v119, v3
	v_pk_fma_f32 v[120:121], v[6:7], v[114:115], v[116:117] op_sel:[0,0,1] op_sel_hi:[1,0,0] neg_hi:[0,0,1]
	v_pk_add_f32 v[2:3], v[0:1], v[118:119]
	v_pk_add_f32 v[6:7], v[4:5], v[120:121]
	v_pk_add_f32 v[4:5], v[4:5], v[120:121] neg_lo:[0,1] neg_hi:[0,1]
	s_waitcnt lgkmcnt(6)
	v_pk_mul_f32 v[116:117], v[102:103], v[6:7] op_sel:[1,0]
	v_pk_add_f32 v[0:1], v[0:1], v[118:119] neg_lo:[0,1] neg_hi:[0,1]
	v_pk_fma_f32 v[122:123], v[102:103], v[6:7], v[116:117] op_sel:[0,0,1] op_sel_hi:[1,1,0]
	v_pk_fma_f32 v[6:7], v[102:103], v[6:7], v[116:117] op_sel:[0,0,1] op_sel_hi:[0,1,0] neg_lo:[0,0,1] neg_hi:[0,0,1]
	v_pk_mul_f32 v[116:117], v[10:11], v[100:101] op_sel_hi:[1,0]
	v_mov_b32_e32 v123, v7
	v_pk_fma_f32 v[124:125], v[10:11], v[114:115], v[116:117] op_sel:[0,0,1] op_sel_hi:[1,1,0]
	v_pk_fma_f32 v[10:11], v[10:11], v[114:115], v[116:117] op_sel:[0,0,1] op_sel_hi:[1,0,0] neg_lo:[0,0,1] neg_hi:[0,0,1]
	v_pk_mul_f32 v[116:117], v[14:15], v[100:101] op_sel_hi:[1,0]
	v_mov_b32_e32 v125, v11
	v_pk_fma_f32 v[126:127], v[14:15], v[114:115], v[116:117] op_sel:[0,0,1] op_sel_hi:[1,0,0] neg_hi:[0,0,1]
	v_pk_add_f32 v[10:11], v[8:9], v[124:125]
	v_pk_add_f32 v[14:15], v[12:13], v[126:127]
	v_pk_add_f32 v[12:13], v[12:13], v[126:127] neg_lo:[0,1] neg_hi:[0,1]
	v_pk_mul_f32 v[116:117], v[102:103], v[14:15] op_sel:[1,0]
	v_pk_add_f32 v[8:9], v[8:9], v[124:125] neg_lo:[0,1] neg_hi:[0,1]
	v_pk_fma_f32 v[128:129], v[102:103], v[14:15], v[116:117] op_sel:[0,0,1] op_sel_hi:[0,1,0] neg_hi:[0,0,1]
	s_nop 0
	v_pk_add_f32 v[14:15], v[10:11], v[128:129]
	v_pk_add_f32 v[10:11], v[10:11], v[128:129] neg_lo:[0,1] neg_hi:[0,1]
	s_waitcnt lgkmcnt(5)
	v_pk_mul_f32 v[116:117], v[104:105], v[14:15] op_sel:[1,0]
	v_pk_add_f32 v[6:7], v[2:3], v[122:123]
	v_pk_fma_f32 v[172:173], v[104:105], v[14:15], v[116:117] op_sel:[0,0,1] op_sel_hi:[1,1,0]
	v_pk_fma_f32 v[14:15], v[104:105], v[14:15], v[116:117] op_sel:[0,0,1] op_sel_hi:[0,1,0] neg_lo:[0,0,1] neg_hi:[0,0,1]
	v_pk_mul_f32 v[116:117], v[18:19], v[100:101] op_sel_hi:[1,0]
	v_pk_add_f32 v[2:3], v[2:3], v[122:123] neg_lo:[0,1] neg_hi:[0,1]
	v_pk_fma_f32 v[174:175], v[18:19], v[114:115], v[116:117] op_sel:[0,0,1] op_sel_hi:[1,1,0]
	v_pk_fma_f32 v[18:19], v[18:19], v[114:115], v[116:117] op_sel:[0,0,1] op_sel_hi:[1,0,0] neg_lo:[0,0,1] neg_hi:[0,0,1]
	v_pk_mul_f32 v[116:117], v[22:23], v[100:101] op_sel_hi:[1,0]
	v_mov_b32_e32 v175, v19
	v_pk_fma_f32 v[176:177], v[22:23], v[114:115], v[116:117] op_sel:[0,0,1] op_sel_hi:[1,0,0] neg_hi:[0,0,1]
	v_pk_add_f32 v[18:19], v[16:17], v[174:175]
	v_pk_add_f32 v[22:23], v[20:21], v[176:177]
	v_pk_add_f32 v[20:21], v[20:21], v[176:177] neg_lo:[0,1] neg_hi:[0,1]
	v_pk_mul_f32 v[116:117], v[102:103], v[22:23] op_sel:[1,0]
	v_pk_add_f32 v[16:17], v[16:17], v[174:175] neg_lo:[0,1] neg_hi:[0,1]
	v_pk_fma_f32 v[178:179], v[102:103], v[22:23], v[116:117] op_sel:[0,0,1] op_sel_hi:[1,1,0]
	v_pk_fma_f32 v[22:23], v[102:103], v[22:23], v[116:117] op_sel:[0,0,1] op_sel_hi:[0,1,0] neg_lo:[0,0,1] neg_hi:[0,0,1]
	v_pk_mul_f32 v[116:117], v[26:27], v[100:101] op_sel_hi:[1,0]
	v_pk_mul_f32 v[100:101], v[30:31], v[100:101] op_sel_hi:[1,0]
	v_pk_fma_f32 v[182:183], v[26:27], v[114:115], v[116:117] op_sel:[0,0,1] op_sel_hi:[1,1,0]
	v_pk_fma_f32 v[26:27], v[26:27], v[114:115], v[116:117] op_sel:[0,0,1] op_sel_hi:[1,0,0] neg_lo:[0,0,1] neg_hi:[0,0,1]
	v_pk_fma_f32 v[116:117], v[30:31], v[114:115], v[100:101] op_sel:[0,0,1] op_sel_hi:[1,0,0] neg_hi:[0,0,1]
	v_mov_b32_e32 v183, v27
	v_pk_add_f32 v[30:31], v[28:29], v[116:117]
	v_pk_add_f32 v[26:27], v[24:25], v[182:183]
	v_pk_mul_f32 v[100:101], v[102:103], v[30:31] op_sel:[1,0]
	v_mov_b32_e32 v179, v23
	v_pk_fma_f32 v[114:115], v[102:103], v[30:31], v[100:101] op_sel:[0,0,1] op_sel_hi:[0,1,0] neg_hi:[0,0,1]
	s_nop 0
	v_pk_add_f32 v[30:31], v[26:27], v[114:115]
	v_pk_add_f32 v[22:23], v[18:19], v[178:179]
	v_pk_mul_f32 v[100:101], v[104:105], v[30:31] op_sel:[1,0]
	v_pk_add_f32 v[28:29], v[28:29], v[116:117] neg_lo:[0,1] neg_hi:[0,1]
	v_pk_fma_f32 v[184:185], v[104:105], v[30:31], v[100:101] op_sel:[0,0,1] op_sel_hi:[0,1,0] neg_hi:[0,0,1]
	s_nop 0
	v_pk_add_f32 v[30:31], v[22:23], v[184:185]
	v_pk_add_f32 v[24:25], v[24:25], v[182:183] neg_lo:[0,1] neg_hi:[0,1]
	s_waitcnt lgkmcnt(3)
; template <int R, class XT, class TWT>
; __device__ __forceinline__ void dit_task(XT X, TWT tw, int s, int task) {
;     const int lgM = 13 - s, lgq = lgM - R, q = 1 << lgq;
;     const int j0 = task & (q - 1), blk = task >> lgq, base = (blk << lgM) + j0;
;     const int pb = PADI(base), qp = (q >= 32) ? q + (q >> 4) : q;
;     f32x2v v[1 << R];
; #pragma unroll
;     for (int k = 0; k < (1 << R); ++k) v[k] = X[pb + k * qp];
; #pragma unroll
;     for (int r = R - 1; r >= 0; --r) {
;         const int pb = R - 1 - r;
; #pragma unroll
;         for (int k = 0; k < (1 << R); ++k) if (!((k >> pb) & 1)) {
;             const int klo = k & ((1 << pb) - 1);
;             const f32x2v w = tw[(j0 + (klo << lgq)) << (s + r)];
;             const f32x2v a = v[k], qv = v[k + (1 << pb)]; const f32x2v b = (f32x2v){qv.x * w.x + qv.y * w.y, qv.y * w.x - qv.x * w.y};
;             v[k] = a + b; v[k + (1 << pb)] = a - b;
;         }
;     }
; #pragma unroll
;     for (int k = 0; k < (1 << R); ++k) X[pb + k * qp] = v[k];
; }
	v_pk_mul_f32 v[100:101], v[96:97], v[30:31] op_sel:[1,0]
	v_pk_add_f32 v[26:27], v[26:27], v[114:115] neg_lo:[0,1] neg_hi:[0,1]
	v_pk_fma_f32 v[186:187], v[96:97], v[30:31], v[100:101] op_sel:[0,0,1] op_sel_hi:[1,1,0]
	v_pk_fma_f32 v[30:31], v[96:97], v[30:31], v[100:101] op_sel:[0,0,1] op_sel_hi:[0,1,0] neg_lo:[0,0,1] neg_hi:[0,0,1]
	v_pk_mul_f32 v[100:101], v[102:103], v[4:5] op_sel_hi:[0,1]
	v_pk_fma_f32 v[118:119], v[102:103], v[4:5], v[100:101] op_sel:[1,0,1] op_sel_hi:[1,1,0] neg_lo:[0,0,1] neg_hi:[0,0,1]
	v_pk_fma_f32 v[4:5], v[102:103], v[4:5], v[100:101] op_sel:[1,0,1] op_sel_hi:[1,1,0]
	v_pk_mul_f32 v[100:101], v[102:103], v[12:13] op_sel_hi:[0,1]
	v_pk_fma_f32 v[120:121], v[102:103], v[12:13], v[100:101] op_sel:[1,0,1] op_sel_hi:[1,1,0] neg_lo:[0,0,1]
	v_mov_b32_e32 v119, v5
	v_pk_add_f32 v[12:13], v[8:9], v[120:121]
	v_pk_add_f32 v[4:5], v[0:1], v[118:119]
	v_pk_mul_f32 v[100:101], v[106:107], v[12:13] op_sel:[1,0]
	v_pk_add_f32 v[18:19], v[18:19], v[178:179] neg_lo:[0,1] neg_hi:[0,1]
	v_pk_fma_f32 v[124:125], v[106:107], v[12:13], v[100:101] op_sel:[0,0,1] op_sel_hi:[1,1,0]
	v_pk_fma_f32 v[12:13], v[106:107], v[12:13], v[100:101] op_sel:[0,0,1] op_sel_hi:[0,1,0] neg_lo:[0,0,1] neg_hi:[0,0,1]
	v_pk_mul_f32 v[100:101], v[102:103], v[20:21] op_sel_hi:[0,1]
	v_pk_fma_f32 v[126:127], v[102:103], v[20:21], v[100:101] op_sel:[1,0,1] op_sel_hi:[1,1,0] neg_lo:[0,0,1] neg_hi:[0,0,1]
	v_pk_fma_f32 v[20:21], v[102:103], v[20:21], v[100:101] op_sel:[1,0,1] op_sel_hi:[1,1,0]
	v_pk_mul_f32 v[100:101], v[102:103], v[28:29] op_sel_hi:[0,1]
	v_pk_fma_f32 v[116:117], v[102:103], v[28:29], v[100:101] op_sel:[1,0,1] op_sel_hi:[1,1,0] neg_lo:[0,0,1]
	v_mov_b32_e32 v127, v21
	v_pk_add_f32 v[28:29], v[24:25], v[116:117]
	v_pk_add_f32 v[20:21], v[16:17], v[126:127]
	v_pk_mul_f32 v[100:101], v[106:107], v[28:29] op_sel:[1,0]
	v_mov_b32_e32 v125, v13
	v_pk_fma_f32 v[102:103], v[106:107], v[28:29], v[100:101] op_sel:[0,0,1] op_sel_hi:[0,1,0] neg_hi:[0,0,1]
	s_nop 0
	v_pk_add_f32 v[28:29], v[20:21], v[102:103]
	v_pk_add_f32 v[12:13], v[4:5], v[124:125]
	s_waitcnt lgkmcnt(1)
	v_pk_mul_f32 v[100:101], v[110:111], v[28:29] op_sel:[1,0]
	v_pk_add_f32 v[8:9], v[8:9], v[120:121] neg_lo:[0,1] neg_hi:[0,1]
	v_pk_fma_f32 v[106:107], v[110:111], v[28:29], v[100:101] op_sel:[0,0,1] op_sel_hi:[0,1,0] neg_hi:[0,0,1]
	v_pk_mul_f32 v[100:101], v[104:105], v[10:11] op_sel_hi:[0,1]
	v_pk_add_f32 v[28:29], v[12:13], v[106:107]
	v_pk_add_f32 v[12:13], v[12:13], v[106:107] neg_lo:[0,1] neg_hi:[0,1]
	v_pk_fma_f32 v[106:107], v[104:105], v[10:11], v[100:101] op_sel:[1,0,1] op_sel_hi:[1,1,0] neg_lo:[0,0,1] neg_hi:[0,0,1]
	v_pk_fma_f32 v[10:11], v[104:105], v[10:11], v[100:101] op_sel:[1,0,1] op_sel_hi:[1,1,0]
	v_pk_mul_f32 v[100:101], v[104:105], v[26:27] op_sel_hi:[0,1]
	v_pk_fma_f32 v[114:115], v[104:105], v[26:27], v[100:101] op_sel:[1,0,1] op_sel_hi:[1,1,0] neg_lo:[0,0,1]
	v_mov_b32_e32 v107, v11
	v_pk_add_f32 v[26:27], v[18:19], v[114:115]
	v_pk_add_f32 v[10:11], v[2:3], v[106:107]
	v_pk_mul_f32 v[100:101], v[98:99], v[26:27] op_sel:[1,0]
	v_pk_add_f32 v[24:25], v[24:25], v[116:117] neg_lo:[0,1] neg_hi:[0,1]
	v_pk_fma_f32 v[104:105], v[98:99], v[26:27], v[100:101] op_sel:[0,0,1] op_sel_hi:[0,1,0] neg_hi:[0,0,1]
	v_pk_mul_f32 v[100:101], v[108:109], v[8:9] op_sel_hi:[0,1]
	v_pk_add_f32 v[26:27], v[10:11], v[104:105]
	v_pk_add_f32 v[10:11], v[10:11], v[104:105] neg_lo:[0,1] neg_hi:[0,1]
	v_pk_fma_f32 v[104:105], v[108:109], v[8:9], v[100:101] op_sel:[1,0,1] op_sel_hi:[1,1,0] neg_lo:[0,0,1] neg_hi:[0,0,1]
	v_pk_fma_f32 v[8:9], v[108:109], v[8:9], v[100:101] op_sel:[1,0,1] op_sel_hi:[1,1,0]
	v_pk_mul_f32 v[100:101], v[108:109], v[24:25] op_sel_hi:[0,1]
	v_pk_fma_f32 v[116:117], v[108:109], v[24:25], v[100:101] op_sel:[1,0,1] op_sel_hi:[1,1,0] neg_lo:[0,0,1]
	v_pk_add_f32 v[16:17], v[16:17], v[126:127] neg_lo:[0,1] neg_hi:[0,1]
	s_nop 0
	v_pk_add_f32 v[24:25], v[16:17], v[116:117]
	v_pk_add_f32 v[0:1], v[0:1], v[118:119] neg_lo:[0,1] neg_hi:[0,1]
	s_waitcnt lgkmcnt(0)
	v_pk_mul_f32 v[100:101], v[112:113], v[24:25] op_sel:[1,0]
	v_mov_b32_e32 v105, v9
	v_pk_fma_f32 v[108:109], v[112:113], v[24:25], v[100:101] op_sel:[0,0,1] op_sel_hi:[0,1,0] neg_hi:[0,0,1]
	v_pk_add_f32 v[22:23], v[22:23], v[184:185] neg_lo:[0,1] neg_hi:[0,1]
	v_pk_add_f32 v[8:9], v[0:1], v[104:105]
	v_pk_mul_f32 v[100:101], v[96:97], v[22:23] op_sel_hi:[0,1]
	v_pk_add_f32 v[20:21], v[20:21], v[102:103] neg_lo:[0,1] neg_hi:[0,1]
	v_pk_add_f32 v[24:25], v[8:9], v[108:109]
	v_pk_add_f32 v[8:9], v[8:9], v[108:109] neg_lo:[0,1] neg_hi:[0,1]
	v_pk_fma_f32 v[108:109], v[96:97], v[22:23], v[100:101] op_sel:[1,0,1] op_sel_hi:[1,1,0] neg_lo:[0,0,1] neg_hi:[0,0,1]
	v_pk_fma_f32 v[22:23], v[96:97], v[22:23], v[100:101] op_sel:[1,0,1] op_sel_hi:[1,1,0]
	v_pk_mul_f32 v[96:97], v[110:111], v[20:21] op_sel_hi:[0,1]
	v_pk_fma_f32 v[100:101], v[110:111], v[20:21], v[96:97] op_sel:[1,0,1] op_sel_hi:[1,1,0] neg_lo:[0,0,1]
	v_pk_add_f32 v[18:19], v[18:19], v[114:115] neg_lo:[0,1] neg_hi:[0,1]
	v_pk_add_f32 v[4:5], v[4:5], v[124:125] neg_lo:[0,1] neg_hi:[0,1]
	v_pk_mul_f32 v[96:97], v[98:99], v[18:19] op_sel_hi:[0,1]
	v_pk_add_f32 v[16:17], v[16:17], v[116:117] neg_lo:[0,1] neg_hi:[0,1]
	v_mov_b32_e32 v173, v15
	v_pk_add_f32 v[20:21], v[4:5], v[100:101]
	v_pk_add_f32 v[4:5], v[4:5], v[100:101] neg_lo:[0,1] neg_hi:[0,1]
	v_pk_fma_f32 v[100:101], v[98:99], v[18:19], v[96:97] op_sel:[1,0,1] op_sel_hi:[1,1,0] neg_lo:[0,0,1] neg_hi:[0,0,1]
	v_pk_fma_f32 v[18:19], v[98:99], v[18:19], v[96:97] op_sel:[1,0,1] op_sel_hi:[1,1,0]
	v_pk_mul_f32 v[96:97], v[112:113], v[16:17] op_sel_hi:[0,1]
	v_pk_add_f32 v[14:15], v[6:7], v[172:173]
	v_mov_b32_e32 v187, v31
	v_pk_fma_f32 v[98:99], v[112:113], v[16:17], v[96:97] op_sel:[1,0,1] op_sel_hi:[1,1,0] neg_lo:[0,0,1]
	v_pk_add_f32 v[30:31], v[14:15], v[186:187]
	v_pk_add_f32 v[6:7], v[6:7], v[172:173] neg_lo:[0,1] neg_hi:[0,1]
	v_mov_b32_e32 v109, v23
	v_pk_add_f32 v[2:3], v[2:3], v[106:107] neg_lo:[0,1] neg_hi:[0,1]
	v_mov_b32_e32 v101, v19
	v_pk_add_f32 v[0:1], v[0:1], v[104:105] neg_lo:[0,1] neg_hi:[0,1]
	v_pk_add_f32 v[14:15], v[14:15], v[186:187] neg_lo:[0,1] neg_hi:[0,1]
	v_pk_add_f32 v[22:23], v[6:7], v[108:109]
	v_pk_add_f32 v[6:7], v[6:7], v[108:109] neg_lo:[0,1] neg_hi:[0,1]
	v_pk_add_f32 v[18:19], v[2:3], v[100:101]
	v_pk_add_f32 v[2:3], v[2:3], v[100:101] neg_lo:[0,1] neg_hi:[0,1]
	v_pk_add_f32 v[16:17], v[0:1], v[98:99]
	v_pk_add_f32 v[0:1], v[0:1], v[98:99] neg_lo:[0,1] neg_hi:[0,1]
	ds_write2_b64 v130, v[30:31], v[28:29] offset1:34
	ds_write2_b64 v130, v[26:27], v[24:25] offset0:68 offset1:102
	ds_write2_b64 v130, v[22:23], v[20:21] offset0:136 offset1:170
	ds_write2_b64 v130, v[18:19], v[16:17] offset0:204 offset1:238
	ds_write2_b64 v94, v[14:15], v[12:13] offset0:16 offset1:50
	ds_write2_b64 v94, v[10:11], v[8:9] offset0:84 offset1:118
	ds_write2_b64 v94, v[6:7], v[4:5] offset0:152 offset1:186
	ds_write2_b64 v94, v[2:3], v[0:1] offset0:220 offset1:254
	s_waitcnt lgkmcnt(0)
	s_barrier
; template <bool LAT>
; __device__ __forceinline__ void hyconv_unit(const Frame& F, LAS f32x2v* X, const TwHalf tw, LAS bf16* OUT, const float* skip, bf16* MIX, int u) {
;     ...
;                 { const bf16* g0 = H0 + (size_t)(ord * 256 + c0) * L + n; const bf16* g1 = H1 + (size_t)(ord * 256 + c0) * L + n; const bf16* v0 = H0 + (size_t)(512 + c0) * L + n; const bf16* v1 = H1 + (size_t)(512 + c0) * L + n;
; #pragma unroll
;                   for (int r = 0; r < 16; ++r) { g[r] = (f32x2v){0.f, 0.f}; zp[r] = g[r]; if (act) { g[r] = (f32x2v){bf2f(g0[r * L]), bf2f(g1[r * L])}; zp[r] = (f32x2v){bf2f(v0[r * L]), bf2f(v1[r * L])}; } } }
	v_lshl_add_u64 v[100:101], v[38:39], 0, s[90:91]
	v_lshl_add_u64 v[98:99], v[46:47], 0, s[90:91]
	v_mov_b32_e32 v0, 0
	v_mov_b32_e32 v2, 0
	v_mov_b32_e32 v3, 0
	v_mov_b32_e32 v4, 0
	v_mov_b32_e32 v5, 0
	s_and_saveexec_b64 s[0:1], s[40:41]
	s_cbranch_execz .LBB0_939
	global_load_ushort v1, v[100:101], off
	global_load_ushort v3, v[98:99], off
	global_load_ushort v4, v[34:35], off
	global_load_ushort v5, v[36:37], off
	s_waitcnt vmcnt(3)
	v_lshlrev_b32_e32 v2, 16, v1
	s_waitcnt vmcnt(2)
	v_lshlrev_b32_e32 v3, 16, v3
	s_waitcnt vmcnt(1)
	v_lshlrev_b32_e32 v4, 16, v4
	s_waitcnt vmcnt(0)
	v_lshlrev_b32_e32 v5, 16, v5
